# lever 7: __shfl_xor 16/32 in the P1/P11 QK-norm and rope epilogues by v_permlane16/32_swap instead of ds_bpermute + lgkmcnt(0) round trips (352 sites, bit-identical)
# speedup vs baseline: 1.0080x; 1.0080x over previous
;     __host__ __device__ bool next(int i, Unit& u) const {
;         const long L = (long)i * G + c; if (L >= nwg) return false;
;         int wgid = (int)L; { const int q = nwg / NXCD, r = nwg % NXCD, xcd = wgid % NXCD, off = wgid / NXCD; wgid = (xcd < r ? xcd * (q + 1) : r * (q + 1) + (xcd - r) * q) + off; }
;         const int nig = WGM * nN, gid = wgid / nig, fm = gid * WGM, gsz = (nM - fm) < WGM ? (nM - fm) : WGM;
;         u.pm = fm + ((wgid % nig) % gsz); u.pn = (wgid % nig) / gsz; u.pb = u.pn; return true;
; __global__ void __launch_bounds__(NWAVES * 64, 2) enc_fwd(Args args) {
;     ...
;             pg8::Gemm g{XN, WIN0, NTOK, L0_IN, DM / 2}; pg8::StaticOrder S; S.init(NTOK, L0_IN, Gg, blk);
;             pg8::EpiHeads0 E{AQ, AK, AV, BQ, BK, BV, args.in[4], args.in[5], args.in[6], args.in[7], (const pg8::f32x2e*)ROPE, QSCALE, QSCALE * KAPPA};
;             pg8::gemm_phase<pg8::EpiHeads0, pg8::StaticOrder, PG8_ALIGN, PG8_SP2, true>(lds, g, S, E);
.LBB0_141:
	s_and_b64 vcc, exec, s[4:5]
	s_cbranch_vccz .LBB0_284
	s_mov_b32 s98, -1
	s_mov_b32 s99, 0
	v_lshlrev_b32_e32 v240, 5, v0
	s_sub_u32 s100, 0x20000, s16
	global_load_dwordx4 v[242:245], v240, s[16:17]
	global_load_dwordx4 v[246:249], v240, s[16:17] offset:16
	v_add_u32_e32 v241, 0x20000, v240
	s_waitcnt vmcnt(0)
	ds_write_b128 v241, v[242:245]
	ds_write_b128 v241, v[246:249] offset:16
	s_waitcnt lgkmcnt(0)
	v_readlane_b32 s0, v254, 10
	s_cmpk_lt_i32 s0, 0x480
	s_cselect_b64 s[2:3], -1, 0
	s_cmpk_gt_i32 s0, 0x47f
	v_readfirstlane_b32 s0, v0
	s_cbranch_scc1 .LBB0_144
	s_ashr_i32 s1, s35, 3
	s_cmp_lt_i32 s34, 0
	s_movk_i32 s4, 0x91
	s_cselect_b32 s4, s4, 0x90
	s_mul_i32 s4, s34, s4
	s_add_i32 s4, s4, s1
	s_mul_hi_i32 s1, s4, 0x38e38e39
	s_lshr_b32 s5, s1, 31
	s_ashr_i32 s1, s1, 4
	s_add_i32 s1, s1, s5
	s_lshl_b32 s5, s1, 3
	s_mulk_i32 s1, 0x48
	s_sub_i32 s1, s4, s1
	s_bfe_i32 s4, s1, 0x80000
	s_bfe_u32 s4, s4, 0x3000c
	s_add_i32 s4, s1, s4
	s_bfe_i32 s6, s4, 0x80000
	s_and_b32 s4, s4, 0xf8
	s_sub_i32 s1, s1, s4
	s_sext_i32_i16 s7, s6
	s_sext_i32_i8 s1, s1
	s_add_i32 s6, s5, s1
	s_ashr_i32 s4, s7, 3

; template <bool F8OUT = false> __device__ __forceinline__ void head_tile_store(const f32x4 (&acc)[2][2][4][2], bf16_t* obase  , int opitch, const float* gain, float scale, const f32x2e* rope, int row0, int fq) {
;     ...
;             if (gain) {
;                 float ss = 0.f;
; #pragma unroll
;                 for (int bj = 0; bj < 2; ++bj)
; #pragma unroll
;                     for (int n = 0; n < 2; ++n) ss += (x[bj][n][0] * x[bj][n][0] + x[bj][n][1] * x[bj][n][1]) + (x[bj][n][2] * x[bj][n][2] + x[bj][n][3] * x[bj][n][3]);
;                 ss += __shfl_xor(ss, 16); ss += __shfl_xor(ss, 32);
;                 const float r = scale / sqrtf(ss * (1.f / 64.f) + 1e-6f);
; #pragma unroll
;                 for (int bj = 0; bj < 2; ++bj)
; #pragma unroll
;                     for (int n = 0; n < 2; ++n) x[bj][n] = x[bj][n] * r * g[bj][n];
.LBB0_165:
	v_mov_b64_e32 v[30:31], v[146:147]
	v_mov_b64_e32 v[26:27], v[150:151]
	v_mov_b64_e32 v[22:23], v[154:155]
	v_mov_b64_e32 v[18:19], v[158:159]
	s_and_b64 vcc, exec, s[6:7]
	v_mov_b64_e32 v[32:33], v[148:149]
	v_mov_b64_e32 v[28:29], v[152:153]
	v_mov_b64_e32 v[24:25], v[156:157]
	v_mov_b64_e32 v[20:21], v[160:161]
	s_cbranch_vccnz .LBB0_167
	v_pk_mul_f32 v[18:19], v[160:161], v[160:161]
	v_pk_mul_f32 v[20:21], v[158:159], v[158:159]
	s_nop 0
	v_pk_mov_b32 v[22:23], v[20:21], v[18:19] op_sel:[1,0]
	v_mov_b32_e32 v21, v19
	v_pk_add_f32 v[18:19], v[22:23], v[20:21]
	v_pk_mul_f32 v[20:21], v[156:157], v[156:157]
	v_pk_mul_f32 v[22:23], v[154:155], v[154:155]
	v_pk_add_f32 v[18:19], v[18:19], v[18:19] op_sel:[0,1] op_sel_hi:[1,0]
	v_pk_mov_b32 v[24:25], v[22:23], v[20:21] op_sel:[1,0]
	v_mov_b32_e32 v23, v21
	v_pk_add_f32 v[20:21], v[24:25], v[22:23]
	v_mul_f32_e32 v22, v146, v146
	v_mul_f32_e32 v23, v147, v147
	v_pk_add_f32 v[20:21], v[20:21], v[20:21] op_sel:[0,1] op_sel_hi:[1,0]
	v_mov_b32_e32 v19, v22
	v_mov_b32_e32 v21, v23
	v_pk_add_f32 v[18:19], v[18:19], v[20:21]
	v_mul_f32_e32 v20, v151, v151
	v_mul_f32_e32 v22, v153, v153
	v_mul_f32_e32 v24, v148, v148
	v_mul_f32_e32 v25, v149, v149
	v_pk_fma_f32 v[20:21], v[150:151], v[150:151], v[20:21] op_sel_hi:[1,1,0]
	v_pk_fma_f32 v[22:23], v[152:153], v[152:153], v[22:23] op_sel_hi:[1,1,0]
	v_mov_b32_e32 v21, v24
	v_mov_b32_e32 v23, v25
	v_pk_add_f32 v[20:21], v[20:21], v[22:23]
	s_nop 0
	v_pk_add_f32 v[18:19], v[18:19], v[20:21]
	v_and_b32_e32 v20, 64, v212
	v_add_f32_e32 v18, v18, v19
	v_xor_b32_e32 v19, 16, v212
	v_add_u32_e32 v20, 64, v20
	v_cmp_lt_i32_e32 vcc, v19, v20
	s_nop 1
	v_cndmask_b32_e32 v19, v212, v19, vcc
	v_lshlrev_b32_e32 v19, 2, v19
	v_mov_b32_e32 v19, v18
	s_nop 1
	v_permlane16_swap_b32_e32 v18, v19
	s_waitcnt lgkmcnt(0)
	v_add_f32_e32 v18, v18, v19
	v_xor_b32_e32 v19, 32, v212
	v_cmp_lt_i32_e32 vcc, v19, v20
	s_nop 1
	v_cndmask_b32_e32 v19, v212, v19, vcc
	v_lshlrev_b32_e32 v19, 2, v19
	v_mov_b32_e32 v19, v18
	s_nop 1
	v_permlane32_swap_b32_e32 v18, v19
	s_waitcnt lgkmcnt(0)
	v_add_f32_e32 v18, v18, v19
	v_fmamk_f32 v18, v18, 0x3c800000, v210
	v_mul_f32_e32 v19, 0x4f800000, v18
	v_cmp_gt_f32_e32 vcc, s28, v18
	s_nop 1
	v_cndmask_b32_e32 v18, v18, v19, vcc
	v_sqrt_f32_e32 v19, v18
	s_nop 0
	v_add_u32_e32 v20, -1, v19
	v_fma_f32 v21, -v20, v19, v18
	v_cmp_ge_f32_e64 s[4:5], 0, v21
	v_add_u32_e32 v21, 1, v19
	s_nop 0
	v_cndmask_b32_e64 v20, v19, v20, s[4:5]
	v_fma_f32 v19, -v21, v19, v18
	v_cmp_lt_f32_e64 s[4:5], 0, v19
	s_nop 1
	v_cndmask_b32_e64 v19, v20, v21, s[4:5]
	v_mul_f32_e32 v20, 0x37800000, v19
	v_cndmask_b32_e32 v19, v19, v20, vcc
	v_cmp_class_f32_e32 vcc, v18, v211
	s_nop 1
	v_cndmask_b32_e32 v18, v19, v18, vcc
	v_div_scale_f32 v19, s[0:1], v18, v18, 1.0
	v_rcp_f32_e32 v20, v19
	s_nop 0
	v_fma_f32 v21, -v19, v20, 1.0
	v_fmac_f32_e32 v20, v21, v20
	v_div_scale_f32 v21, vcc, 1.0, v18, 1.0
	v_mul_f32_e32 v22, v21, v20
	v_fma_f32 v23, -v19, v22, v21
	v_fmac_f32_e32 v22, v23, v20
	v_fma_f32 v19, -v19, v22, v21
	v_div_fmas_f32 v19, v19, v20, v22
	v_div_fixup_f32 v30, v19, v18, 1.0
	v_pk_mul_f32 v[18:19], v[158:159], v[30:31] op_sel_hi:[1,0]
	v_pk_mul_f32 v[20:21], v[160:161], v[30:31] op_sel_hi:[1,0]
	v_pk_mul_f32 v[22:23], v[154:155], v[30:31] op_sel_hi:[1,0]
	v_pk_mul_f32 v[24:25], v[156:157], v[30:31] op_sel_hi:[1,0]
	v_pk_mul_f32 v[26:27], v[150:151], v[30:31] op_sel_hi:[1,0]
	v_pk_mul_f32 v[28:29], v[152:153], v[30:31] op_sel_hi:[1,0]
	v_pk_mul_f32 v[164:165], v[146:147], v[30:31] op_sel_hi:[1,0]
	v_pk_mul_f32 v[30:31], v[148:149], v[30:31] op_sel_hi:[1,0]
	s_waitcnt vmcnt(0)
	v_pk_mul_f32 v[20:21], v[16:17], v[20:21]
	v_pk_mul_f32 v[18:19], v[14:15], v[18:19]
	v_pk_mul_f32 v[24:25], v[12:13], v[24:25]
	v_pk_mul_f32 v[22:23], v[10:11], v[22:23]
	v_pk_mul_f32 v[28:29], v[8:9], v[28:29]
	v_pk_mul_f32 v[26:27], v[6:7], v[26:27]
	v_pk_mul_f32 v[32:33], v[4:5], v[30:31]
	v_pk_mul_f32 v[30:31], v[2:3], v[164:165]
.LBB0_167:
	v_and_b32_e32 v162, 2, v162
	v_readlane_b32 s0, v255, 21
	v_cmp_eq_u32_e64 s[4:5], 0, v162
	v_and_b32_e32 v162, 8, v190
	v_readlane_b32 s1, v255, 22
	v_lshlrev_b32_e32 v174, 3, v162
	v_and_b32_e32 v185, 63, v188
	v_cndmask_b32_e64 v162, 0, 1, s[0:1]
	v_lshl_add_u64 v[186:187], s[16:17], 0, v[174:175]
	v_cmp_ne_u32_e64 s[8:9], 1, v162
	s_andn2_b64 vcc, exec, s[0:1]
	v_lshlrev_b32_e32 v198, 7, v185
	s_cbranch_vccnz .LBB0_169
; template <bool F8OUT = false> __device__ __forceinline__ void head_tile_store(const f32x4 (&acc)[2][2][4][2], bf16_t* obase  , int opitch, const float* gain, float scale, const f32x2e* rope, int row0, int fq) {
;     ...
;             if (rope) {
;                 const int t = row & 8191; const bool second = (fq & 2) != 0;
; #pragma unroll
;                 for (int bj = 0; bj < 2; ++bj) { const int pos = bj ? (t & 63) : (t >> 6); const f32x2e* tb = rope + pos * 16 + 8 * (fq & 1);
; #pragma unroll
;                     for (int n = 0; n < 2; ++n)
; #pragma unroll
;                         for (int e = 0; e < 4; ++e) { const float p = __shfl_xor(x[bj][n][e], 32); const f32x2e cs = tb[4 * n + e]; const float v = x[bj][n][e];
;                             x[bj][n][e] = second ? (p * cs.y + v * cs.x) : (v * cs.x - p * cs.y); } }
	v_and_b32_e32 v163, 64, v212
	v_xor_b32_e32 v162, 32, v212
	v_add_u32_e32 v163, 64, v163
	v_cmp_lt_i32_e32 vcc, v162, v163
	v_mov_b32_e32 v199, v175
	s_nop 0
	v_cndmask_b32_e32 v162, v212, v162, vcc
	v_lshlrev_b32_e32 v189, 2, v162
	v_lshlrev_b32_e32 v162, 1, v188
	v_and_b32_e32 v174, 0x3f80, v162
	v_lshl_add_u64 v[196:197], v[186:187], 0, v[174:175]
	v_add_u32_e32 v238, s100, v196
	ds_read_b128 v[162:165], v238 offset:48
	ds_read_b128 v[192:195], v238 offset:32
	ds_read_b128 v[214:217], v238 offset:16
	ds_read_b128 v[218:221], v238
	v_mov_b32_e32 v200, v18
	v_mov_b32_e32 v250, v18
	s_nop 1
	v_permlane32_swap_b32_e32 v250, v200
	v_cndmask_b32_e64 v200, v250, v200, s[98:99]
	v_mov_b32_e32 v201, v19
	v_mov_b32_e32 v251, v19
	s_nop 1
	v_permlane32_swap_b32_e32 v251, v201
	v_cndmask_b32_e64 v201, v251, v201, s[98:99]
	s_waitcnt lgkmcnt(0)
	v_mov_b32_e32 v196, v219
	v_mov_b32_e32 v197, v221
	s_waitcnt lgkmcnt(0)
	v_pk_mul_f32 v[196:197], v[196:197], v[200:201]
	v_mov_b32_e32 v219, v220
	v_cndmask_b32_e64 v197, v197, -v197, s[4:5]
	v_cndmask_b32_e64 v196, v196, -v196, s[4:5]
	v_pk_fma_f32 v[18:19], v[18:19], v[218:219], v[196:197]
	v_mov_b32_e32 v196, v20
	v_mov_b32_e32 v252, v20
	s_nop 1
	v_permlane32_swap_b32_e32 v252, v196
	v_cndmask_b32_e64 v196, v252, v196, s[98:99]
	v_mov_b32_e32 v197, v21
	v_mov_b32_e32 v253, v21
	s_nop 1
	v_permlane32_swap_b32_e32 v253, v197
	v_cndmask_b32_e64 v197, v253, v197, s[98:99]
	v_mov_b32_e32 v200, v215
	v_mov_b32_e32 v201, v217
	v_mov_b32_e32 v215, v216
	s_waitcnt lgkmcnt(0)
	v_pk_mul_f32 v[196:197], v[200:201], v[196:197]
	s_nop 0
	v_cndmask_b32_e64 v197, v197, -v197, s[4:5]
	v_cndmask_b32_e64 v196, v196, -v196, s[4:5]
	v_pk_fma_f32 v[20:21], v[20:21], v[214:215], v[196:197]
	v_mov_b32_e32 v196, v22
	v_mov_b32_e32 v250, v22
	s_nop 1
	v_permlane32_swap_b32_e32 v250, v196
	v_cndmask_b32_e64 v196, v250, v196, s[98:99]
	v_mov_b32_e32 v197, v23
	v_mov_b32_e32 v251, v23
	s_nop 1
	v_permlane32_swap_b32_e32 v251, v197
	v_cndmask_b32_e64 v197, v251, v197, s[98:99]
	v_mov_b32_e32 v200, v193
	v_mov_b32_e32 v201, v195
	v_mov_b32_e32 v193, v194
	s_waitcnt lgkmcnt(0)
	v_pk_mul_f32 v[196:197], v[200:201], v[196:197]
	s_nop 0
	v_cndmask_b32_e64 v195, v197, -v197, s[4:5]
	v_cndmask_b32_e64 v194, v196, -v196, s[4:5]
	v_pk_fma_f32 v[22:23], v[22:23], v[192:193], v[194:195]
	v_mov_b32_e32 v192, v24
	v_mov_b32_e32 v252, v24
	s_nop 1
	v_permlane32_swap_b32_e32 v252, v192
	v_cndmask_b32_e64 v192, v252, v192, s[98:99]
	v_mov_b32_e32 v193, v25
	v_mov_b32_e32 v253, v25
	s_nop 1
	v_permlane32_swap_b32_e32 v253, v193
	v_cndmask_b32_e64 v193, v253, v193, s[98:99]
	v_mov_b32_e32 v194, v163
	v_mov_b32_e32 v195, v165
	v_mov_b32_e32 v163, v164
	v_lshl_add_u64 v[196:197], v[186:187], 0, v[198:199]
	s_waitcnt lgkmcnt(0)
	v_pk_mul_f32 v[192:193], v[194:195], v[192:193]
	v_mov_b32_e32 v200, v26
	v_mov_b32_e32 v250, v26
	s_nop 1
	v_permlane32_swap_b32_e32 v250, v200
	v_cndmask_b32_e64 v200, v250, v200, s[98:99]
	v_cndmask_b32_e64 v165, v193, -v193, s[4:5]
	v_cndmask_b32_e64 v164, v192, -v192, s[4:5]
	v_pk_fma_f32 v[24:25], v[24:25], v[162:163], v[164:165]
	v_add_u32_e32 v238, s100, v196
	ds_read_b128 v[162:165], v238 offset:48
	ds_read_b128 v[192:195], v238 offset:32
	ds_read_b128 v[214:217], v238 offset:16
	ds_read_b128 v[218:221], v238
	v_mov_b32_e32 v201, v27
	v_mov_b32_e32 v251, v27
	s_nop 1
	v_permlane32_swap_b32_e32 v251, v201
	v_cndmask_b32_e64 v201, v251, v201, s[98:99]
	s_waitcnt lgkmcnt(0)
	v_mov_b32_e32 v196, v219
	v_mov_b32_e32 v197, v221
	s_waitcnt lgkmcnt(0)
	v_pk_mul_f32 v[196:197], v[196:197], v[200:201]
	v_mov_b32_e32 v219, v220
	v_cndmask_b32_e64 v197, v197, -v197, s[4:5]
	v_cndmask_b32_e64 v196, v196, -v196, s[4:5]
	v_pk_fma_f32 v[26:27], v[26:27], v[218:219], v[196:197]
	v_mov_b32_e32 v196, v28
	v_mov_b32_e32 v252, v28
	s_nop 1
	v_permlane32_swap_b32_e32 v252, v196
	v_cndmask_b32_e64 v196, v252, v196, s[98:99]
	v_mov_b32_e32 v197, v29
	v_mov_b32_e32 v253, v29
	s_nop 1
	v_permlane32_swap_b32_e32 v253, v197
	v_cndmask_b32_e64 v197, v253, v197, s[98:99]
	v_mov_b32_e32 v200, v215
	v_mov_b32_e32 v201, v217
	v_mov_b32_e32 v215, v216
	s_waitcnt lgkmcnt(0)
	v_pk_mul_f32 v[196:197], v[200:201], v[196:197]
	s_nop 0
	v_cndmask_b32_e64 v197, v197, -v197, s[4:5]
	v_cndmask_b32_e64 v196, v196, -v196, s[4:5]
	v_pk_fma_f32 v[28:29], v[28:29], v[214:215], v[196:197]
	v_mov_b32_e32 v196, v30
	v_mov_b32_e32 v250, v30
	s_nop 1
	v_permlane32_swap_b32_e32 v250, v196
	v_cndmask_b32_e64 v196, v250, v196, s[98:99]
	v_mov_b32_e32 v197, v31
	v_mov_b32_e32 v251, v31
	s_nop 1
	v_permlane32_swap_b32_e32 v251, v197
	v_cndmask_b32_e64 v197, v251, v197, s[98:99]
	v_mov_b32_e32 v200, v193
	v_mov_b32_e32 v201, v195
	v_mov_b32_e32 v193, v194
	s_waitcnt lgkmcnt(0)
	v_pk_mul_f32 v[196:197], v[200:201], v[196:197]
	s_nop 0
	v_cndmask_b32_e64 v195, v197, -v197, s[4:5]
	v_cndmask_b32_e64 v194, v196, -v196, s[4:5]
	v_pk_fma_f32 v[30:31], v[30:31], v[192:193], v[194:195]
	v_mov_b32_e32 v192, v32
	v_mov_b32_e32 v252, v32
	s_nop 1
	v_permlane32_swap_b32_e32 v252, v192
	v_cndmask_b32_e64 v192, v252, v192, s[98:99]
	v_mov_b32_e32 v193, v33
	v_mov_b32_e32 v253, v33
	s_nop 1
	v_permlane32_swap_b32_e32 v253, v193
	v_cndmask_b32_e64 v193, v253, v193, s[98:99]
	v_mov_b32_e32 v194, v163
	v_mov_b32_e32 v195, v165
	v_mov_b32_e32 v163, v164
	s_waitcnt lgkmcnt(0)
	v_pk_mul_f32 v[192:193], v[194:195], v[192:193]
	s_nop 0
	v_cndmask_b32_e64 v165, v193, -v193, s[4:5]
	v_cndmask_b32_e64 v164, v192, -v192, s[4:5]
	v_pk_fma_f32 v[32:33], v[32:33], v[162:163], v[164:165]
; __device__ __forceinline__ unsigned pk4_fp8(float a, float b, float c, float d) { unsigned w = 0u; w = __builtin_amdgcn_cvt_pk_fp8_f32(a, b, w, false); w = __builtin_amdgcn_cvt_pk_fp8_f32(c, d, w, true); return w; }
; template <bool F8OUT = false> __device__ __forceinline__ void head_tile_store(const f32x4 (&acc)[2][2][4][2], bf16_t* obase  , int opitch, const float* gain, float scale, const f32x2e* rope, int row0, int fq) {
;     ...
;             if (gain) {
;                 float ss = 0.f;
; #pragma unroll
;                 for (int bj = 0; bj < 2; ++bj)
; #pragma unroll
;                     for (int n = 0; n < 2; ++n) ss += (x[bj][n][0] * x[bj][n][0] + x[bj][n][1] * x[bj][n][1]) + (x[bj][n][2] * x[bj][n][2] + x[bj][n][3] * x[bj][n][3]);
;                 ss += __shfl_xor(ss, 16); ss += __shfl_xor(ss, 32);
;                 const float r = scale / sqrtf(ss * (1.f / 64.f) + 1e-6f);
; #pragma unroll
;                 for (int bj = 0; bj < 2; ++bj)
; #pragma unroll
;                     for (int n = 0; n < 2; ++n) x[bj][n] = x[bj][n] * r * g[bj][n];
;             }
;             if (rope) {
;                 const int t = row & 8191; const bool second = (fq & 2) != 0;
; #pragma unroll
;                 for (int bj = 0; bj < 2; ++bj) { const int pos = bj ? (t & 63) : (t >> 6); const f32x2e* tb = rope + pos * 16 + 8 * (fq & 1);
; #pragma unroll
;                     for (int n = 0; n < 2; ++n)
; #pragma unroll
;                         for (int e = 0; e < 4; ++e) { const float p = __shfl_xor(x[bj][n][e], 32); const f32x2e cs = tb[4 * n + e]; const float v = x[bj][n][e];
;                             x[bj][n][e] = second ? (p * cs.y + v * cs.x) : (v * cs.x - p * cs.y); } }
;             }
;             if constexpr (F8OUT) { unsigned char* rowp8 = (unsigned char*)obase + (size_t)row * opitch + 8 * fq; typedef unsigned u32x2_ __attribute__((ext_vector_type(2)));
; #pragma unroll
;                 for (int bj = 0; bj < 2; ++bj) *(u32x2_*)(rowp8 + 32 * bj) = (u32x2_){pk4_fp8(x[bj][0][0], x[bj][0][1], x[bj][0][2], x[bj][0][3]), pk4_fp8(x[bj][1][0], x[bj][1][1], x[bj][1][2], x[bj][1][3])};
;                 continue; }
.LBB0_169:
	v_mov_b32_e32 v162, v175
	v_mov_b32_e32 v163, v175
	v_cvt_pk_fp8_f32 v162, v18, v19
	v_cvt_pk_fp8_f32 v163, v22, v23
	v_mov_b32_e32 v18, v175
	v_mov_b32_e32 v19, v175
	v_cvt_pk_fp8_f32 v18, v26, v27
	v_cvt_pk_fp8_f32 v19, v30, v31
	v_readlane_b32 s0, v255, 27
	v_cvt_pk_fp8_f32 v162, v20, v21 op_sel:[0,0,1]
	v_cvt_pk_fp8_f32 v163, v24, v25 op_sel:[0,0,1]
	v_readlane_b32 s1, v255, 28
	v_ashrrev_i32_e32 v189, 31, v188
	v_cvt_pk_fp8_f32 v18, v28, v29 op_sel:[0,0,1]
	v_cvt_pk_fp8_f32 v19, v32, v33 op_sel:[0,0,1]
	v_lshl_add_u64 v[190:191], s[0:1], 0, v[190:191]
	v_lshlrev_b64 v[20:21], 7, v[188:189]
	v_lshl_add_u64 v[20:21], v[190:191], 0, v[20:21]
	global_store_dwordx2 v[20:21], v[162:163], off
	global_store_dwordx2 v[20:21], v[18:19], off offset:32
	v_mov_b64_e32 v[18:19], v[130:131]
	v_mov_b64_e32 v[22:23], v[134:135]
	v_mov_b64_e32 v[30:31], v[138:139]
	v_mov_b64_e32 v[26:27], v[142:143]
	s_and_b64 vcc, exec, s[6:7]
	v_mov_b64_e32 v[20:21], v[132:133]
	v_mov_b64_e32 v[24:25], v[136:137]
	v_mov_b64_e32 v[32:33], v[140:141]
	v_mov_b64_e32 v[28:29], v[144:145]
	s_cbranch_vccnz .LBB0_171
	v_pk_mul_f32 v[18:19], v[144:145], v[144:145]
	v_pk_mul_f32 v[20:21], v[142:143], v[142:143]
	s_nop 0
	v_pk_mov_b32 v[22:23], v[20:21], v[18:19] op_sel:[1,0]
	v_mov_b32_e32 v21, v19
	v_pk_add_f32 v[18:19], v[22:23], v[20:21]
	v_pk_mul_f32 v[20:21], v[140:141], v[140:141]
	v_pk_mul_f32 v[22:23], v[138:139], v[138:139]
	v_pk_add_f32 v[18:19], v[18:19], v[18:19] op_sel:[0,1] op_sel_hi:[1,0]
	v_pk_mov_b32 v[24:25], v[22:23], v[20:21] op_sel:[1,0]
	v_mov_b32_e32 v23, v21
	v_pk_add_f32 v[20:21], v[24:25], v[22:23]
	v_mul_f32_e32 v22, v130, v130
	v_mul_f32_e32 v23, v131, v131
	v_pk_add_f32 v[20:21], v[20:21], v[20:21] op_sel:[0,1] op_sel_hi:[1,0]
	v_mov_b32_e32 v19, v22
	v_mov_b32_e32 v21, v23
	v_pk_add_f32 v[18:19], v[18:19], v[20:21]
	v_mul_f32_e32 v20, v135, v135
	v_mul_f32_e32 v22, v137, v137
	v_mul_f32_e32 v24, v132, v132
	v_mul_f32_e32 v25, v133, v133
	v_pk_fma_f32 v[20:21], v[134:135], v[134:135], v[20:21] op_sel_hi:[1,1,0]
	v_pk_fma_f32 v[22:23], v[136:137], v[136:137], v[22:23] op_sel_hi:[1,1,0]
	v_mov_b32_e32 v21, v24
	v_mov_b32_e32 v23, v25
	v_pk_add_f32 v[20:21], v[20:21], v[22:23]
	s_nop 0
	v_pk_add_f32 v[18:19], v[18:19], v[20:21]
	v_and_b32_e32 v20, 64, v212
	v_add_f32_e32 v18, v18, v19
	v_xor_b32_e32 v19, 16, v212
	v_add_u32_e32 v20, 64, v20
	v_cmp_lt_i32_e32 vcc, v19, v20
	s_nop 1
	v_cndmask_b32_e32 v19, v212, v19, vcc
	v_lshlrev_b32_e32 v19, 2, v19
	v_mov_b32_e32 v19, v18
	s_nop 1
	v_permlane16_swap_b32_e32 v18, v19
	s_waitcnt lgkmcnt(0)
	v_add_f32_e32 v18, v18, v19
	v_xor_b32_e32 v19, 32, v212
	v_cmp_lt_i32_e32 vcc, v19, v20
	s_nop 1
	v_cndmask_b32_e32 v19, v212, v19, vcc
	v_lshlrev_b32_e32 v19, 2, v19
	v_mov_b32_e32 v19, v18
	s_nop 1
	v_permlane32_swap_b32_e32 v18, v19
	s_waitcnt lgkmcnt(0)
	v_add_f32_e32 v18, v18, v19
	v_fmamk_f32 v18, v18, 0x3c800000, v210
	v_mul_f32_e32 v19, 0x4f800000, v18
	v_cmp_gt_f32_e32 vcc, s28, v18
	s_nop 1
	v_cndmask_b32_e32 v18, v18, v19, vcc
	v_sqrt_f32_e32 v19, v18
	s_nop 0
	v_add_u32_e32 v20, -1, v19
	v_fma_f32 v21, -v20, v19, v18
	v_cmp_ge_f32_e64 s[10:11], 0, v21
	v_add_u32_e32 v21, 1, v19
	s_nop 0
	v_cndmask_b32_e64 v20, v19, v20, s[10:11]
	v_fma_f32 v19, -v21, v19, v18
	v_cmp_lt_f32_e64 s[10:11], 0, v19
	s_nop 1
	v_cndmask_b32_e64 v19, v20, v21, s[10:11]
	v_mul_f32_e32 v20, 0x37800000, v19
	v_cndmask_b32_e32 v19, v19, v20, vcc
	v_cmp_class_f32_e32 vcc, v18, v211
	s_nop 1
	v_cndmask_b32_e32 v18, v19, v18, vcc
	v_div_scale_f32 v19, s[0:1], v18, v18, 1.0
	v_rcp_f32_e32 v20, v19
	s_nop 0
	v_fma_f32 v21, -v19, v20, 1.0
	v_fmac_f32_e32 v20, v21, v20
	v_div_scale_f32 v21, vcc, 1.0, v18, 1.0
	v_mul_f32_e32 v22, v21, v20
	v_fma_f32 v23, -v19, v22, v21
	v_fmac_f32_e32 v22, v23, v20
	v_fma_f32 v19, -v19, v22, v21
	v_div_fmas_f32 v19, v19, v20, v22
	v_div_fixup_f32 v18, v19, v18, 1.0
	v_pk_mul_f32 v[20:21], v[142:143], v[18:19] op_sel_hi:[1,0]
	v_pk_mul_f32 v[22:23], v[144:145], v[18:19] op_sel_hi:[1,0]
	s_waitcnt vmcnt(0)
	v_pk_mul_f32 v[26:27], v[14:15], v[20:21]
	v_pk_mul_f32 v[28:29], v[16:17], v[22:23]
	v_pk_mul_f32 v[20:21], v[138:139], v[18:19] op_sel_hi:[1,0]
	v_pk_mul_f32 v[22:23], v[140:141], v[18:19] op_sel_hi:[1,0]
	v_pk_mul_f32 v[30:31], v[10:11], v[20:21]
	v_pk_mul_f32 v[32:33], v[12:13], v[22:23]
	v_pk_mul_f32 v[20:21], v[134:135], v[18:19] op_sel_hi:[1,0]
	v_pk_mul_f32 v[22:23], v[136:137], v[18:19] op_sel_hi:[1,0]
	v_pk_mul_f32 v[162:163], v[130:131], v[18:19] op_sel_hi:[1,0]
	v_pk_mul_f32 v[18:19], v[132:133], v[18:19] op_sel_hi:[1,0]
	v_pk_mul_f32 v[24:25], v[8:9], v[22:23]
	v_pk_mul_f32 v[22:23], v[6:7], v[20:21]
	v_pk_mul_f32 v[20:21], v[4:5], v[18:19]
	v_pk_mul_f32 v[18:19], v[2:3], v[162:163]
; template <bool F8OUT = false> __device__ __forceinline__ void head_tile_store(const f32x4 (&acc)[2][2][4][2], bf16_t* obase  , int opitch, const float* gain, float scale, const f32x2e* rope, int row0, int fq) {
;     ...
;             if (rope) {
;                 const int t = row & 8191; const bool second = (fq & 2) != 0;
; #pragma unroll
;                 for (int bj = 0; bj < 2; ++bj) { const int pos = bj ? (t & 63) : (t >> 6); const f32x2e* tb = rope + pos * 16 + 8 * (fq & 1);
; #pragma unroll
;                     for (int n = 0; n < 2; ++n)
; #pragma unroll
;                         for (int e = 0; e < 4; ++e) { const float p = __shfl_xor(x[bj][n][e], 32); const f32x2e cs = tb[4 * n + e]; const float v = x[bj][n][e];
;                             x[bj][n][e] = second ? (p * cs.y + v * cs.x) : (v * cs.x - p * cs.y); } }
.LBB0_171:
	v_add_u32_e32 v194, 16, v188
	v_and_b32_e32 v162, 63, v194
	s_and_b64 vcc, exec, s[8:9]
	v_lshlrev_b32_e32 v192, 7, v162
	s_cbranch_vccnz .LBB0_173
	v_and_b32_e32 v163, 64, v212
	v_xor_b32_e32 v162, 32, v212
	v_add_u32_e32 v163, 64, v163
	v_cmp_lt_i32_e32 vcc, v162, v163
	v_mov_b32_e32 v193, v175
	s_nop 0
	v_cndmask_b32_e32 v162, v212, v162, vcc
	v_lshlrev_b32_e32 v189, 2, v162
	v_lshlrev_b32_e32 v162, 1, v194
	v_and_b32_e32 v174, 0x3f80, v162
	v_lshl_add_u64 v[196:197], v[186:187], 0, v[174:175]
	v_add_u32_e32 v238, s100, v196
	ds_read_b128 v[162:165], v238 offset:48
	ds_read_b128 v[214:217], v238 offset:32
	ds_read_b128 v[218:221], v238 offset:16
	ds_read_b128 v[222:225], v238
	v_mov_b32_e32 v200, v26
	v_mov_b32_e32 v250, v26
	s_nop 1
	v_permlane32_swap_b32_e32 v250, v200
	v_cndmask_b32_e64 v200, v250, v200, s[98:99]
	v_mov_b32_e32 v201, v27
	v_mov_b32_e32 v251, v27
	s_nop 1
	v_permlane32_swap_b32_e32 v251, v201
	v_cndmask_b32_e64 v201, v251, v201, s[98:99]
	s_waitcnt lgkmcnt(0)
	v_mov_b32_e32 v196, v223
	v_mov_b32_e32 v197, v225
	s_waitcnt lgkmcnt(0)
	v_pk_mul_f32 v[196:197], v[196:197], v[200:201]
	v_mov_b32_e32 v223, v224
	v_cndmask_b32_e64 v197, v197, -v197, s[4:5]
	v_cndmask_b32_e64 v196, v196, -v196, s[4:5]
	v_pk_fma_f32 v[26:27], v[26:27], v[222:223], v[196:197]
	v_mov_b32_e32 v196, v28
	v_mov_b32_e32 v252, v28
	s_nop 1
	v_permlane32_swap_b32_e32 v252, v196
	v_cndmask_b32_e64 v196, v252, v196, s[98:99]
	v_mov_b32_e32 v197, v29
	v_mov_b32_e32 v253, v29
	s_nop 1
	v_permlane32_swap_b32_e32 v253, v197
	v_cndmask_b32_e64 v197, v253, v197, s[98:99]
	v_mov_b32_e32 v200, v219
	v_mov_b32_e32 v201, v221
	v_mov_b32_e32 v219, v220
	s_waitcnt lgkmcnt(0)
	v_pk_mul_f32 v[196:197], v[200:201], v[196:197]
	s_nop 0
	v_cndmask_b32_e64 v197, v197, -v197, s[4:5]
	v_cndmask_b32_e64 v196, v196, -v196, s[4:5]
	v_pk_fma_f32 v[28:29], v[28:29], v[218:219], v[196:197]
	v_mov_b32_e32 v196, v30
	v_mov_b32_e32 v250, v30
	s_nop 1
	v_permlane32_swap_b32_e32 v250, v196
	v_cndmask_b32_e64 v196, v250, v196, s[98:99]
	v_mov_b32_e32 v197, v31
	v_mov_b32_e32 v251, v31
	s_nop 1
	v_permlane32_swap_b32_e32 v251, v197
	v_cndmask_b32_e64 v197, v251, v197, s[98:99]
	v_mov_b32_e32 v200, v215
	v_mov_b32_e32 v201, v217
	v_mov_b32_e32 v215, v216
	s_waitcnt lgkmcnt(0)
	v_pk_mul_f32 v[196:197], v[200:201], v[196:197]
	s_nop 0
	v_cndmask_b32_e64 v197, v197, -v197, s[4:5]
	v_cndmask_b32_e64 v196, v196, -v196, s[4:5]
	v_pk_fma_f32 v[30:31], v[30:31], v[214:215], v[196:197]
	v_mov_b32_e32 v196, v32
	v_mov_b32_e32 v252, v32
	s_nop 1
	v_permlane32_swap_b32_e32 v252, v196
	v_cndmask_b32_e64 v196, v252, v196, s[98:99]
	v_mov_b32_e32 v197, v33
	v_mov_b32_e32 v253, v33
	s_nop 1
	v_permlane32_swap_b32_e32 v253, v197
	v_cndmask_b32_e64 v197, v253, v197, s[98:99]
	v_mov_b32_e32 v200, v163
	v_mov_b32_e32 v201, v165
	v_mov_b32_e32 v163, v164
	s_waitcnt lgkmcnt(0)
	v_pk_mul_f32 v[196:197], v[200:201], v[196:197]
	s_nop 0
	v_cndmask_b32_e64 v165, v197, -v197, s[4:5]
	v_cndmask_b32_e64 v164, v196, -v196, s[4:5]
	v_lshl_add_u64 v[196:197], v[186:187], 0, v[192:193]
	v_pk_fma_f32 v[32:33], v[32:33], v[162:163], v[164:165]
	v_add_u32_e32 v238, s100, v196
	ds_read_b128 v[162:165], v238 offset:48
	ds_read_b128 v[214:217], v238 offset:32
	ds_read_b128 v[218:221], v238 offset:16
	ds_read_b128 v[222:225], v238
	v_mov_b32_e32 v200, v22
	v_mov_b32_e32 v250, v22
	s_nop 1
	v_permlane32_swap_b32_e32 v250, v200
	v_cndmask_b32_e64 v200, v250, v200, s[98:99]
	v_mov_b32_e32 v201, v23
	v_mov_b32_e32 v251, v23
	s_nop 1
	v_permlane32_swap_b32_e32 v251, v201
	v_cndmask_b32_e64 v201, v251, v201, s[98:99]
	s_waitcnt lgkmcnt(0)
	v_mov_b32_e32 v196, v223
	v_mov_b32_e32 v197, v225
	s_waitcnt lgkmcnt(0)
	v_pk_mul_f32 v[196:197], v[196:197], v[200:201]
	v_mov_b32_e32 v223, v224
	v_cndmask_b32_e64 v197, v197, -v197, s[4:5]
	v_cndmask_b32_e64 v196, v196, -v196, s[4:5]
	v_pk_fma_f32 v[22:23], v[22:23], v[222:223], v[196:197]
	v_mov_b32_e32 v196, v24
	v_mov_b32_e32 v252, v24
	s_nop 1
	v_permlane32_swap_b32_e32 v252, v196
	v_cndmask_b32_e64 v196, v252, v196, s[98:99]
	v_mov_b32_e32 v197, v25
	v_mov_b32_e32 v253, v25
	s_nop 1
	v_permlane32_swap_b32_e32 v253, v197
	v_cndmask_b32_e64 v197, v253, v197, s[98:99]
	v_mov_b32_e32 v200, v219
	v_mov_b32_e32 v201, v221
	v_mov_b32_e32 v219, v220
	s_waitcnt lgkmcnt(0)
	v_pk_mul_f32 v[196:197], v[200:201], v[196:197]
	s_nop 0
	v_cndmask_b32_e64 v197, v197, -v197, s[4:5]
	v_cndmask_b32_e64 v196, v196, -v196, s[4:5]
	v_pk_fma_f32 v[24:25], v[24:25], v[218:219], v[196:197]
	v_mov_b32_e32 v196, v18
	v_mov_b32_e32 v250, v18
	s_nop 1
	v_permlane32_swap_b32_e32 v250, v196
	v_cndmask_b32_e64 v196, v250, v196, s[98:99]
	v_mov_b32_e32 v197, v19
	v_mov_b32_e32 v251, v19
	s_nop 1
	v_permlane32_swap_b32_e32 v251, v197
	v_cndmask_b32_e64 v197, v251, v197, s[98:99]
	v_mov_b32_e32 v200, v215
	v_mov_b32_e32 v201, v217
	v_mov_b32_e32 v215, v216
	s_waitcnt lgkmcnt(0)
	v_pk_mul_f32 v[196:197], v[200:201], v[196:197]
	s_nop 0
	v_cndmask_b32_e64 v197, v197, -v197, s[4:5]
	v_cndmask_b32_e64 v196, v196, -v196, s[4:5]
	v_pk_fma_f32 v[18:19], v[18:19], v[214:215], v[196:197]
	v_mov_b32_e32 v196, v20
	v_mov_b32_e32 v252, v20
	s_nop 1
	v_permlane32_swap_b32_e32 v252, v196
	v_cndmask_b32_e64 v196, v252, v196, s[98:99]
	v_mov_b32_e32 v197, v21
	v_mov_b32_e32 v253, v21
	s_nop 1
	v_permlane32_swap_b32_e32 v253, v197
	v_cndmask_b32_e64 v197, v253, v197, s[98:99]
	v_mov_b32_e32 v200, v163
	v_mov_b32_e32 v201, v165
	v_mov_b32_e32 v163, v164
	s_waitcnt lgkmcnt(0)
	v_pk_mul_f32 v[196:197], v[200:201], v[196:197]
	s_nop 0
	v_cndmask_b32_e64 v165, v197, -v197, s[4:5]
	v_cndmask_b32_e64 v164, v196, -v196, s[4:5]
	v_pk_fma_f32 v[20:21], v[20:21], v[162:163], v[164:165]
; __device__ __forceinline__ unsigned pk4_fp8(float a, float b, float c, float d) { unsigned w = 0u; w = __builtin_amdgcn_cvt_pk_fp8_f32(a, b, w, false); w = __builtin_amdgcn_cvt_pk_fp8_f32(c, d, w, true); return w; }
; template <bool F8OUT = false> __device__ __forceinline__ void head_tile_store(const f32x4 (&acc)[2][2][4][2], bf16_t* obase  , int opitch, const float* gain, float scale, const f32x2e* rope, int row0, int fq) {
;     ...
;             if (gain) {
;                 float ss = 0.f;
; #pragma unroll
;                 for (int bj = 0; bj < 2; ++bj)
; #pragma unroll
;                     for (int n = 0; n < 2; ++n) ss += (x[bj][n][0] * x[bj][n][0] + x[bj][n][1] * x[bj][n][1]) + (x[bj][n][2] * x[bj][n][2] + x[bj][n][3] * x[bj][n][3]);
;                 ss += __shfl_xor(ss, 16); ss += __shfl_xor(ss, 32);
;                 const float r = scale / sqrtf(ss * (1.f / 64.f) + 1e-6f);
; #pragma unroll
;                 for (int bj = 0; bj < 2; ++bj)
; #pragma unroll
;                     for (int n = 0; n < 2; ++n) x[bj][n] = x[bj][n] * r * g[bj][n];
;             }
;             if (rope) {
;                 const int t = row & 8191; const bool second = (fq & 2) != 0;
; #pragma unroll
;                 for (int bj = 0; bj < 2; ++bj) { const int pos = bj ? (t & 63) : (t >> 6); const f32x2e* tb = rope + pos * 16 + 8 * (fq & 1);
; #pragma unroll
;                     for (int n = 0; n < 2; ++n)
; #pragma unroll
;                         for (int e = 0; e < 4; ++e) { const float p = __shfl_xor(x[bj][n][e], 32); const f32x2e cs = tb[4 * n + e]; const float v = x[bj][n][e];
;                             x[bj][n][e] = second ? (p * cs.y + v * cs.x) : (v * cs.x - p * cs.y); } }
;             }
;             if constexpr (F8OUT) { unsigned char* rowp8 = (unsigned char*)obase + (size_t)row * opitch + 8 * fq; typedef unsigned u32x2_ __attribute__((ext_vector_type(2)));
; #pragma unroll
;                 for (int bj = 0; bj < 2; ++bj) *(u32x2_*)(rowp8 + 32 * bj) = (u32x2_){pk4_fp8(x[bj][0][0], x[bj][0][1], x[bj][0][2], x[bj][0][3]), pk4_fp8(x[bj][1][0], x[bj][1][1], x[bj][1][2], x[bj][1][3])};
;                 continue; }
.LBB0_173:
	v_mov_b32_e32 v164, v175
	v_cvt_pk_fp8_f32 v164, v26, v27
	v_mov_b32_e32 v26, v175
	v_mov_b32_e32 v27, v175
	v_cvt_pk_fp8_f32 v26, v22, v23
	v_cvt_pk_fp8_f32 v27, v18, v19
	v_mov_b32_e32 v165, v175
	v_cvt_pk_fp8_f32 v165, v30, v31
	v_cvt_pk_fp8_f32 v26, v24, v25 op_sel:[0,0,1]
	v_cvt_pk_fp8_f32 v27, v20, v21 op_sel:[0,0,1]
	v_ashrrev_i32_e32 v195, 31, v194
	v_lshlrev_b64 v[162:163], 7, v[194:195]
	v_cvt_pk_fp8_f32 v164, v28, v29 op_sel:[0,0,1]
	v_cvt_pk_fp8_f32 v165, v32, v33 op_sel:[0,0,1]
	v_lshl_add_u64 v[162:163], v[190:191], 0, v[162:163]
	global_store_dwordx2 v[162:163], v[26:27], off offset:32
	v_mov_b64_e32 v[18:19], v[114:115]
	v_mov_b64_e32 v[22:23], v[118:119]
	v_mov_b64_e32 v[30:31], v[122:123]
	v_mov_b64_e32 v[26:27], v[126:127]
	s_and_b64 vcc, exec, s[6:7]
	v_mov_b64_e32 v[20:21], v[116:117]
	v_mov_b64_e32 v[24:25], v[120:121]
	v_mov_b64_e32 v[32:33], v[124:125]
	v_mov_b64_e32 v[28:29], v[128:129]
	global_store_dwordx2 v[162:163], v[164:165], off
	s_cbranch_vccnz .LBB0_175
	v_pk_mul_f32 v[18:19], v[128:129], v[128:129]
	v_pk_mul_f32 v[20:21], v[126:127], v[126:127]
	s_nop 0
	v_pk_mov_b32 v[22:23], v[20:21], v[18:19] op_sel:[1,0]
	v_mov_b32_e32 v21, v19
	v_pk_add_f32 v[18:19], v[22:23], v[20:21]
	v_pk_mul_f32 v[20:21], v[124:125], v[124:125]
	v_pk_mul_f32 v[22:23], v[122:123], v[122:123]
	v_pk_add_f32 v[18:19], v[18:19], v[18:19] op_sel:[0,1] op_sel_hi:[1,0]
	v_pk_mov_b32 v[24:25], v[22:23], v[20:21] op_sel:[1,0]
	v_mov_b32_e32 v23, v21
	v_pk_add_f32 v[20:21], v[24:25], v[22:23]
	v_mul_f32_e32 v22, v114, v114
	v_mul_f32_e32 v23, v115, v115
	v_pk_add_f32 v[20:21], v[20:21], v[20:21] op_sel:[0,1] op_sel_hi:[1,0]
	v_mov_b32_e32 v19, v22
	v_mov_b32_e32 v21, v23
	v_pk_add_f32 v[18:19], v[18:19], v[20:21]
	v_mul_f32_e32 v20, v119, v119
	v_mul_f32_e32 v22, v121, v121
	v_mul_f32_e32 v24, v116, v116
	v_mul_f32_e32 v25, v117, v117
	v_pk_fma_f32 v[20:21], v[118:119], v[118:119], v[20:21] op_sel_hi:[1,1,0]
	v_pk_fma_f32 v[22:23], v[120:121], v[120:121], v[22:23] op_sel_hi:[1,1,0]
	v_mov_b32_e32 v21, v24
	v_mov_b32_e32 v23, v25
	v_pk_add_f32 v[20:21], v[20:21], v[22:23]
	s_nop 0
	v_pk_add_f32 v[18:19], v[18:19], v[20:21]
	v_and_b32_e32 v20, 64, v212
	v_add_f32_e32 v18, v18, v19
	v_xor_b32_e32 v19, 16, v212
	v_add_u32_e32 v20, 64, v20
	v_cmp_lt_i32_e32 vcc, v19, v20
	s_nop 1
	v_cndmask_b32_e32 v19, v212, v19, vcc
	v_lshlrev_b32_e32 v19, 2, v19
	v_mov_b32_e32 v19, v18
	s_nop 1
	v_permlane16_swap_b32_e32 v18, v19
	s_waitcnt lgkmcnt(0)
	v_add_f32_e32 v18, v18, v19
	v_xor_b32_e32 v19, 32, v212
	v_cmp_lt_i32_e32 vcc, v19, v20
	s_nop 1
	v_cndmask_b32_e32 v19, v212, v19, vcc
	v_lshlrev_b32_e32 v19, 2, v19
	v_mov_b32_e32 v19, v18
	s_nop 1
	v_permlane32_swap_b32_e32 v18, v19
	s_waitcnt lgkmcnt(0)
	v_add_f32_e32 v18, v18, v19
	v_fmamk_f32 v18, v18, 0x3c800000, v210
	v_mul_f32_e32 v19, 0x4f800000, v18
	v_cmp_gt_f32_e32 vcc, s28, v18
	s_nop 1
	v_cndmask_b32_e32 v18, v18, v19, vcc
	v_sqrt_f32_e32 v19, v18
	s_nop 0
	v_add_u32_e32 v20, -1, v19
	v_fma_f32 v21, -v20, v19, v18
	v_cmp_ge_f32_e64 s[10:11], 0, v21
	v_add_u32_e32 v21, 1, v19
	s_nop 0
	v_cndmask_b32_e64 v20, v19, v20, s[10:11]
	v_fma_f32 v19, -v21, v19, v18
	v_cmp_lt_f32_e64 s[10:11], 0, v19
	s_nop 1
	v_cndmask_b32_e64 v19, v20, v21, s[10:11]
	v_mul_f32_e32 v20, 0x37800000, v19
	v_cndmask_b32_e32 v19, v19, v20, vcc
	v_cmp_class_f32_e32 vcc, v18, v211
	s_nop 1
	v_cndmask_b32_e32 v18, v19, v18, vcc
	v_div_scale_f32 v19, s[0:1], v18, v18, 1.0
	v_rcp_f32_e32 v20, v19
	s_nop 0
	v_fma_f32 v21, -v19, v20, 1.0
	v_fmac_f32_e32 v20, v21, v20
	v_div_scale_f32 v21, vcc, 1.0, v18, 1.0
	v_mul_f32_e32 v22, v21, v20
	v_fma_f32 v23, -v19, v22, v21
	v_fmac_f32_e32 v22, v23, v20
	v_fma_f32 v19, -v19, v22, v21
	v_div_fmas_f32 v19, v19, v20, v22
	v_div_fixup_f32 v18, v19, v18, 1.0
	v_pk_mul_f32 v[20:21], v[126:127], v[18:19] op_sel_hi:[1,0]
	v_pk_mul_f32 v[22:23], v[128:129], v[18:19] op_sel_hi:[1,0]
	s_waitcnt vmcnt(0)
	v_pk_mul_f32 v[26:27], v[14:15], v[20:21]
	v_pk_mul_f32 v[28:29], v[16:17], v[22:23]
	v_pk_mul_f32 v[20:21], v[122:123], v[18:19] op_sel_hi:[1,0]
	v_pk_mul_f32 v[22:23], v[124:125], v[18:19] op_sel_hi:[1,0]
	v_pk_mul_f32 v[30:31], v[10:11], v[20:21]
	v_pk_mul_f32 v[32:33], v[12:13], v[22:23]
	v_pk_mul_f32 v[20:21], v[118:119], v[18:19] op_sel_hi:[1,0]
	v_pk_mul_f32 v[22:23], v[120:121], v[18:19] op_sel_hi:[1,0]
	v_pk_mul_f32 v[162:163], v[114:115], v[18:19] op_sel_hi:[1,0]
	v_pk_mul_f32 v[18:19], v[116:117], v[18:19] op_sel_hi:[1,0]
	v_pk_mul_f32 v[24:25], v[8:9], v[22:23]
	v_pk_mul_f32 v[22:23], v[6:7], v[20:21]
	v_pk_mul_f32 v[20:21], v[4:5], v[18:19]
	v_pk_mul_f32 v[18:19], v[2:3], v[162:163]
; template <bool F8OUT = false> __device__ __forceinline__ void head_tile_store(const f32x4 (&acc)[2][2][4][2], bf16_t* obase  , int opitch, const float* gain, float scale, const f32x2e* rope, int row0, int fq) {
;     ...
;             if (rope) {
;                 const int t = row & 8191; const bool second = (fq & 2) != 0;
; #pragma unroll
;                 for (int bj = 0; bj < 2; ++bj) { const int pos = bj ? (t & 63) : (t >> 6); const f32x2e* tb = rope + pos * 16 + 8 * (fq & 1);
; #pragma unroll
;                     for (int n = 0; n < 2; ++n)
; #pragma unroll
;                         for (int e = 0; e < 4; ++e) { const float p = __shfl_xor(x[bj][n][e], 32); const f32x2e cs = tb[4 * n + e]; const float v = x[bj][n][e];
;                             x[bj][n][e] = second ? (p * cs.y + v * cs.x) : (v * cs.x - p * cs.y); } }
.LBB0_175:
	v_xor_b32_e32 v162, 32, v185
	v_add_u32_e32 v196, 32, v188
	s_and_b64 vcc, exec, s[8:9]
	v_lshlrev_b32_e32 v194, 7, v162
	s_cbranch_vccnz .LBB0_177
	v_and_b32_e32 v163, 64, v212
	v_xor_b32_e32 v162, 32, v212
	v_add_u32_e32 v163, 64, v163
	v_cmp_lt_i32_e32 vcc, v162, v163
	v_mov_b32_e32 v195, v175
	s_nop 0
	v_cndmask_b32_e32 v162, v212, v162, vcc
	v_lshlrev_b32_e32 v185, 2, v162
	v_lshlrev_b32_e32 v162, 1, v196
	v_and_b32_e32 v174, 0x3f80, v162
	v_lshl_add_u64 v[200:201], v[186:187], 0, v[174:175]
	v_add_u32_e32 v238, s100, v200
	ds_read_b128 v[162:165], v238 offset:48
	ds_read_b128 v[214:217], v238 offset:32
	ds_read_b128 v[218:221], v238 offset:16
	ds_read_b128 v[222:225], v238
	v_mov_b32_e32 v226, v26
	v_mov_b32_e32 v250, v26
	s_nop 1
	v_permlane32_swap_b32_e32 v250, v226
	v_cndmask_b32_e64 v226, v250, v226, s[98:99]
	v_mov_b32_e32 v227, v27
	v_mov_b32_e32 v251, v27
	s_nop 1
	v_permlane32_swap_b32_e32 v251, v227
	v_cndmask_b32_e64 v227, v251, v227, s[98:99]
	s_waitcnt lgkmcnt(0)
	v_mov_b32_e32 v200, v223
	v_mov_b32_e32 v201, v225
	s_waitcnt lgkmcnt(0)
	v_pk_mul_f32 v[200:201], v[200:201], v[226:227]
	v_mov_b32_e32 v223, v224
	v_cndmask_b32_e64 v201, v201, -v201, s[4:5]
	v_cndmask_b32_e64 v200, v200, -v200, s[4:5]
	v_pk_fma_f32 v[26:27], v[26:27], v[222:223], v[200:201]
	v_mov_b32_e32 v200, v28
	v_mov_b32_e32 v252, v28
	s_nop 1
	v_permlane32_swap_b32_e32 v252, v200
	v_cndmask_b32_e64 v200, v252, v200, s[98:99]
	v_mov_b32_e32 v201, v29
	v_mov_b32_e32 v253, v29
	s_nop 1
	v_permlane32_swap_b32_e32 v253, v201
	v_cndmask_b32_e64 v201, v253, v201, s[98:99]
	v_mov_b32_e32 v222, v219
	v_mov_b32_e32 v223, v221
	v_mov_b32_e32 v219, v220
	v_mov_b32_e32 v226, v22
	v_mov_b32_e32 v250, v22
	s_nop 1
	v_permlane32_swap_b32_e32 v250, v226
	v_cndmask_b32_e64 v226, v250, v226, s[98:99]
	s_waitcnt lgkmcnt(1)
	v_pk_mul_f32 v[200:201], v[222:223], v[200:201]
	v_mov_b32_e32 v227, v23
	v_mov_b32_e32 v251, v23
	s_nop 1
	v_permlane32_swap_b32_e32 v251, v227
	v_cndmask_b32_e64 v227, v251, v227, s[98:99]
	v_cndmask_b32_e64 v201, v201, -v201, s[4:5]
	v_cndmask_b32_e64 v200, v200, -v200, s[4:5]
	v_pk_fma_f32 v[28:29], v[28:29], v[218:219], v[200:201]
	v_mov_b32_e32 v200, v30
	v_mov_b32_e32 v252, v30
	s_nop 1
	v_permlane32_swap_b32_e32 v252, v200
	v_cndmask_b32_e64 v200, v252, v200, s[98:99]
	v_mov_b32_e32 v201, v31
	v_mov_b32_e32 v253, v31
	s_nop 1
	v_permlane32_swap_b32_e32 v253, v201
	v_cndmask_b32_e64 v201, v253, v201, s[98:99]
	v_mov_b32_e32 v218, v215
	v_mov_b32_e32 v219, v217
	v_mov_b32_e32 v215, v216
	s_waitcnt lgkmcnt(0)
	v_pk_mul_f32 v[200:201], v[218:219], v[200:201]
	s_nop 0
	v_cndmask_b32_e64 v201, v201, -v201, s[4:5]
	v_cndmask_b32_e64 v200, v200, -v200, s[4:5]
	v_pk_fma_f32 v[30:31], v[30:31], v[214:215], v[200:201]
	v_mov_b32_e32 v200, v32
	v_mov_b32_e32 v250, v32
	s_nop 1
	v_permlane32_swap_b32_e32 v250, v200
	v_cndmask_b32_e64 v200, v250, v200, s[98:99]
	v_mov_b32_e32 v201, v33
	v_mov_b32_e32 v251, v33
	s_nop 1
	v_permlane32_swap_b32_e32 v251, v201
	v_cndmask_b32_e64 v201, v251, v201, s[98:99]
	v_mov_b32_e32 v214, v163
	v_mov_b32_e32 v215, v165
	v_mov_b32_e32 v163, v164
	s_waitcnt lgkmcnt(0)
	v_pk_mul_f32 v[200:201], v[214:215], v[200:201]
	s_nop 0
	v_cndmask_b32_e64 v165, v201, -v201, s[4:5]
	v_cndmask_b32_e64 v164, v200, -v200, s[4:5]
	v_lshl_add_u64 v[200:201], v[186:187], 0, v[194:195]
	v_pk_fma_f32 v[32:33], v[32:33], v[162:163], v[164:165]
	v_add_u32_e32 v238, s100, v200
	ds_read_b128 v[162:165], v238 offset:48
	ds_read_b128 v[214:217], v238 offset:32
	ds_read_b128 v[218:221], v238 offset:16
	ds_read_b128 v[222:225], v238
	s_waitcnt lgkmcnt(0)
	v_mov_b32_e32 v200, v223
	v_mov_b32_e32 v201, v225
	v_pk_mul_f32 v[200:201], v[200:201], v[226:227]
	v_mov_b32_e32 v223, v224
	v_cndmask_b32_e64 v201, v201, -v201, s[4:5]
	v_cndmask_b32_e64 v200, v200, -v200, s[4:5]
	v_pk_fma_f32 v[22:23], v[22:23], v[222:223], v[200:201]
	v_mov_b32_e32 v200, v24
	v_mov_b32_e32 v252, v24
	s_nop 1
	v_permlane32_swap_b32_e32 v252, v200
	v_cndmask_b32_e64 v200, v252, v200, s[98:99]
	v_mov_b32_e32 v201, v25
	v_mov_b32_e32 v253, v25
	s_nop 1
	v_permlane32_swap_b32_e32 v253, v201
	v_cndmask_b32_e64 v201, v253, v201, s[98:99]
	v_mov_b32_e32 v222, v219
	v_mov_b32_e32 v223, v221
	v_mov_b32_e32 v219, v220
	s_waitcnt lgkmcnt(0)
	v_pk_mul_f32 v[200:201], v[222:223], v[200:201]
	s_nop 0
	v_cndmask_b32_e64 v201, v201, -v201, s[4:5]
	v_cndmask_b32_e64 v200, v200, -v200, s[4:5]
	v_pk_fma_f32 v[24:25], v[24:25], v[218:219], v[200:201]
	v_mov_b32_e32 v200, v18
	v_mov_b32_e32 v250, v18
	s_nop 1
	v_permlane32_swap_b32_e32 v250, v200
	v_cndmask_b32_e64 v200, v250, v200, s[98:99]
	v_mov_b32_e32 v201, v19
	v_mov_b32_e32 v251, v19
	s_nop 1
	v_permlane32_swap_b32_e32 v251, v201
	v_cndmask_b32_e64 v201, v251, v201, s[98:99]
	v_mov_b32_e32 v218, v215
	v_mov_b32_e32 v219, v217
	v_mov_b32_e32 v215, v216
	s_waitcnt lgkmcnt(0)
	v_pk_mul_f32 v[200:201], v[218:219], v[200:201]
	s_nop 0
	v_cndmask_b32_e64 v201, v201, -v201, s[4:5]
	v_cndmask_b32_e64 v200, v200, -v200, s[4:5]
	v_pk_fma_f32 v[18:19], v[18:19], v[214:215], v[200:201]
	v_mov_b32_e32 v200, v20
	v_mov_b32_e32 v252, v20
	s_nop 1
	v_permlane32_swap_b32_e32 v252, v200
	v_cndmask_b32_e64 v200, v252, v200, s[98:99]
	v_mov_b32_e32 v201, v21
	v_mov_b32_e32 v253, v21
	s_nop 1
	v_permlane32_swap_b32_e32 v253, v201
	v_cndmask_b32_e64 v201, v253, v201, s[98:99]
	v_mov_b32_e32 v214, v163
	v_mov_b32_e32 v215, v165
	v_mov_b32_e32 v163, v164
	s_waitcnt lgkmcnt(0)
	v_pk_mul_f32 v[200:201], v[214:215], v[200:201]
	s_nop 0
	v_cndmask_b32_e64 v165, v201, -v201, s[4:5]
	v_cndmask_b32_e64 v164, v200, -v200, s[4:5]
	v_pk_fma_f32 v[20:21], v[20:21], v[162:163], v[164:165]
; __device__ __forceinline__ unsigned pk4_fp8(float a, float b, float c, float d) { unsigned w = 0u; w = __builtin_amdgcn_cvt_pk_fp8_f32(a, b, w, false); w = __builtin_amdgcn_cvt_pk_fp8_f32(c, d, w, true); return w; }
; template <bool F8OUT = false> __device__ __forceinline__ void head_tile_store(const f32x4 (&acc)[2][2][4][2], bf16_t* obase  , int opitch, const float* gain, float scale, const f32x2e* rope, int row0, int fq) {
;     ...
;             if (gain) {
;                 float ss = 0.f;
; #pragma unroll
;                 for (int bj = 0; bj < 2; ++bj)
; #pragma unroll
;                     for (int n = 0; n < 2; ++n) ss += (x[bj][n][0] * x[bj][n][0] + x[bj][n][1] * x[bj][n][1]) + (x[bj][n][2] * x[bj][n][2] + x[bj][n][3] * x[bj][n][3]);
;                 ss += __shfl_xor(ss, 16); ss += __shfl_xor(ss, 32);
;                 const float r = scale / sqrtf(ss * (1.f / 64.f) + 1e-6f);
; #pragma unroll
;                 for (int bj = 0; bj < 2; ++bj)
; #pragma unroll
;                     for (int n = 0; n < 2; ++n) x[bj][n] = x[bj][n] * r * g[bj][n];
;             }
;             if (rope) {
;                 const int t = row & 8191; const bool second = (fq & 2) != 0;
; #pragma unroll
;                 for (int bj = 0; bj < 2; ++bj) { const int pos = bj ? (t & 63) : (t >> 6); const f32x2e* tb = rope + pos * 16 + 8 * (fq & 1);
; #pragma unroll
;                     for (int n = 0; n < 2; ++n)
; #pragma unroll
;                         for (int e = 0; e < 4; ++e) { const float p = __shfl_xor(x[bj][n][e], 32); const f32x2e cs = tb[4 * n + e]; const float v = x[bj][n][e];
;                             x[bj][n][e] = second ? (p * cs.y + v * cs.x) : (v * cs.x - p * cs.y); } }
;             }
;             if constexpr (F8OUT) { unsigned char* rowp8 = (unsigned char*)obase + (size_t)row * opitch + 8 * fq; typedef unsigned u32x2_ __attribute__((ext_vector_type(2)));
; #pragma unroll
;                 for (int bj = 0; bj < 2; ++bj) *(u32x2_*)(rowp8 + 32 * bj) = (u32x2_){pk4_fp8(x[bj][0][0], x[bj][0][1], x[bj][0][2], x[bj][0][3]), pk4_fp8(x[bj][1][0], x[bj][1][1], x[bj][1][2], x[bj][1][3])};
;                 continue; }
.LBB0_177:
	v_mov_b32_e32 v164, v175
	v_cvt_pk_fp8_f32 v164, v26, v27
	v_mov_b32_e32 v26, v175
	v_mov_b32_e32 v27, v175
	v_cvt_pk_fp8_f32 v26, v22, v23
	v_cvt_pk_fp8_f32 v27, v18, v19
	v_mov_b32_e32 v165, v175
	v_cvt_pk_fp8_f32 v165, v30, v31
	v_cvt_pk_fp8_f32 v26, v24, v25 op_sel:[0,0,1]
	v_cvt_pk_fp8_f32 v27, v20, v21 op_sel:[0,0,1]
	v_ashrrev_i32_e32 v197, 31, v196
	v_lshlrev_b64 v[162:163], 7, v[196:197]
	v_cvt_pk_fp8_f32 v164, v28, v29 op_sel:[0,0,1]
	v_cvt_pk_fp8_f32 v165, v32, v33 op_sel:[0,0,1]
	v_lshl_add_u64 v[162:163], v[190:191], 0, v[162:163]
	global_store_dwordx2 v[162:163], v[26:27], off offset:32
	v_mov_b64_e32 v[18:19], v[98:99]
	v_mov_b64_e32 v[22:23], v[102:103]
	v_mov_b64_e32 v[30:31], v[106:107]
	v_mov_b64_e32 v[26:27], v[110:111]
	s_and_b64 vcc, exec, s[6:7]
	v_mov_b64_e32 v[20:21], v[100:101]
	v_mov_b64_e32 v[24:25], v[104:105]
	v_mov_b64_e32 v[32:33], v[108:109]
	v_mov_b64_e32 v[28:29], v[112:113]
	global_store_dwordx2 v[162:163], v[164:165], off
	s_cbranch_vccnz .LBB0_179
	v_pk_mul_f32 v[18:19], v[112:113], v[112:113]
	v_pk_mul_f32 v[20:21], v[110:111], v[110:111]
	s_nop 0
	v_pk_mov_b32 v[22:23], v[20:21], v[18:19] op_sel:[1,0]
	v_mov_b32_e32 v21, v19
	v_pk_add_f32 v[18:19], v[22:23], v[20:21]
	v_pk_mul_f32 v[20:21], v[108:109], v[108:109]
	v_pk_mul_f32 v[22:23], v[106:107], v[106:107]
	v_pk_add_f32 v[18:19], v[18:19], v[18:19] op_sel:[0,1] op_sel_hi:[1,0]
	v_pk_mov_b32 v[24:25], v[22:23], v[20:21] op_sel:[1,0]
	v_mov_b32_e32 v23, v21
	v_pk_add_f32 v[20:21], v[24:25], v[22:23]
	v_mul_f32_e32 v22, v98, v98
	v_mul_f32_e32 v23, v99, v99
	v_pk_add_f32 v[20:21], v[20:21], v[20:21] op_sel:[0,1] op_sel_hi:[1,0]
	v_mov_b32_e32 v19, v22
	v_mov_b32_e32 v21, v23
	v_pk_add_f32 v[18:19], v[18:19], v[20:21]
	v_mul_f32_e32 v20, v103, v103
	v_mul_f32_e32 v22, v105, v105
	v_mul_f32_e32 v24, v100, v100
	v_mul_f32_e32 v25, v101, v101
	v_pk_fma_f32 v[20:21], v[102:103], v[102:103], v[20:21] op_sel_hi:[1,1,0]
	v_pk_fma_f32 v[22:23], v[104:105], v[104:105], v[22:23] op_sel_hi:[1,1,0]
	v_mov_b32_e32 v21, v24
	v_mov_b32_e32 v23, v25
	v_pk_add_f32 v[20:21], v[20:21], v[22:23]
	s_nop 0
	v_pk_add_f32 v[18:19], v[18:19], v[20:21]
	v_and_b32_e32 v20, 64, v212
	v_add_f32_e32 v18, v18, v19
	v_xor_b32_e32 v19, 16, v212
	v_add_u32_e32 v20, 64, v20
	v_cmp_lt_i32_e32 vcc, v19, v20
	s_nop 1
	v_cndmask_b32_e32 v19, v212, v19, vcc
	v_lshlrev_b32_e32 v19, 2, v19
	v_mov_b32_e32 v19, v18
	s_nop 1
	v_permlane16_swap_b32_e32 v18, v19
	s_waitcnt lgkmcnt(0)
	v_add_f32_e32 v18, v18, v19
	v_xor_b32_e32 v19, 32, v212
	v_cmp_lt_i32_e32 vcc, v19, v20
	s_nop 1
	v_cndmask_b32_e32 v19, v212, v19, vcc
	v_lshlrev_b32_e32 v19, 2, v19
	v_mov_b32_e32 v19, v18
	s_nop 1
	v_permlane32_swap_b32_e32 v18, v19
	s_waitcnt lgkmcnt(0)
	v_add_f32_e32 v18, v18, v19
	v_fmamk_f32 v18, v18, 0x3c800000, v210
	v_mul_f32_e32 v19, 0x4f800000, v18
	v_cmp_gt_f32_e32 vcc, s28, v18
	s_nop 1
	v_cndmask_b32_e32 v18, v18, v19, vcc
	v_sqrt_f32_e32 v19, v18
	s_nop 0
	v_add_u32_e32 v20, -1, v19
	v_fma_f32 v21, -v20, v19, v18
	v_cmp_ge_f32_e64 s[10:11], 0, v21
	v_add_u32_e32 v21, 1, v19
	s_nop 0
	v_cndmask_b32_e64 v20, v19, v20, s[10:11]
	v_fma_f32 v19, -v21, v19, v18
	v_cmp_lt_f32_e64 s[10:11], 0, v19
	s_nop 1
	v_cndmask_b32_e64 v19, v20, v21, s[10:11]
	v_mul_f32_e32 v20, 0x37800000, v19
	v_cndmask_b32_e32 v19, v19, v20, vcc
	v_cmp_class_f32_e32 vcc, v18, v211
	s_nop 1
	v_cndmask_b32_e32 v18, v19, v18, vcc
	v_div_scale_f32 v19, s[0:1], v18, v18, 1.0
	v_rcp_f32_e32 v20, v19
	s_nop 0
	v_fma_f32 v21, -v19, v20, 1.0
	v_fmac_f32_e32 v20, v21, v20
	v_div_scale_f32 v21, vcc, 1.0, v18, 1.0
	v_mul_f32_e32 v22, v21, v20
	v_fma_f32 v23, -v19, v22, v21
	v_fmac_f32_e32 v22, v23, v20
	v_fma_f32 v19, -v19, v22, v21
	v_div_fmas_f32 v19, v19, v20, v22
	v_div_fixup_f32 v18, v19, v18, 1.0
	v_pk_mul_f32 v[20:21], v[110:111], v[18:19] op_sel_hi:[1,0]
	v_pk_mul_f32 v[22:23], v[112:113], v[18:19] op_sel_hi:[1,0]
	s_waitcnt vmcnt(0)
	v_pk_mul_f32 v[26:27], v[14:15], v[20:21]
	v_pk_mul_f32 v[28:29], v[16:17], v[22:23]
	v_pk_mul_f32 v[20:21], v[106:107], v[18:19] op_sel_hi:[1,0]
	v_pk_mul_f32 v[22:23], v[108:109], v[18:19] op_sel_hi:[1,0]
	v_pk_mul_f32 v[30:31], v[10:11], v[20:21]
	v_pk_mul_f32 v[32:33], v[12:13], v[22:23]
	v_pk_mul_f32 v[20:21], v[102:103], v[18:19] op_sel_hi:[1,0]
	v_pk_mul_f32 v[22:23], v[104:105], v[18:19] op_sel_hi:[1,0]
	v_pk_mul_f32 v[162:163], v[98:99], v[18:19] op_sel_hi:[1,0]
	v_pk_mul_f32 v[18:19], v[100:101], v[18:19] op_sel_hi:[1,0]
	v_pk_mul_f32 v[24:25], v[8:9], v[22:23]
	v_pk_mul_f32 v[22:23], v[6:7], v[20:21]
	v_pk_mul_f32 v[20:21], v[4:5], v[18:19]
	v_pk_mul_f32 v[18:19], v[2:3], v[162:163]
; template <bool F8OUT = false> __device__ __forceinline__ void head_tile_store(const f32x4 (&acc)[2][2][4][2], bf16_t* obase  , int opitch, const float* gain, float scale, const f32x2e* rope, int row0, int fq) {
;     ...
;             if (rope) {
;                 const int t = row & 8191; const bool second = (fq & 2) != 0;
; #pragma unroll
;                 for (int bj = 0; bj < 2; ++bj) { const int pos = bj ? (t & 63) : (t >> 6); const f32x2e* tb = rope + pos * 16 + 8 * (fq & 1);
; #pragma unroll
;                     for (int n = 0; n < 2; ++n)
; #pragma unroll
;                         for (int e = 0; e < 4; ++e) { const float p = __shfl_xor(x[bj][n][e], 32); const f32x2e cs = tb[4 * n + e]; const float v = x[bj][n][e];
;                             x[bj][n][e] = second ? (p * cs.y + v * cs.x) : (v * cs.x - p * cs.y); } }
;             }
.LBB0_179:
	v_add_u32_e32 v200, 48, v188
	v_and_b32_e32 v162, 63, v200
	s_and_b64 vcc, exec, s[8:9]
	v_lshlrev_b32_e32 v196, 7, v162
	s_cbranch_vccnz .LBB0_181
	v_and_b32_e32 v163, 64, v212
	v_xor_b32_e32 v162, 32, v212
	v_add_u32_e32 v163, 64, v163
	v_cmp_lt_i32_e32 vcc, v162, v163
	v_mov_b32_e32 v197, v175
	s_nop 0
	v_cndmask_b32_e32 v162, v212, v162, vcc
	v_lshlrev_b32_e32 v185, 2, v162
	v_lshlrev_b32_e32 v162, 1, v200
	v_and_b32_e32 v174, 0x3f80, v162
	v_lshl_add_u64 v[222:223], v[186:187], 0, v[174:175]
	v_add_u32_e32 v238, s100, v222
	ds_read_b128 v[162:165], v238 offset:48
	ds_read_b128 v[214:217], v238 offset:32
	ds_read_b128 v[218:221], v238 offset:16
	ds_read_b128 v[222:225], v238
	v_mov_b32_e32 v226, v26
	v_mov_b32_e32 v250, v26
	s_nop 1
	v_permlane32_swap_b32_e32 v250, v226
	v_cndmask_b32_e64 v226, v250, v226, s[98:99]
	v_mov_b32_e32 v227, v27
	v_mov_b32_e32 v251, v27
	s_nop 1
	v_permlane32_swap_b32_e32 v251, v227
	v_cndmask_b32_e64 v227, v251, v227, s[98:99]
	s_waitcnt lgkmcnt(0)
	v_mov_b32_e32 v228, v223
	v_mov_b32_e32 v229, v225
	s_waitcnt lgkmcnt(0)
	v_pk_mul_f32 v[226:227], v[228:229], v[226:227]
	v_mov_b32_e32 v223, v224
	v_cndmask_b32_e64 v225, v227, -v227, s[4:5]
	v_cndmask_b32_e64 v224, v226, -v226, s[4:5]
	v_pk_fma_f32 v[26:27], v[26:27], v[222:223], v[224:225]
	v_mov_b32_e32 v222, v28
	v_mov_b32_e32 v252, v28
	s_nop 1
	v_permlane32_swap_b32_e32 v252, v222
	v_cndmask_b32_e64 v222, v252, v222, s[98:99]
	v_mov_b32_e32 v223, v29
	v_mov_b32_e32 v253, v29
	s_nop 1
	v_permlane32_swap_b32_e32 v253, v223
	v_cndmask_b32_e64 v223, v253, v223, s[98:99]
	v_mov_b32_e32 v224, v219
	v_mov_b32_e32 v225, v221
	v_mov_b32_e32 v219, v220
	v_mov_b32_e32 v226, v22
	v_mov_b32_e32 v250, v22
	s_nop 1
	v_permlane32_swap_b32_e32 v250, v226
	v_cndmask_b32_e64 v226, v250, v226, s[98:99]
	s_waitcnt lgkmcnt(1)
	v_pk_mul_f32 v[222:223], v[224:225], v[222:223]
	v_mov_b32_e32 v227, v23
	v_mov_b32_e32 v251, v23
	s_nop 1
	v_permlane32_swap_b32_e32 v251, v227
	v_cndmask_b32_e64 v227, v251, v227, s[98:99]
	v_cndmask_b32_e64 v221, v223, -v223, s[4:5]
	v_cndmask_b32_e64 v220, v222, -v222, s[4:5]
	v_pk_fma_f32 v[28:29], v[28:29], v[218:219], v[220:221]
	v_mov_b32_e32 v218, v30
	v_mov_b32_e32 v252, v30
	s_nop 1
	v_permlane32_swap_b32_e32 v252, v218
	v_cndmask_b32_e64 v218, v252, v218, s[98:99]
	v_mov_b32_e32 v219, v31
	v_mov_b32_e32 v253, v31
	s_nop 1
	v_permlane32_swap_b32_e32 v253, v219
	v_cndmask_b32_e64 v219, v253, v219, s[98:99]
	v_mov_b32_e32 v220, v215
	v_mov_b32_e32 v221, v217
	v_mov_b32_e32 v215, v216
	v_lshl_add_u64 v[222:223], v[186:187], 0, v[196:197]
	s_waitcnt lgkmcnt(0)
	v_pk_mul_f32 v[218:219], v[220:221], v[218:219]
	s_nop 0
	v_cndmask_b32_e64 v217, v219, -v219, s[4:5]
	v_cndmask_b32_e64 v216, v218, -v218, s[4:5]
	v_pk_fma_f32 v[30:31], v[30:31], v[214:215], v[216:217]
	v_mov_b32_e32 v214, v32
	v_mov_b32_e32 v250, v32
	s_nop 1
	v_permlane32_swap_b32_e32 v250, v214
	v_cndmask_b32_e64 v214, v250, v214, s[98:99]
	v_mov_b32_e32 v215, v33
	v_mov_b32_e32 v251, v33
	s_nop 1
	v_permlane32_swap_b32_e32 v251, v215
	v_cndmask_b32_e64 v215, v251, v215, s[98:99]
	v_mov_b32_e32 v216, v163
	v_mov_b32_e32 v217, v165
	v_mov_b32_e32 v163, v164
	s_waitcnt lgkmcnt(0)
	v_pk_mul_f32 v[214:215], v[216:217], v[214:215]
	s_nop 0
	v_cndmask_b32_e64 v165, v215, -v215, s[4:5]
	v_cndmask_b32_e64 v164, v214, -v214, s[4:5]
	v_pk_fma_f32 v[32:33], v[32:33], v[162:163], v[164:165]
	v_add_u32_e32 v238, s100, v222
	ds_read_b128 v[162:165], v238 offset:48
	ds_read_b128 v[214:217], v238 offset:32
	ds_read_b128 v[218:221], v238 offset:16
	ds_read_b128 v[222:225], v238
	s_waitcnt lgkmcnt(0)
	v_mov_b32_e32 v228, v223
	v_mov_b32_e32 v229, v225
	v_pk_mul_f32 v[226:227], v[228:229], v[226:227]
	v_mov_b32_e32 v223, v224
	v_cndmask_b32_e64 v225, v227, -v227, s[4:5]
	v_cndmask_b32_e64 v224, v226, -v226, s[4:5]
	v_pk_fma_f32 v[22:23], v[22:23], v[222:223], v[224:225]
	v_mov_b32_e32 v222, v24
	v_mov_b32_e32 v252, v24
	s_nop 1
	v_permlane32_swap_b32_e32 v252, v222
	v_cndmask_b32_e64 v222, v252, v222, s[98:99]
	v_mov_b32_e32 v223, v25
	v_mov_b32_e32 v253, v25
	s_nop 1
	v_permlane32_swap_b32_e32 v253, v223
	v_cndmask_b32_e64 v223, v253, v223, s[98:99]
	v_mov_b32_e32 v224, v219
	v_mov_b32_e32 v225, v221
	v_mov_b32_e32 v219, v220
	s_waitcnt lgkmcnt(0)
	v_pk_mul_f32 v[222:223], v[224:225], v[222:223]
	s_nop 0
	v_cndmask_b32_e64 v221, v223, -v223, s[4:5]
	v_cndmask_b32_e64 v220, v222, -v222, s[4:5]
	v_pk_fma_f32 v[24:25], v[24:25], v[218:219], v[220:221]
	v_mov_b32_e32 v218, v18
	v_mov_b32_e32 v250, v18
	s_nop 1
	v_permlane32_swap_b32_e32 v250, v218
	v_cndmask_b32_e64 v218, v250, v218, s[98:99]
	v_mov_b32_e32 v219, v19
	v_mov_b32_e32 v251, v19
	s_nop 1
	v_permlane32_swap_b32_e32 v251, v219
	v_cndmask_b32_e64 v219, v251, v219, s[98:99]
	v_mov_b32_e32 v220, v215
	v_mov_b32_e32 v221, v217
	v_mov_b32_e32 v215, v216
	s_waitcnt lgkmcnt(0)
	v_pk_mul_f32 v[218:219], v[220:221], v[218:219]
	s_nop 0
	v_cndmask_b32_e64 v217, v219, -v219, s[4:5]
	v_cndmask_b32_e64 v216, v218, -v218, s[4:5]
	v_pk_fma_f32 v[18:19], v[18:19], v[214:215], v[216:217]
	v_mov_b32_e32 v214, v20
	v_mov_b32_e32 v252, v20
	s_nop 1
	v_permlane32_swap_b32_e32 v252, v214
	v_cndmask_b32_e64 v214, v252, v214, s[98:99]
	v_mov_b32_e32 v215, v21
	v_mov_b32_e32 v253, v21
	s_nop 1
	v_permlane32_swap_b32_e32 v253, v215
	v_cndmask_b32_e64 v215, v253, v215, s[98:99]
	v_mov_b32_e32 v216, v163
	v_mov_b32_e32 v217, v165
	v_mov_b32_e32 v163, v164
	s_waitcnt lgkmcnt(0)
	v_pk_mul_f32 v[214:215], v[216:217], v[214:215]
	s_nop 0
	v_cndmask_b32_e64 v165, v215, -v215, s[4:5]
	v_cndmask_b32_e64 v164, v214, -v214, s[4:5]
	v_pk_fma_f32 v[20:21], v[20:21], v[162:163], v[164:165]
; __device__ __forceinline__ unsigned pk4_fp8(float a, float b, float c, float d) { unsigned w = 0u; w = __builtin_amdgcn_cvt_pk_fp8_f32(a, b, w, false); w = __builtin_amdgcn_cvt_pk_fp8_f32(c, d, w, true); return w; }
; template <bool F8OUT = false> __device__ __forceinline__ void head_tile_store(const f32x4 (&acc)[2][2][4][2], bf16_t* obase  , int opitch, const float* gain, float scale, const f32x2e* rope, int row0, int fq) {
;     ...
;             if (gain) {
;                 float ss = 0.f;
; #pragma unroll
;                 for (int bj = 0; bj < 2; ++bj)
; #pragma unroll
;                     for (int n = 0; n < 2; ++n) ss += (x[bj][n][0] * x[bj][n][0] + x[bj][n][1] * x[bj][n][1]) + (x[bj][n][2] * x[bj][n][2] + x[bj][n][3] * x[bj][n][3]);
;                 ss += __shfl_xor(ss, 16); ss += __shfl_xor(ss, 32);
;                 const float r = scale / sqrtf(ss * (1.f / 64.f) + 1e-6f);
; #pragma unroll
;                 for (int bj = 0; bj < 2; ++bj)
; #pragma unroll
;                     for (int n = 0; n < 2; ++n) x[bj][n] = x[bj][n] * r * g[bj][n];
;     ...
;             if constexpr (F8OUT) { unsigned char* rowp8 = (unsigned char*)obase + (size_t)row * opitch + 8 * fq; typedef unsigned u32x2_ __attribute__((ext_vector_type(2)));
; #pragma unroll
;                 for (int bj = 0; bj < 2; ++bj) *(u32x2_*)(rowp8 + 32 * bj) = (u32x2_){pk4_fp8(x[bj][0][0], x[bj][0][1], x[bj][0][2], x[bj][0][3]), pk4_fp8(x[bj][1][0], x[bj][1][1], x[bj][1][2], x[bj][1][3])};
.LBB0_181:
	v_mov_b32_e32 v164, v175
	v_cvt_pk_fp8_f32 v164, v26, v27
	v_mov_b32_e32 v26, v175
	v_mov_b32_e32 v27, v175
	v_cvt_pk_fp8_f32 v26, v22, v23
	v_cvt_pk_fp8_f32 v27, v18, v19
	v_mov_b32_e32 v165, v175
	v_cvt_pk_fp8_f32 v165, v30, v31
	v_cvt_pk_fp8_f32 v26, v24, v25 op_sel:[0,0,1]
	v_cvt_pk_fp8_f32 v27, v20, v21 op_sel:[0,0,1]
	v_ashrrev_i32_e32 v201, 31, v200
	v_lshlrev_b64 v[162:163], 7, v[200:201]
	v_cvt_pk_fp8_f32 v164, v28, v29 op_sel:[0,0,1]
	v_cvt_pk_fp8_f32 v165, v32, v33 op_sel:[0,0,1]
	v_lshl_add_u64 v[162:163], v[190:191], 0, v[162:163]
	global_store_dwordx2 v[162:163], v[26:27], off offset:32
	v_mov_b64_e32 v[18:19], v[82:83]
	v_mov_b64_e32 v[22:23], v[86:87]
	v_mov_b64_e32 v[30:31], v[90:91]
	v_mov_b64_e32 v[26:27], v[94:95]
	s_and_b64 vcc, exec, s[6:7]
	v_mov_b64_e32 v[20:21], v[84:85]
	v_mov_b64_e32 v[24:25], v[88:89]
	v_mov_b64_e32 v[32:33], v[92:93]
	v_mov_b64_e32 v[28:29], v[96:97]
	global_store_dwordx2 v[162:163], v[164:165], off
	s_cbranch_vccnz .LBB0_183
	v_pk_mul_f32 v[18:19], v[96:97], v[96:97]
	v_pk_mul_f32 v[20:21], v[94:95], v[94:95]
	s_nop 0
	v_pk_mov_b32 v[22:23], v[20:21], v[18:19] op_sel:[1,0]
	v_mov_b32_e32 v21, v19
	v_pk_add_f32 v[18:19], v[22:23], v[20:21]
	v_pk_mul_f32 v[20:21], v[92:93], v[92:93]
	v_pk_mul_f32 v[22:23], v[90:91], v[90:91]
	v_pk_add_f32 v[18:19], v[18:19], v[18:19] op_sel:[0,1] op_sel_hi:[1,0]
	v_pk_mov_b32 v[24:25], v[22:23], v[20:21] op_sel:[1,0]
	v_mov_b32_e32 v23, v21
	v_pk_add_f32 v[20:21], v[24:25], v[22:23]
	v_mul_f32_e32 v22, v82, v82
	v_mul_f32_e32 v23, v83, v83
	v_pk_add_f32 v[20:21], v[20:21], v[20:21] op_sel:[0,1] op_sel_hi:[1,0]
	v_mov_b32_e32 v19, v22
	v_mov_b32_e32 v21, v23
	v_pk_add_f32 v[18:19], v[18:19], v[20:21]
	v_mul_f32_e32 v20, v87, v87
	v_mul_f32_e32 v22, v89, v89
	v_mul_f32_e32 v24, v84, v84
	v_mul_f32_e32 v25, v85, v85
	v_pk_fma_f32 v[20:21], v[86:87], v[86:87], v[20:21] op_sel_hi:[1,1,0]
	v_pk_fma_f32 v[22:23], v[88:89], v[88:89], v[22:23] op_sel_hi:[1,1,0]
	v_mov_b32_e32 v21, v24
	v_mov_b32_e32 v23, v25
	v_pk_add_f32 v[20:21], v[20:21], v[22:23]
	s_nop 0
	v_pk_add_f32 v[18:19], v[18:19], v[20:21]
	v_and_b32_e32 v20, 64, v212
	v_add_f32_e32 v18, v18, v19
	v_xor_b32_e32 v19, 16, v212
	v_add_u32_e32 v20, 64, v20
	v_cmp_lt_i32_e32 vcc, v19, v20
	s_nop 1
	v_cndmask_b32_e32 v19, v212, v19, vcc
	v_lshlrev_b32_e32 v19, 2, v19
	v_mov_b32_e32 v19, v18
	s_nop 1
	v_permlane16_swap_b32_e32 v18, v19
	s_waitcnt lgkmcnt(0)
	v_add_f32_e32 v18, v18, v19
	v_xor_b32_e32 v19, 32, v212
	v_cmp_lt_i32_e32 vcc, v19, v20
	s_nop 1
	v_cndmask_b32_e32 v19, v212, v19, vcc
	v_lshlrev_b32_e32 v19, 2, v19
	v_mov_b32_e32 v19, v18
	s_nop 1
	v_permlane32_swap_b32_e32 v18, v19
	s_waitcnt lgkmcnt(0)
	v_add_f32_e32 v18, v18, v19
	v_fmamk_f32 v18, v18, 0x3c800000, v210
	v_mul_f32_e32 v19, 0x4f800000, v18
	v_cmp_gt_f32_e32 vcc, s28, v18
	s_nop 1
	v_cndmask_b32_e32 v18, v18, v19, vcc
	v_sqrt_f32_e32 v19, v18
	s_nop 0
	v_add_u32_e32 v20, -1, v19
	v_fma_f32 v21, -v20, v19, v18
	v_cmp_ge_f32_e64 s[10:11], 0, v21
	v_add_u32_e32 v21, 1, v19
	s_nop 0
	v_cndmask_b32_e64 v20, v19, v20, s[10:11]
	v_fma_f32 v19, -v21, v19, v18
	v_cmp_lt_f32_e64 s[10:11], 0, v19
	s_nop 1
	v_cndmask_b32_e64 v19, v20, v21, s[10:11]
	v_mul_f32_e32 v20, 0x37800000, v19
	v_cndmask_b32_e32 v19, v19, v20, vcc
	v_cmp_class_f32_e32 vcc, v18, v211
	s_nop 1
	v_cndmask_b32_e32 v18, v19, v18, vcc
	v_div_scale_f32 v19, s[0:1], v18, v18, 1.0
	v_rcp_f32_e32 v20, v19
	s_nop 0
	v_fma_f32 v21, -v19, v20, 1.0
	v_fmac_f32_e32 v20, v21, v20
	v_div_scale_f32 v21, vcc, 1.0, v18, 1.0
	v_mul_f32_e32 v22, v21, v20
	v_fma_f32 v23, -v19, v22, v21
	v_fmac_f32_e32 v22, v23, v20
	v_fma_f32 v19, -v19, v22, v21
	v_div_fmas_f32 v19, v19, v20, v22
	v_div_fixup_f32 v18, v19, v18, 1.0
	v_pk_mul_f32 v[20:21], v[94:95], v[18:19] op_sel_hi:[1,0]
	v_pk_mul_f32 v[22:23], v[96:97], v[18:19] op_sel_hi:[1,0]
	s_waitcnt vmcnt(0)
	v_pk_mul_f32 v[26:27], v[14:15], v[20:21]
	v_pk_mul_f32 v[28:29], v[16:17], v[22:23]
	v_pk_mul_f32 v[20:21], v[90:91], v[18:19] op_sel_hi:[1,0]
	v_pk_mul_f32 v[22:23], v[92:93], v[18:19] op_sel_hi:[1,0]
	v_pk_mul_f32 v[30:31], v[10:11], v[20:21]
	v_pk_mul_f32 v[32:33], v[12:13], v[22:23]
	v_pk_mul_f32 v[20:21], v[86:87], v[18:19] op_sel_hi:[1,0]
	v_pk_mul_f32 v[22:23], v[88:89], v[18:19] op_sel_hi:[1,0]
	v_pk_mul_f32 v[162:163], v[82:83], v[18:19] op_sel_hi:[1,0]
	v_pk_mul_f32 v[18:19], v[84:85], v[18:19] op_sel_hi:[1,0]
	v_pk_mul_f32 v[24:25], v[8:9], v[22:23]
	v_pk_mul_f32 v[22:23], v[6:7], v[20:21]
	v_pk_mul_f32 v[20:21], v[4:5], v[18:19]
	v_pk_mul_f32 v[18:19], v[2:3], v[162:163]
; template <bool F8OUT = false> __device__ __forceinline__ void head_tile_store(const f32x4 (&acc)[2][2][4][2], bf16_t* obase  , int opitch, const float* gain, float scale, const f32x2e* rope, int row0, int fq) {
;     ...
;             if (rope) {
;                 const int t = row & 8191; const bool second = (fq & 2) != 0;
; #pragma unroll
;                 for (int bj = 0; bj < 2; ++bj) { const int pos = bj ? (t & 63) : (t >> 6); const f32x2e* tb = rope + pos * 16 + 8 * (fq & 1);
; #pragma unroll
;                     for (int n = 0; n < 2; ++n)
; #pragma unroll
;                         for (int e = 0; e < 4; ++e) { const float p = __shfl_xor(x[bj][n][e], 32); const f32x2e cs = tb[4 * n + e]; const float v = x[bj][n][e];
;                             x[bj][n][e] = second ? (p * cs.y + v * cs.x) : (v * cs.x - p * cs.y); } }
;             }
.LBB0_183:
	s_and_b64 vcc, exec, s[8:9]
	v_add_u32_e32 v200, 0x80, v188
	s_cbranch_vccnz .LBB0_185
	v_and_b32_e32 v163, 64, v212
	v_xor_b32_e32 v162, 32, v212
	v_add_u32_e32 v163, 64, v163
	v_cmp_lt_i32_e32 vcc, v162, v163
	v_mov_b32_e32 v199, v175
	v_lshl_add_u64 v[198:199], v[186:187], 0, v[198:199]
	v_cndmask_b32_e32 v162, v212, v162, vcc
	v_lshlrev_b32_e32 v185, 2, v162
	v_lshlrev_b32_e32 v162, 1, v200
	v_and_b32_e32 v174, 0x3f80, v162
	v_lshl_add_u64 v[222:223], v[186:187], 0, v[174:175]
	v_add_u32_e32 v238, s100, v222
	ds_read_b128 v[162:165], v238 offset:48
	ds_read_b128 v[214:217], v238 offset:32
	ds_read_b128 v[218:221], v238 offset:16
	ds_read_b128 v[222:225], v238
	v_mov_b32_e32 v226, v26
	v_mov_b32_e32 v250, v26
	s_nop 1
	v_permlane32_swap_b32_e32 v250, v226
	v_cndmask_b32_e64 v226, v250, v226, s[98:99]
	v_mov_b32_e32 v227, v27
	v_mov_b32_e32 v251, v27
	s_nop 1
	v_permlane32_swap_b32_e32 v251, v227
	v_cndmask_b32_e64 v227, v251, v227, s[98:99]
	s_waitcnt lgkmcnt(0)
	v_mov_b32_e32 v228, v223
	v_mov_b32_e32 v229, v225
	s_waitcnt lgkmcnt(0)
	v_pk_mul_f32 v[226:227], v[228:229], v[226:227]
	v_mov_b32_e32 v223, v224
	v_cndmask_b32_e64 v225, v227, -v227, s[4:5]
	v_cndmask_b32_e64 v224, v226, -v226, s[4:5]
	v_pk_fma_f32 v[26:27], v[26:27], v[222:223], v[224:225]
	v_mov_b32_e32 v222, v28
	v_mov_b32_e32 v252, v28
	s_nop 1
	v_permlane32_swap_b32_e32 v252, v222
	v_cndmask_b32_e64 v222, v252, v222, s[98:99]
	v_mov_b32_e32 v223, v29
	v_mov_b32_e32 v253, v29
	s_nop 1
	v_permlane32_swap_b32_e32 v253, v223
	v_cndmask_b32_e64 v223, v253, v223, s[98:99]
	v_mov_b32_e32 v224, v219
	v_mov_b32_e32 v225, v221
	v_mov_b32_e32 v219, v220
	v_mov_b32_e32 v226, v22
	v_mov_b32_e32 v250, v22
	s_nop 1
	v_permlane32_swap_b32_e32 v250, v226
	v_cndmask_b32_e64 v226, v250, v226, s[98:99]
	s_waitcnt lgkmcnt(1)
	v_pk_mul_f32 v[222:223], v[224:225], v[222:223]
	v_mov_b32_e32 v227, v23
	v_mov_b32_e32 v251, v23
	s_nop 1
	v_permlane32_swap_b32_e32 v251, v227
	v_cndmask_b32_e64 v227, v251, v227, s[98:99]
	v_cndmask_b32_e64 v221, v223, -v223, s[4:5]
	v_cndmask_b32_e64 v220, v222, -v222, s[4:5]
	v_pk_fma_f32 v[28:29], v[28:29], v[218:219], v[220:221]
	v_mov_b32_e32 v218, v30
	v_mov_b32_e32 v252, v30
	s_nop 1
	v_permlane32_swap_b32_e32 v252, v218
	v_cndmask_b32_e64 v218, v252, v218, s[98:99]
	v_mov_b32_e32 v219, v31
	v_mov_b32_e32 v253, v31
	s_nop 1
	v_permlane32_swap_b32_e32 v253, v219
	v_cndmask_b32_e64 v219, v253, v219, s[98:99]
	v_mov_b32_e32 v220, v215
	v_mov_b32_e32 v221, v217
	v_mov_b32_e32 v215, v216
	s_waitcnt lgkmcnt(0)
	v_pk_mul_f32 v[218:219], v[220:221], v[218:219]
	s_nop 0
	v_cndmask_b32_e64 v217, v219, -v219, s[4:5]
	v_cndmask_b32_e64 v216, v218, -v218, s[4:5]
	v_pk_fma_f32 v[30:31], v[30:31], v[214:215], v[216:217]
	v_mov_b32_e32 v214, v32
	v_mov_b32_e32 v250, v32
	s_nop 1
	v_permlane32_swap_b32_e32 v250, v214
	v_cndmask_b32_e64 v214, v250, v214, s[98:99]
	v_mov_b32_e32 v215, v33
	v_mov_b32_e32 v251, v33
	s_nop 1
	v_permlane32_swap_b32_e32 v251, v215
	v_cndmask_b32_e64 v215, v251, v215, s[98:99]
	v_mov_b32_e32 v216, v163
	v_mov_b32_e32 v217, v165
	v_mov_b32_e32 v163, v164
	s_waitcnt lgkmcnt(0)
	v_pk_mul_f32 v[214:215], v[216:217], v[214:215]
	s_nop 0
	v_cndmask_b32_e64 v165, v215, -v215, s[4:5]
	v_cndmask_b32_e64 v164, v214, -v214, s[4:5]
	v_pk_fma_f32 v[32:33], v[32:33], v[162:163], v[164:165]
	v_add_u32_e32 v238, s100, v198
	ds_read_b128 v[162:165], v238 offset:48
	ds_read_b128 v[214:217], v238 offset:32
	ds_read_b128 v[218:221], v238 offset:16
	ds_read_b128 v[222:225], v238
	s_waitcnt lgkmcnt(0)
	v_mov_b32_e32 v198, v223
	v_mov_b32_e32 v199, v225
	v_pk_mul_f32 v[198:199], v[198:199], v[226:227]
	v_mov_b32_e32 v223, v224
	v_cndmask_b32_e64 v199, v199, -v199, s[4:5]
	v_cndmask_b32_e64 v198, v198, -v198, s[4:5]
	v_pk_fma_f32 v[22:23], v[22:23], v[222:223], v[198:199]
	v_mov_b32_e32 v198, v24
	v_mov_b32_e32 v252, v24
	s_nop 1
	v_permlane32_swap_b32_e32 v252, v198
	v_cndmask_b32_e64 v198, v252, v198, s[98:99]
	v_mov_b32_e32 v199, v25
	v_mov_b32_e32 v253, v25
	s_nop 1
	v_permlane32_swap_b32_e32 v253, v199
	v_cndmask_b32_e64 v199, v253, v199, s[98:99]
	v_mov_b32_e32 v222, v219
	v_mov_b32_e32 v223, v221
	v_mov_b32_e32 v219, v220
	s_waitcnt lgkmcnt(0)
	v_pk_mul_f32 v[198:199], v[222:223], v[198:199]
	s_nop 0
	v_cndmask_b32_e64 v199, v199, -v199, s[4:5]
	v_cndmask_b32_e64 v198, v198, -v198, s[4:5]
	v_pk_fma_f32 v[24:25], v[24:25], v[218:219], v[198:199]
	v_mov_b32_e32 v198, v18
	v_mov_b32_e32 v250, v18
	s_nop 1
	v_permlane32_swap_b32_e32 v250, v198
	v_cndmask_b32_e64 v198, v250, v198, s[98:99]
	v_mov_b32_e32 v199, v19
	v_mov_b32_e32 v251, v19
	s_nop 1
	v_permlane32_swap_b32_e32 v251, v199
	v_cndmask_b32_e64 v199, v251, v199, s[98:99]
	v_mov_b32_e32 v218, v215
	v_mov_b32_e32 v219, v217
	v_mov_b32_e32 v215, v216
	s_waitcnt lgkmcnt(0)
	v_pk_mul_f32 v[198:199], v[218:219], v[198:199]
	s_nop 0
	v_cndmask_b32_e64 v199, v199, -v199, s[4:5]
	v_cndmask_b32_e64 v198, v198, -v198, s[4:5]
	v_pk_fma_f32 v[18:19], v[18:19], v[214:215], v[198:199]
	v_mov_b32_e32 v198, v20
	v_mov_b32_e32 v252, v20
	s_nop 1
	v_permlane32_swap_b32_e32 v252, v198
	v_cndmask_b32_e64 v198, v252, v198, s[98:99]
	v_mov_b32_e32 v199, v21
	v_mov_b32_e32 v253, v21
	s_nop 1
	v_permlane32_swap_b32_e32 v253, v199
	v_cndmask_b32_e64 v199, v253, v199, s[98:99]
	v_mov_b32_e32 v214, v163
	v_mov_b32_e32 v215, v165
	v_mov_b32_e32 v163, v164
	s_waitcnt lgkmcnt(0)
	v_pk_mul_f32 v[198:199], v[214:215], v[198:199]
	s_nop 0
	v_cndmask_b32_e64 v165, v199, -v199, s[4:5]
	v_cndmask_b32_e64 v164, v198, -v198, s[4:5]
	v_pk_fma_f32 v[20:21], v[20:21], v[162:163], v[164:165]
; __device__ __forceinline__ unsigned pk4_fp8(float a, float b, float c, float d) { unsigned w = 0u; w = __builtin_amdgcn_cvt_pk_fp8_f32(a, b, w, false); w = __builtin_amdgcn_cvt_pk_fp8_f32(c, d, w, true); return w; }
; template <bool F8OUT = false> __device__ __forceinline__ void head_tile_store(const f32x4 (&acc)[2][2][4][2], bf16_t* obase  , int opitch, const float* gain, float scale, const f32x2e* rope, int row0, int fq) {
;     ...
;             if (gain) {
;                 float ss = 0.f;
; #pragma unroll
;                 for (int bj = 0; bj < 2; ++bj)
; #pragma unroll
;                     for (int n = 0; n < 2; ++n) ss += (x[bj][n][0] * x[bj][n][0] + x[bj][n][1] * x[bj][n][1]) + (x[bj][n][2] * x[bj][n][2] + x[bj][n][3] * x[bj][n][3]);
;                 ss += __shfl_xor(ss, 16); ss += __shfl_xor(ss, 32);
;                 const float r = scale / sqrtf(ss * (1.f / 64.f) + 1e-6f);
; #pragma unroll
;                 for (int bj = 0; bj < 2; ++bj)
; #pragma unroll
;                     for (int n = 0; n < 2; ++n) x[bj][n] = x[bj][n] * r * g[bj][n];
;     ...
;             if constexpr (F8OUT) { unsigned char* rowp8 = (unsigned char*)obase + (size_t)row * opitch + 8 * fq; typedef unsigned u32x2_ __attribute__((ext_vector_type(2)));
; #pragma unroll
;                 for (int bj = 0; bj < 2; ++bj) *(u32x2_*)(rowp8 + 32 * bj) = (u32x2_){pk4_fp8(x[bj][0][0], x[bj][0][1], x[bj][0][2], x[bj][0][3]), pk4_fp8(x[bj][1][0], x[bj][1][1], x[bj][1][2], x[bj][1][3])};
.LBB0_185:
	v_mov_b32_e32 v164, v175
	v_cvt_pk_fp8_f32 v164, v26, v27
	v_mov_b32_e32 v26, v175
	v_mov_b32_e32 v27, v175
	v_cvt_pk_fp8_f32 v26, v22, v23
	v_cvt_pk_fp8_f32 v27, v18, v19
	v_mov_b32_e32 v165, v175
	v_cvt_pk_fp8_f32 v165, v30, v31
	v_cvt_pk_fp8_f32 v26, v24, v25 op_sel:[0,0,1]
	v_cvt_pk_fp8_f32 v27, v20, v21 op_sel:[0,0,1]
	v_ashrrev_i32_e32 v201, 31, v200
	v_lshlrev_b64 v[162:163], 7, v[200:201]
	v_cvt_pk_fp8_f32 v164, v28, v29 op_sel:[0,0,1]
	v_cvt_pk_fp8_f32 v165, v32, v33 op_sel:[0,0,1]
	v_lshl_add_u64 v[162:163], v[190:191], 0, v[162:163]
	global_store_dwordx2 v[162:163], v[26:27], off offset:32
	v_mov_b64_e32 v[18:19], v[66:67]
	v_mov_b64_e32 v[22:23], v[70:71]
	v_mov_b64_e32 v[30:31], v[74:75]
	v_mov_b64_e32 v[26:27], v[78:79]
	s_and_b64 vcc, exec, s[6:7]
	v_mov_b64_e32 v[20:21], v[68:69]
	v_mov_b64_e32 v[24:25], v[72:73]
	v_mov_b64_e32 v[32:33], v[76:77]
	v_mov_b64_e32 v[28:29], v[80:81]
	global_store_dwordx2 v[162:163], v[164:165], off
	s_cbranch_vccnz .LBB0_187
	v_pk_mul_f32 v[18:19], v[80:81], v[80:81]
	v_pk_mul_f32 v[20:21], v[78:79], v[78:79]
	s_nop 0
	v_pk_mov_b32 v[22:23], v[20:21], v[18:19] op_sel:[1,0]
	v_mov_b32_e32 v21, v19
	v_pk_add_f32 v[18:19], v[22:23], v[20:21]
	v_pk_mul_f32 v[20:21], v[76:77], v[76:77]
	v_pk_mul_f32 v[22:23], v[74:75], v[74:75]
	v_pk_add_f32 v[18:19], v[18:19], v[18:19] op_sel:[0,1] op_sel_hi:[1,0]
	v_pk_mov_b32 v[24:25], v[22:23], v[20:21] op_sel:[1,0]
	v_mov_b32_e32 v23, v21
	v_pk_add_f32 v[20:21], v[24:25], v[22:23]
	v_mul_f32_e32 v22, v66, v66
	v_mul_f32_e32 v23, v67, v67
	v_pk_add_f32 v[20:21], v[20:21], v[20:21] op_sel:[0,1] op_sel_hi:[1,0]
	v_mov_b32_e32 v19, v22
	v_mov_b32_e32 v21, v23
	v_pk_add_f32 v[18:19], v[18:19], v[20:21]
	v_mul_f32_e32 v20, v71, v71
	v_mul_f32_e32 v22, v73, v73
	v_mul_f32_e32 v24, v68, v68
	v_mul_f32_e32 v25, v69, v69
	v_pk_fma_f32 v[20:21], v[70:71], v[70:71], v[20:21] op_sel_hi:[1,1,0]
	v_pk_fma_f32 v[22:23], v[72:73], v[72:73], v[22:23] op_sel_hi:[1,1,0]
	v_mov_b32_e32 v21, v24
	v_mov_b32_e32 v23, v25
	v_pk_add_f32 v[20:21], v[20:21], v[22:23]
	s_nop 0
	v_pk_add_f32 v[18:19], v[18:19], v[20:21]
	v_and_b32_e32 v20, 64, v212
	v_add_f32_e32 v18, v18, v19
	v_xor_b32_e32 v19, 16, v212
	v_add_u32_e32 v20, 64, v20
	v_cmp_lt_i32_e32 vcc, v19, v20
	s_nop 1
	v_cndmask_b32_e32 v19, v212, v19, vcc
	v_lshlrev_b32_e32 v19, 2, v19
	v_mov_b32_e32 v19, v18
	s_nop 1
	v_permlane16_swap_b32_e32 v18, v19
	s_waitcnt lgkmcnt(0)
	v_add_f32_e32 v18, v18, v19
	v_xor_b32_e32 v19, 32, v212
	v_cmp_lt_i32_e32 vcc, v19, v20
	s_nop 1
	v_cndmask_b32_e32 v19, v212, v19, vcc
	v_lshlrev_b32_e32 v19, 2, v19
	v_mov_b32_e32 v19, v18
	s_nop 1
	v_permlane32_swap_b32_e32 v18, v19
	s_waitcnt lgkmcnt(0)
	v_add_f32_e32 v18, v18, v19
	v_fmamk_f32 v18, v18, 0x3c800000, v210
	v_mul_f32_e32 v19, 0x4f800000, v18
	v_cmp_gt_f32_e32 vcc, s28, v18
	s_nop 1
	v_cndmask_b32_e32 v18, v18, v19, vcc
	v_sqrt_f32_e32 v19, v18
	s_nop 0
	v_add_u32_e32 v20, -1, v19
	v_fma_f32 v21, -v20, v19, v18
	v_cmp_ge_f32_e64 s[10:11], 0, v21
	v_add_u32_e32 v21, 1, v19
	s_nop 0
	v_cndmask_b32_e64 v20, v19, v20, s[10:11]
	v_fma_f32 v19, -v21, v19, v18
	v_cmp_lt_f32_e64 s[10:11], 0, v19
	s_nop 1
	v_cndmask_b32_e64 v19, v20, v21, s[10:11]
	v_mul_f32_e32 v20, 0x37800000, v19
	v_cndmask_b32_e32 v19, v19, v20, vcc
	v_cmp_class_f32_e32 vcc, v18, v211
	s_nop 1
	v_cndmask_b32_e32 v18, v19, v18, vcc
	v_div_scale_f32 v19, s[0:1], v18, v18, 1.0
	v_rcp_f32_e32 v20, v19
	s_nop 0
	v_fma_f32 v21, -v19, v20, 1.0
	v_fmac_f32_e32 v20, v21, v20
	v_div_scale_f32 v21, vcc, 1.0, v18, 1.0
	v_mul_f32_e32 v22, v21, v20
	v_fma_f32 v23, -v19, v22, v21
	v_fmac_f32_e32 v22, v23, v20
	v_fma_f32 v19, -v19, v22, v21
	v_div_fmas_f32 v19, v19, v20, v22
	v_div_fixup_f32 v18, v19, v18, 1.0
	v_pk_mul_f32 v[20:21], v[78:79], v[18:19] op_sel_hi:[1,0]
	v_pk_mul_f32 v[22:23], v[80:81], v[18:19] op_sel_hi:[1,0]
	s_waitcnt vmcnt(0)
	v_pk_mul_f32 v[26:27], v[14:15], v[20:21]
	v_pk_mul_f32 v[28:29], v[16:17], v[22:23]
	v_pk_mul_f32 v[20:21], v[74:75], v[18:19] op_sel_hi:[1,0]
	v_pk_mul_f32 v[22:23], v[76:77], v[18:19] op_sel_hi:[1,0]
	v_pk_mul_f32 v[30:31], v[10:11], v[20:21]
	v_pk_mul_f32 v[32:33], v[12:13], v[22:23]
	v_pk_mul_f32 v[20:21], v[70:71], v[18:19] op_sel_hi:[1,0]
	v_pk_mul_f32 v[22:23], v[72:73], v[18:19] op_sel_hi:[1,0]
	v_pk_mul_f32 v[162:163], v[66:67], v[18:19] op_sel_hi:[1,0]
	v_pk_mul_f32 v[18:19], v[68:69], v[18:19] op_sel_hi:[1,0]
	v_pk_mul_f32 v[24:25], v[8:9], v[22:23]
	v_pk_mul_f32 v[22:23], v[6:7], v[20:21]
	v_pk_mul_f32 v[20:21], v[4:5], v[18:19]
	v_pk_mul_f32 v[18:19], v[2:3], v[162:163]
; template <bool F8OUT = false> __device__ __forceinline__ void head_tile_store(const f32x4 (&acc)[2][2][4][2], bf16_t* obase  , int opitch, const float* gain, float scale, const f32x2e* rope, int row0, int fq) {
;     ...
;             if (rope) {
;                 const int t = row & 8191; const bool second = (fq & 2) != 0;
; #pragma unroll
;                 for (int bj = 0; bj < 2; ++bj) { const int pos = bj ? (t & 63) : (t >> 6); const f32x2e* tb = rope + pos * 16 + 8 * (fq & 1);
; #pragma unroll
;                     for (int n = 0; n < 2; ++n)
; #pragma unroll
;                         for (int e = 0; e < 4; ++e) { const float p = __shfl_xor(x[bj][n][e], 32); const f32x2e cs = tb[4 * n + e]; const float v = x[bj][n][e];
;                             x[bj][n][e] = second ? (p * cs.y + v * cs.x) : (v * cs.x - p * cs.y); } }
;             }
.LBB0_187:
	s_and_b64 vcc, exec, s[8:9]
	v_add_u32_e32 v198, 0x90, v188
	s_cbranch_vccnz .LBB0_189
	v_and_b32_e32 v163, 64, v212
	v_xor_b32_e32 v162, 32, v212
	v_add_u32_e32 v163, 64, v163
	v_cmp_lt_i32_e32 vcc, v162, v163
	v_mov_b32_e32 v193, v175
	v_lshl_add_u64 v[192:193], v[186:187], 0, v[192:193]
	v_cndmask_b32_e32 v162, v212, v162, vcc
	v_lshlrev_b32_e32 v185, 2, v162
	v_lshlrev_b32_e32 v162, 1, v198
	v_and_b32_e32 v174, 0x3f80, v162
	v_lshl_add_u64 v[200:201], v[186:187], 0, v[174:175]
	v_add_u32_e32 v238, s100, v200
	ds_read_b128 v[162:165], v238 offset:48
	ds_read_b128 v[214:217], v238 offset:32
	ds_read_b128 v[218:221], v238 offset:16
	ds_read_b128 v[222:225], v238
	v_mov_b32_e32 v226, v26
	v_mov_b32_e32 v250, v26
	s_nop 1
	v_permlane32_swap_b32_e32 v250, v226
	v_cndmask_b32_e64 v226, v250, v226, s[98:99]
	v_mov_b32_e32 v227, v27
	v_mov_b32_e32 v251, v27
	s_nop 1
	v_permlane32_swap_b32_e32 v251, v227
	v_cndmask_b32_e64 v227, v251, v227, s[98:99]
	s_waitcnt lgkmcnt(0)
	v_mov_b32_e32 v200, v223
	v_mov_b32_e32 v201, v225
	s_waitcnt lgkmcnt(0)
	v_pk_mul_f32 v[200:201], v[200:201], v[226:227]
	v_mov_b32_e32 v223, v224
	v_cndmask_b32_e64 v201, v201, -v201, s[4:5]
	v_cndmask_b32_e64 v200, v200, -v200, s[4:5]
	v_pk_fma_f32 v[26:27], v[26:27], v[222:223], v[200:201]
	v_mov_b32_e32 v200, v28
	v_mov_b32_e32 v252, v28
	s_nop 1
	v_permlane32_swap_b32_e32 v252, v200
	v_cndmask_b32_e64 v200, v252, v200, s[98:99]
	v_mov_b32_e32 v201, v29
	v_mov_b32_e32 v253, v29
	s_nop 1
	v_permlane32_swap_b32_e32 v253, v201
	v_cndmask_b32_e64 v201, v253, v201, s[98:99]
	v_mov_b32_e32 v222, v219
	v_mov_b32_e32 v223, v221
	v_mov_b32_e32 v219, v220
	s_waitcnt lgkmcnt(0)
	v_pk_mul_f32 v[200:201], v[222:223], v[200:201]
	s_nop 0
	v_cndmask_b32_e64 v201, v201, -v201, s[4:5]
	v_cndmask_b32_e64 v200, v200, -v200, s[4:5]
	v_pk_fma_f32 v[28:29], v[28:29], v[218:219], v[200:201]
	v_mov_b32_e32 v200, v30
	v_mov_b32_e32 v250, v30
	s_nop 1
	v_permlane32_swap_b32_e32 v250, v200
	v_cndmask_b32_e64 v200, v250, v200, s[98:99]
	v_mov_b32_e32 v201, v31
	v_mov_b32_e32 v251, v31
	s_nop 1
	v_permlane32_swap_b32_e32 v251, v201
	v_cndmask_b32_e64 v201, v251, v201, s[98:99]
	v_mov_b32_e32 v218, v215
	v_mov_b32_e32 v219, v217
	v_mov_b32_e32 v215, v216
	s_waitcnt lgkmcnt(0)
	v_pk_mul_f32 v[200:201], v[218:219], v[200:201]
	s_nop 0
	v_cndmask_b32_e64 v201, v201, -v201, s[4:5]
	v_cndmask_b32_e64 v200, v200, -v200, s[4:5]
	v_pk_fma_f32 v[30:31], v[30:31], v[214:215], v[200:201]
	v_mov_b32_e32 v200, v32
	v_mov_b32_e32 v252, v32
	s_nop 1
	v_permlane32_swap_b32_e32 v252, v200
	v_cndmask_b32_e64 v200, v252, v200, s[98:99]
	v_mov_b32_e32 v201, v33
	v_mov_b32_e32 v253, v33
	s_nop 1
	v_permlane32_swap_b32_e32 v253, v201
	v_cndmask_b32_e64 v201, v253, v201, s[98:99]
	v_mov_b32_e32 v214, v163
	v_mov_b32_e32 v215, v165
	v_mov_b32_e32 v163, v164
	s_waitcnt lgkmcnt(0)
	v_pk_mul_f32 v[200:201], v[214:215], v[200:201]
	s_nop 0
	v_cndmask_b32_e64 v165, v201, -v201, s[4:5]
	v_cndmask_b32_e64 v164, v200, -v200, s[4:5]
	v_pk_fma_f32 v[32:33], v[32:33], v[162:163], v[164:165]
	v_add_u32_e32 v238, s100, v192
	ds_read_b128 v[162:165], v238 offset:48
	ds_read_b128 v[214:217], v238 offset:32
	ds_read_b128 v[218:221], v238 offset:16
	ds_read_b128 v[222:225], v238
	v_mov_b32_e32 v200, v22
	v_mov_b32_e32 v250, v22
	s_nop 1
	v_permlane32_swap_b32_e32 v250, v200
	v_cndmask_b32_e64 v200, v250, v200, s[98:99]
	v_mov_b32_e32 v201, v23
	v_mov_b32_e32 v251, v23
	s_nop 1
	v_permlane32_swap_b32_e32 v251, v201
	v_cndmask_b32_e64 v201, v251, v201, s[98:99]
	s_waitcnt lgkmcnt(0)
	v_mov_b32_e32 v192, v223
	v_mov_b32_e32 v193, v225
	s_waitcnt lgkmcnt(0)
	v_pk_mul_f32 v[192:193], v[192:193], v[200:201]
	v_mov_b32_e32 v223, v224
	v_cndmask_b32_e64 v193, v193, -v193, s[4:5]
	v_cndmask_b32_e64 v192, v192, -v192, s[4:5]
	v_pk_fma_f32 v[22:23], v[22:23], v[222:223], v[192:193]
	v_mov_b32_e32 v192, v24
	v_mov_b32_e32 v252, v24
	s_nop 1
	v_permlane32_swap_b32_e32 v252, v192
	v_cndmask_b32_e64 v192, v252, v192, s[98:99]
	v_mov_b32_e32 v193, v25
	v_mov_b32_e32 v253, v25
	s_nop 1
	v_permlane32_swap_b32_e32 v253, v193
	v_cndmask_b32_e64 v193, v253, v193, s[98:99]
	v_mov_b32_e32 v200, v219
	v_mov_b32_e32 v201, v221
	v_mov_b32_e32 v219, v220
	s_waitcnt lgkmcnt(0)
	v_pk_mul_f32 v[192:193], v[200:201], v[192:193]
	s_nop 0
	v_cndmask_b32_e64 v193, v193, -v193, s[4:5]
	v_cndmask_b32_e64 v192, v192, -v192, s[4:5]
	v_pk_fma_f32 v[24:25], v[24:25], v[218:219], v[192:193]
	v_mov_b32_e32 v192, v18
	v_mov_b32_e32 v250, v18
	s_nop 1
	v_permlane32_swap_b32_e32 v250, v192
	v_cndmask_b32_e64 v192, v250, v192, s[98:99]
	v_mov_b32_e32 v193, v19
	v_mov_b32_e32 v251, v19
	s_nop 1
	v_permlane32_swap_b32_e32 v251, v193
	v_cndmask_b32_e64 v193, v251, v193, s[98:99]
	v_mov_b32_e32 v200, v215
	v_mov_b32_e32 v201, v217
	v_mov_b32_e32 v215, v216
	s_waitcnt lgkmcnt(0)
	v_pk_mul_f32 v[192:193], v[200:201], v[192:193]
	s_nop 0
	v_cndmask_b32_e64 v193, v193, -v193, s[4:5]
	v_cndmask_b32_e64 v192, v192, -v192, s[4:5]
	v_pk_fma_f32 v[18:19], v[18:19], v[214:215], v[192:193]
	v_mov_b32_e32 v192, v20
	v_mov_b32_e32 v252, v20
	s_nop 1
	v_permlane32_swap_b32_e32 v252, v192
	v_cndmask_b32_e64 v192, v252, v192, s[98:99]
	v_mov_b32_e32 v193, v21
	v_mov_b32_e32 v253, v21
	s_nop 1
	v_permlane32_swap_b32_e32 v253, v193
	v_cndmask_b32_e64 v193, v253, v193, s[98:99]
	v_mov_b32_e32 v200, v163
	v_mov_b32_e32 v201, v165
	v_mov_b32_e32 v163, v164
	s_waitcnt lgkmcnt(0)
	v_pk_mul_f32 v[192:193], v[200:201], v[192:193]
	s_nop 0
	v_cndmask_b32_e64 v165, v193, -v193, s[4:5]
	v_cndmask_b32_e64 v164, v192, -v192, s[4:5]
	v_pk_fma_f32 v[20:21], v[20:21], v[162:163], v[164:165]
; __device__ __forceinline__ unsigned pk4_fp8(float a, float b, float c, float d) { unsigned w = 0u; w = __builtin_amdgcn_cvt_pk_fp8_f32(a, b, w, false); w = __builtin_amdgcn_cvt_pk_fp8_f32(c, d, w, true); return w; }
; template <bool F8OUT = false> __device__ __forceinline__ void head_tile_store(const f32x4 (&acc)[2][2][4][2], bf16_t* obase  , int opitch, const float* gain, float scale, const f32x2e* rope, int row0, int fq) {
;     ...
;             if (gain) {
;                 float ss = 0.f;
; #pragma unroll
;                 for (int bj = 0; bj < 2; ++bj)
; #pragma unroll
;                     for (int n = 0; n < 2; ++n) ss += (x[bj][n][0] * x[bj][n][0] + x[bj][n][1] * x[bj][n][1]) + (x[bj][n][2] * x[bj][n][2] + x[bj][n][3] * x[bj][n][3]);
;                 ss += __shfl_xor(ss, 16); ss += __shfl_xor(ss, 32);
;                 const float r = scale / sqrtf(ss * (1.f / 64.f) + 1e-6f);
; #pragma unroll
;                 for (int bj = 0; bj < 2; ++bj)
; #pragma unroll
;                     for (int n = 0; n < 2; ++n) x[bj][n] = x[bj][n] * r * g[bj][n];
;     ...
;             if constexpr (F8OUT) { unsigned char* rowp8 = (unsigned char*)obase + (size_t)row * opitch + 8 * fq; typedef unsigned u32x2_ __attribute__((ext_vector_type(2)));
; #pragma unroll
;                 for (int bj = 0; bj < 2; ++bj) *(u32x2_*)(rowp8 + 32 * bj) = (u32x2_){pk4_fp8(x[bj][0][0], x[bj][0][1], x[bj][0][2], x[bj][0][3]), pk4_fp8(x[bj][1][0], x[bj][1][1], x[bj][1][2], x[bj][1][3])};
.LBB0_189:
	v_mov_b32_e32 v164, v175
	v_cvt_pk_fp8_f32 v164, v26, v27
	v_mov_b32_e32 v26, v175
	v_mov_b32_e32 v27, v175
	v_cvt_pk_fp8_f32 v26, v22, v23
	v_cvt_pk_fp8_f32 v27, v18, v19
	v_mov_b32_e32 v165, v175
	v_cvt_pk_fp8_f32 v165, v30, v31
	v_cvt_pk_fp8_f32 v26, v24, v25 op_sel:[0,0,1]
	v_cvt_pk_fp8_f32 v27, v20, v21 op_sel:[0,0,1]
	v_ashrrev_i32_e32 v199, 31, v198
	v_lshlrev_b64 v[162:163], 7, v[198:199]
	v_cvt_pk_fp8_f32 v164, v28, v29 op_sel:[0,0,1]
	v_cvt_pk_fp8_f32 v165, v32, v33 op_sel:[0,0,1]
	v_lshl_add_u64 v[162:163], v[190:191], 0, v[162:163]
	global_store_dwordx2 v[162:163], v[26:27], off offset:32
	v_mov_b64_e32 v[18:19], v[50:51]
	v_mov_b64_e32 v[22:23], v[54:55]
	v_mov_b64_e32 v[30:31], v[58:59]
	v_mov_b64_e32 v[26:27], v[62:63]
	s_and_b64 vcc, exec, s[6:7]
	v_mov_b64_e32 v[20:21], v[52:53]
	v_mov_b64_e32 v[24:25], v[56:57]
	v_mov_b64_e32 v[32:33], v[60:61]
	v_mov_b64_e32 v[28:29], v[64:65]
	global_store_dwordx2 v[162:163], v[164:165], off
	s_cbranch_vccnz .LBB0_191
	v_pk_mul_f32 v[18:19], v[64:65], v[64:65]
	v_pk_mul_f32 v[20:21], v[62:63], v[62:63]
	s_nop 0
	v_pk_mov_b32 v[22:23], v[20:21], v[18:19] op_sel:[1,0]
	v_mov_b32_e32 v21, v19
	v_pk_add_f32 v[18:19], v[22:23], v[20:21]
	v_pk_mul_f32 v[20:21], v[60:61], v[60:61]
	v_pk_mul_f32 v[22:23], v[58:59], v[58:59]
	v_pk_add_f32 v[18:19], v[18:19], v[18:19] op_sel:[0,1] op_sel_hi:[1,0]
	v_pk_mov_b32 v[24:25], v[22:23], v[20:21] op_sel:[1,0]
	v_mov_b32_e32 v23, v21
	v_pk_add_f32 v[20:21], v[24:25], v[22:23]
	v_mul_f32_e32 v22, v50, v50
	v_mul_f32_e32 v23, v51, v51
	v_pk_add_f32 v[20:21], v[20:21], v[20:21] op_sel:[0,1] op_sel_hi:[1,0]
	v_mov_b32_e32 v19, v22
	v_mov_b32_e32 v21, v23
	v_pk_add_f32 v[18:19], v[18:19], v[20:21]
	v_mul_f32_e32 v20, v55, v55
	v_mul_f32_e32 v22, v57, v57
	v_mul_f32_e32 v24, v52, v52
	v_mul_f32_e32 v25, v53, v53
	v_pk_fma_f32 v[20:21], v[54:55], v[54:55], v[20:21] op_sel_hi:[1,1,0]
	v_pk_fma_f32 v[22:23], v[56:57], v[56:57], v[22:23] op_sel_hi:[1,1,0]
	v_mov_b32_e32 v21, v24
	v_mov_b32_e32 v23, v25
	v_pk_add_f32 v[20:21], v[20:21], v[22:23]
	s_nop 0
	v_pk_add_f32 v[18:19], v[18:19], v[20:21]
	v_and_b32_e32 v20, 64, v212
	v_add_f32_e32 v18, v18, v19
	v_xor_b32_e32 v19, 16, v212
	v_add_u32_e32 v20, 64, v20
	v_cmp_lt_i32_e32 vcc, v19, v20
	s_nop 1
	v_cndmask_b32_e32 v19, v212, v19, vcc
	v_lshlrev_b32_e32 v19, 2, v19
	v_mov_b32_e32 v19, v18
	s_nop 1
	v_permlane16_swap_b32_e32 v18, v19
	s_waitcnt lgkmcnt(0)
	v_add_f32_e32 v18, v18, v19
	v_xor_b32_e32 v19, 32, v212
	v_cmp_lt_i32_e32 vcc, v19, v20
	s_nop 1
	v_cndmask_b32_e32 v19, v212, v19, vcc
	v_lshlrev_b32_e32 v19, 2, v19
	v_mov_b32_e32 v19, v18
	s_nop 1
	v_permlane32_swap_b32_e32 v18, v19
	s_waitcnt lgkmcnt(0)
	v_add_f32_e32 v18, v18, v19
	v_fmamk_f32 v18, v18, 0x3c800000, v210
	v_mul_f32_e32 v19, 0x4f800000, v18
	v_cmp_gt_f32_e32 vcc, s28, v18
	s_nop 1
	v_cndmask_b32_e32 v18, v18, v19, vcc
	v_sqrt_f32_e32 v19, v18
	s_nop 0
	v_add_u32_e32 v20, -1, v19
	v_fma_f32 v21, -v20, v19, v18
	v_cmp_ge_f32_e64 s[10:11], 0, v21
	v_add_u32_e32 v21, 1, v19
	s_nop 0
	v_cndmask_b32_e64 v20, v19, v20, s[10:11]
	v_fma_f32 v19, -v21, v19, v18
	v_cmp_lt_f32_e64 s[10:11], 0, v19
	s_nop 1
	v_cndmask_b32_e64 v19, v20, v21, s[10:11]
	v_mul_f32_e32 v20, 0x37800000, v19
	v_cndmask_b32_e32 v19, v19, v20, vcc
	v_cmp_class_f32_e32 vcc, v18, v211
	s_nop 1
	v_cndmask_b32_e32 v18, v19, v18, vcc
	v_div_scale_f32 v19, s[0:1], v18, v18, 1.0
	v_rcp_f32_e32 v20, v19
	s_nop 0
	v_fma_f32 v21, -v19, v20, 1.0
	v_fmac_f32_e32 v20, v21, v20
	v_div_scale_f32 v21, vcc, 1.0, v18, 1.0
	v_mul_f32_e32 v22, v21, v20
	v_fma_f32 v23, -v19, v22, v21
	v_fmac_f32_e32 v22, v23, v20
	v_fma_f32 v19, -v19, v22, v21
	v_div_fmas_f32 v19, v19, v20, v22
	v_div_fixup_f32 v18, v19, v18, 1.0
	v_pk_mul_f32 v[20:21], v[62:63], v[18:19] op_sel_hi:[1,0]
	v_pk_mul_f32 v[22:23], v[64:65], v[18:19] op_sel_hi:[1,0]
	s_waitcnt vmcnt(0)
	v_pk_mul_f32 v[26:27], v[14:15], v[20:21]
	v_pk_mul_f32 v[28:29], v[16:17], v[22:23]
	v_pk_mul_f32 v[20:21], v[58:59], v[18:19] op_sel_hi:[1,0]
	v_pk_mul_f32 v[22:23], v[60:61], v[18:19] op_sel_hi:[1,0]
	v_pk_mul_f32 v[30:31], v[10:11], v[20:21]
	v_pk_mul_f32 v[32:33], v[12:13], v[22:23]
	v_pk_mul_f32 v[20:21], v[54:55], v[18:19] op_sel_hi:[1,0]
	v_pk_mul_f32 v[22:23], v[56:57], v[18:19] op_sel_hi:[1,0]
	v_pk_mul_f32 v[162:163], v[50:51], v[18:19] op_sel_hi:[1,0]
	v_pk_mul_f32 v[18:19], v[52:53], v[18:19] op_sel_hi:[1,0]
	v_pk_mul_f32 v[24:25], v[8:9], v[22:23]
	v_pk_mul_f32 v[22:23], v[6:7], v[20:21]
	v_pk_mul_f32 v[20:21], v[4:5], v[18:19]
	v_pk_mul_f32 v[18:19], v[2:3], v[162:163]
; template <bool F8OUT = false> __device__ __forceinline__ void head_tile_store(const f32x4 (&acc)[2][2][4][2], bf16_t* obase  , int opitch, const float* gain, float scale, const f32x2e* rope, int row0, int fq) {
;     ...
;             if (rope) {
;                 const int t = row & 8191; const bool second = (fq & 2) != 0;
; #pragma unroll
;                 for (int bj = 0; bj < 2; ++bj) { const int pos = bj ? (t & 63) : (t >> 6); const f32x2e* tb = rope + pos * 16 + 8 * (fq & 1);
; #pragma unroll
;                     for (int n = 0; n < 2; ++n)
; #pragma unroll
;                         for (int e = 0; e < 4; ++e) { const float p = __shfl_xor(x[bj][n][e], 32); const f32x2e cs = tb[4 * n + e]; const float v = x[bj][n][e];
;                             x[bj][n][e] = second ? (p * cs.y + v * cs.x) : (v * cs.x - p * cs.y); } }
;             }
.LBB0_191:
	s_and_b64 vcc, exec, s[8:9]
	v_add_u32_e32 v192, 0xa0, v188
	s_cbranch_vccnz .LBB0_193
	v_and_b32_e32 v163, 64, v212
	v_xor_b32_e32 v162, 32, v212
	v_add_u32_e32 v163, 64, v163
	v_cmp_lt_i32_e32 vcc, v162, v163
	v_mov_b32_e32 v195, v175
	v_lshl_add_u64 v[194:195], v[186:187], 0, v[194:195]
	v_cndmask_b32_e32 v162, v212, v162, vcc
	v_lshlrev_b32_e32 v185, 2, v162
	v_lshlrev_b32_e32 v162, 1, v192
	v_and_b32_e32 v174, 0x3f80, v162
	v_lshl_add_u64 v[218:219], v[186:187], 0, v[174:175]
	v_add_u32_e32 v238, s100, v218
	ds_read_b128 v[162:165], v238 offset:48
	ds_read_b128 v[198:201], v238 offset:32
	ds_read_b128 v[214:217], v238 offset:16
	ds_read_b128 v[218:221], v238
	v_mov_b32_e32 v222, v26
	v_mov_b32_e32 v250, v26
	s_nop 1
	v_permlane32_swap_b32_e32 v250, v222
	v_cndmask_b32_e64 v222, v250, v222, s[98:99]
	v_mov_b32_e32 v223, v27
	v_mov_b32_e32 v251, v27
	s_nop 1
	v_permlane32_swap_b32_e32 v251, v223
	v_cndmask_b32_e64 v223, v251, v223, s[98:99]
	s_waitcnt lgkmcnt(0)
	v_mov_b32_e32 v224, v219
	v_mov_b32_e32 v225, v221
	s_waitcnt lgkmcnt(0)
	v_pk_mul_f32 v[222:223], v[224:225], v[222:223]
	v_mov_b32_e32 v219, v220
	v_cndmask_b32_e64 v221, v223, -v223, s[4:5]
	v_cndmask_b32_e64 v220, v222, -v222, s[4:5]
	v_pk_fma_f32 v[26:27], v[26:27], v[218:219], v[220:221]
	v_mov_b32_e32 v218, v28
	v_mov_b32_e32 v252, v28
	s_nop 1
	v_permlane32_swap_b32_e32 v252, v218
	v_cndmask_b32_e64 v218, v252, v218, s[98:99]
	v_mov_b32_e32 v219, v29
	v_mov_b32_e32 v253, v29
	s_nop 1
	v_permlane32_swap_b32_e32 v253, v219
	v_cndmask_b32_e64 v219, v253, v219, s[98:99]
	v_mov_b32_e32 v220, v215
	v_mov_b32_e32 v221, v217
	v_mov_b32_e32 v215, v216
	v_mov_b32_e32 v222, v22
	v_mov_b32_e32 v250, v22
	s_nop 1
	v_permlane32_swap_b32_e32 v250, v222
	v_cndmask_b32_e64 v222, v250, v222, s[98:99]
	s_waitcnt lgkmcnt(1)
	v_pk_mul_f32 v[218:219], v[220:221], v[218:219]
	v_mov_b32_e32 v223, v23
	v_mov_b32_e32 v251, v23
	s_nop 1
	v_permlane32_swap_b32_e32 v251, v223
	v_cndmask_b32_e64 v223, v251, v223, s[98:99]
	v_cndmask_b32_e64 v217, v219, -v219, s[4:5]
	v_cndmask_b32_e64 v216, v218, -v218, s[4:5]
	v_pk_fma_f32 v[28:29], v[28:29], v[214:215], v[216:217]
	v_mov_b32_e32 v214, v30
	v_mov_b32_e32 v252, v30
	s_nop 1
	v_permlane32_swap_b32_e32 v252, v214
	v_cndmask_b32_e64 v214, v252, v214, s[98:99]
	v_mov_b32_e32 v215, v31
	v_mov_b32_e32 v253, v31
	s_nop 1
	v_permlane32_swap_b32_e32 v253, v215
	v_cndmask_b32_e64 v215, v253, v215, s[98:99]
	v_mov_b32_e32 v216, v199
	v_mov_b32_e32 v217, v201
	v_mov_b32_e32 v199, v200
	s_waitcnt lgkmcnt(0)
	v_pk_mul_f32 v[214:215], v[216:217], v[214:215]
	s_nop 0
	v_cndmask_b32_e64 v201, v215, -v215, s[4:5]
	v_cndmask_b32_e64 v200, v214, -v214, s[4:5]
	v_pk_fma_f32 v[30:31], v[30:31], v[198:199], v[200:201]
	v_mov_b32_e32 v198, v32
	v_mov_b32_e32 v250, v32
	s_nop 1
	v_permlane32_swap_b32_e32 v250, v198
	v_cndmask_b32_e64 v198, v250, v198, s[98:99]
	v_mov_b32_e32 v199, v33
	v_mov_b32_e32 v251, v33
	s_nop 1
	v_permlane32_swap_b32_e32 v251, v199
	v_cndmask_b32_e64 v199, v251, v199, s[98:99]
	v_mov_b32_e32 v200, v163
	v_mov_b32_e32 v201, v165
	v_mov_b32_e32 v163, v164
	s_waitcnt lgkmcnt(0)
	v_pk_mul_f32 v[198:199], v[200:201], v[198:199]
	s_nop 0
	v_cndmask_b32_e64 v165, v199, -v199, s[4:5]
	v_cndmask_b32_e64 v164, v198, -v198, s[4:5]
	v_pk_fma_f32 v[32:33], v[32:33], v[162:163], v[164:165]
	v_add_u32_e32 v238, s100, v194
	ds_read_b128 v[162:165], v238 offset:48
	ds_read_b128 v[198:201], v238 offset:32
	ds_read_b128 v[214:217], v238 offset:16
	ds_read_b128 v[218:221], v238
	s_waitcnt lgkmcnt(0)
	v_mov_b32_e32 v194, v219
	v_mov_b32_e32 v195, v221
	v_pk_mul_f32 v[194:195], v[194:195], v[222:223]
	v_mov_b32_e32 v219, v220
	v_cndmask_b32_e64 v195, v195, -v195, s[4:5]
	v_cndmask_b32_e64 v194, v194, -v194, s[4:5]
	v_pk_fma_f32 v[22:23], v[22:23], v[218:219], v[194:195]
	v_mov_b32_e32 v194, v24
	v_mov_b32_e32 v252, v24
	s_nop 1
	v_permlane32_swap_b32_e32 v252, v194
	v_cndmask_b32_e64 v194, v252, v194, s[98:99]
	v_mov_b32_e32 v195, v25
	v_mov_b32_e32 v253, v25
	s_nop 1
	v_permlane32_swap_b32_e32 v253, v195
	v_cndmask_b32_e64 v195, v253, v195, s[98:99]
	v_mov_b32_e32 v218, v215
	v_mov_b32_e32 v219, v217
	v_mov_b32_e32 v215, v216
	s_waitcnt lgkmcnt(0)
	v_pk_mul_f32 v[194:195], v[218:219], v[194:195]
	s_nop 0
	v_cndmask_b32_e64 v195, v195, -v195, s[4:5]
	v_cndmask_b32_e64 v194, v194, -v194, s[4:5]
	v_pk_fma_f32 v[24:25], v[24:25], v[214:215], v[194:195]
	v_mov_b32_e32 v194, v18
	v_mov_b32_e32 v250, v18
	s_nop 1
	v_permlane32_swap_b32_e32 v250, v194
	v_cndmask_b32_e64 v194, v250, v194, s[98:99]
	v_mov_b32_e32 v195, v19
	v_mov_b32_e32 v251, v19
	s_nop 1
	v_permlane32_swap_b32_e32 v251, v195
	v_cndmask_b32_e64 v195, v251, v195, s[98:99]
	v_mov_b32_e32 v214, v199
	v_mov_b32_e32 v215, v201
	v_mov_b32_e32 v199, v200
	s_waitcnt lgkmcnt(0)
	v_pk_mul_f32 v[194:195], v[214:215], v[194:195]
	s_nop 0
	v_cndmask_b32_e64 v195, v195, -v195, s[4:5]
	v_cndmask_b32_e64 v194, v194, -v194, s[4:5]
	v_pk_fma_f32 v[18:19], v[18:19], v[198:199], v[194:195]
	v_mov_b32_e32 v194, v20
	v_mov_b32_e32 v252, v20
	s_nop 1
	v_permlane32_swap_b32_e32 v252, v194
	v_cndmask_b32_e64 v194, v252, v194, s[98:99]
	v_mov_b32_e32 v195, v21
	v_mov_b32_e32 v253, v21
	s_nop 1
	v_permlane32_swap_b32_e32 v253, v195
	v_cndmask_b32_e64 v195, v253, v195, s[98:99]
	v_mov_b32_e32 v198, v163
	v_mov_b32_e32 v199, v165
	v_mov_b32_e32 v163, v164
	s_waitcnt lgkmcnt(0)
	v_pk_mul_f32 v[194:195], v[198:199], v[194:195]
	s_nop 0
	v_cndmask_b32_e64 v165, v195, -v195, s[4:5]
	v_cndmask_b32_e64 v164, v194, -v194, s[4:5]
	v_pk_fma_f32 v[20:21], v[20:21], v[162:163], v[164:165]
; __device__ __forceinline__ unsigned pk4_fp8(float a, float b, float c, float d) { unsigned w = 0u; w = __builtin_amdgcn_cvt_pk_fp8_f32(a, b, w, false); w = __builtin_amdgcn_cvt_pk_fp8_f32(c, d, w, true); return w; }
; template <bool F8OUT = false> __device__ __forceinline__ void head_tile_store(const f32x4 (&acc)[2][2][4][2], bf16_t* obase  , int opitch, const float* gain, float scale, const f32x2e* rope, int row0, int fq) {
;     ...
;             if (gain) {
;                 float ss = 0.f;
; #pragma unroll
;                 for (int bj = 0; bj < 2; ++bj)
; #pragma unroll
;                     for (int n = 0; n < 2; ++n) ss += (x[bj][n][0] * x[bj][n][0] + x[bj][n][1] * x[bj][n][1]) + (x[bj][n][2] * x[bj][n][2] + x[bj][n][3] * x[bj][n][3]);
;                 ss += __shfl_xor(ss, 16); ss += __shfl_xor(ss, 32);
;                 const float r = scale / sqrtf(ss * (1.f / 64.f) + 1e-6f);
; #pragma unroll
;                 for (int bj = 0; bj < 2; ++bj)
; #pragma unroll
;                     for (int n = 0; n < 2; ++n) x[bj][n] = x[bj][n] * r * g[bj][n];
;     ...
;             if constexpr (F8OUT) { unsigned char* rowp8 = (unsigned char*)obase + (size_t)row * opitch + 8 * fq; typedef unsigned u32x2_ __attribute__((ext_vector_type(2)));
; #pragma unroll
;                 for (int bj = 0; bj < 2; ++bj) *(u32x2_*)(rowp8 + 32 * bj) = (u32x2_){pk4_fp8(x[bj][0][0], x[bj][0][1], x[bj][0][2], x[bj][0][3]), pk4_fp8(x[bj][1][0], x[bj][1][1], x[bj][1][2], x[bj][1][3])};
.LBB0_193:
	v_mov_b32_e32 v164, v175
	v_cvt_pk_fp8_f32 v164, v26, v27
	v_mov_b32_e32 v26, v175
	v_mov_b32_e32 v27, v175
	v_cvt_pk_fp8_f32 v26, v22, v23
	v_cvt_pk_fp8_f32 v27, v18, v19
	v_mov_b32_e32 v165, v175
	v_cvt_pk_fp8_f32 v165, v30, v31
	v_cvt_pk_fp8_f32 v26, v24, v25 op_sel:[0,0,1]
	v_cvt_pk_fp8_f32 v27, v20, v21 op_sel:[0,0,1]
	v_ashrrev_i32_e32 v193, 31, v192
	v_lshlrev_b64 v[162:163], 7, v[192:193]
	v_cvt_pk_fp8_f32 v164, v28, v29 op_sel:[0,0,1]
	v_cvt_pk_fp8_f32 v165, v32, v33 op_sel:[0,0,1]
	v_lshl_add_u64 v[162:163], v[190:191], 0, v[162:163]
	global_store_dwordx2 v[162:163], v[26:27], off offset:32
	v_mov_b64_e32 v[18:19], v[34:35]
	v_mov_b64_e32 v[22:23], v[38:39]
	v_mov_b64_e32 v[30:31], v[42:43]
	v_mov_b64_e32 v[26:27], v[46:47]
	s_and_b64 vcc, exec, s[6:7]
	v_mov_b64_e32 v[20:21], v[36:37]
	v_mov_b64_e32 v[24:25], v[40:41]
	v_mov_b64_e32 v[32:33], v[44:45]
	v_mov_b64_e32 v[28:29], v[48:49]
	global_store_dwordx2 v[162:163], v[164:165], off
	s_cbranch_vccnz .LBB0_195
	v_pk_mul_f32 v[18:19], v[48:49], v[48:49]
	v_pk_mul_f32 v[20:21], v[46:47], v[46:47]
	s_nop 0
	v_pk_mov_b32 v[22:23], v[20:21], v[18:19] op_sel:[1,0]
	v_mov_b32_e32 v21, v19
	v_pk_add_f32 v[18:19], v[22:23], v[20:21]
	v_pk_mul_f32 v[20:21], v[44:45], v[44:45]
	v_pk_mul_f32 v[22:23], v[42:43], v[42:43]
	v_pk_add_f32 v[18:19], v[18:19], v[18:19] op_sel:[0,1] op_sel_hi:[1,0]
	v_pk_mov_b32 v[24:25], v[22:23], v[20:21] op_sel:[1,0]
	v_mov_b32_e32 v23, v21
	v_pk_add_f32 v[20:21], v[24:25], v[22:23]
	v_mul_f32_e32 v22, v34, v34
	v_mul_f32_e32 v23, v35, v35
	v_pk_add_f32 v[20:21], v[20:21], v[20:21] op_sel:[0,1] op_sel_hi:[1,0]
	v_mov_b32_e32 v19, v22
	v_mov_b32_e32 v21, v23
	v_pk_add_f32 v[18:19], v[18:19], v[20:21]
	v_mul_f32_e32 v20, v39, v39
	v_mul_f32_e32 v22, v41, v41
	v_mul_f32_e32 v24, v36, v36
	v_mul_f32_e32 v25, v37, v37
	v_pk_fma_f32 v[20:21], v[38:39], v[38:39], v[20:21] op_sel_hi:[1,1,0]
	v_pk_fma_f32 v[22:23], v[40:41], v[40:41], v[22:23] op_sel_hi:[1,1,0]
	v_mov_b32_e32 v21, v24
	v_mov_b32_e32 v23, v25
	v_pk_add_f32 v[20:21], v[20:21], v[22:23]
	s_nop 0
	v_pk_add_f32 v[18:19], v[18:19], v[20:21]
	v_and_b32_e32 v20, 64, v212
	v_add_f32_e32 v18, v18, v19
	v_xor_b32_e32 v19, 16, v212
	v_add_u32_e32 v20, 64, v20
	v_cmp_lt_i32_e32 vcc, v19, v20
	s_nop 1
	v_cndmask_b32_e32 v19, v212, v19, vcc
	v_lshlrev_b32_e32 v19, 2, v19
	v_mov_b32_e32 v19, v18
	s_nop 1
	v_permlane16_swap_b32_e32 v18, v19
	s_waitcnt lgkmcnt(0)
	v_add_f32_e32 v18, v18, v19
	v_xor_b32_e32 v19, 32, v212
	v_cmp_lt_i32_e32 vcc, v19, v20
	s_nop 1
	v_cndmask_b32_e32 v19, v212, v19, vcc
	v_lshlrev_b32_e32 v19, 2, v19
	v_mov_b32_e32 v19, v18
	s_nop 1
	v_permlane32_swap_b32_e32 v18, v19
	s_waitcnt lgkmcnt(0)
	v_add_f32_e32 v18, v18, v19
	v_fmamk_f32 v18, v18, 0x3c800000, v210
	v_mul_f32_e32 v19, 0x4f800000, v18
	v_cmp_gt_f32_e32 vcc, s28, v18
	s_nop 1
	v_cndmask_b32_e32 v18, v18, v19, vcc
	v_sqrt_f32_e32 v19, v18
	s_nop 0
	v_add_u32_e32 v20, -1, v19
	v_fma_f32 v21, -v20, v19, v18
	v_cmp_ge_f32_e64 s[6:7], 0, v21
	v_add_u32_e32 v21, 1, v19
	s_nop 0
	v_cndmask_b32_e64 v20, v19, v20, s[6:7]
	v_fma_f32 v19, -v21, v19, v18
	v_cmp_lt_f32_e64 s[6:7], 0, v19
	s_nop 1
	v_cndmask_b32_e64 v19, v20, v21, s[6:7]
	v_mul_f32_e32 v20, 0x37800000, v19
	v_cndmask_b32_e32 v19, v19, v20, vcc
	v_cmp_class_f32_e32 vcc, v18, v211
	s_nop 1
	v_cndmask_b32_e32 v18, v19, v18, vcc
	v_div_scale_f32 v19, s[0:1], v18, v18, 1.0
	v_rcp_f32_e32 v20, v19
	s_nop 0
	v_fma_f32 v21, -v19, v20, 1.0
	v_fmac_f32_e32 v20, v21, v20
	v_div_scale_f32 v21, vcc, 1.0, v18, 1.0
	v_mul_f32_e32 v22, v21, v20
	v_fma_f32 v23, -v19, v22, v21
	v_fmac_f32_e32 v22, v23, v20
	v_fma_f32 v19, -v19, v22, v21
	v_div_fmas_f32 v19, v19, v20, v22
	v_div_fixup_f32 v18, v19, v18, 1.0
	v_pk_mul_f32 v[20:21], v[46:47], v[18:19] op_sel_hi:[1,0]
	v_pk_mul_f32 v[22:23], v[48:49], v[18:19] op_sel_hi:[1,0]
	s_waitcnt vmcnt(0)
	v_pk_mul_f32 v[26:27], v[14:15], v[20:21]
	v_pk_mul_f32 v[28:29], v[16:17], v[22:23]
	v_pk_mul_f32 v[14:15], v[42:43], v[18:19] op_sel_hi:[1,0]
	v_pk_mul_f32 v[16:17], v[44:45], v[18:19] op_sel_hi:[1,0]
	v_pk_mul_f32 v[30:31], v[10:11], v[14:15]
	v_pk_mul_f32 v[32:33], v[12:13], v[16:17]
	v_pk_mul_f32 v[10:11], v[38:39], v[18:19] op_sel_hi:[1,0]
	v_pk_mul_f32 v[12:13], v[40:41], v[18:19] op_sel_hi:[1,0]
	v_pk_mul_f32 v[22:23], v[6:7], v[10:11]
	v_pk_mul_f32 v[24:25], v[8:9], v[12:13]
	v_pk_mul_f32 v[6:7], v[34:35], v[18:19] op_sel_hi:[1,0]
	v_pk_mul_f32 v[8:9], v[36:37], v[18:19] op_sel_hi:[1,0]
	v_pk_mul_f32 v[18:19], v[2:3], v[6:7]
	v_pk_mul_f32 v[20:21], v[4:5], v[8:9]
; template <bool F8OUT = false> __device__ __forceinline__ void head_tile_store(const f32x4 (&acc)[2][2][4][2], bf16_t* obase  , int opitch, const float* gain, float scale, const f32x2e* rope, int row0, int fq) {
;     ...
;             if (rope) {
;                 const int t = row & 8191; const bool second = (fq & 2) != 0;
; #pragma unroll
;                 for (int bj = 0; bj < 2; ++bj) { const int pos = bj ? (t & 63) : (t >> 6); const f32x2e* tb = rope + pos * 16 + 8 * (fq & 1);
; #pragma unroll
;                     for (int n = 0; n < 2; ++n)
; #pragma unroll
;                         for (int e = 0; e < 4; ++e) { const float p = __shfl_xor(x[bj][n][e], 32); const f32x2e cs = tb[4 * n + e]; const float v = x[bj][n][e];
;                             x[bj][n][e] = second ? (p * cs.y + v * cs.x) : (v * cs.x - p * cs.y); } }
;             }
.LBB0_195:
	s_and_b64 vcc, exec, s[8:9]
	s_waitcnt vmcnt(0)
	v_add_u32_e32 v6, 0xb0, v188
	s_cbranch_vccnz .LBB0_197
	v_and_b32_e32 v3, 64, v212
	v_xor_b32_e32 v2, 32, v212
	v_add_u32_e32 v3, 64, v3
	v_cmp_lt_i32_e32 vcc, v2, v3
	v_mov_b32_e32 v197, v175
	s_nop 0
	v_cndmask_b32_e32 v2, v212, v2, vcc
	v_lshlrev_b32_e32 v7, 2, v2
	v_lshlrev_b32_e32 v2, 1, v6
	v_and_b32_e32 v174, 0x3f80, v2
	v_lshl_add_u64 v[16:17], v[186:187], 0, v[174:175]
	v_add_u32_e32 v238, s100, v16
	ds_read_b128 v[2:5], v238 offset:48
	ds_read_b128 v[8:11], v238 offset:32
	ds_read_b128 v[12:15], v238 offset:16
	ds_read_b128 v[162:165], v238
	v_mov_b32_e32 v188, v26
	v_mov_b32_e32 v250, v26
	s_nop 1
	v_permlane32_swap_b32_e32 v250, v188
	v_cndmask_b32_e64 v188, v250, v188, s[98:99]
	v_mov_b32_e32 v189, v27
	v_mov_b32_e32 v251, v27
	s_nop 1
	v_permlane32_swap_b32_e32 v251, v189
	v_cndmask_b32_e64 v189, v251, v189, s[98:99]
	s_waitcnt lgkmcnt(0)
	v_mov_b32_e32 v16, v163
	v_mov_b32_e32 v17, v165
	s_waitcnt lgkmcnt(0)
	v_pk_mul_f32 v[16:17], v[16:17], v[188:189]
	v_mov_b32_e32 v163, v164
	v_cndmask_b32_e64 v17, v17, -v17, s[4:5]
	v_cndmask_b32_e64 v16, v16, -v16, s[4:5]
	v_pk_fma_f32 v[26:27], v[26:27], v[162:163], v[16:17]
	v_mov_b32_e32 v16, v28
	v_mov_b32_e32 v252, v28
	s_nop 1
	v_permlane32_swap_b32_e32 v252, v16
	v_cndmask_b32_e64 v16, v252, v16, s[98:99]
	v_mov_b32_e32 v17, v29
	v_mov_b32_e32 v253, v29
	s_nop 1
	v_permlane32_swap_b32_e32 v253, v17
	v_cndmask_b32_e64 v17, v253, v17, s[98:99]
	v_mov_b32_e32 v162, v13
	v_mov_b32_e32 v163, v15
	v_mov_b32_e32 v13, v14
	s_waitcnt lgkmcnt(0)
	v_pk_mul_f32 v[16:17], v[162:163], v[16:17]
	s_nop 0
	v_cndmask_b32_e64 v15, v17, -v17, s[4:5]
	v_cndmask_b32_e64 v14, v16, -v16, s[4:5]
	v_pk_fma_f32 v[28:29], v[28:29], v[12:13], v[14:15]
	v_mov_b32_e32 v12, v30
	v_mov_b32_e32 v250, v30
	s_nop 1
	v_permlane32_swap_b32_e32 v250, v12
	v_cndmask_b32_e64 v12, v250, v12, s[98:99]
	v_mov_b32_e32 v13, v31
	v_mov_b32_e32 v251, v31
	s_nop 1
	v_permlane32_swap_b32_e32 v251, v13
	v_cndmask_b32_e64 v13, v251, v13, s[98:99]
	v_mov_b32_e32 v14, v9
	v_mov_b32_e32 v15, v11
	v_mov_b32_e32 v9, v10
	v_lshl_add_u64 v[16:17], v[186:187], 0, v[196:197]
	s_waitcnt lgkmcnt(0)
	v_pk_mul_f32 v[12:13], v[14:15], v[12:13]
	v_mov_b32_e32 v186, v22
	v_mov_b32_e32 v252, v22
	s_nop 1
	v_permlane32_swap_b32_e32 v252, v186
	v_cndmask_b32_e64 v186, v252, v186, s[98:99]
	v_cndmask_b32_e64 v11, v13, -v13, s[4:5]
	v_cndmask_b32_e64 v10, v12, -v12, s[4:5]
	v_pk_fma_f32 v[30:31], v[30:31], v[8:9], v[10:11]
	v_mov_b32_e32 v8, v32
	v_mov_b32_e32 v253, v32
	s_nop 1
	v_permlane32_swap_b32_e32 v253, v8
	v_cndmask_b32_e64 v8, v253, v8, s[98:99]
	v_mov_b32_e32 v9, v33
	v_mov_b32_e32 v250, v33
	s_nop 1
	v_permlane32_swap_b32_e32 v250, v9
	v_cndmask_b32_e64 v9, v250, v9, s[98:99]
	v_mov_b32_e32 v10, v3
	v_mov_b32_e32 v11, v5
	v_mov_b32_e32 v3, v4
	v_mov_b32_e32 v187, v23
	v_mov_b32_e32 v251, v23
	s_nop 1
	v_permlane32_swap_b32_e32 v251, v187
	v_cndmask_b32_e64 v187, v251, v187, s[98:99]
	s_waitcnt lgkmcnt(1)
	v_pk_mul_f32 v[8:9], v[10:11], v[8:9]
	s_nop 0
	v_cndmask_b32_e64 v5, v9, -v9, s[4:5]
	v_cndmask_b32_e64 v4, v8, -v8, s[4:5]
	v_pk_fma_f32 v[32:33], v[32:33], v[2:3], v[4:5]
	v_add_u32_e32 v238, s100, v16
	ds_read_b128 v[2:5], v238 offset:48
	ds_read_b128 v[8:11], v238 offset:32
	ds_read_b128 v[12:15], v238 offset:16
	ds_read_b128 v[162:165], v238
	s_waitcnt lgkmcnt(0)
	v_mov_b32_e32 v16, v163
	v_mov_b32_e32 v17, v165
	s_waitcnt lgkmcnt(0)
	v_pk_mul_f32 v[16:17], v[16:17], v[186:187]
	v_mov_b32_e32 v163, v164
	v_cndmask_b32_e64 v17, v17, -v17, s[4:5]
	v_cndmask_b32_e64 v16, v16, -v16, s[4:5]
	v_pk_fma_f32 v[22:23], v[22:23], v[162:163], v[16:17]
	v_mov_b32_e32 v16, v24
	v_mov_b32_e32 v252, v24
	s_nop 1
	v_permlane32_swap_b32_e32 v252, v16
	v_cndmask_b32_e64 v16, v252, v16, s[98:99]
	v_mov_b32_e32 v17, v25
	v_mov_b32_e32 v253, v25
	s_nop 1
	v_permlane32_swap_b32_e32 v253, v17
	v_cndmask_b32_e64 v17, v253, v17, s[98:99]
	v_mov_b32_e32 v162, v13
	v_mov_b32_e32 v163, v15
	v_mov_b32_e32 v13, v14
	s_waitcnt lgkmcnt(0)
	v_pk_mul_f32 v[16:17], v[162:163], v[16:17]
	s_nop 0
	v_cndmask_b32_e64 v15, v17, -v17, s[4:5]
	v_cndmask_b32_e64 v14, v16, -v16, s[4:5]
	v_pk_fma_f32 v[24:25], v[24:25], v[12:13], v[14:15]
	v_mov_b32_e32 v12, v18
	v_mov_b32_e32 v250, v18
	s_nop 1
	v_permlane32_swap_b32_e32 v250, v12
	v_cndmask_b32_e64 v12, v250, v12, s[98:99]
	v_mov_b32_e32 v13, v19
	v_mov_b32_e32 v251, v19
	s_nop 1
	v_permlane32_swap_b32_e32 v251, v13
	v_cndmask_b32_e64 v13, v251, v13, s[98:99]
	v_mov_b32_e32 v14, v9
	v_mov_b32_e32 v15, v11
	v_mov_b32_e32 v9, v10
	s_waitcnt lgkmcnt(0)
	v_pk_mul_f32 v[12:13], v[14:15], v[12:13]
	s_nop 0
	v_cndmask_b32_e64 v11, v13, -v13, s[4:5]
	v_cndmask_b32_e64 v10, v12, -v12, s[4:5]
	v_pk_fma_f32 v[18:19], v[18:19], v[8:9], v[10:11]
	v_mov_b32_e32 v8, v20
	v_mov_b32_e32 v252, v20
	s_nop 1
	v_permlane32_swap_b32_e32 v252, v8
	v_cndmask_b32_e64 v8, v252, v8, s[98:99]
	v_mov_b32_e32 v9, v21
	v_mov_b32_e32 v253, v21
	s_nop 1
	v_permlane32_swap_b32_e32 v253, v9
	v_cndmask_b32_e64 v9, v253, v9, s[98:99]
	v_mov_b32_e32 v10, v3
	v_mov_b32_e32 v11, v5
	v_mov_b32_e32 v3, v4
	s_waitcnt lgkmcnt(0)
	v_pk_mul_f32 v[8:9], v[10:11], v[8:9]
	s_nop 0
	v_cndmask_b32_e64 v5, v9, -v9, s[4:5]
	v_cndmask_b32_e64 v4, v8, -v8, s[4:5]
	v_pk_fma_f32 v[20:21], v[20:21], v[2:3], v[4:5]

; template <bool F8OUT = false> __device__ __forceinline__ void head_tile_store(const f32x4 (&acc)[2][2][4][2], bf16_t* obase  , int opitch, const float* gain, float scale, const f32x2e* rope, int row0, int fq) {
;     ...
;             const int row = row0 + ai * HALF + m * 16;
;             f32x4 x[2][2];
; #pragma unroll
;             for (int bj = 0; bj < 2; ++bj)
; #pragma unroll
;                 for (int n = 0; n < 2; ++n) x[bj][n] = acc[ai][bj][m][n];
;             if (gain) {
;                 float ss = 0.f;
; #pragma unroll
;                 for (int bj = 0; bj < 2; ++bj)
; #pragma unroll
;                     for (int n = 0; n < 2; ++n) ss += (x[bj][n][0] * x[bj][n][0] + x[bj][n][1] * x[bj][n][1]) + (x[bj][n][2] * x[bj][n][2] + x[bj][n][3] * x[bj][n][3]);
;                 ss += __shfl_xor(ss, 16); ss += __shfl_xor(ss, 32);
;                 const float r = scale / sqrtf(ss * (1.f / 64.f) + 1e-6f);
; #pragma unroll
;                 for (int bj = 0; bj < 2; ++bj)
; #pragma unroll
;                     for (int n = 0; n < 2; ++n) x[bj][n] = x[bj][n] * r * g[bj][n];
.LBB0_202:
	v_mov_b64_e32 v[30:31], v[146:147]
	v_mov_b64_e32 v[26:27], v[150:151]
	v_mov_b64_e32 v[22:23], v[154:155]
	v_mov_b64_e32 v[18:19], v[158:159]
	s_and_b64 vcc, exec, s[6:7]
	v_mov_b64_e32 v[32:33], v[148:149]
	v_mov_b64_e32 v[28:29], v[152:153]
	v_mov_b64_e32 v[24:25], v[156:157]
	v_mov_b64_e32 v[20:21], v[160:161]
	s_cbranch_vccnz .LBB0_204
	v_pk_mul_f32 v[18:19], v[160:161], v[160:161]
	v_pk_mul_f32 v[20:21], v[158:159], v[158:159]
	s_nop 0
	v_pk_mov_b32 v[22:23], v[20:21], v[18:19] op_sel:[1,0]
	v_mov_b32_e32 v21, v19
	v_pk_add_f32 v[18:19], v[22:23], v[20:21]
	v_pk_mul_f32 v[20:21], v[156:157], v[156:157]
	v_pk_mul_f32 v[22:23], v[154:155], v[154:155]
	v_pk_add_f32 v[18:19], v[18:19], v[18:19] op_sel:[0,1] op_sel_hi:[1,0]
	v_pk_mov_b32 v[24:25], v[22:23], v[20:21] op_sel:[1,0]
	v_mov_b32_e32 v23, v21
	v_pk_add_f32 v[20:21], v[24:25], v[22:23]
	v_mul_f32_e32 v22, v146, v146
	v_mul_f32_e32 v23, v147, v147
	v_pk_add_f32 v[20:21], v[20:21], v[20:21] op_sel:[0,1] op_sel_hi:[1,0]
	v_mov_b32_e32 v19, v22
	v_mov_b32_e32 v21, v23
	v_pk_add_f32 v[18:19], v[18:19], v[20:21]
	v_mul_f32_e32 v20, v151, v151
	v_mul_f32_e32 v22, v153, v153
	v_mul_f32_e32 v24, v148, v148
	v_mul_f32_e32 v25, v149, v149
	v_pk_fma_f32 v[20:21], v[150:151], v[150:151], v[20:21] op_sel_hi:[1,1,0]
	v_pk_fma_f32 v[22:23], v[152:153], v[152:153], v[22:23] op_sel_hi:[1,1,0]
	v_mov_b32_e32 v21, v24
	v_mov_b32_e32 v23, v25
	v_pk_add_f32 v[20:21], v[20:21], v[22:23]
	s_nop 0
	v_pk_add_f32 v[18:19], v[18:19], v[20:21]
	v_and_b32_e32 v20, 64, v212
	v_add_f32_e32 v18, v18, v19
	v_xor_b32_e32 v19, 16, v212
	v_add_u32_e32 v20, 64, v20
	v_cmp_lt_i32_e32 vcc, v19, v20
	s_nop 1
	v_cndmask_b32_e32 v19, v212, v19, vcc
	v_lshlrev_b32_e32 v19, 2, v19
	v_mov_b32_e32 v19, v18
	s_nop 1
	v_permlane16_swap_b32_e32 v18, v19
	s_waitcnt lgkmcnt(0)
	v_add_f32_e32 v18, v18, v19
	v_xor_b32_e32 v19, 32, v212
	v_cmp_lt_i32_e32 vcc, v19, v20
	s_nop 1
	v_cndmask_b32_e32 v19, v212, v19, vcc
	v_lshlrev_b32_e32 v19, 2, v19
	v_mov_b32_e32 v19, v18
	s_nop 1
	v_permlane32_swap_b32_e32 v18, v19
	s_waitcnt lgkmcnt(0)
	v_add_f32_e32 v18, v18, v19
	v_fmamk_f32 v18, v18, 0x3c800000, v210
	v_mul_f32_e32 v19, 0x4f800000, v18
	v_cmp_gt_f32_e32 vcc, s28, v18
	s_nop 1
	v_cndmask_b32_e32 v18, v18, v19, vcc
	v_sqrt_f32_e32 v19, v18
	s_nop 0
	v_add_u32_e32 v20, -1, v19
	v_fma_f32 v21, -v20, v19, v18
	v_cmp_ge_f32_e64 s[4:5], 0, v21
	v_add_u32_e32 v21, 1, v19
	s_nop 0
	v_cndmask_b32_e64 v20, v19, v20, s[4:5]
	v_fma_f32 v19, -v21, v19, v18
	v_cmp_lt_f32_e64 s[4:5], 0, v19
	s_nop 1
	v_cndmask_b32_e64 v19, v20, v21, s[4:5]
	v_mul_f32_e32 v20, 0x37800000, v19
	v_cndmask_b32_e32 v19, v19, v20, vcc
	v_cmp_class_f32_e32 vcc, v18, v211
	s_nop 1
	v_cndmask_b32_e32 v18, v19, v18, vcc
	v_div_scale_f32 v19, s[0:1], v18, v18, s29
	v_rcp_f32_e32 v20, v19
	s_nop 0
	v_fma_f32 v21, -v19, v20, 1.0
	v_fmac_f32_e32 v20, v21, v20
	v_div_scale_f32 v21, vcc, s29, v18, s29
	v_mul_f32_e32 v22, v21, v20
	v_fma_f32 v23, -v19, v22, v21
	v_fmac_f32_e32 v22, v23, v20
	v_fma_f32 v19, -v19, v22, v21
	v_div_fmas_f32 v19, v19, v20, v22
	v_div_fixup_f32 v30, v19, v18, s29
	v_pk_mul_f32 v[18:19], v[158:159], v[30:31] op_sel_hi:[1,0]
	v_pk_mul_f32 v[20:21], v[160:161], v[30:31] op_sel_hi:[1,0]
	v_pk_mul_f32 v[22:23], v[154:155], v[30:31] op_sel_hi:[1,0]
	v_pk_mul_f32 v[24:25], v[156:157], v[30:31] op_sel_hi:[1,0]
	v_pk_mul_f32 v[26:27], v[150:151], v[30:31] op_sel_hi:[1,0]
	v_pk_mul_f32 v[28:29], v[152:153], v[30:31] op_sel_hi:[1,0]
	v_pk_mul_f32 v[164:165], v[146:147], v[30:31] op_sel_hi:[1,0]
	v_pk_mul_f32 v[30:31], v[148:149], v[30:31] op_sel_hi:[1,0]
	s_waitcnt vmcnt(0)
	v_pk_mul_f32 v[20:21], v[16:17], v[20:21]
	v_pk_mul_f32 v[18:19], v[14:15], v[18:19]
	v_pk_mul_f32 v[24:25], v[12:13], v[24:25]
	v_pk_mul_f32 v[22:23], v[10:11], v[22:23]
	v_pk_mul_f32 v[28:29], v[8:9], v[28:29]
	v_pk_mul_f32 v[26:27], v[6:7], v[26:27]
	v_pk_mul_f32 v[32:33], v[4:5], v[30:31]
	v_pk_mul_f32 v[30:31], v[2:3], v[164:165]

; __device__ __forceinline__ unsigned pk4_fp8(float a, float b, float c, float d) { unsigned w = 0u; w = __builtin_amdgcn_cvt_pk_fp8_f32(a, b, w, false); w = __builtin_amdgcn_cvt_pk_fp8_f32(c, d, w, true); return w; }
; template <bool F8OUT = false> __device__ __forceinline__ void head_tile_store(const f32x4 (&acc)[2][2][4][2], bf16_t* obase  , int opitch, const float* gain, float scale, const f32x2e* rope, int row0, int fq) {
;     ...
;             if (gain) {
;                 float ss = 0.f;
; #pragma unroll
;                 for (int bj = 0; bj < 2; ++bj)
; #pragma unroll
;                     for (int n = 0; n < 2; ++n) ss += (x[bj][n][0] * x[bj][n][0] + x[bj][n][1] * x[bj][n][1]) + (x[bj][n][2] * x[bj][n][2] + x[bj][n][3] * x[bj][n][3]);
;                 ss += __shfl_xor(ss, 16); ss += __shfl_xor(ss, 32);
;                 const float r = scale / sqrtf(ss * (1.f / 64.f) + 1e-6f);
; #pragma unroll
;                 for (int bj = 0; bj < 2; ++bj)
; #pragma unroll
;                     for (int n = 0; n < 2; ++n) x[bj][n] = x[bj][n] * r * g[bj][n];
;     ...
;             if constexpr (F8OUT) { unsigned char* rowp8 = (unsigned char*)obase + (size_t)row * opitch + 8 * fq; typedef unsigned u32x2_ __attribute__((ext_vector_type(2)));
; #pragma unroll
;                 for (int bj = 0; bj < 2; ++bj) *(u32x2_*)(rowp8 + 32 * bj) = (u32x2_){pk4_fp8(x[bj][0][0], x[bj][0][1], x[bj][0][2], x[bj][0][3]), pk4_fp8(x[bj][1][0], x[bj][1][1], x[bj][1][2], x[bj][1][3])};
.LBB0_206:
	v_mov_b32_e32 v162, v175
	v_mov_b32_e32 v163, v175
	v_cvt_pk_fp8_f32 v162, v18, v19
	v_cvt_pk_fp8_f32 v163, v22, v23
	v_mov_b32_e32 v18, v175
	v_mov_b32_e32 v19, v175
	v_cvt_pk_fp8_f32 v18, v26, v27
	v_cvt_pk_fp8_f32 v19, v30, v31
	s_lshl_b32 s0, s18, 6
	s_add_u32 s0, s70, s0
	v_cvt_pk_fp8_f32 v162, v20, v21 op_sel:[0,0,1]
	v_cvt_pk_fp8_f32 v163, v24, v25 op_sel:[0,0,1]
	s_addc_u32 s1, s71, 0
	v_ashrrev_i32_e32 v189, 31, v188
	v_cvt_pk_fp8_f32 v18, v28, v29 op_sel:[0,0,1]
	v_cvt_pk_fp8_f32 v19, v32, v33 op_sel:[0,0,1]
	v_lshl_add_u64 v[190:191], s[0:1], 0, v[190:191]
	v_lshlrev_b64 v[20:21], 9, v[188:189]
	v_lshl_add_u64 v[20:21], v[190:191], 0, v[20:21]
	global_store_dwordx2 v[20:21], v[162:163], off
	global_store_dwordx2 v[20:21], v[18:19], off offset:32
	v_mov_b64_e32 v[18:19], v[130:131]
	v_mov_b64_e32 v[22:23], v[134:135]
	v_mov_b64_e32 v[30:31], v[138:139]
	v_mov_b64_e32 v[26:27], v[142:143]
	s_and_b64 vcc, exec, s[6:7]
	v_mov_b64_e32 v[20:21], v[132:133]
	v_mov_b64_e32 v[24:25], v[136:137]
	v_mov_b64_e32 v[32:33], v[140:141]
	v_mov_b64_e32 v[28:29], v[144:145]
	s_cbranch_vccnz .LBB0_208
	v_pk_mul_f32 v[18:19], v[144:145], v[144:145]
	v_pk_mul_f32 v[20:21], v[142:143], v[142:143]
	s_nop 0
	v_pk_mov_b32 v[22:23], v[20:21], v[18:19] op_sel:[1,0]
	v_mov_b32_e32 v21, v19
	v_pk_add_f32 v[18:19], v[22:23], v[20:21]
	v_pk_mul_f32 v[20:21], v[140:141], v[140:141]
	v_pk_mul_f32 v[22:23], v[138:139], v[138:139]
	v_pk_add_f32 v[18:19], v[18:19], v[18:19] op_sel:[0,1] op_sel_hi:[1,0]
	v_pk_mov_b32 v[24:25], v[22:23], v[20:21] op_sel:[1,0]
	v_mov_b32_e32 v23, v21
	v_pk_add_f32 v[20:21], v[24:25], v[22:23]
	v_mul_f32_e32 v22, v130, v130
	v_mul_f32_e32 v23, v131, v131
	v_pk_add_f32 v[20:21], v[20:21], v[20:21] op_sel:[0,1] op_sel_hi:[1,0]
	v_mov_b32_e32 v19, v22
	v_mov_b32_e32 v21, v23
	v_pk_add_f32 v[18:19], v[18:19], v[20:21]
	v_mul_f32_e32 v20, v135, v135
	v_mul_f32_e32 v22, v137, v137
	v_mul_f32_e32 v24, v132, v132
	v_mul_f32_e32 v25, v133, v133
	v_pk_fma_f32 v[20:21], v[134:135], v[134:135], v[20:21] op_sel_hi:[1,1,0]
	v_pk_fma_f32 v[22:23], v[136:137], v[136:137], v[22:23] op_sel_hi:[1,1,0]
	v_mov_b32_e32 v21, v24
	v_mov_b32_e32 v23, v25
	v_pk_add_f32 v[20:21], v[20:21], v[22:23]
	s_nop 0
	v_pk_add_f32 v[18:19], v[18:19], v[20:21]
	v_and_b32_e32 v20, 64, v212
	v_add_f32_e32 v18, v18, v19
	v_xor_b32_e32 v19, 16, v212
	v_add_u32_e32 v20, 64, v20
	v_cmp_lt_i32_e32 vcc, v19, v20
	s_nop 1
	v_cndmask_b32_e32 v19, v212, v19, vcc
	v_lshlrev_b32_e32 v19, 2, v19
	v_mov_b32_e32 v19, v18
	s_nop 1
	v_permlane16_swap_b32_e32 v18, v19
	s_waitcnt lgkmcnt(0)
	v_add_f32_e32 v18, v18, v19
	v_xor_b32_e32 v19, 32, v212
	v_cmp_lt_i32_e32 vcc, v19, v20
	s_nop 1
	v_cndmask_b32_e32 v19, v212, v19, vcc
	v_lshlrev_b32_e32 v19, 2, v19
	v_mov_b32_e32 v19, v18
	s_nop 1
	v_permlane32_swap_b32_e32 v18, v19
	s_waitcnt lgkmcnt(0)
	v_add_f32_e32 v18, v18, v19
	v_fmamk_f32 v18, v18, 0x3c800000, v210
	v_mul_f32_e32 v19, 0x4f800000, v18
	v_cmp_gt_f32_e32 vcc, s28, v18
	s_nop 1
	v_cndmask_b32_e32 v18, v18, v19, vcc
	v_sqrt_f32_e32 v19, v18
	s_nop 0
	v_add_u32_e32 v20, -1, v19
	v_fma_f32 v21, -v20, v19, v18
	v_cmp_ge_f32_e64 s[10:11], 0, v21
	v_add_u32_e32 v21, 1, v19
	s_nop 0
	v_cndmask_b32_e64 v20, v19, v20, s[10:11]
	v_fma_f32 v19, -v21, v19, v18
	v_cmp_lt_f32_e64 s[10:11], 0, v19
	s_nop 1
	v_cndmask_b32_e64 v19, v20, v21, s[10:11]
	v_mul_f32_e32 v20, 0x37800000, v19
	v_cndmask_b32_e32 v19, v19, v20, vcc
	v_cmp_class_f32_e32 vcc, v18, v211
	s_nop 1
	v_cndmask_b32_e32 v18, v19, v18, vcc
	v_div_scale_f32 v19, s[0:1], v18, v18, s29
	v_rcp_f32_e32 v20, v19
	s_nop 0
	v_fma_f32 v21, -v19, v20, 1.0
	v_fmac_f32_e32 v20, v21, v20
	v_div_scale_f32 v21, vcc, s29, v18, s29
	v_mul_f32_e32 v22, v21, v20
	v_fma_f32 v23, -v19, v22, v21
	v_fmac_f32_e32 v22, v23, v20
	v_fma_f32 v19, -v19, v22, v21
	v_div_fmas_f32 v19, v19, v20, v22
	v_div_fixup_f32 v18, v19, v18, s29
	v_pk_mul_f32 v[20:21], v[142:143], v[18:19] op_sel_hi:[1,0]
	v_pk_mul_f32 v[22:23], v[144:145], v[18:19] op_sel_hi:[1,0]
	s_waitcnt vmcnt(0)
	v_pk_mul_f32 v[26:27], v[14:15], v[20:21]
	v_pk_mul_f32 v[28:29], v[16:17], v[22:23]
	v_pk_mul_f32 v[20:21], v[138:139], v[18:19] op_sel_hi:[1,0]
	v_pk_mul_f32 v[22:23], v[140:141], v[18:19] op_sel_hi:[1,0]
	v_pk_mul_f32 v[30:31], v[10:11], v[20:21]
	v_pk_mul_f32 v[32:33], v[12:13], v[22:23]
	v_pk_mul_f32 v[20:21], v[134:135], v[18:19] op_sel_hi:[1,0]
	v_pk_mul_f32 v[22:23], v[136:137], v[18:19] op_sel_hi:[1,0]
	v_pk_mul_f32 v[162:163], v[130:131], v[18:19] op_sel_hi:[1,0]
	v_pk_mul_f32 v[18:19], v[132:133], v[18:19] op_sel_hi:[1,0]
	v_pk_mul_f32 v[24:25], v[8:9], v[22:23]
	v_pk_mul_f32 v[22:23], v[6:7], v[20:21]
	v_pk_mul_f32 v[20:21], v[4:5], v[18:19]
	v_pk_mul_f32 v[18:19], v[2:3], v[162:163]

; __device__ __forceinline__ unsigned pk4_fp8(float a, float b, float c, float d) { unsigned w = 0u; w = __builtin_amdgcn_cvt_pk_fp8_f32(a, b, w, false); w = __builtin_amdgcn_cvt_pk_fp8_f32(c, d, w, true); return w; }
; template <bool F8OUT = false> __device__ __forceinline__ void head_tile_store(const f32x4 (&acc)[2][2][4][2], bf16_t* obase  , int opitch, const float* gain, float scale, const f32x2e* rope, int row0, int fq) {
;     ...
;             if (gain) {
;                 float ss = 0.f;
; #pragma unroll
;                 for (int bj = 0; bj < 2; ++bj)
; #pragma unroll
;                     for (int n = 0; n < 2; ++n) ss += (x[bj][n][0] * x[bj][n][0] + x[bj][n][1] * x[bj][n][1]) + (x[bj][n][2] * x[bj][n][2] + x[bj][n][3] * x[bj][n][3]);
;                 ss += __shfl_xor(ss, 16); ss += __shfl_xor(ss, 32);
;                 const float r = scale / sqrtf(ss * (1.f / 64.f) + 1e-6f);
; #pragma unroll
;                 for (int bj = 0; bj < 2; ++bj)
; #pragma unroll
;                     for (int n = 0; n < 2; ++n) x[bj][n] = x[bj][n] * r * g[bj][n];
;     ...
;             if constexpr (F8OUT) { unsigned char* rowp8 = (unsigned char*)obase + (size_t)row * opitch + 8 * fq; typedef unsigned u32x2_ __attribute__((ext_vector_type(2)));
; #pragma unroll
;                 for (int bj = 0; bj < 2; ++bj) *(u32x2_*)(rowp8 + 32 * bj) = (u32x2_){pk4_fp8(x[bj][0][0], x[bj][0][1], x[bj][0][2], x[bj][0][3]), pk4_fp8(x[bj][1][0], x[bj][1][1], x[bj][1][2], x[bj][1][3])};
.LBB0_210:
	v_mov_b32_e32 v164, v175
	v_cvt_pk_fp8_f32 v164, v26, v27
	v_mov_b32_e32 v26, v175
	v_mov_b32_e32 v27, v175
	v_cvt_pk_fp8_f32 v26, v22, v23
	v_cvt_pk_fp8_f32 v27, v18, v19
	v_mov_b32_e32 v165, v175
	v_cvt_pk_fp8_f32 v165, v30, v31
	v_cvt_pk_fp8_f32 v26, v24, v25 op_sel:[0,0,1]
	v_cvt_pk_fp8_f32 v27, v20, v21 op_sel:[0,0,1]
	v_ashrrev_i32_e32 v195, 31, v194
	v_lshlrev_b64 v[162:163], 9, v[194:195]
	v_cvt_pk_fp8_f32 v164, v28, v29 op_sel:[0,0,1]
	v_cvt_pk_fp8_f32 v165, v32, v33 op_sel:[0,0,1]
	v_lshl_add_u64 v[162:163], v[190:191], 0, v[162:163]
	global_store_dwordx2 v[162:163], v[26:27], off offset:32
	v_mov_b64_e32 v[18:19], v[114:115]
	v_mov_b64_e32 v[22:23], v[118:119]
	v_mov_b64_e32 v[30:31], v[122:123]
	v_mov_b64_e32 v[26:27], v[126:127]
	s_and_b64 vcc, exec, s[6:7]
	v_mov_b64_e32 v[20:21], v[116:117]
	v_mov_b64_e32 v[24:25], v[120:121]
	v_mov_b64_e32 v[32:33], v[124:125]
	v_mov_b64_e32 v[28:29], v[128:129]
	global_store_dwordx2 v[162:163], v[164:165], off
	s_cbranch_vccnz .LBB0_212
	v_pk_mul_f32 v[18:19], v[128:129], v[128:129]
	v_pk_mul_f32 v[20:21], v[126:127], v[126:127]
	s_nop 0
	v_pk_mov_b32 v[22:23], v[20:21], v[18:19] op_sel:[1,0]
	v_mov_b32_e32 v21, v19
	v_pk_add_f32 v[18:19], v[22:23], v[20:21]
	v_pk_mul_f32 v[20:21], v[124:125], v[124:125]
	v_pk_mul_f32 v[22:23], v[122:123], v[122:123]
	v_pk_add_f32 v[18:19], v[18:19], v[18:19] op_sel:[0,1] op_sel_hi:[1,0]
	v_pk_mov_b32 v[24:25], v[22:23], v[20:21] op_sel:[1,0]
	v_mov_b32_e32 v23, v21
	v_pk_add_f32 v[20:21], v[24:25], v[22:23]
	v_mul_f32_e32 v22, v114, v114
	v_mul_f32_e32 v23, v115, v115
	v_pk_add_f32 v[20:21], v[20:21], v[20:21] op_sel:[0,1] op_sel_hi:[1,0]
	v_mov_b32_e32 v19, v22
	v_mov_b32_e32 v21, v23
	v_pk_add_f32 v[18:19], v[18:19], v[20:21]
	v_mul_f32_e32 v20, v119, v119
	v_mul_f32_e32 v22, v121, v121
	v_mul_f32_e32 v24, v116, v116
	v_mul_f32_e32 v25, v117, v117
	v_pk_fma_f32 v[20:21], v[118:119], v[118:119], v[20:21] op_sel_hi:[1,1,0]
	v_pk_fma_f32 v[22:23], v[120:121], v[120:121], v[22:23] op_sel_hi:[1,1,0]
	v_mov_b32_e32 v21, v24
	v_mov_b32_e32 v23, v25
	v_pk_add_f32 v[20:21], v[20:21], v[22:23]
	s_nop 0
	v_pk_add_f32 v[18:19], v[18:19], v[20:21]
	v_and_b32_e32 v20, 64, v212
	v_add_f32_e32 v18, v18, v19
	v_xor_b32_e32 v19, 16, v212
	v_add_u32_e32 v20, 64, v20
	v_cmp_lt_i32_e32 vcc, v19, v20
	s_nop 1
	v_cndmask_b32_e32 v19, v212, v19, vcc
	v_lshlrev_b32_e32 v19, 2, v19
	v_mov_b32_e32 v19, v18
	s_nop 1
	v_permlane16_swap_b32_e32 v18, v19
	s_waitcnt lgkmcnt(0)
	v_add_f32_e32 v18, v18, v19
	v_xor_b32_e32 v19, 32, v212
	v_cmp_lt_i32_e32 vcc, v19, v20
	s_nop 1
	v_cndmask_b32_e32 v19, v212, v19, vcc
	v_lshlrev_b32_e32 v19, 2, v19
	v_mov_b32_e32 v19, v18
	s_nop 1
	v_permlane32_swap_b32_e32 v18, v19
	s_waitcnt lgkmcnt(0)
	v_add_f32_e32 v18, v18, v19
	v_fmamk_f32 v18, v18, 0x3c800000, v210
	v_mul_f32_e32 v19, 0x4f800000, v18
	v_cmp_gt_f32_e32 vcc, s28, v18
	s_nop 1
	v_cndmask_b32_e32 v18, v18, v19, vcc
	v_sqrt_f32_e32 v19, v18
	s_nop 0
	v_add_u32_e32 v20, -1, v19
	v_fma_f32 v21, -v20, v19, v18
	v_cmp_ge_f32_e64 s[10:11], 0, v21
	v_add_u32_e32 v21, 1, v19
	s_nop 0
	v_cndmask_b32_e64 v20, v19, v20, s[10:11]
	v_fma_f32 v19, -v21, v19, v18
	v_cmp_lt_f32_e64 s[10:11], 0, v19
	s_nop 1
	v_cndmask_b32_e64 v19, v20, v21, s[10:11]
	v_mul_f32_e32 v20, 0x37800000, v19
	v_cndmask_b32_e32 v19, v19, v20, vcc
	v_cmp_class_f32_e32 vcc, v18, v211
	s_nop 1
	v_cndmask_b32_e32 v18, v19, v18, vcc
	v_div_scale_f32 v19, s[0:1], v18, v18, s29
	v_rcp_f32_e32 v20, v19
	s_nop 0
	v_fma_f32 v21, -v19, v20, 1.0
	v_fmac_f32_e32 v20, v21, v20
	v_div_scale_f32 v21, vcc, s29, v18, s29
	v_mul_f32_e32 v22, v21, v20
	v_fma_f32 v23, -v19, v22, v21
	v_fmac_f32_e32 v22, v23, v20
	v_fma_f32 v19, -v19, v22, v21
	v_div_fmas_f32 v19, v19, v20, v22
	v_div_fixup_f32 v18, v19, v18, s29
	v_pk_mul_f32 v[20:21], v[126:127], v[18:19] op_sel_hi:[1,0]
	v_pk_mul_f32 v[22:23], v[128:129], v[18:19] op_sel_hi:[1,0]
	s_waitcnt vmcnt(0)
	v_pk_mul_f32 v[26:27], v[14:15], v[20:21]
	v_pk_mul_f32 v[28:29], v[16:17], v[22:23]
	v_pk_mul_f32 v[20:21], v[122:123], v[18:19] op_sel_hi:[1,0]
	v_pk_mul_f32 v[22:23], v[124:125], v[18:19] op_sel_hi:[1,0]
	v_pk_mul_f32 v[30:31], v[10:11], v[20:21]
	v_pk_mul_f32 v[32:33], v[12:13], v[22:23]
	v_pk_mul_f32 v[20:21], v[118:119], v[18:19] op_sel_hi:[1,0]
	v_pk_mul_f32 v[22:23], v[120:121], v[18:19] op_sel_hi:[1,0]
	v_pk_mul_f32 v[162:163], v[114:115], v[18:19] op_sel_hi:[1,0]
	v_pk_mul_f32 v[18:19], v[116:117], v[18:19] op_sel_hi:[1,0]
	v_pk_mul_f32 v[24:25], v[8:9], v[22:23]
	v_pk_mul_f32 v[22:23], v[6:7], v[20:21]
	v_pk_mul_f32 v[20:21], v[4:5], v[18:19]
	v_pk_mul_f32 v[18:19], v[2:3], v[162:163]

; __device__ __forceinline__ unsigned pk4_fp8(float a, float b, float c, float d) { unsigned w = 0u; w = __builtin_amdgcn_cvt_pk_fp8_f32(a, b, w, false); w = __builtin_amdgcn_cvt_pk_fp8_f32(c, d, w, true); return w; }
; template <bool F8OUT = false> __device__ __forceinline__ void head_tile_store(const f32x4 (&acc)[2][2][4][2], bf16_t* obase  , int opitch, const float* gain, float scale, const f32x2e* rope, int row0, int fq) {
;     ...
;             if (gain) {
;                 float ss = 0.f;
; #pragma unroll
;                 for (int bj = 0; bj < 2; ++bj)
; #pragma unroll
;                     for (int n = 0; n < 2; ++n) ss += (x[bj][n][0] * x[bj][n][0] + x[bj][n][1] * x[bj][n][1]) + (x[bj][n][2] * x[bj][n][2] + x[bj][n][3] * x[bj][n][3]);
;                 ss += __shfl_xor(ss, 16); ss += __shfl_xor(ss, 32);
;                 const float r = scale / sqrtf(ss * (1.f / 64.f) + 1e-6f);
; #pragma unroll
;                 for (int bj = 0; bj < 2; ++bj)
; #pragma unroll
;                     for (int n = 0; n < 2; ++n) x[bj][n] = x[bj][n] * r * g[bj][n];
;     ...
;             if constexpr (F8OUT) { unsigned char* rowp8 = (unsigned char*)obase + (size_t)row * opitch + 8 * fq; typedef unsigned u32x2_ __attribute__((ext_vector_type(2)));
; #pragma unroll
;                 for (int bj = 0; bj < 2; ++bj) *(u32x2_*)(rowp8 + 32 * bj) = (u32x2_){pk4_fp8(x[bj][0][0], x[bj][0][1], x[bj][0][2], x[bj][0][3]), pk4_fp8(x[bj][1][0], x[bj][1][1], x[bj][1][2], x[bj][1][3])};
.LBB0_214:
	v_mov_b32_e32 v164, v175
	v_cvt_pk_fp8_f32 v164, v26, v27
	v_mov_b32_e32 v26, v175
	v_mov_b32_e32 v27, v175
	v_cvt_pk_fp8_f32 v26, v22, v23
	v_cvt_pk_fp8_f32 v27, v18, v19
	v_mov_b32_e32 v165, v175
	v_cvt_pk_fp8_f32 v165, v30, v31
	v_cvt_pk_fp8_f32 v26, v24, v25 op_sel:[0,0,1]
	v_cvt_pk_fp8_f32 v27, v20, v21 op_sel:[0,0,1]
	v_ashrrev_i32_e32 v197, 31, v196
	v_lshlrev_b64 v[162:163], 9, v[196:197]
	v_cvt_pk_fp8_f32 v164, v28, v29 op_sel:[0,0,1]
	v_cvt_pk_fp8_f32 v165, v32, v33 op_sel:[0,0,1]
	v_lshl_add_u64 v[162:163], v[190:191], 0, v[162:163]
	global_store_dwordx2 v[162:163], v[26:27], off offset:32
	v_mov_b64_e32 v[18:19], v[98:99]
	v_mov_b64_e32 v[22:23], v[102:103]
	v_mov_b64_e32 v[30:31], v[106:107]
	v_mov_b64_e32 v[26:27], v[110:111]
	s_and_b64 vcc, exec, s[6:7]
	v_mov_b64_e32 v[20:21], v[100:101]
	v_mov_b64_e32 v[24:25], v[104:105]
	v_mov_b64_e32 v[32:33], v[108:109]
	v_mov_b64_e32 v[28:29], v[112:113]
	global_store_dwordx2 v[162:163], v[164:165], off
	s_cbranch_vccnz .LBB0_216
	v_pk_mul_f32 v[18:19], v[112:113], v[112:113]
	v_pk_mul_f32 v[20:21], v[110:111], v[110:111]
	s_nop 0
	v_pk_mov_b32 v[22:23], v[20:21], v[18:19] op_sel:[1,0]
	v_mov_b32_e32 v21, v19
	v_pk_add_f32 v[18:19], v[22:23], v[20:21]
	v_pk_mul_f32 v[20:21], v[108:109], v[108:109]
	v_pk_mul_f32 v[22:23], v[106:107], v[106:107]
	v_pk_add_f32 v[18:19], v[18:19], v[18:19] op_sel:[0,1] op_sel_hi:[1,0]
	v_pk_mov_b32 v[24:25], v[22:23], v[20:21] op_sel:[1,0]
	v_mov_b32_e32 v23, v21
	v_pk_add_f32 v[20:21], v[24:25], v[22:23]
	v_mul_f32_e32 v22, v98, v98
	v_mul_f32_e32 v23, v99, v99
	v_pk_add_f32 v[20:21], v[20:21], v[20:21] op_sel:[0,1] op_sel_hi:[1,0]
	v_mov_b32_e32 v19, v22
	v_mov_b32_e32 v21, v23
	v_pk_add_f32 v[18:19], v[18:19], v[20:21]
	v_mul_f32_e32 v20, v103, v103
	v_mul_f32_e32 v22, v105, v105
	v_mul_f32_e32 v24, v100, v100
	v_mul_f32_e32 v25, v101, v101
	v_pk_fma_f32 v[20:21], v[102:103], v[102:103], v[20:21] op_sel_hi:[1,1,0]
	v_pk_fma_f32 v[22:23], v[104:105], v[104:105], v[22:23] op_sel_hi:[1,1,0]
	v_mov_b32_e32 v21, v24
	v_mov_b32_e32 v23, v25
	v_pk_add_f32 v[20:21], v[20:21], v[22:23]
	s_nop 0
	v_pk_add_f32 v[18:19], v[18:19], v[20:21]
	v_and_b32_e32 v20, 64, v212
	v_add_f32_e32 v18, v18, v19
	v_xor_b32_e32 v19, 16, v212
	v_add_u32_e32 v20, 64, v20
	v_cmp_lt_i32_e32 vcc, v19, v20
	s_nop 1
	v_cndmask_b32_e32 v19, v212, v19, vcc
	v_lshlrev_b32_e32 v19, 2, v19
	v_mov_b32_e32 v19, v18
	s_nop 1
	v_permlane16_swap_b32_e32 v18, v19
	s_waitcnt lgkmcnt(0)
	v_add_f32_e32 v18, v18, v19
	v_xor_b32_e32 v19, 32, v212
	v_cmp_lt_i32_e32 vcc, v19, v20
	s_nop 1
	v_cndmask_b32_e32 v19, v212, v19, vcc
	v_lshlrev_b32_e32 v19, 2, v19
	v_mov_b32_e32 v19, v18
	s_nop 1
	v_permlane32_swap_b32_e32 v18, v19
	s_waitcnt lgkmcnt(0)
	v_add_f32_e32 v18, v18, v19
	v_fmamk_f32 v18, v18, 0x3c800000, v210
	v_mul_f32_e32 v19, 0x4f800000, v18
	v_cmp_gt_f32_e32 vcc, s28, v18
	s_nop 1
	v_cndmask_b32_e32 v18, v18, v19, vcc
	v_sqrt_f32_e32 v19, v18
	s_nop 0
	v_add_u32_e32 v20, -1, v19
	v_fma_f32 v21, -v20, v19, v18
	v_cmp_ge_f32_e64 s[10:11], 0, v21
	v_add_u32_e32 v21, 1, v19
	s_nop 0
	v_cndmask_b32_e64 v20, v19, v20, s[10:11]
	v_fma_f32 v19, -v21, v19, v18
	v_cmp_lt_f32_e64 s[10:11], 0, v19
	s_nop 1
	v_cndmask_b32_e64 v19, v20, v21, s[10:11]
	v_mul_f32_e32 v20, 0x37800000, v19
	v_cndmask_b32_e32 v19, v19, v20, vcc
	v_cmp_class_f32_e32 vcc, v18, v211
	s_nop 1
	v_cndmask_b32_e32 v18, v19, v18, vcc
	v_div_scale_f32 v19, s[0:1], v18, v18, s29
	v_rcp_f32_e32 v20, v19
	s_nop 0
	v_fma_f32 v21, -v19, v20, 1.0
	v_fmac_f32_e32 v20, v21, v20
	v_div_scale_f32 v21, vcc, s29, v18, s29
	v_mul_f32_e32 v22, v21, v20
	v_fma_f32 v23, -v19, v22, v21
	v_fmac_f32_e32 v22, v23, v20
	v_fma_f32 v19, -v19, v22, v21
	v_div_fmas_f32 v19, v19, v20, v22
	v_div_fixup_f32 v18, v19, v18, s29
	v_pk_mul_f32 v[20:21], v[110:111], v[18:19] op_sel_hi:[1,0]
	v_pk_mul_f32 v[22:23], v[112:113], v[18:19] op_sel_hi:[1,0]
	s_waitcnt vmcnt(0)
	v_pk_mul_f32 v[26:27], v[14:15], v[20:21]
	v_pk_mul_f32 v[28:29], v[16:17], v[22:23]
	v_pk_mul_f32 v[20:21], v[106:107], v[18:19] op_sel_hi:[1,0]
	v_pk_mul_f32 v[22:23], v[108:109], v[18:19] op_sel_hi:[1,0]
	v_pk_mul_f32 v[30:31], v[10:11], v[20:21]
	v_pk_mul_f32 v[32:33], v[12:13], v[22:23]
	v_pk_mul_f32 v[20:21], v[102:103], v[18:19] op_sel_hi:[1,0]
	v_pk_mul_f32 v[22:23], v[104:105], v[18:19] op_sel_hi:[1,0]
	v_pk_mul_f32 v[162:163], v[98:99], v[18:19] op_sel_hi:[1,0]
	v_pk_mul_f32 v[18:19], v[100:101], v[18:19] op_sel_hi:[1,0]
	v_pk_mul_f32 v[24:25], v[8:9], v[22:23]
	v_pk_mul_f32 v[22:23], v[6:7], v[20:21]
	v_pk_mul_f32 v[20:21], v[4:5], v[18:19]
	v_pk_mul_f32 v[18:19], v[2:3], v[162:163]

; __device__ __forceinline__ unsigned pk4_fp8(float a, float b, float c, float d) { unsigned w = 0u; w = __builtin_amdgcn_cvt_pk_fp8_f32(a, b, w, false); w = __builtin_amdgcn_cvt_pk_fp8_f32(c, d, w, true); return w; }
; template <bool F8OUT = false> __device__ __forceinline__ void head_tile_store(const f32x4 (&acc)[2][2][4][2], bf16_t* obase  , int opitch, const float* gain, float scale, const f32x2e* rope, int row0, int fq) {
;     ...
;             if (gain) {
;                 float ss = 0.f;
; #pragma unroll
;                 for (int bj = 0; bj < 2; ++bj)
; #pragma unroll
;                     for (int n = 0; n < 2; ++n) ss += (x[bj][n][0] * x[bj][n][0] + x[bj][n][1] * x[bj][n][1]) + (x[bj][n][2] * x[bj][n][2] + x[bj][n][3] * x[bj][n][3]);
;                 ss += __shfl_xor(ss, 16); ss += __shfl_xor(ss, 32);
;                 const float r = scale / sqrtf(ss * (1.f / 64.f) + 1e-6f);
; #pragma unroll
;                 for (int bj = 0; bj < 2; ++bj)
; #pragma unroll
;                     for (int n = 0; n < 2; ++n) x[bj][n] = x[bj][n] * r * g[bj][n];
;     ...
;             if constexpr (F8OUT) { unsigned char* rowp8 = (unsigned char*)obase + (size_t)row * opitch + 8 * fq; typedef unsigned u32x2_ __attribute__((ext_vector_type(2)));
; #pragma unroll
;                 for (int bj = 0; bj < 2; ++bj) *(u32x2_*)(rowp8 + 32 * bj) = (u32x2_){pk4_fp8(x[bj][0][0], x[bj][0][1], x[bj][0][2], x[bj][0][3]), pk4_fp8(x[bj][1][0], x[bj][1][1], x[bj][1][2], x[bj][1][3])};
.LBB0_218:
	v_mov_b32_e32 v164, v175
	v_cvt_pk_fp8_f32 v164, v26, v27
	v_mov_b32_e32 v26, v175
	v_mov_b32_e32 v27, v175
	v_cvt_pk_fp8_f32 v26, v22, v23
	v_cvt_pk_fp8_f32 v27, v18, v19
	v_mov_b32_e32 v165, v175
	v_cvt_pk_fp8_f32 v165, v30, v31
	v_cvt_pk_fp8_f32 v26, v24, v25 op_sel:[0,0,1]
	v_cvt_pk_fp8_f32 v27, v20, v21 op_sel:[0,0,1]
	v_ashrrev_i32_e32 v201, 31, v200
	v_lshlrev_b64 v[162:163], 9, v[200:201]
	v_cvt_pk_fp8_f32 v164, v28, v29 op_sel:[0,0,1]
	v_cvt_pk_fp8_f32 v165, v32, v33 op_sel:[0,0,1]
	v_lshl_add_u64 v[162:163], v[190:191], 0, v[162:163]
	global_store_dwordx2 v[162:163], v[26:27], off offset:32
	v_mov_b64_e32 v[18:19], v[82:83]
	v_mov_b64_e32 v[22:23], v[86:87]
	v_mov_b64_e32 v[30:31], v[90:91]
	v_mov_b64_e32 v[26:27], v[94:95]
	s_and_b64 vcc, exec, s[6:7]
	v_mov_b64_e32 v[20:21], v[84:85]
	v_mov_b64_e32 v[24:25], v[88:89]
	v_mov_b64_e32 v[32:33], v[92:93]
	v_mov_b64_e32 v[28:29], v[96:97]
	global_store_dwordx2 v[162:163], v[164:165], off
	s_cbranch_vccnz .LBB0_220
	v_pk_mul_f32 v[18:19], v[96:97], v[96:97]
	v_pk_mul_f32 v[20:21], v[94:95], v[94:95]
	s_nop 0
	v_pk_mov_b32 v[22:23], v[20:21], v[18:19] op_sel:[1,0]
	v_mov_b32_e32 v21, v19
	v_pk_add_f32 v[18:19], v[22:23], v[20:21]
	v_pk_mul_f32 v[20:21], v[92:93], v[92:93]
	v_pk_mul_f32 v[22:23], v[90:91], v[90:91]
	v_pk_add_f32 v[18:19], v[18:19], v[18:19] op_sel:[0,1] op_sel_hi:[1,0]
	v_pk_mov_b32 v[24:25], v[22:23], v[20:21] op_sel:[1,0]
	v_mov_b32_e32 v23, v21
	v_pk_add_f32 v[20:21], v[24:25], v[22:23]
	v_mul_f32_e32 v22, v82, v82
	v_mul_f32_e32 v23, v83, v83
	v_pk_add_f32 v[20:21], v[20:21], v[20:21] op_sel:[0,1] op_sel_hi:[1,0]
	v_mov_b32_e32 v19, v22
	v_mov_b32_e32 v21, v23
	v_pk_add_f32 v[18:19], v[18:19], v[20:21]
	v_mul_f32_e32 v20, v87, v87
	v_mul_f32_e32 v22, v89, v89
	v_mul_f32_e32 v24, v84, v84
	v_mul_f32_e32 v25, v85, v85
	v_pk_fma_f32 v[20:21], v[86:87], v[86:87], v[20:21] op_sel_hi:[1,1,0]
	v_pk_fma_f32 v[22:23], v[88:89], v[88:89], v[22:23] op_sel_hi:[1,1,0]
	v_mov_b32_e32 v21, v24
	v_mov_b32_e32 v23, v25
	v_pk_add_f32 v[20:21], v[20:21], v[22:23]
	s_nop 0
	v_pk_add_f32 v[18:19], v[18:19], v[20:21]
	v_and_b32_e32 v20, 64, v212
	v_add_f32_e32 v18, v18, v19
	v_xor_b32_e32 v19, 16, v212
	v_add_u32_e32 v20, 64, v20
	v_cmp_lt_i32_e32 vcc, v19, v20
	s_nop 1
	v_cndmask_b32_e32 v19, v212, v19, vcc
	v_lshlrev_b32_e32 v19, 2, v19
	v_mov_b32_e32 v19, v18
	s_nop 1
	v_permlane16_swap_b32_e32 v18, v19
	s_waitcnt lgkmcnt(0)
	v_add_f32_e32 v18, v18, v19
	v_xor_b32_e32 v19, 32, v212
	v_cmp_lt_i32_e32 vcc, v19, v20
	s_nop 1
	v_cndmask_b32_e32 v19, v212, v19, vcc
	v_lshlrev_b32_e32 v19, 2, v19
	v_mov_b32_e32 v19, v18
	s_nop 1
	v_permlane32_swap_b32_e32 v18, v19
	s_waitcnt lgkmcnt(0)
	v_add_f32_e32 v18, v18, v19
	v_fmamk_f32 v18, v18, 0x3c800000, v210
	v_mul_f32_e32 v19, 0x4f800000, v18
	v_cmp_gt_f32_e32 vcc, s28, v18
	s_nop 1
	v_cndmask_b32_e32 v18, v18, v19, vcc
	v_sqrt_f32_e32 v19, v18
	s_nop 0
	v_add_u32_e32 v20, -1, v19
	v_fma_f32 v21, -v20, v19, v18
	v_cmp_ge_f32_e64 s[10:11], 0, v21
	v_add_u32_e32 v21, 1, v19
	s_nop 0
	v_cndmask_b32_e64 v20, v19, v20, s[10:11]
	v_fma_f32 v19, -v21, v19, v18
	v_cmp_lt_f32_e64 s[10:11], 0, v19
	s_nop 1
	v_cndmask_b32_e64 v19, v20, v21, s[10:11]
	v_mul_f32_e32 v20, 0x37800000, v19
	v_cndmask_b32_e32 v19, v19, v20, vcc
	v_cmp_class_f32_e32 vcc, v18, v211
	s_nop 1
	v_cndmask_b32_e32 v18, v19, v18, vcc
	v_div_scale_f32 v19, s[0:1], v18, v18, s29
	v_rcp_f32_e32 v20, v19
	s_nop 0
	v_fma_f32 v21, -v19, v20, 1.0
	v_fmac_f32_e32 v20, v21, v20
	v_div_scale_f32 v21, vcc, s29, v18, s29
	v_mul_f32_e32 v22, v21, v20
	v_fma_f32 v23, -v19, v22, v21
	v_fmac_f32_e32 v22, v23, v20
	v_fma_f32 v19, -v19, v22, v21
	v_div_fmas_f32 v19, v19, v20, v22
	v_div_fixup_f32 v18, v19, v18, s29
	v_pk_mul_f32 v[20:21], v[94:95], v[18:19] op_sel_hi:[1,0]
	v_pk_mul_f32 v[22:23], v[96:97], v[18:19] op_sel_hi:[1,0]
	s_waitcnt vmcnt(0)
	v_pk_mul_f32 v[26:27], v[14:15], v[20:21]
	v_pk_mul_f32 v[28:29], v[16:17], v[22:23]
	v_pk_mul_f32 v[20:21], v[90:91], v[18:19] op_sel_hi:[1,0]
	v_pk_mul_f32 v[22:23], v[92:93], v[18:19] op_sel_hi:[1,0]
	v_pk_mul_f32 v[30:31], v[10:11], v[20:21]
	v_pk_mul_f32 v[32:33], v[12:13], v[22:23]
	v_pk_mul_f32 v[20:21], v[86:87], v[18:19] op_sel_hi:[1,0]
	v_pk_mul_f32 v[22:23], v[88:89], v[18:19] op_sel_hi:[1,0]
	v_pk_mul_f32 v[162:163], v[82:83], v[18:19] op_sel_hi:[1,0]
	v_pk_mul_f32 v[18:19], v[84:85], v[18:19] op_sel_hi:[1,0]
	v_pk_mul_f32 v[24:25], v[8:9], v[22:23]
	v_pk_mul_f32 v[22:23], v[6:7], v[20:21]
	v_pk_mul_f32 v[20:21], v[4:5], v[18:19]
	v_pk_mul_f32 v[18:19], v[2:3], v[162:163]

; __device__ __forceinline__ unsigned pk4_fp8(float a, float b, float c, float d) { unsigned w = 0u; w = __builtin_amdgcn_cvt_pk_fp8_f32(a, b, w, false); w = __builtin_amdgcn_cvt_pk_fp8_f32(c, d, w, true); return w; }
; template <bool F8OUT = false> __device__ __forceinline__ void head_tile_store(const f32x4 (&acc)[2][2][4][2], bf16_t* obase  , int opitch, const float* gain, float scale, const f32x2e* rope, int row0, int fq) {
;     ...
;             if (gain) {
;                 float ss = 0.f;
; #pragma unroll
;                 for (int bj = 0; bj < 2; ++bj)
; #pragma unroll
;                     for (int n = 0; n < 2; ++n) ss += (x[bj][n][0] * x[bj][n][0] + x[bj][n][1] * x[bj][n][1]) + (x[bj][n][2] * x[bj][n][2] + x[bj][n][3] * x[bj][n][3]);
;                 ss += __shfl_xor(ss, 16); ss += __shfl_xor(ss, 32);
;                 const float r = scale / sqrtf(ss * (1.f / 64.f) + 1e-6f);
; #pragma unroll
;                 for (int bj = 0; bj < 2; ++bj)
; #pragma unroll
;                     for (int n = 0; n < 2; ++n) x[bj][n] = x[bj][n] * r * g[bj][n];
;     ...
;             if constexpr (F8OUT) { unsigned char* rowp8 = (unsigned char*)obase + (size_t)row * opitch + 8 * fq; typedef unsigned u32x2_ __attribute__((ext_vector_type(2)));
; #pragma unroll
;                 for (int bj = 0; bj < 2; ++bj) *(u32x2_*)(rowp8 + 32 * bj) = (u32x2_){pk4_fp8(x[bj][0][0], x[bj][0][1], x[bj][0][2], x[bj][0][3]), pk4_fp8(x[bj][1][0], x[bj][1][1], x[bj][1][2], x[bj][1][3])};
.LBB0_222:
	v_mov_b32_e32 v164, v175
	v_cvt_pk_fp8_f32 v164, v26, v27
	v_mov_b32_e32 v26, v175
	v_mov_b32_e32 v27, v175
	v_cvt_pk_fp8_f32 v26, v22, v23
	v_cvt_pk_fp8_f32 v27, v18, v19
	v_mov_b32_e32 v165, v175
	v_cvt_pk_fp8_f32 v165, v30, v31
	v_cvt_pk_fp8_f32 v26, v24, v25 op_sel:[0,0,1]
	v_cvt_pk_fp8_f32 v27, v20, v21 op_sel:[0,0,1]
	v_ashrrev_i32_e32 v201, 31, v200
	v_lshlrev_b64 v[162:163], 9, v[200:201]
	v_cvt_pk_fp8_f32 v164, v28, v29 op_sel:[0,0,1]
	v_cvt_pk_fp8_f32 v165, v32, v33 op_sel:[0,0,1]
	v_lshl_add_u64 v[162:163], v[190:191], 0, v[162:163]
	global_store_dwordx2 v[162:163], v[26:27], off offset:32
	v_mov_b64_e32 v[18:19], v[66:67]
	v_mov_b64_e32 v[22:23], v[70:71]
	v_mov_b64_e32 v[30:31], v[74:75]
	v_mov_b64_e32 v[26:27], v[78:79]
	s_and_b64 vcc, exec, s[6:7]
	v_mov_b64_e32 v[20:21], v[68:69]
	v_mov_b64_e32 v[24:25], v[72:73]
	v_mov_b64_e32 v[32:33], v[76:77]
	v_mov_b64_e32 v[28:29], v[80:81]
	global_store_dwordx2 v[162:163], v[164:165], off
	s_cbranch_vccnz .LBB0_224
	v_pk_mul_f32 v[18:19], v[80:81], v[80:81]
	v_pk_mul_f32 v[20:21], v[78:79], v[78:79]
	s_nop 0
	v_pk_mov_b32 v[22:23], v[20:21], v[18:19] op_sel:[1,0]
	v_mov_b32_e32 v21, v19
	v_pk_add_f32 v[18:19], v[22:23], v[20:21]
	v_pk_mul_f32 v[20:21], v[76:77], v[76:77]
	v_pk_mul_f32 v[22:23], v[74:75], v[74:75]
	v_pk_add_f32 v[18:19], v[18:19], v[18:19] op_sel:[0,1] op_sel_hi:[1,0]
	v_pk_mov_b32 v[24:25], v[22:23], v[20:21] op_sel:[1,0]
	v_mov_b32_e32 v23, v21
	v_pk_add_f32 v[20:21], v[24:25], v[22:23]
	v_mul_f32_e32 v22, v66, v66
	v_mul_f32_e32 v23, v67, v67
	v_pk_add_f32 v[20:21], v[20:21], v[20:21] op_sel:[0,1] op_sel_hi:[1,0]
	v_mov_b32_e32 v19, v22
	v_mov_b32_e32 v21, v23
	v_pk_add_f32 v[18:19], v[18:19], v[20:21]
	v_mul_f32_e32 v20, v71, v71
	v_mul_f32_e32 v22, v73, v73
	v_mul_f32_e32 v24, v68, v68
	v_mul_f32_e32 v25, v69, v69
	v_pk_fma_f32 v[20:21], v[70:71], v[70:71], v[20:21] op_sel_hi:[1,1,0]
	v_pk_fma_f32 v[22:23], v[72:73], v[72:73], v[22:23] op_sel_hi:[1,1,0]
	v_mov_b32_e32 v21, v24
	v_mov_b32_e32 v23, v25
	v_pk_add_f32 v[20:21], v[20:21], v[22:23]
	s_nop 0
	v_pk_add_f32 v[18:19], v[18:19], v[20:21]
	v_and_b32_e32 v20, 64, v212
	v_add_f32_e32 v18, v18, v19
	v_xor_b32_e32 v19, 16, v212
	v_add_u32_e32 v20, 64, v20
	v_cmp_lt_i32_e32 vcc, v19, v20
	s_nop 1
	v_cndmask_b32_e32 v19, v212, v19, vcc
	v_lshlrev_b32_e32 v19, 2, v19
	v_mov_b32_e32 v19, v18
	s_nop 1
	v_permlane16_swap_b32_e32 v18, v19
	s_waitcnt lgkmcnt(0)
	v_add_f32_e32 v18, v18, v19
	v_xor_b32_e32 v19, 32, v212
	v_cmp_lt_i32_e32 vcc, v19, v20
	s_nop 1
	v_cndmask_b32_e32 v19, v212, v19, vcc
	v_lshlrev_b32_e32 v19, 2, v19
	v_mov_b32_e32 v19, v18
	s_nop 1
	v_permlane32_swap_b32_e32 v18, v19
	s_waitcnt lgkmcnt(0)
	v_add_f32_e32 v18, v18, v19
	v_fmamk_f32 v18, v18, 0x3c800000, v210
	v_mul_f32_e32 v19, 0x4f800000, v18
	v_cmp_gt_f32_e32 vcc, s28, v18
	s_nop 1
	v_cndmask_b32_e32 v18, v18, v19, vcc
	v_sqrt_f32_e32 v19, v18
	s_nop 0
	v_add_u32_e32 v20, -1, v19
	v_fma_f32 v21, -v20, v19, v18
	v_cmp_ge_f32_e64 s[10:11], 0, v21
	v_add_u32_e32 v21, 1, v19
	s_nop 0
	v_cndmask_b32_e64 v20, v19, v20, s[10:11]
	v_fma_f32 v19, -v21, v19, v18
	v_cmp_lt_f32_e64 s[10:11], 0, v19
	s_nop 1
	v_cndmask_b32_e64 v19, v20, v21, s[10:11]
	v_mul_f32_e32 v20, 0x37800000, v19
	v_cndmask_b32_e32 v19, v19, v20, vcc
	v_cmp_class_f32_e32 vcc, v18, v211
	s_nop 1
	v_cndmask_b32_e32 v18, v19, v18, vcc
	v_div_scale_f32 v19, s[0:1], v18, v18, s29
	v_rcp_f32_e32 v20, v19
	s_nop 0
	v_fma_f32 v21, -v19, v20, 1.0
	v_fmac_f32_e32 v20, v21, v20
	v_div_scale_f32 v21, vcc, s29, v18, s29
	v_mul_f32_e32 v22, v21, v20
	v_fma_f32 v23, -v19, v22, v21
	v_fmac_f32_e32 v22, v23, v20
	v_fma_f32 v19, -v19, v22, v21
	v_div_fmas_f32 v19, v19, v20, v22
	v_div_fixup_f32 v18, v19, v18, s29
	v_pk_mul_f32 v[20:21], v[78:79], v[18:19] op_sel_hi:[1,0]
	v_pk_mul_f32 v[22:23], v[80:81], v[18:19] op_sel_hi:[1,0]
	s_waitcnt vmcnt(0)
	v_pk_mul_f32 v[26:27], v[14:15], v[20:21]
	v_pk_mul_f32 v[28:29], v[16:17], v[22:23]
	v_pk_mul_f32 v[20:21], v[74:75], v[18:19] op_sel_hi:[1,0]
	v_pk_mul_f32 v[22:23], v[76:77], v[18:19] op_sel_hi:[1,0]
	v_pk_mul_f32 v[30:31], v[10:11], v[20:21]
	v_pk_mul_f32 v[32:33], v[12:13], v[22:23]
	v_pk_mul_f32 v[20:21], v[70:71], v[18:19] op_sel_hi:[1,0]
	v_pk_mul_f32 v[22:23], v[72:73], v[18:19] op_sel_hi:[1,0]
	v_pk_mul_f32 v[162:163], v[66:67], v[18:19] op_sel_hi:[1,0]
	v_pk_mul_f32 v[18:19], v[68:69], v[18:19] op_sel_hi:[1,0]
	v_pk_mul_f32 v[24:25], v[8:9], v[22:23]
	v_pk_mul_f32 v[22:23], v[6:7], v[20:21]
	v_pk_mul_f32 v[20:21], v[4:5], v[18:19]
	v_pk_mul_f32 v[18:19], v[2:3], v[162:163]

; __device__ __forceinline__ unsigned pk4_fp8(float a, float b, float c, float d) { unsigned w = 0u; w = __builtin_amdgcn_cvt_pk_fp8_f32(a, b, w, false); w = __builtin_amdgcn_cvt_pk_fp8_f32(c, d, w, true); return w; }
; template <bool F8OUT = false> __device__ __forceinline__ void head_tile_store(const f32x4 (&acc)[2][2][4][2], bf16_t* obase  , int opitch, const float* gain, float scale, const f32x2e* rope, int row0, int fq) {
;     ...
;             if (gain) {
;                 float ss = 0.f;
; #pragma unroll
;                 for (int bj = 0; bj < 2; ++bj)
; #pragma unroll
;                     for (int n = 0; n < 2; ++n) ss += (x[bj][n][0] * x[bj][n][0] + x[bj][n][1] * x[bj][n][1]) + (x[bj][n][2] * x[bj][n][2] + x[bj][n][3] * x[bj][n][3]);
;                 ss += __shfl_xor(ss, 16); ss += __shfl_xor(ss, 32);
;                 const float r = scale / sqrtf(ss * (1.f / 64.f) + 1e-6f);
; #pragma unroll
;                 for (int bj = 0; bj < 2; ++bj)
; #pragma unroll
;                     for (int n = 0; n < 2; ++n) x[bj][n] = x[bj][n] * r * g[bj][n];
;     ...
;             if constexpr (F8OUT) { unsigned char* rowp8 = (unsigned char*)obase + (size_t)row * opitch + 8 * fq; typedef unsigned u32x2_ __attribute__((ext_vector_type(2)));
; #pragma unroll
;                 for (int bj = 0; bj < 2; ++bj) *(u32x2_*)(rowp8 + 32 * bj) = (u32x2_){pk4_fp8(x[bj][0][0], x[bj][0][1], x[bj][0][2], x[bj][0][3]), pk4_fp8(x[bj][1][0], x[bj][1][1], x[bj][1][2], x[bj][1][3])};
.LBB0_226:
	v_mov_b32_e32 v164, v175
	v_cvt_pk_fp8_f32 v164, v26, v27
	v_mov_b32_e32 v26, v175
	v_mov_b32_e32 v27, v175
	v_cvt_pk_fp8_f32 v26, v22, v23
	v_cvt_pk_fp8_f32 v27, v18, v19
	v_mov_b32_e32 v165, v175
	v_cvt_pk_fp8_f32 v165, v30, v31
	v_cvt_pk_fp8_f32 v26, v24, v25 op_sel:[0,0,1]
	v_cvt_pk_fp8_f32 v27, v20, v21 op_sel:[0,0,1]
	v_ashrrev_i32_e32 v199, 31, v198
	v_lshlrev_b64 v[162:163], 9, v[198:199]
	v_cvt_pk_fp8_f32 v164, v28, v29 op_sel:[0,0,1]
	v_cvt_pk_fp8_f32 v165, v32, v33 op_sel:[0,0,1]
	v_lshl_add_u64 v[162:163], v[190:191], 0, v[162:163]
	global_store_dwordx2 v[162:163], v[26:27], off offset:32
	v_mov_b64_e32 v[18:19], v[50:51]
	v_mov_b64_e32 v[22:23], v[54:55]
	v_mov_b64_e32 v[30:31], v[58:59]
	v_mov_b64_e32 v[26:27], v[62:63]
	s_and_b64 vcc, exec, s[6:7]
	v_mov_b64_e32 v[20:21], v[52:53]
	v_mov_b64_e32 v[24:25], v[56:57]
	v_mov_b64_e32 v[32:33], v[60:61]
	v_mov_b64_e32 v[28:29], v[64:65]
	global_store_dwordx2 v[162:163], v[164:165], off
	s_cbranch_vccnz .LBB0_228
	v_pk_mul_f32 v[18:19], v[64:65], v[64:65]
	v_pk_mul_f32 v[20:21], v[62:63], v[62:63]
	s_nop 0
	v_pk_mov_b32 v[22:23], v[20:21], v[18:19] op_sel:[1,0]
	v_mov_b32_e32 v21, v19
	v_pk_add_f32 v[18:19], v[22:23], v[20:21]
	v_pk_mul_f32 v[20:21], v[60:61], v[60:61]
	v_pk_mul_f32 v[22:23], v[58:59], v[58:59]
	v_pk_add_f32 v[18:19], v[18:19], v[18:19] op_sel:[0,1] op_sel_hi:[1,0]
	v_pk_mov_b32 v[24:25], v[22:23], v[20:21] op_sel:[1,0]
	v_mov_b32_e32 v23, v21
	v_pk_add_f32 v[20:21], v[24:25], v[22:23]
	v_mul_f32_e32 v22, v50, v50
	v_mul_f32_e32 v23, v51, v51
	v_pk_add_f32 v[20:21], v[20:21], v[20:21] op_sel:[0,1] op_sel_hi:[1,0]
	v_mov_b32_e32 v19, v22
	v_mov_b32_e32 v21, v23
	v_pk_add_f32 v[18:19], v[18:19], v[20:21]
	v_mul_f32_e32 v20, v55, v55
	v_mul_f32_e32 v22, v57, v57
	v_mul_f32_e32 v24, v52, v52
	v_mul_f32_e32 v25, v53, v53
	v_pk_fma_f32 v[20:21], v[54:55], v[54:55], v[20:21] op_sel_hi:[1,1,0]
	v_pk_fma_f32 v[22:23], v[56:57], v[56:57], v[22:23] op_sel_hi:[1,1,0]
	v_mov_b32_e32 v21, v24
	v_mov_b32_e32 v23, v25
	v_pk_add_f32 v[20:21], v[20:21], v[22:23]
	s_nop 0
	v_pk_add_f32 v[18:19], v[18:19], v[20:21]
	v_and_b32_e32 v20, 64, v212
	v_add_f32_e32 v18, v18, v19
	v_xor_b32_e32 v19, 16, v212
	v_add_u32_e32 v20, 64, v20
	v_cmp_lt_i32_e32 vcc, v19, v20
	s_nop 1
	v_cndmask_b32_e32 v19, v212, v19, vcc
	v_lshlrev_b32_e32 v19, 2, v19
	v_mov_b32_e32 v19, v18
	s_nop 1
	v_permlane16_swap_b32_e32 v18, v19
	s_waitcnt lgkmcnt(0)
	v_add_f32_e32 v18, v18, v19
	v_xor_b32_e32 v19, 32, v212
	v_cmp_lt_i32_e32 vcc, v19, v20
	s_nop 1
	v_cndmask_b32_e32 v19, v212, v19, vcc
	v_lshlrev_b32_e32 v19, 2, v19
	v_mov_b32_e32 v19, v18
	s_nop 1
	v_permlane32_swap_b32_e32 v18, v19
	s_waitcnt lgkmcnt(0)
	v_add_f32_e32 v18, v18, v19
	v_fmamk_f32 v18, v18, 0x3c800000, v210
	v_mul_f32_e32 v19, 0x4f800000, v18
	v_cmp_gt_f32_e32 vcc, s28, v18
	s_nop 1
	v_cndmask_b32_e32 v18, v18, v19, vcc
	v_sqrt_f32_e32 v19, v18
	s_nop 0
	v_add_u32_e32 v20, -1, v19
	v_fma_f32 v21, -v20, v19, v18
	v_cmp_ge_f32_e64 s[10:11], 0, v21
	v_add_u32_e32 v21, 1, v19
	s_nop 0
	v_cndmask_b32_e64 v20, v19, v20, s[10:11]
	v_fma_f32 v19, -v21, v19, v18
	v_cmp_lt_f32_e64 s[10:11], 0, v19
	s_nop 1
	v_cndmask_b32_e64 v19, v20, v21, s[10:11]
	v_mul_f32_e32 v20, 0x37800000, v19
	v_cndmask_b32_e32 v19, v19, v20, vcc
	v_cmp_class_f32_e32 vcc, v18, v211
	s_nop 1
	v_cndmask_b32_e32 v18, v19, v18, vcc
	v_div_scale_f32 v19, s[0:1], v18, v18, s29
	v_rcp_f32_e32 v20, v19
	s_nop 0
	v_fma_f32 v21, -v19, v20, 1.0
	v_fmac_f32_e32 v20, v21, v20
	v_div_scale_f32 v21, vcc, s29, v18, s29
	v_mul_f32_e32 v22, v21, v20
	v_fma_f32 v23, -v19, v22, v21
	v_fmac_f32_e32 v22, v23, v20
	v_fma_f32 v19, -v19, v22, v21
	v_div_fmas_f32 v19, v19, v20, v22
	v_div_fixup_f32 v18, v19, v18, s29
	v_pk_mul_f32 v[20:21], v[62:63], v[18:19] op_sel_hi:[1,0]
	v_pk_mul_f32 v[22:23], v[64:65], v[18:19] op_sel_hi:[1,0]
	s_waitcnt vmcnt(0)
	v_pk_mul_f32 v[26:27], v[14:15], v[20:21]
	v_pk_mul_f32 v[28:29], v[16:17], v[22:23]
	v_pk_mul_f32 v[20:21], v[58:59], v[18:19] op_sel_hi:[1,0]
	v_pk_mul_f32 v[22:23], v[60:61], v[18:19] op_sel_hi:[1,0]
	v_pk_mul_f32 v[30:31], v[10:11], v[20:21]
	v_pk_mul_f32 v[32:33], v[12:13], v[22:23]
	v_pk_mul_f32 v[20:21], v[54:55], v[18:19] op_sel_hi:[1,0]
	v_pk_mul_f32 v[22:23], v[56:57], v[18:19] op_sel_hi:[1,0]
	v_pk_mul_f32 v[162:163], v[50:51], v[18:19] op_sel_hi:[1,0]
	v_pk_mul_f32 v[18:19], v[52:53], v[18:19] op_sel_hi:[1,0]
	v_pk_mul_f32 v[24:25], v[8:9], v[22:23]
	v_pk_mul_f32 v[22:23], v[6:7], v[20:21]
	v_pk_mul_f32 v[20:21], v[4:5], v[18:19]
	v_pk_mul_f32 v[18:19], v[2:3], v[162:163]

; __device__ __forceinline__ unsigned pk4_fp8(float a, float b, float c, float d) { unsigned w = 0u; w = __builtin_amdgcn_cvt_pk_fp8_f32(a, b, w, false); w = __builtin_amdgcn_cvt_pk_fp8_f32(c, d, w, true); return w; }
; template <bool F8OUT = false> __device__ __forceinline__ void head_tile_store(const f32x4 (&acc)[2][2][4][2], bf16_t* obase  , int opitch, const float* gain, float scale, const f32x2e* rope, int row0, int fq) {
;     ...
;             if (gain) {
;                 float ss = 0.f;
; #pragma unroll
;                 for (int bj = 0; bj < 2; ++bj)
; #pragma unroll
;                     for (int n = 0; n < 2; ++n) ss += (x[bj][n][0] * x[bj][n][0] + x[bj][n][1] * x[bj][n][1]) + (x[bj][n][2] * x[bj][n][2] + x[bj][n][3] * x[bj][n][3]);
;                 ss += __shfl_xor(ss, 16); ss += __shfl_xor(ss, 32);
;                 const float r = scale / sqrtf(ss * (1.f / 64.f) + 1e-6f);
; #pragma unroll
;                 for (int bj = 0; bj < 2; ++bj)
; #pragma unroll
;                     for (int n = 0; n < 2; ++n) x[bj][n] = x[bj][n] * r * g[bj][n];
;     ...
;             if constexpr (F8OUT) { unsigned char* rowp8 = (unsigned char*)obase + (size_t)row * opitch + 8 * fq; typedef unsigned u32x2_ __attribute__((ext_vector_type(2)));
; #pragma unroll
;                 for (int bj = 0; bj < 2; ++bj) *(u32x2_*)(rowp8 + 32 * bj) = (u32x2_){pk4_fp8(x[bj][0][0], x[bj][0][1], x[bj][0][2], x[bj][0][3]), pk4_fp8(x[bj][1][0], x[bj][1][1], x[bj][1][2], x[bj][1][3])};
.LBB0_230:
	v_mov_b32_e32 v164, v175
	v_cvt_pk_fp8_f32 v164, v26, v27
	v_mov_b32_e32 v26, v175
	v_mov_b32_e32 v27, v175
	v_cvt_pk_fp8_f32 v26, v22, v23
	v_cvt_pk_fp8_f32 v27, v18, v19
	v_mov_b32_e32 v165, v175
	v_cvt_pk_fp8_f32 v165, v30, v31
	v_cvt_pk_fp8_f32 v26, v24, v25 op_sel:[0,0,1]
	v_cvt_pk_fp8_f32 v27, v20, v21 op_sel:[0,0,1]
	v_ashrrev_i32_e32 v193, 31, v192
	v_lshlrev_b64 v[162:163], 9, v[192:193]
	v_cvt_pk_fp8_f32 v164, v28, v29 op_sel:[0,0,1]
	v_cvt_pk_fp8_f32 v165, v32, v33 op_sel:[0,0,1]
	v_lshl_add_u64 v[162:163], v[190:191], 0, v[162:163]
	global_store_dwordx2 v[162:163], v[26:27], off offset:32
	v_mov_b64_e32 v[18:19], v[34:35]
	v_mov_b64_e32 v[22:23], v[38:39]
	v_mov_b64_e32 v[30:31], v[42:43]
	v_mov_b64_e32 v[26:27], v[46:47]
	s_and_b64 vcc, exec, s[6:7]
	v_mov_b64_e32 v[20:21], v[36:37]
	v_mov_b64_e32 v[24:25], v[40:41]
	v_mov_b64_e32 v[32:33], v[44:45]
	v_mov_b64_e32 v[28:29], v[48:49]
	global_store_dwordx2 v[162:163], v[164:165], off
	s_cbranch_vccnz .LBB0_232
	v_pk_mul_f32 v[18:19], v[48:49], v[48:49]
	v_pk_mul_f32 v[20:21], v[46:47], v[46:47]
	s_nop 0
	v_pk_mov_b32 v[22:23], v[20:21], v[18:19] op_sel:[1,0]
	v_mov_b32_e32 v21, v19
	v_pk_add_f32 v[18:19], v[22:23], v[20:21]
	v_pk_mul_f32 v[20:21], v[44:45], v[44:45]
	v_pk_mul_f32 v[22:23], v[42:43], v[42:43]
	v_pk_add_f32 v[18:19], v[18:19], v[18:19] op_sel:[0,1] op_sel_hi:[1,0]
	v_pk_mov_b32 v[24:25], v[22:23], v[20:21] op_sel:[1,0]
	v_mov_b32_e32 v23, v21
	v_pk_add_f32 v[20:21], v[24:25], v[22:23]
	v_mul_f32_e32 v22, v34, v34
	v_mul_f32_e32 v23, v35, v35
	v_pk_add_f32 v[20:21], v[20:21], v[20:21] op_sel:[0,1] op_sel_hi:[1,0]
	v_mov_b32_e32 v19, v22
	v_mov_b32_e32 v21, v23
	v_pk_add_f32 v[18:19], v[18:19], v[20:21]
	v_mul_f32_e32 v20, v39, v39
	v_mul_f32_e32 v22, v41, v41
	v_mul_f32_e32 v24, v36, v36
	v_mul_f32_e32 v25, v37, v37
	v_pk_fma_f32 v[20:21], v[38:39], v[38:39], v[20:21] op_sel_hi:[1,1,0]
	v_pk_fma_f32 v[22:23], v[40:41], v[40:41], v[22:23] op_sel_hi:[1,1,0]
	v_mov_b32_e32 v21, v24
	v_mov_b32_e32 v23, v25
	v_pk_add_f32 v[20:21], v[20:21], v[22:23]
	s_nop 0
	v_pk_add_f32 v[18:19], v[18:19], v[20:21]
	v_and_b32_e32 v20, 64, v212
	v_add_f32_e32 v18, v18, v19
	v_xor_b32_e32 v19, 16, v212
	v_add_u32_e32 v20, 64, v20
	v_cmp_lt_i32_e32 vcc, v19, v20
	s_nop 1
	v_cndmask_b32_e32 v19, v212, v19, vcc
	v_lshlrev_b32_e32 v19, 2, v19
	v_mov_b32_e32 v19, v18
	s_nop 1
	v_permlane16_swap_b32_e32 v18, v19
	s_waitcnt lgkmcnt(0)
	v_add_f32_e32 v18, v18, v19
	v_xor_b32_e32 v19, 32, v212
	v_cmp_lt_i32_e32 vcc, v19, v20
	s_nop 1
	v_cndmask_b32_e32 v19, v212, v19, vcc
	v_lshlrev_b32_e32 v19, 2, v19
	v_mov_b32_e32 v19, v18
	s_nop 1
	v_permlane32_swap_b32_e32 v18, v19
	s_waitcnt lgkmcnt(0)
	v_add_f32_e32 v18, v18, v19
	v_fmamk_f32 v18, v18, 0x3c800000, v210
	v_mul_f32_e32 v19, 0x4f800000, v18
	v_cmp_gt_f32_e32 vcc, s28, v18
	s_nop 1
	v_cndmask_b32_e32 v18, v18, v19, vcc
	v_sqrt_f32_e32 v19, v18
	s_nop 0
	v_add_u32_e32 v20, -1, v19
	v_fma_f32 v21, -v20, v19, v18
	v_cmp_ge_f32_e64 s[6:7], 0, v21
	v_add_u32_e32 v21, 1, v19
	s_nop 0
	v_cndmask_b32_e64 v20, v19, v20, s[6:7]
	v_fma_f32 v19, -v21, v19, v18
	v_cmp_lt_f32_e64 s[6:7], 0, v19
	s_nop 1
	v_cndmask_b32_e64 v19, v20, v21, s[6:7]
	v_mul_f32_e32 v20, 0x37800000, v19
	v_cndmask_b32_e32 v19, v19, v20, vcc
	v_cmp_class_f32_e32 vcc, v18, v211
	s_nop 1
	v_cndmask_b32_e32 v18, v19, v18, vcc
	v_div_scale_f32 v19, s[0:1], v18, v18, s29
	v_rcp_f32_e32 v20, v19
	s_nop 0
	v_fma_f32 v21, -v19, v20, 1.0
	v_fmac_f32_e32 v20, v21, v20
	v_div_scale_f32 v21, vcc, s29, v18, s29
	v_mul_f32_e32 v22, v21, v20
	v_fma_f32 v23, -v19, v22, v21
	v_fmac_f32_e32 v22, v23, v20
	v_fma_f32 v19, -v19, v22, v21
	v_div_fmas_f32 v19, v19, v20, v22
	v_div_fixup_f32 v18, v19, v18, s29
	v_pk_mul_f32 v[20:21], v[46:47], v[18:19] op_sel_hi:[1,0]
	v_pk_mul_f32 v[22:23], v[48:49], v[18:19] op_sel_hi:[1,0]
	s_waitcnt vmcnt(0)
	v_pk_mul_f32 v[26:27], v[14:15], v[20:21]
	v_pk_mul_f32 v[28:29], v[16:17], v[22:23]
	v_pk_mul_f32 v[14:15], v[42:43], v[18:19] op_sel_hi:[1,0]
	v_pk_mul_f32 v[16:17], v[44:45], v[18:19] op_sel_hi:[1,0]
	v_pk_mul_f32 v[30:31], v[10:11], v[14:15]
	v_pk_mul_f32 v[32:33], v[12:13], v[16:17]
	v_pk_mul_f32 v[10:11], v[38:39], v[18:19] op_sel_hi:[1,0]
	v_pk_mul_f32 v[12:13], v[40:41], v[18:19] op_sel_hi:[1,0]
	v_pk_mul_f32 v[22:23], v[6:7], v[10:11]
	v_pk_mul_f32 v[24:25], v[8:9], v[12:13]
	v_pk_mul_f32 v[6:7], v[34:35], v[18:19] op_sel_hi:[1,0]
	v_pk_mul_f32 v[8:9], v[36:37], v[18:19] op_sel_hi:[1,0]
	v_pk_mul_f32 v[18:19], v[2:3], v[6:7]
	v_pk_mul_f32 v[20:21], v[4:5], v[8:9]

; __device__ __forceinline__ unsigned cvt_pk_bf16(float lo, float hi) { unsigned r; asm volatile("v_cvt_pk_bf16_f32 %0, %1, %2" : "=v"(r) : "v"(lo), "v"(hi)); return r; }
; template <bool F8OUT = false> __device__ __forceinline__ void head_tile_store(const f32x4 (&acc)[2][2][4][2], bf16_t* obase  , int opitch, const float* gain, float scale, const f32x2e* rope, int row0, int fq) {
;     ...
;             const int row = row0 + ai * HALF + m * 16;
;             f32x4 x[2][2];
; #pragma unroll
;             for (int bj = 0; bj < 2; ++bj)
; #pragma unroll
;                 for (int n = 0; n < 2; ++n) x[bj][n] = acc[ai][bj][m][n];
;             if (gain) {
;                 float ss = 0.f;
; #pragma unroll
;                 for (int bj = 0; bj < 2; ++bj)
; #pragma unroll
;                     for (int n = 0; n < 2; ++n) ss += (x[bj][n][0] * x[bj][n][0] + x[bj][n][1] * x[bj][n][1]) + (x[bj][n][2] * x[bj][n][2] + x[bj][n][3] * x[bj][n][3]);
;                 ss += __shfl_xor(ss, 16); ss += __shfl_xor(ss, 32);
;                 const float r = scale / sqrtf(ss * (1.f / 64.f) + 1e-6f);
; #pragma unroll
;                 for (int bj = 0; bj < 2; ++bj)
; #pragma unroll
;                     for (int n = 0; n < 2; ++n) x[bj][n] = x[bj][n] * r * g[bj][n];
;     ...
;             bf16_t* rowp = obase + (size_t)row * opitch + 8 * fq;
; #pragma unroll
;             for (int bj = 0; bj < 2; ++bj) { u32x4 w; w.x = cvt_pk_bf16(x[bj][0][0], x[bj][0][1]); w.y = cvt_pk_bf16(x[bj][0][2], x[bj][0][3]); w.z = cvt_pk_bf16(x[bj][1][0], x[bj][1][1]); w.w = cvt_pk_bf16(x[bj][1][2], x[bj][1][3]);
;                 *(u32x4*)(rowp + 32 * bj) = w; }
.LBB0_242:
	s_and_b64 vcc, exec, s[4:5]
	v_mov_b32_e32 v27, v149
	v_mov_b32_e32 v26, v148
	v_mov_b32_e32 v163, v147
	v_mov_b32_e32 v162, v146
	v_mov_b32_e32 v25, v153
	v_mov_b32_e32 v24, v152
	v_mov_b32_e32 v29, v151
	v_mov_b32_e32 v28, v150
	v_mov_b32_e32 v33, v157
	v_mov_b32_e32 v32, v156
	v_mov_b32_e32 v187, v155
	v_mov_b32_e32 v186, v154
	v_mov_b32_e32 v31, v161
	v_mov_b32_e32 v30, v160
	v_mov_b32_e32 v165, v159
	v_mov_b32_e32 v164, v158
	s_cbranch_vccnz .LBB0_244
	v_pk_mul_f32 v[22:23], v[160:161], v[160:161]
	v_pk_mul_f32 v[24:25], v[158:159], v[158:159]
	v_mul_f32_e32 v19, v146, v146
	v_pk_mov_b32 v[26:27], v[24:25], v[22:23] op_sel:[1,0]
	v_mov_b32_e32 v25, v23
	v_pk_add_f32 v[22:23], v[26:27], v[24:25]
	v_pk_mul_f32 v[24:25], v[156:157], v[156:157]
	v_pk_mul_f32 v[26:27], v[154:155], v[154:155]
	v_pk_add_f32 v[22:23], v[22:23], v[22:23] op_sel:[0,1] op_sel_hi:[1,0]
	v_pk_mov_b32 v[28:29], v[26:27], v[24:25] op_sel:[1,0]
	v_mov_b32_e32 v27, v25
	v_pk_add_f32 v[24:25], v[28:29], v[26:27]
	v_mul_f32_e32 v26, v147, v147
	v_pk_add_f32 v[24:25], v[24:25], v[24:25] op_sel:[0,1] op_sel_hi:[1,0]
	v_mov_b32_e32 v23, v19
	v_mov_b32_e32 v25, v26
	v_pk_add_f32 v[22:23], v[22:23], v[24:25]
	v_mul_f32_e32 v24, v151, v151
	v_mul_f32_e32 v27, v148, v148
	v_pk_fma_f32 v[24:25], v[150:151], v[150:151], v[24:25] op_sel_hi:[1,1,0]
	v_mul_f32_e32 v26, v153, v153
	v_mul_f32_e32 v28, v149, v149
	v_mov_b32_e32 v25, v27
	v_pk_fma_f32 v[26:27], v[152:153], v[152:153], v[26:27] op_sel_hi:[1,1,0]
	s_nop 0
	v_mov_b32_e32 v27, v28
	v_pk_add_f32 v[24:25], v[24:25], v[26:27]
	s_nop 0
	v_pk_add_f32 v[22:23], v[22:23], v[24:25]
	s_nop 0
	v_add_f32_e32 v19, v22, v23
	v_and_b32_e32 v23, 64, v212
	v_xor_b32_e32 v22, 16, v212
	v_add_u32_e32 v23, 64, v23
	v_cmp_lt_i32_e32 vcc, v22, v23
	s_nop 1
	v_cndmask_b32_e32 v22, v212, v22, vcc
	v_lshlrev_b32_e32 v22, 2, v22
	v_mov_b32_e32 v22, v19
	s_nop 1
	v_permlane16_swap_b32_e32 v19, v22
	s_waitcnt lgkmcnt(0)
	v_add_f32_e32 v19, v19, v22
	v_xor_b32_e32 v22, 32, v212
	v_cmp_lt_i32_e32 vcc, v22, v23
	s_nop 1
	v_cndmask_b32_e32 v22, v212, v22, vcc
	v_lshlrev_b32_e32 v22, 2, v22
	v_mov_b32_e32 v22, v19
	s_nop 1
	v_permlane32_swap_b32_e32 v19, v22
	s_waitcnt lgkmcnt(0)
	v_add_f32_e32 v19, v19, v22
	v_fmamk_f32 v19, v19, 0x3c800000, v210
	v_mul_f32_e32 v22, 0x4f800000, v19
	v_cmp_gt_f32_e32 vcc, s28, v19
	s_nop 1
	v_cndmask_b32_e32 v19, v19, v22, vcc
	v_sqrt_f32_e32 v22, v19
	s_nop 0
	v_add_u32_e32 v23, -1, v22
	v_fma_f32 v24, -v23, v22, v19
	v_cmp_ge_f32_e64 s[6:7], 0, v24
	v_add_u32_e32 v24, 1, v22
	s_nop 0
	v_cndmask_b32_e64 v23, v22, v23, s[6:7]
	v_fma_f32 v22, -v24, v22, v19
	v_cmp_lt_f32_e64 s[6:7], 0, v22
	s_nop 1
	v_cndmask_b32_e64 v22, v23, v24, s[6:7]
	v_mul_f32_e32 v23, 0x37800000, v22
	v_cndmask_b32_e32 v22, v22, v23, vcc
	v_cmp_class_f32_e32 vcc, v19, v211
	s_nop 1
	v_cndmask_b32_e32 v19, v22, v19, vcc
	v_div_scale_f32 v22, s[0:1], v19, v19, 1.0
	v_rcp_f32_e32 v23, v22
	s_nop 0
	v_fma_f32 v24, -v22, v23, 1.0
	v_fmac_f32_e32 v23, v24, v23
	v_div_scale_f32 v24, vcc, 1.0, v19, 1.0
	v_mul_f32_e32 v25, v24, v23
	v_fma_f32 v26, -v22, v25, v24
	v_fmac_f32_e32 v25, v26, v23
	v_fma_f32 v22, -v22, v25, v24
	v_div_fmas_f32 v22, v22, v23, v25
	v_div_fixup_f32 v22, v22, v19, 1.0
	v_pk_mul_f32 v[24:25], v[158:159], v[22:23] op_sel_hi:[1,0]
	v_pk_mul_f32 v[26:27], v[160:161], v[22:23] op_sel_hi:[1,0]
	s_waitcnt vmcnt(0)
	v_pk_mul_f32 v[164:165], v[14:15], v[24:25]
	v_pk_mul_f32 v[30:31], v[16:17], v[26:27]
	v_pk_mul_f32 v[24:25], v[154:155], v[22:23] op_sel_hi:[1,0]
	v_pk_mul_f32 v[26:27], v[156:157], v[22:23] op_sel_hi:[1,0]
	v_pk_mul_f32 v[186:187], v[6:7], v[24:25]
	v_pk_mul_f32 v[32:33], v[8:9], v[26:27]
	v_pk_mul_f32 v[26:27], v[150:151], v[22:23] op_sel_hi:[1,0]
	v_pk_mul_f32 v[24:25], v[152:153], v[22:23] op_sel_hi:[1,0]
	v_pk_mul_f32 v[162:163], v[146:147], v[22:23] op_sel_hi:[1,0]
	v_pk_mul_f32 v[22:23], v[148:149], v[22:23] op_sel_hi:[1,0]
	v_pk_mul_f32 v[24:25], v[12:13], v[24:25]
	v_pk_mul_f32 v[28:29], v[10:11], v[26:27]
	v_pk_mul_f32 v[26:27], v[4:5], v[22:23]
	v_pk_mul_f32 v[162:163], v[2:3], v[162:163]
.LBB0_244:
	s_lshl_b32 s0, s18, 7
	s_add_u32 s0, s90, s0
	s_addc_u32 s1, s91, 0
	v_ashrrev_i32_e32 v19, 31, v18
	v_lshl_add_u64 v[20:21], v[20:21], 1, s[0:1]
	v_lshlrev_b64 v[22:23], 10, v[18:19]
	v_lshl_add_u64 v[22:23], v[20:21], 0, v[22:23]
	v_cvt_pk_bf16_f32 v188, v164, v165
	v_cvt_pk_bf16_f32 v189, v30, v31
	v_cvt_pk_bf16_f32 v190, v186, v187
	v_cvt_pk_bf16_f32 v191, v32, v33
	global_store_dwordx4 v[22:23], v[188:191], off
	v_cvt_pk_bf16_f32 v28, v28, v29
	v_cvt_pk_bf16_f32 v29, v24, v25
	v_cvt_pk_bf16_f32 v30, v162, v163
	v_cvt_pk_bf16_f32 v31, v26, v27
	global_store_dwordx4 v[22:23], v[28:31], off offset:64
	s_and_b64 vcc, exec, s[4:5]
	v_mov_b32_e32 v27, v133
	v_mov_b32_e32 v26, v132
	v_mov_b32_e32 v31, v131
	v_mov_b32_e32 v30, v130
	v_mov_b32_e32 v25, v137
	v_mov_b32_e32 v24, v136
	v_mov_b32_e32 v29, v135
	v_mov_b32_e32 v28, v134
	v_mov_b32_e32 v163, v141
	v_mov_b32_e32 v162, v140
	v_mov_b32_e32 v187, v139
	v_mov_b32_e32 v186, v138
	v_mov_b32_e32 v33, v145
	v_mov_b32_e32 v32, v144
	v_mov_b32_e32 v165, v143
	v_mov_b32_e32 v164, v142
	s_cbranch_vccnz .LBB0_246
; __device__ __forceinline__ unsigned cvt_pk_bf16(float lo, float hi) { unsigned r; asm volatile("v_cvt_pk_bf16_f32 %0, %1, %2" : "=v"(r) : "v"(lo), "v"(hi)); return r; }
; template <bool F8OUT = false> __device__ __forceinline__ void head_tile_store(const f32x4 (&acc)[2][2][4][2], bf16_t* obase  , int opitch, const float* gain, float scale, const f32x2e* rope, int row0, int fq) {
;     ...
;             if (gain) {
;                 float ss = 0.f;
; #pragma unroll
;                 for (int bj = 0; bj < 2; ++bj)
; #pragma unroll
;                     for (int n = 0; n < 2; ++n) ss += (x[bj][n][0] * x[bj][n][0] + x[bj][n][1] * x[bj][n][1]) + (x[bj][n][2] * x[bj][n][2] + x[bj][n][3] * x[bj][n][3]);
;                 ss += __shfl_xor(ss, 16); ss += __shfl_xor(ss, 32);
;                 const float r = scale / sqrtf(ss * (1.f / 64.f) + 1e-6f);
; #pragma unroll
;                 for (int bj = 0; bj < 2; ++bj)
; #pragma unroll
;                     for (int n = 0; n < 2; ++n) x[bj][n] = x[bj][n] * r * g[bj][n];
;     ...
;             bf16_t* rowp = obase + (size_t)row * opitch + 8 * fq;
; #pragma unroll
;             for (int bj = 0; bj < 2; ++bj) { u32x4 w; w.x = cvt_pk_bf16(x[bj][0][0], x[bj][0][1]); w.y = cvt_pk_bf16(x[bj][0][2], x[bj][0][3]); w.z = cvt_pk_bf16(x[bj][1][0], x[bj][1][1]); w.w = cvt_pk_bf16(x[bj][1][2], x[bj][1][3]);
;                 *(u32x4*)(rowp + 32 * bj) = w; }
	v_pk_mul_f32 v[24:25], v[144:145], v[144:145]
	v_pk_mul_f32 v[26:27], v[142:143], v[142:143]
	s_nop 0
	v_pk_mov_b32 v[28:29], v[26:27], v[24:25] op_sel:[1,0]
	v_mov_b32_e32 v27, v25
	v_pk_add_f32 v[24:25], v[28:29], v[26:27]
	v_pk_mul_f32 v[26:27], v[140:141], v[140:141]
	v_pk_mul_f32 v[28:29], v[138:139], v[138:139]
	v_pk_add_f32 v[24:25], v[24:25], v[24:25] op_sel:[0,1] op_sel_hi:[1,0]
	v_pk_mov_b32 v[30:31], v[28:29], v[26:27] op_sel:[1,0]
	v_mov_b32_e32 v29, v27
	v_pk_add_f32 v[26:27], v[30:31], v[28:29]
	v_mul_f32_e32 v28, v130, v130
	v_mul_f32_e32 v29, v131, v131
	v_pk_add_f32 v[26:27], v[26:27], v[26:27] op_sel:[0,1] op_sel_hi:[1,0]
	v_mov_b32_e32 v25, v28
	v_mov_b32_e32 v27, v29
	v_pk_add_f32 v[24:25], v[24:25], v[26:27]
	v_mul_f32_e32 v26, v135, v135
	v_mul_f32_e32 v28, v137, v137
	v_mul_f32_e32 v30, v132, v132
	v_mul_f32_e32 v31, v133, v133
	v_pk_fma_f32 v[26:27], v[134:135], v[134:135], v[26:27] op_sel_hi:[1,1,0]
	v_pk_fma_f32 v[28:29], v[136:137], v[136:137], v[28:29] op_sel_hi:[1,1,0]
	v_mov_b32_e32 v27, v30
	v_mov_b32_e32 v29, v31
	v_pk_add_f32 v[26:27], v[26:27], v[28:29]
	s_nop 0
	v_pk_add_f32 v[24:25], v[24:25], v[26:27]
	v_and_b32_e32 v26, 64, v212
	v_add_f32_e32 v24, v24, v25
	v_xor_b32_e32 v25, 16, v212
	v_add_u32_e32 v26, 64, v26
	v_cmp_lt_i32_e32 vcc, v25, v26
	s_nop 1
	v_cndmask_b32_e32 v25, v212, v25, vcc
	v_lshlrev_b32_e32 v25, 2, v25
	v_mov_b32_e32 v25, v24
	s_nop 1
	v_permlane16_swap_b32_e32 v24, v25
	s_waitcnt lgkmcnt(0)
	v_add_f32_e32 v24, v24, v25
	v_xor_b32_e32 v25, 32, v212
	v_cmp_lt_i32_e32 vcc, v25, v26
	s_nop 1
	v_cndmask_b32_e32 v25, v212, v25, vcc
	v_lshlrev_b32_e32 v25, 2, v25
	v_mov_b32_e32 v25, v24
	s_nop 1
	v_permlane32_swap_b32_e32 v24, v25
	s_waitcnt lgkmcnt(0)
	v_add_f32_e32 v24, v24, v25
	v_fmamk_f32 v24, v24, 0x3c800000, v210
	v_mul_f32_e32 v25, 0x4f800000, v24
	v_cmp_gt_f32_e32 vcc, s28, v24
	s_nop 1
	v_cndmask_b32_e32 v24, v24, v25, vcc
	v_sqrt_f32_e32 v25, v24
	s_nop 0
	v_add_u32_e32 v26, -1, v25
	v_fma_f32 v27, -v26, v25, v24
	v_cmp_ge_f32_e64 s[6:7], 0, v27
	v_add_u32_e32 v27, 1, v25
	s_nop 0
	v_cndmask_b32_e64 v26, v25, v26, s[6:7]
	v_fma_f32 v25, -v27, v25, v24
	v_cmp_lt_f32_e64 s[6:7], 0, v25
	s_nop 1
	v_cndmask_b32_e64 v25, v26, v27, s[6:7]
	v_mul_f32_e32 v26, 0x37800000, v25
	v_cndmask_b32_e32 v25, v25, v26, vcc
	v_cmp_class_f32_e32 vcc, v24, v211
	s_nop 1
	v_cndmask_b32_e32 v24, v25, v24, vcc
	v_div_scale_f32 v25, s[0:1], v24, v24, 1.0
	v_rcp_f32_e32 v26, v25
	s_nop 0
	v_fma_f32 v27, -v25, v26, 1.0
	v_fmac_f32_e32 v26, v27, v26
	v_div_scale_f32 v27, vcc, 1.0, v24, 1.0
	v_mul_f32_e32 v28, v27, v26
	v_fma_f32 v29, -v25, v28, v27
	v_fmac_f32_e32 v28, v29, v26
	v_fma_f32 v25, -v25, v28, v27
	v_div_fmas_f32 v25, v25, v26, v28
	v_div_fixup_f32 v26, v25, v24, 1.0
	v_pk_mul_f32 v[24:25], v[142:143], v[26:27] op_sel_hi:[1,0]
	v_pk_mul_f32 v[28:29], v[144:145], v[26:27] op_sel_hi:[1,0]
	s_waitcnt vmcnt(0)
	v_pk_mul_f32 v[164:165], v[14:15], v[24:25]
	v_pk_mul_f32 v[32:33], v[16:17], v[28:29]
	v_pk_mul_f32 v[24:25], v[138:139], v[26:27] op_sel_hi:[1,0]
	v_pk_mul_f32 v[28:29], v[140:141], v[26:27] op_sel_hi:[1,0]
	v_pk_mul_f32 v[186:187], v[6:7], v[24:25]
	v_pk_mul_f32 v[162:163], v[8:9], v[28:29]
	v_pk_mul_f32 v[28:29], v[134:135], v[26:27] op_sel_hi:[1,0]
	v_pk_mul_f32 v[24:25], v[136:137], v[26:27] op_sel_hi:[1,0]
	v_pk_mul_f32 v[30:31], v[130:131], v[26:27] op_sel_hi:[1,0]
	v_pk_mul_f32 v[26:27], v[132:133], v[26:27] op_sel_hi:[1,0]
	v_pk_mul_f32 v[24:25], v[12:13], v[24:25]
	v_pk_mul_f32 v[28:29], v[10:11], v[28:29]
	v_pk_mul_f32 v[26:27], v[4:5], v[26:27]
	v_pk_mul_f32 v[30:31], v[2:3], v[30:31]
.LBB0_246:
	v_cvt_pk_bf16_f32 v188, v164, v165
	v_cvt_pk_bf16_f32 v189, v32, v33
	v_add_co_u32_e32 v32, vcc, 0x4000, v22
	v_lshl_add_u64 v[192:193], v[22:23], 0, s[92:93]
	s_nop 0
	v_addc_co_u32_e32 v33, vcc, 0, v23, vcc
	v_cvt_pk_bf16_f32 v190, v186, v187
	v_cvt_pk_bf16_f32 v191, v162, v163
	global_store_dwordx4 v[32:33], v[188:191], off
	v_cvt_pk_bf16_f32 v28, v28, v29
	v_cvt_pk_bf16_f32 v29, v24, v25
	v_cvt_pk_bf16_f32 v30, v30, v31
	v_cvt_pk_bf16_f32 v31, v26, v27
	global_store_dwordx4 v[192:193], v[28:31], off offset:64
	s_and_b64 vcc, exec, s[4:5]
	v_mov_b32_e32 v27, v117
	v_mov_b32_e32 v26, v116
	v_mov_b32_e32 v31, v115
	v_mov_b32_e32 v30, v114
	v_mov_b32_e32 v25, v121
	v_mov_b32_e32 v24, v120
	v_mov_b32_e32 v29, v119
	v_mov_b32_e32 v28, v118
	v_mov_b32_e32 v163, v125
	v_mov_b32_e32 v162, v124
	v_mov_b32_e32 v187, v123
	v_mov_b32_e32 v186, v122
	v_mov_b32_e32 v33, v129
	v_mov_b32_e32 v32, v128
	v_mov_b32_e32 v165, v127
	v_mov_b32_e32 v164, v126
	s_cbranch_vccnz .LBB0_248
; __device__ __forceinline__ unsigned cvt_pk_bf16(float lo, float hi) { unsigned r; asm volatile("v_cvt_pk_bf16_f32 %0, %1, %2" : "=v"(r) : "v"(lo), "v"(hi)); return r; }
; template <bool F8OUT = false> __device__ __forceinline__ void head_tile_store(const f32x4 (&acc)[2][2][4][2], bf16_t* obase  , int opitch, const float* gain, float scale, const f32x2e* rope, int row0, int fq) {
;     ...
;             if (gain) {
;                 float ss = 0.f;
; #pragma unroll
;                 for (int bj = 0; bj < 2; ++bj)
; #pragma unroll
;                     for (int n = 0; n < 2; ++n) ss += (x[bj][n][0] * x[bj][n][0] + x[bj][n][1] * x[bj][n][1]) + (x[bj][n][2] * x[bj][n][2] + x[bj][n][3] * x[bj][n][3]);
;                 ss += __shfl_xor(ss, 16); ss += __shfl_xor(ss, 32);
;                 const float r = scale / sqrtf(ss * (1.f / 64.f) + 1e-6f);
; #pragma unroll
;                 for (int bj = 0; bj < 2; ++bj)
; #pragma unroll
;                     for (int n = 0; n < 2; ++n) x[bj][n] = x[bj][n] * r * g[bj][n];
;     ...
;             bf16_t* rowp = obase + (size_t)row * opitch + 8 * fq;
; #pragma unroll
;             for (int bj = 0; bj < 2; ++bj) { u32x4 w; w.x = cvt_pk_bf16(x[bj][0][0], x[bj][0][1]); w.y = cvt_pk_bf16(x[bj][0][2], x[bj][0][3]); w.z = cvt_pk_bf16(x[bj][1][0], x[bj][1][1]); w.w = cvt_pk_bf16(x[bj][1][2], x[bj][1][3]);
;                 *(u32x4*)(rowp + 32 * bj) = w; }
	v_pk_mul_f32 v[24:25], v[128:129], v[128:129]
	v_pk_mul_f32 v[26:27], v[126:127], v[126:127]
	s_nop 0
	v_pk_mov_b32 v[28:29], v[26:27], v[24:25] op_sel:[1,0]
	v_mov_b32_e32 v27, v25
	v_pk_add_f32 v[24:25], v[28:29], v[26:27]
	v_pk_mul_f32 v[26:27], v[124:125], v[124:125]
	v_pk_mul_f32 v[28:29], v[122:123], v[122:123]
	v_pk_add_f32 v[24:25], v[24:25], v[24:25] op_sel:[0,1] op_sel_hi:[1,0]
	v_pk_mov_b32 v[30:31], v[28:29], v[26:27] op_sel:[1,0]
	v_mov_b32_e32 v29, v27
	v_pk_add_f32 v[26:27], v[30:31], v[28:29]
	v_mul_f32_e32 v28, v114, v114
	v_mul_f32_e32 v29, v115, v115
	v_pk_add_f32 v[26:27], v[26:27], v[26:27] op_sel:[0,1] op_sel_hi:[1,0]
	v_mov_b32_e32 v25, v28
	v_mov_b32_e32 v27, v29
	v_pk_add_f32 v[24:25], v[24:25], v[26:27]
	v_mul_f32_e32 v26, v119, v119
	v_mul_f32_e32 v28, v121, v121
	v_mul_f32_e32 v30, v116, v116
	v_mul_f32_e32 v31, v117, v117
	v_pk_fma_f32 v[26:27], v[118:119], v[118:119], v[26:27] op_sel_hi:[1,1,0]
	v_pk_fma_f32 v[28:29], v[120:121], v[120:121], v[28:29] op_sel_hi:[1,1,0]
	v_mov_b32_e32 v27, v30
	v_mov_b32_e32 v29, v31
	v_pk_add_f32 v[26:27], v[26:27], v[28:29]
	s_nop 0
	v_pk_add_f32 v[24:25], v[24:25], v[26:27]
	v_and_b32_e32 v26, 64, v212
	v_add_f32_e32 v24, v24, v25
	v_xor_b32_e32 v25, 16, v212
	v_add_u32_e32 v26, 64, v26
	v_cmp_lt_i32_e32 vcc, v25, v26
	s_nop 1
	v_cndmask_b32_e32 v25, v212, v25, vcc
	v_lshlrev_b32_e32 v25, 2, v25
	v_mov_b32_e32 v25, v24
	s_nop 1
	v_permlane16_swap_b32_e32 v24, v25
	s_waitcnt lgkmcnt(0)
	v_add_f32_e32 v24, v24, v25
	v_xor_b32_e32 v25, 32, v212
	v_cmp_lt_i32_e32 vcc, v25, v26
	s_nop 1
	v_cndmask_b32_e32 v25, v212, v25, vcc
	v_lshlrev_b32_e32 v25, 2, v25
	v_mov_b32_e32 v25, v24
	s_nop 1
	v_permlane32_swap_b32_e32 v24, v25
	s_waitcnt lgkmcnt(0)
	v_add_f32_e32 v24, v24, v25
	v_fmamk_f32 v24, v24, 0x3c800000, v210
	v_mul_f32_e32 v25, 0x4f800000, v24
	v_cmp_gt_f32_e32 vcc, s28, v24
	s_nop 1
	v_cndmask_b32_e32 v24, v24, v25, vcc
	v_sqrt_f32_e32 v25, v24
	s_nop 0
	v_add_u32_e32 v26, -1, v25
	v_fma_f32 v27, -v26, v25, v24
	v_cmp_ge_f32_e64 s[6:7], 0, v27
	v_add_u32_e32 v27, 1, v25
	s_nop 0
	v_cndmask_b32_e64 v26, v25, v26, s[6:7]
	v_fma_f32 v25, -v27, v25, v24
	v_cmp_lt_f32_e64 s[6:7], 0, v25
	s_nop 1
	v_cndmask_b32_e64 v25, v26, v27, s[6:7]
	v_mul_f32_e32 v26, 0x37800000, v25
	v_cndmask_b32_e32 v25, v25, v26, vcc
	v_cmp_class_f32_e32 vcc, v24, v211
	s_nop 1
	v_cndmask_b32_e32 v24, v25, v24, vcc
	v_div_scale_f32 v25, s[0:1], v24, v24, 1.0
	v_rcp_f32_e32 v26, v25
	s_nop 0
	v_fma_f32 v27, -v25, v26, 1.0
	v_fmac_f32_e32 v26, v27, v26
	v_div_scale_f32 v27, vcc, 1.0, v24, 1.0
	v_mul_f32_e32 v28, v27, v26
	v_fma_f32 v29, -v25, v28, v27
	v_fmac_f32_e32 v28, v29, v26
	v_fma_f32 v25, -v25, v28, v27
	v_div_fmas_f32 v25, v25, v26, v28
	v_div_fixup_f32 v26, v25, v24, 1.0
	v_pk_mul_f32 v[24:25], v[126:127], v[26:27] op_sel_hi:[1,0]
	v_pk_mul_f32 v[28:29], v[128:129], v[26:27] op_sel_hi:[1,0]
	s_waitcnt vmcnt(0)
	v_pk_mul_f32 v[164:165], v[14:15], v[24:25]
	v_pk_mul_f32 v[32:33], v[16:17], v[28:29]
	v_pk_mul_f32 v[24:25], v[122:123], v[26:27] op_sel_hi:[1,0]
	v_pk_mul_f32 v[28:29], v[124:125], v[26:27] op_sel_hi:[1,0]
	v_pk_mul_f32 v[186:187], v[6:7], v[24:25]
	v_pk_mul_f32 v[162:163], v[8:9], v[28:29]
	v_pk_mul_f32 v[28:29], v[118:119], v[26:27] op_sel_hi:[1,0]
	v_pk_mul_f32 v[24:25], v[120:121], v[26:27] op_sel_hi:[1,0]
	v_pk_mul_f32 v[30:31], v[114:115], v[26:27] op_sel_hi:[1,0]
	v_pk_mul_f32 v[26:27], v[116:117], v[26:27] op_sel_hi:[1,0]
	v_pk_mul_f32 v[24:25], v[12:13], v[24:25]
	v_pk_mul_f32 v[28:29], v[10:11], v[28:29]
	v_pk_mul_f32 v[26:27], v[4:5], v[26:27]
	v_pk_mul_f32 v[30:31], v[2:3], v[30:31]
.LBB0_248:
	s_mov_b64 s[0:1], 0x8000
	v_lshl_add_u64 v[192:193], v[22:23], 0, s[0:1]
	v_add_co_u32_e32 v22, vcc, 0x8000, v22
	v_cvt_pk_bf16_f32 v188, v164, v165
	v_cvt_pk_bf16_f32 v189, v32, v33
	v_cvt_pk_bf16_f32 v190, v186, v187
	v_cvt_pk_bf16_f32 v191, v162, v163
	s_nop 1
	v_addc_co_u32_e32 v23, vcc, 0, v23, vcc
	global_store_dwordx4 v[22:23], v[188:191], off
	v_cvt_pk_bf16_f32 v22, v28, v29
	v_cvt_pk_bf16_f32 v23, v24, v25
	v_cvt_pk_bf16_f32 v24, v30, v31
	v_cvt_pk_bf16_f32 v25, v26, v27
	global_store_dwordx4 v[192:193], v[22:25], off offset:64
	s_and_b64 vcc, exec, s[4:5]
	v_mov_b32_e32 v27, v101
	v_mov_b32_e32 v26, v100
	v_mov_b32_e32 v31, v99
	v_mov_b32_e32 v30, v98
	v_mov_b32_e32 v25, v105
	v_mov_b32_e32 v24, v104
	v_mov_b32_e32 v29, v103
	v_mov_b32_e32 v28, v102
	v_mov_b32_e32 v163, v109
	v_mov_b32_e32 v162, v108
	v_mov_b32_e32 v187, v107
	v_mov_b32_e32 v186, v106
	v_mov_b32_e32 v33, v113
	v_mov_b32_e32 v32, v112
	v_mov_b32_e32 v165, v111
	v_mov_b32_e32 v164, v110
	s_cbranch_vccnz .LBB0_250
; __device__ __forceinline__ unsigned cvt_pk_bf16(float lo, float hi) { unsigned r; asm volatile("v_cvt_pk_bf16_f32 %0, %1, %2" : "=v"(r) : "v"(lo), "v"(hi)); return r; }
; template <bool F8OUT = false> __device__ __forceinline__ void head_tile_store(const f32x4 (&acc)[2][2][4][2], bf16_t* obase  , int opitch, const float* gain, float scale, const f32x2e* rope, int row0, int fq) {
;     ...
;             if (gain) {
;                 float ss = 0.f;
; #pragma unroll
;                 for (int bj = 0; bj < 2; ++bj)
; #pragma unroll
;                     for (int n = 0; n < 2; ++n) ss += (x[bj][n][0] * x[bj][n][0] + x[bj][n][1] * x[bj][n][1]) + (x[bj][n][2] * x[bj][n][2] + x[bj][n][3] * x[bj][n][3]);
;                 ss += __shfl_xor(ss, 16); ss += __shfl_xor(ss, 32);
;                 const float r = scale / sqrtf(ss * (1.f / 64.f) + 1e-6f);
; #pragma unroll
;                 for (int bj = 0; bj < 2; ++bj)
; #pragma unroll
;                     for (int n = 0; n < 2; ++n) x[bj][n] = x[bj][n] * r * g[bj][n];
;     ...
;             bf16_t* rowp = obase + (size_t)row * opitch + 8 * fq;
; #pragma unroll
;             for (int bj = 0; bj < 2; ++bj) { u32x4 w; w.x = cvt_pk_bf16(x[bj][0][0], x[bj][0][1]); w.y = cvt_pk_bf16(x[bj][0][2], x[bj][0][3]); w.z = cvt_pk_bf16(x[bj][1][0], x[bj][1][1]); w.w = cvt_pk_bf16(x[bj][1][2], x[bj][1][3]);
;                 *(u32x4*)(rowp + 32 * bj) = w; }
	v_pk_mul_f32 v[22:23], v[112:113], v[112:113]
	v_pk_mul_f32 v[24:25], v[110:111], v[110:111]
	s_nop 0
	v_pk_mov_b32 v[26:27], v[24:25], v[22:23] op_sel:[1,0]
	v_mov_b32_e32 v25, v23
	v_pk_add_f32 v[22:23], v[26:27], v[24:25]
	v_pk_mul_f32 v[24:25], v[108:109], v[108:109]
	v_pk_mul_f32 v[26:27], v[106:107], v[106:107]
	v_pk_add_f32 v[22:23], v[22:23], v[22:23] op_sel:[0,1] op_sel_hi:[1,0]
	v_pk_mov_b32 v[28:29], v[26:27], v[24:25] op_sel:[1,0]
	v_mov_b32_e32 v27, v25
	v_pk_add_f32 v[24:25], v[28:29], v[26:27]
	v_mul_f32_e32 v26, v98, v98
	v_mul_f32_e32 v27, v99, v99
	v_pk_add_f32 v[24:25], v[24:25], v[24:25] op_sel:[0,1] op_sel_hi:[1,0]
	v_mov_b32_e32 v23, v26
	v_mov_b32_e32 v25, v27
	v_pk_add_f32 v[22:23], v[22:23], v[24:25]
	v_mul_f32_e32 v24, v103, v103
	v_mul_f32_e32 v26, v105, v105
	v_mul_f32_e32 v28, v100, v100
	v_mul_f32_e32 v29, v101, v101
	v_pk_fma_f32 v[24:25], v[102:103], v[102:103], v[24:25] op_sel_hi:[1,1,0]
	v_pk_fma_f32 v[26:27], v[104:105], v[104:105], v[26:27] op_sel_hi:[1,1,0]
	v_mov_b32_e32 v25, v28
	v_mov_b32_e32 v27, v29
	v_pk_add_f32 v[24:25], v[24:25], v[26:27]
	s_nop 0
	v_pk_add_f32 v[22:23], v[22:23], v[24:25]
	v_and_b32_e32 v24, 64, v212
	v_add_f32_e32 v22, v22, v23
	v_xor_b32_e32 v23, 16, v212
	v_add_u32_e32 v24, 64, v24
	v_cmp_lt_i32_e32 vcc, v23, v24
	s_nop 1
	v_cndmask_b32_e32 v23, v212, v23, vcc
	v_lshlrev_b32_e32 v23, 2, v23
	v_mov_b32_e32 v23, v22
	s_nop 1
	v_permlane16_swap_b32_e32 v22, v23
	s_waitcnt lgkmcnt(0)
	v_add_f32_e32 v22, v22, v23
	v_xor_b32_e32 v23, 32, v212
	v_cmp_lt_i32_e32 vcc, v23, v24
	s_nop 1
	v_cndmask_b32_e32 v23, v212, v23, vcc
	v_lshlrev_b32_e32 v23, 2, v23
	v_mov_b32_e32 v23, v22
	s_nop 1
	v_permlane32_swap_b32_e32 v22, v23
	s_waitcnt lgkmcnt(0)
	v_add_f32_e32 v22, v22, v23
	v_fmamk_f32 v22, v22, 0x3c800000, v210
	v_mul_f32_e32 v23, 0x4f800000, v22
	v_cmp_gt_f32_e32 vcc, s28, v22
	s_nop 1
	v_cndmask_b32_e32 v22, v22, v23, vcc
	v_sqrt_f32_e32 v23, v22
	s_nop 0
	v_add_u32_e32 v24, -1, v23
	v_fma_f32 v25, -v24, v23, v22
	v_cmp_ge_f32_e64 s[6:7], 0, v25
	v_add_u32_e32 v25, 1, v23
	s_nop 0
	v_cndmask_b32_e64 v24, v23, v24, s[6:7]
	v_fma_f32 v23, -v25, v23, v22
	v_cmp_lt_f32_e64 s[6:7], 0, v23
	s_nop 1
	v_cndmask_b32_e64 v23, v24, v25, s[6:7]
	v_mul_f32_e32 v24, 0x37800000, v23
	v_cndmask_b32_e32 v23, v23, v24, vcc
	v_cmp_class_f32_e32 vcc, v22, v211
	s_nop 1
	v_cndmask_b32_e32 v22, v23, v22, vcc
	v_div_scale_f32 v23, s[0:1], v22, v22, 1.0
	v_rcp_f32_e32 v24, v23
	s_nop 0
	v_fma_f32 v25, -v23, v24, 1.0
	v_fmac_f32_e32 v24, v25, v24
	v_div_scale_f32 v25, vcc, 1.0, v22, 1.0
	v_mul_f32_e32 v26, v25, v24
	v_fma_f32 v27, -v23, v26, v25
	v_fmac_f32_e32 v26, v27, v24
	v_fma_f32 v23, -v23, v26, v25
	v_div_fmas_f32 v23, v23, v24, v26
	v_div_fixup_f32 v22, v23, v22, 1.0
	v_pk_mul_f32 v[24:25], v[110:111], v[22:23] op_sel_hi:[1,0]
	v_pk_mul_f32 v[26:27], v[112:113], v[22:23] op_sel_hi:[1,0]
	s_waitcnt vmcnt(0)
	v_pk_mul_f32 v[164:165], v[14:15], v[24:25]
	v_pk_mul_f32 v[32:33], v[16:17], v[26:27]
	v_pk_mul_f32 v[24:25], v[106:107], v[22:23] op_sel_hi:[1,0]
	v_pk_mul_f32 v[26:27], v[108:109], v[22:23] op_sel_hi:[1,0]
	v_pk_mul_f32 v[186:187], v[6:7], v[24:25]
	v_pk_mul_f32 v[162:163], v[8:9], v[26:27]
	v_pk_mul_f32 v[26:27], v[102:103], v[22:23] op_sel_hi:[1,0]
	v_pk_mul_f32 v[24:25], v[104:105], v[22:23] op_sel_hi:[1,0]
	v_pk_mul_f32 v[30:31], v[98:99], v[22:23] op_sel_hi:[1,0]
	v_pk_mul_f32 v[22:23], v[100:101], v[22:23] op_sel_hi:[1,0]
	v_pk_mul_f32 v[24:25], v[12:13], v[24:25]
	v_pk_mul_f32 v[28:29], v[10:11], v[26:27]
	v_pk_mul_f32 v[26:27], v[4:5], v[22:23]
	v_pk_mul_f32 v[30:31], v[2:3], v[30:31]
.LBB0_250:
	v_lshlrev_b64 v[22:23], 10, v[18:19]
	v_lshl_add_u64 v[22:23], v[20:21], 0, v[22:23]
	v_cvt_pk_bf16_f32 v188, v164, v165
	v_cvt_pk_bf16_f32 v189, v32, v33
	v_add_co_u32_e32 v32, vcc, 0xc000, v22
	v_lshl_add_u64 v[192:193], v[22:23], 0, s[34:35]
	s_nop 0
	v_addc_co_u32_e32 v33, vcc, 0, v23, vcc
	v_cvt_pk_bf16_f32 v190, v186, v187
	v_cvt_pk_bf16_f32 v191, v162, v163
	global_store_dwordx4 v[32:33], v[188:191], off
	v_cvt_pk_bf16_f32 v28, v28, v29
	v_cvt_pk_bf16_f32 v29, v24, v25
	v_cvt_pk_bf16_f32 v30, v30, v31
	v_cvt_pk_bf16_f32 v31, v26, v27
	global_store_dwordx4 v[192:193], v[28:31], off offset:64
	s_and_b64 vcc, exec, s[4:5]
	v_mov_b32_e32 v27, v85
	v_mov_b32_e32 v26, v84
	v_mov_b32_e32 v31, v83
	v_mov_b32_e32 v30, v82
	v_mov_b32_e32 v25, v89
	v_mov_b32_e32 v24, v88
	v_mov_b32_e32 v29, v87
	v_mov_b32_e32 v28, v86
	v_mov_b32_e32 v163, v93
	v_mov_b32_e32 v162, v92
	v_mov_b32_e32 v187, v91
	v_mov_b32_e32 v186, v90
	v_mov_b32_e32 v33, v97
	v_mov_b32_e32 v32, v96
	v_mov_b32_e32 v165, v95
	v_mov_b32_e32 v164, v94
	s_cbranch_vccnz .LBB0_252
; __device__ __forceinline__ unsigned cvt_pk_bf16(float lo, float hi) { unsigned r; asm volatile("v_cvt_pk_bf16_f32 %0, %1, %2" : "=v"(r) : "v"(lo), "v"(hi)); return r; }
; template <bool F8OUT = false> __device__ __forceinline__ void head_tile_store(const f32x4 (&acc)[2][2][4][2], bf16_t* obase  , int opitch, const float* gain, float scale, const f32x2e* rope, int row0, int fq) {
;     ...
;             if (gain) {
;                 float ss = 0.f;
; #pragma unroll
;                 for (int bj = 0; bj < 2; ++bj)
; #pragma unroll
;                     for (int n = 0; n < 2; ++n) ss += (x[bj][n][0] * x[bj][n][0] + x[bj][n][1] * x[bj][n][1]) + (x[bj][n][2] * x[bj][n][2] + x[bj][n][3] * x[bj][n][3]);
;                 ss += __shfl_xor(ss, 16); ss += __shfl_xor(ss, 32);
;                 const float r = scale / sqrtf(ss * (1.f / 64.f) + 1e-6f);
; #pragma unroll
;                 for (int bj = 0; bj < 2; ++bj)
; #pragma unroll
;                     for (int n = 0; n < 2; ++n) x[bj][n] = x[bj][n] * r * g[bj][n];
;     ...
;             bf16_t* rowp = obase + (size_t)row * opitch + 8 * fq;
; #pragma unroll
;             for (int bj = 0; bj < 2; ++bj) { u32x4 w; w.x = cvt_pk_bf16(x[bj][0][0], x[bj][0][1]); w.y = cvt_pk_bf16(x[bj][0][2], x[bj][0][3]); w.z = cvt_pk_bf16(x[bj][1][0], x[bj][1][1]); w.w = cvt_pk_bf16(x[bj][1][2], x[bj][1][3]);
;                 *(u32x4*)(rowp + 32 * bj) = w; }
	v_pk_mul_f32 v[24:25], v[96:97], v[96:97]
	v_pk_mul_f32 v[26:27], v[94:95], v[94:95]
	s_nop 0
	v_pk_mov_b32 v[28:29], v[26:27], v[24:25] op_sel:[1,0]
	v_mov_b32_e32 v27, v25
	v_pk_add_f32 v[24:25], v[28:29], v[26:27]
	v_pk_mul_f32 v[26:27], v[92:93], v[92:93]
	v_pk_mul_f32 v[28:29], v[90:91], v[90:91]
	v_pk_add_f32 v[24:25], v[24:25], v[24:25] op_sel:[0,1] op_sel_hi:[1,0]
	v_pk_mov_b32 v[30:31], v[28:29], v[26:27] op_sel:[1,0]
	v_mov_b32_e32 v29, v27
	v_pk_add_f32 v[26:27], v[30:31], v[28:29]
	v_mul_f32_e32 v28, v82, v82
	v_mul_f32_e32 v29, v83, v83
	v_pk_add_f32 v[26:27], v[26:27], v[26:27] op_sel:[0,1] op_sel_hi:[1,0]
	v_mov_b32_e32 v25, v28
	v_mov_b32_e32 v27, v29
	v_pk_add_f32 v[24:25], v[24:25], v[26:27]
	v_mul_f32_e32 v26, v87, v87
	v_mul_f32_e32 v28, v89, v89
	v_mul_f32_e32 v30, v84, v84
	v_mul_f32_e32 v31, v85, v85
	v_pk_fma_f32 v[26:27], v[86:87], v[86:87], v[26:27] op_sel_hi:[1,1,0]
	v_pk_fma_f32 v[28:29], v[88:89], v[88:89], v[28:29] op_sel_hi:[1,1,0]
	v_mov_b32_e32 v27, v30
	v_mov_b32_e32 v29, v31
	v_pk_add_f32 v[26:27], v[26:27], v[28:29]
	s_nop 0
	v_pk_add_f32 v[24:25], v[24:25], v[26:27]
	v_and_b32_e32 v26, 64, v212
	v_add_f32_e32 v24, v24, v25
	v_xor_b32_e32 v25, 16, v212
	v_add_u32_e32 v26, 64, v26
	v_cmp_lt_i32_e32 vcc, v25, v26
	s_nop 1
	v_cndmask_b32_e32 v25, v212, v25, vcc
	v_lshlrev_b32_e32 v25, 2, v25
	v_mov_b32_e32 v25, v24
	s_nop 1
	v_permlane16_swap_b32_e32 v24, v25
	s_waitcnt lgkmcnt(0)
	v_add_f32_e32 v24, v24, v25
	v_xor_b32_e32 v25, 32, v212
	v_cmp_lt_i32_e32 vcc, v25, v26
	s_nop 1
	v_cndmask_b32_e32 v25, v212, v25, vcc
	v_lshlrev_b32_e32 v25, 2, v25
	v_mov_b32_e32 v25, v24
	s_nop 1
	v_permlane32_swap_b32_e32 v24, v25
	s_waitcnt lgkmcnt(0)
	v_add_f32_e32 v24, v24, v25
	v_fmamk_f32 v24, v24, 0x3c800000, v210
	v_mul_f32_e32 v25, 0x4f800000, v24
	v_cmp_gt_f32_e32 vcc, s28, v24
	s_nop 1
	v_cndmask_b32_e32 v24, v24, v25, vcc
	v_sqrt_f32_e32 v25, v24
	s_nop 0
	v_add_u32_e32 v26, -1, v25
	v_fma_f32 v27, -v26, v25, v24
	v_cmp_ge_f32_e64 s[6:7], 0, v27
	v_add_u32_e32 v27, 1, v25
	s_nop 0
	v_cndmask_b32_e64 v26, v25, v26, s[6:7]
	v_fma_f32 v25, -v27, v25, v24
	v_cmp_lt_f32_e64 s[6:7], 0, v25
	s_nop 1
	v_cndmask_b32_e64 v25, v26, v27, s[6:7]
	v_mul_f32_e32 v26, 0x37800000, v25
	v_cndmask_b32_e32 v25, v25, v26, vcc
	v_cmp_class_f32_e32 vcc, v24, v211
	s_nop 1
	v_cndmask_b32_e32 v24, v25, v24, vcc
	v_div_scale_f32 v25, s[0:1], v24, v24, 1.0
	v_rcp_f32_e32 v26, v25
	s_nop 0
	v_fma_f32 v27, -v25, v26, 1.0
	v_fmac_f32_e32 v26, v27, v26
	v_div_scale_f32 v27, vcc, 1.0, v24, 1.0
	v_mul_f32_e32 v28, v27, v26
	v_fma_f32 v29, -v25, v28, v27
	v_fmac_f32_e32 v28, v29, v26
	v_fma_f32 v25, -v25, v28, v27
	v_div_fmas_f32 v25, v25, v26, v28
	v_div_fixup_f32 v26, v25, v24, 1.0
	v_pk_mul_f32 v[24:25], v[94:95], v[26:27] op_sel_hi:[1,0]
	v_pk_mul_f32 v[28:29], v[96:97], v[26:27] op_sel_hi:[1,0]
	s_waitcnt vmcnt(0)
	v_pk_mul_f32 v[164:165], v[14:15], v[24:25]
	v_pk_mul_f32 v[32:33], v[16:17], v[28:29]
	v_pk_mul_f32 v[24:25], v[90:91], v[26:27] op_sel_hi:[1,0]
	v_pk_mul_f32 v[28:29], v[92:93], v[26:27] op_sel_hi:[1,0]
	v_pk_mul_f32 v[186:187], v[6:7], v[24:25]
	v_pk_mul_f32 v[162:163], v[8:9], v[28:29]
	v_pk_mul_f32 v[28:29], v[86:87], v[26:27] op_sel_hi:[1,0]
	v_pk_mul_f32 v[24:25], v[88:89], v[26:27] op_sel_hi:[1,0]
	v_pk_mul_f32 v[30:31], v[82:83], v[26:27] op_sel_hi:[1,0]
	v_pk_mul_f32 v[26:27], v[84:85], v[26:27] op_sel_hi:[1,0]
	v_pk_mul_f32 v[24:25], v[12:13], v[24:25]
	v_pk_mul_f32 v[28:29], v[10:11], v[28:29]
	v_pk_mul_f32 v[26:27], v[4:5], v[26:27]
	v_pk_mul_f32 v[30:31], v[2:3], v[30:31]
.LBB0_252:
	s_mov_b64 s[0:1], 0x20000
	v_lshl_add_u64 v[192:193], v[22:23], 0, s[0:1]
	v_add_co_u32_e32 v22, vcc, 0x20000, v22
	v_cvt_pk_bf16_f32 v188, v164, v165
	v_cvt_pk_bf16_f32 v189, v32, v33
	v_cvt_pk_bf16_f32 v190, v186, v187
	v_cvt_pk_bf16_f32 v191, v162, v163
	s_nop 1
	v_addc_co_u32_e32 v23, vcc, 0, v23, vcc
	global_store_dwordx4 v[22:23], v[188:191], off
	v_cvt_pk_bf16_f32 v22, v28, v29
	v_cvt_pk_bf16_f32 v23, v24, v25
	v_cvt_pk_bf16_f32 v24, v30, v31
	v_cvt_pk_bf16_f32 v25, v26, v27
	global_store_dwordx4 v[192:193], v[22:25], off offset:64
	s_and_b64 vcc, exec, s[4:5]
	v_mov_b32_e32 v27, v69
	v_mov_b32_e32 v26, v68
	v_mov_b32_e32 v31, v67
	v_mov_b32_e32 v30, v66
	v_mov_b32_e32 v25, v73
	v_mov_b32_e32 v24, v72
	v_mov_b32_e32 v29, v71
	v_mov_b32_e32 v28, v70
	v_mov_b32_e32 v163, v77
	v_mov_b32_e32 v162, v76
	v_mov_b32_e32 v187, v75
	v_mov_b32_e32 v186, v74
	v_mov_b32_e32 v33, v81
	v_mov_b32_e32 v32, v80
	v_mov_b32_e32 v165, v79
	v_mov_b32_e32 v164, v78
	s_cbranch_vccnz .LBB0_254
; __device__ __forceinline__ unsigned cvt_pk_bf16(float lo, float hi) { unsigned r; asm volatile("v_cvt_pk_bf16_f32 %0, %1, %2" : "=v"(r) : "v"(lo), "v"(hi)); return r; }
; template <bool F8OUT = false> __device__ __forceinline__ void head_tile_store(const f32x4 (&acc)[2][2][4][2], bf16_t* obase  , int opitch, const float* gain, float scale, const f32x2e* rope, int row0, int fq) {
;     ...
;             if (gain) {
;                 float ss = 0.f;
; #pragma unroll
;                 for (int bj = 0; bj < 2; ++bj)
; #pragma unroll
;                     for (int n = 0; n < 2; ++n) ss += (x[bj][n][0] * x[bj][n][0] + x[bj][n][1] * x[bj][n][1]) + (x[bj][n][2] * x[bj][n][2] + x[bj][n][3] * x[bj][n][3]);
;                 ss += __shfl_xor(ss, 16); ss += __shfl_xor(ss, 32);
;                 const float r = scale / sqrtf(ss * (1.f / 64.f) + 1e-6f);
; #pragma unroll
;                 for (int bj = 0; bj < 2; ++bj)
; #pragma unroll
;                     for (int n = 0; n < 2; ++n) x[bj][n] = x[bj][n] * r * g[bj][n];
;     ...
;             bf16_t* rowp = obase + (size_t)row * opitch + 8 * fq;
; #pragma unroll
;             for (int bj = 0; bj < 2; ++bj) { u32x4 w; w.x = cvt_pk_bf16(x[bj][0][0], x[bj][0][1]); w.y = cvt_pk_bf16(x[bj][0][2], x[bj][0][3]); w.z = cvt_pk_bf16(x[bj][1][0], x[bj][1][1]); w.w = cvt_pk_bf16(x[bj][1][2], x[bj][1][3]);
;                 *(u32x4*)(rowp + 32 * bj) = w; }
	v_pk_mul_f32 v[22:23], v[80:81], v[80:81]
	v_pk_mul_f32 v[24:25], v[78:79], v[78:79]
	s_nop 0
	v_pk_mov_b32 v[26:27], v[24:25], v[22:23] op_sel:[1,0]
	v_mov_b32_e32 v25, v23
	v_pk_add_f32 v[22:23], v[26:27], v[24:25]
	v_pk_mul_f32 v[24:25], v[76:77], v[76:77]
	v_pk_mul_f32 v[26:27], v[74:75], v[74:75]
	v_pk_add_f32 v[22:23], v[22:23], v[22:23] op_sel:[0,1] op_sel_hi:[1,0]
	v_pk_mov_b32 v[28:29], v[26:27], v[24:25] op_sel:[1,0]
	v_mov_b32_e32 v27, v25
	v_pk_add_f32 v[24:25], v[28:29], v[26:27]
	v_mul_f32_e32 v26, v66, v66
	v_mul_f32_e32 v27, v67, v67
	v_pk_add_f32 v[24:25], v[24:25], v[24:25] op_sel:[0,1] op_sel_hi:[1,0]
	v_mov_b32_e32 v23, v26
	v_mov_b32_e32 v25, v27
	v_pk_add_f32 v[22:23], v[22:23], v[24:25]
	v_mul_f32_e32 v24, v71, v71
	v_mul_f32_e32 v26, v73, v73
	v_mul_f32_e32 v28, v68, v68
	v_mul_f32_e32 v29, v69, v69
	v_pk_fma_f32 v[24:25], v[70:71], v[70:71], v[24:25] op_sel_hi:[1,1,0]
	v_pk_fma_f32 v[26:27], v[72:73], v[72:73], v[26:27] op_sel_hi:[1,1,0]
	v_mov_b32_e32 v25, v28
	v_mov_b32_e32 v27, v29
	v_pk_add_f32 v[24:25], v[24:25], v[26:27]
	s_nop 0
	v_pk_add_f32 v[22:23], v[22:23], v[24:25]
	v_and_b32_e32 v24, 64, v212
	v_add_f32_e32 v22, v22, v23
	v_xor_b32_e32 v23, 16, v212
	v_add_u32_e32 v24, 64, v24
	v_cmp_lt_i32_e32 vcc, v23, v24
	s_nop 1
	v_cndmask_b32_e32 v23, v212, v23, vcc
	v_lshlrev_b32_e32 v23, 2, v23
	v_mov_b32_e32 v23, v22
	s_nop 1
	v_permlane16_swap_b32_e32 v22, v23
	s_waitcnt lgkmcnt(0)
	v_add_f32_e32 v22, v22, v23
	v_xor_b32_e32 v23, 32, v212
	v_cmp_lt_i32_e32 vcc, v23, v24
	s_nop 1
	v_cndmask_b32_e32 v23, v212, v23, vcc
	v_lshlrev_b32_e32 v23, 2, v23
	v_mov_b32_e32 v23, v22
	s_nop 1
	v_permlane32_swap_b32_e32 v22, v23
	s_waitcnt lgkmcnt(0)
	v_add_f32_e32 v22, v22, v23
	v_fmamk_f32 v22, v22, 0x3c800000, v210
	v_mul_f32_e32 v23, 0x4f800000, v22
	v_cmp_gt_f32_e32 vcc, s28, v22
	s_nop 1
	v_cndmask_b32_e32 v22, v22, v23, vcc
	v_sqrt_f32_e32 v23, v22
	s_nop 0
	v_add_u32_e32 v24, -1, v23
	v_fma_f32 v25, -v24, v23, v22
	v_cmp_ge_f32_e64 s[6:7], 0, v25
	v_add_u32_e32 v25, 1, v23
	s_nop 0
	v_cndmask_b32_e64 v24, v23, v24, s[6:7]
	v_fma_f32 v23, -v25, v23, v22
	v_cmp_lt_f32_e64 s[6:7], 0, v23
	s_nop 1
	v_cndmask_b32_e64 v23, v24, v25, s[6:7]
	v_mul_f32_e32 v24, 0x37800000, v23
	v_cndmask_b32_e32 v23, v23, v24, vcc
	v_cmp_class_f32_e32 vcc, v22, v211
	s_nop 1
	v_cndmask_b32_e32 v22, v23, v22, vcc
	v_div_scale_f32 v23, s[0:1], v22, v22, 1.0
	v_rcp_f32_e32 v24, v23
	s_nop 0
	v_fma_f32 v25, -v23, v24, 1.0
	v_fmac_f32_e32 v24, v25, v24
	v_div_scale_f32 v25, vcc, 1.0, v22, 1.0
	v_mul_f32_e32 v26, v25, v24
	v_fma_f32 v27, -v23, v26, v25
	v_fmac_f32_e32 v26, v27, v24
	v_fma_f32 v23, -v23, v26, v25
	v_div_fmas_f32 v23, v23, v24, v26
	v_div_fixup_f32 v22, v23, v22, 1.0
	v_pk_mul_f32 v[24:25], v[78:79], v[22:23] op_sel_hi:[1,0]
	v_pk_mul_f32 v[26:27], v[80:81], v[22:23] op_sel_hi:[1,0]
	s_waitcnt vmcnt(0)
	v_pk_mul_f32 v[164:165], v[14:15], v[24:25]
	v_pk_mul_f32 v[32:33], v[16:17], v[26:27]
	v_pk_mul_f32 v[24:25], v[74:75], v[22:23] op_sel_hi:[1,0]
	v_pk_mul_f32 v[26:27], v[76:77], v[22:23] op_sel_hi:[1,0]
	v_pk_mul_f32 v[186:187], v[6:7], v[24:25]
	v_pk_mul_f32 v[162:163], v[8:9], v[26:27]
	v_pk_mul_f32 v[26:27], v[70:71], v[22:23] op_sel_hi:[1,0]
	v_pk_mul_f32 v[24:25], v[72:73], v[22:23] op_sel_hi:[1,0]
	v_pk_mul_f32 v[30:31], v[66:67], v[22:23] op_sel_hi:[1,0]
	v_pk_mul_f32 v[22:23], v[68:69], v[22:23] op_sel_hi:[1,0]
	v_pk_mul_f32 v[24:25], v[12:13], v[24:25]
	v_pk_mul_f32 v[28:29], v[10:11], v[26:27]
	v_pk_mul_f32 v[26:27], v[4:5], v[22:23]
	v_pk_mul_f32 v[30:31], v[2:3], v[30:31]
.LBB0_254:
	v_lshlrev_b64 v[22:23], 10, v[18:19]
	v_lshl_add_u64 v[22:23], v[20:21], 0, v[22:23]
	v_cvt_pk_bf16_f32 v188, v164, v165
	v_cvt_pk_bf16_f32 v189, v32, v33
	v_add_co_u32_e32 v32, vcc, 0x24000, v22
	v_lshl_add_u64 v[192:193], v[22:23], 0, s[30:31]
	s_nop 0
	v_addc_co_u32_e32 v33, vcc, 0, v23, vcc
	v_cvt_pk_bf16_f32 v190, v186, v187
	v_cvt_pk_bf16_f32 v191, v162, v163
	global_store_dwordx4 v[32:33], v[188:191], off
	v_cvt_pk_bf16_f32 v28, v28, v29
	v_cvt_pk_bf16_f32 v29, v24, v25
	v_cvt_pk_bf16_f32 v30, v30, v31
	v_cvt_pk_bf16_f32 v31, v26, v27
	global_store_dwordx4 v[192:193], v[28:31], off offset:64
	s_and_b64 vcc, exec, s[4:5]
	v_mov_b32_e32 v27, v53
	v_mov_b32_e32 v26, v52
	v_mov_b32_e32 v31, v51
	v_mov_b32_e32 v30, v50
	v_mov_b32_e32 v25, v57
	v_mov_b32_e32 v24, v56
	v_mov_b32_e32 v29, v55
	v_mov_b32_e32 v28, v54
	v_mov_b32_e32 v163, v61
	v_mov_b32_e32 v162, v60
	v_mov_b32_e32 v187, v59
	v_mov_b32_e32 v186, v58
	v_mov_b32_e32 v33, v65
	v_mov_b32_e32 v32, v64
	v_mov_b32_e32 v165, v63
	v_mov_b32_e32 v164, v62
	s_cbranch_vccnz .LBB0_256
; template <bool F8OUT = false> __device__ __forceinline__ void head_tile_store(const f32x4 (&acc)[2][2][4][2], bf16_t* obase  , int opitch, const float* gain, float scale, const f32x2e* rope, int row0, int fq) {
;     ...
;             if (gain) {
;                 float ss = 0.f;
; #pragma unroll
;                 for (int bj = 0; bj < 2; ++bj)
; #pragma unroll
;                     for (int n = 0; n < 2; ++n) ss += (x[bj][n][0] * x[bj][n][0] + x[bj][n][1] * x[bj][n][1]) + (x[bj][n][2] * x[bj][n][2] + x[bj][n][3] * x[bj][n][3]);
;                 ss += __shfl_xor(ss, 16); ss += __shfl_xor(ss, 32);
;                 const float r = scale / sqrtf(ss * (1.f / 64.f) + 1e-6f);
; #pragma unroll
;                 for (int bj = 0; bj < 2; ++bj)
; #pragma unroll
;                     for (int n = 0; n < 2; ++n) x[bj][n] = x[bj][n] * r * g[bj][n];
	v_pk_mul_f32 v[24:25], v[64:65], v[64:65]
	v_pk_mul_f32 v[26:27], v[62:63], v[62:63]
	s_nop 0
	v_pk_mov_b32 v[28:29], v[26:27], v[24:25] op_sel:[1,0]
	v_mov_b32_e32 v27, v25
	v_pk_add_f32 v[24:25], v[28:29], v[26:27]
	v_pk_mul_f32 v[26:27], v[60:61], v[60:61]
	v_pk_mul_f32 v[28:29], v[58:59], v[58:59]
	v_pk_add_f32 v[24:25], v[24:25], v[24:25] op_sel:[0,1] op_sel_hi:[1,0]
	v_pk_mov_b32 v[30:31], v[28:29], v[26:27] op_sel:[1,0]
	v_mov_b32_e32 v29, v27
	v_pk_add_f32 v[26:27], v[30:31], v[28:29]
	v_mul_f32_e32 v28, v50, v50
	v_mul_f32_e32 v29, v51, v51
	v_pk_add_f32 v[26:27], v[26:27], v[26:27] op_sel:[0,1] op_sel_hi:[1,0]
	v_mov_b32_e32 v25, v28
	v_mov_b32_e32 v27, v29
	v_pk_add_f32 v[24:25], v[24:25], v[26:27]
	v_mul_f32_e32 v26, v55, v55
	v_mul_f32_e32 v28, v57, v57
	v_mul_f32_e32 v30, v52, v52
	v_mul_f32_e32 v31, v53, v53
	v_pk_fma_f32 v[26:27], v[54:55], v[54:55], v[26:27] op_sel_hi:[1,1,0]
	v_pk_fma_f32 v[28:29], v[56:57], v[56:57], v[28:29] op_sel_hi:[1,1,0]
	v_mov_b32_e32 v27, v30
	v_mov_b32_e32 v29, v31
	v_pk_add_f32 v[26:27], v[26:27], v[28:29]
	s_nop 0
	v_pk_add_f32 v[24:25], v[24:25], v[26:27]
	v_and_b32_e32 v26, 64, v212
	v_add_f32_e32 v24, v24, v25
	v_xor_b32_e32 v25, 16, v212
	v_add_u32_e32 v26, 64, v26
	v_cmp_lt_i32_e32 vcc, v25, v26
	s_nop 1
	v_cndmask_b32_e32 v25, v212, v25, vcc
	v_lshlrev_b32_e32 v25, 2, v25
	v_mov_b32_e32 v25, v24
	s_nop 1
	v_permlane16_swap_b32_e32 v24, v25
	s_waitcnt lgkmcnt(0)
	v_add_f32_e32 v24, v24, v25
	v_xor_b32_e32 v25, 32, v212
	v_cmp_lt_i32_e32 vcc, v25, v26
	s_nop 1
	v_cndmask_b32_e32 v25, v212, v25, vcc
	v_lshlrev_b32_e32 v25, 2, v25
	v_mov_b32_e32 v25, v24
	s_nop 1
	v_permlane32_swap_b32_e32 v24, v25
	s_waitcnt lgkmcnt(0)
	v_add_f32_e32 v24, v24, v25
	v_fmamk_f32 v24, v24, 0x3c800000, v210
	v_mul_f32_e32 v25, 0x4f800000, v24
	v_cmp_gt_f32_e32 vcc, s28, v24
	s_nop 1
	v_cndmask_b32_e32 v24, v24, v25, vcc
	v_sqrt_f32_e32 v25, v24
	s_nop 0
	v_add_u32_e32 v26, -1, v25
	v_fma_f32 v27, -v26, v25, v24
	v_cmp_ge_f32_e64 s[6:7], 0, v27
	v_add_u32_e32 v27, 1, v25
	s_nop 0
	v_cndmask_b32_e64 v26, v25, v26, s[6:7]
	v_fma_f32 v25, -v27, v25, v24
	v_cmp_lt_f32_e64 s[6:7], 0, v25
	s_nop 1
	v_cndmask_b32_e64 v25, v26, v27, s[6:7]
	v_mul_f32_e32 v26, 0x37800000, v25
	v_cndmask_b32_e32 v25, v25, v26, vcc
	v_cmp_class_f32_e32 vcc, v24, v211
	s_nop 1
	v_cndmask_b32_e32 v24, v25, v24, vcc
	v_div_scale_f32 v25, s[0:1], v24, v24, 1.0
	v_rcp_f32_e32 v26, v25
	s_nop 0
	v_fma_f32 v27, -v25, v26, 1.0
	v_fmac_f32_e32 v26, v27, v26
	v_div_scale_f32 v27, vcc, 1.0, v24, 1.0
	v_mul_f32_e32 v28, v27, v26
	v_fma_f32 v29, -v25, v28, v27
	v_fmac_f32_e32 v28, v29, v26
	v_fma_f32 v25, -v25, v28, v27
	v_div_fmas_f32 v25, v25, v26, v28
	v_div_fixup_f32 v26, v25, v24, 1.0
	v_pk_mul_f32 v[24:25], v[62:63], v[26:27] op_sel_hi:[1,0]
	v_pk_mul_f32 v[28:29], v[64:65], v[26:27] op_sel_hi:[1,0]
	s_waitcnt vmcnt(0)
	v_pk_mul_f32 v[164:165], v[14:15], v[24:25]
	v_pk_mul_f32 v[32:33], v[16:17], v[28:29]
	v_pk_mul_f32 v[24:25], v[58:59], v[26:27] op_sel_hi:[1,0]
	v_pk_mul_f32 v[28:29], v[60:61], v[26:27] op_sel_hi:[1,0]
	v_pk_mul_f32 v[186:187], v[6:7], v[24:25]
	v_pk_mul_f32 v[162:163], v[8:9], v[28:29]
	v_pk_mul_f32 v[28:29], v[54:55], v[26:27] op_sel_hi:[1,0]
	v_pk_mul_f32 v[24:25], v[56:57], v[26:27] op_sel_hi:[1,0]
	v_pk_mul_f32 v[30:31], v[50:51], v[26:27] op_sel_hi:[1,0]
	v_pk_mul_f32 v[26:27], v[52:53], v[26:27] op_sel_hi:[1,0]
	v_pk_mul_f32 v[24:25], v[12:13], v[24:25]
	v_pk_mul_f32 v[28:29], v[10:11], v[28:29]
	v_pk_mul_f32 v[26:27], v[4:5], v[26:27]
	v_pk_mul_f32 v[30:31], v[2:3], v[30:31]
; __device__ __forceinline__ unsigned cvt_pk_bf16(float lo, float hi) { unsigned r; asm volatile("v_cvt_pk_bf16_f32 %0, %1, %2" : "=v"(r) : "v"(lo), "v"(hi)); return r; }
; template <bool F8OUT = false> __device__ __forceinline__ void head_tile_store(const f32x4 (&acc)[2][2][4][2], bf16_t* obase  , int opitch, const float* gain, float scale, const f32x2e* rope, int row0, int fq) {
;     ...
;             if (gain) {
;                 float ss = 0.f;
; #pragma unroll
;                 for (int bj = 0; bj < 2; ++bj)
; #pragma unroll
;                     for (int n = 0; n < 2; ++n) ss += (x[bj][n][0] * x[bj][n][0] + x[bj][n][1] * x[bj][n][1]) + (x[bj][n][2] * x[bj][n][2] + x[bj][n][3] * x[bj][n][3]);
;                 ss += __shfl_xor(ss, 16); ss += __shfl_xor(ss, 32);
;                 const float r = scale / sqrtf(ss * (1.f / 64.f) + 1e-6f);
; #pragma unroll
;                 for (int bj = 0; bj < 2; ++bj)
; #pragma unroll
;                     for (int n = 0; n < 2; ++n) x[bj][n] = x[bj][n] * r * g[bj][n];
;     ...
;             bf16_t* rowp = obase + (size_t)row * opitch + 8 * fq;
; #pragma unroll
;             for (int bj = 0; bj < 2; ++bj) { u32x4 w; w.x = cvt_pk_bf16(x[bj][0][0], x[bj][0][1]); w.y = cvt_pk_bf16(x[bj][0][2], x[bj][0][3]); w.z = cvt_pk_bf16(x[bj][1][0], x[bj][1][1]); w.w = cvt_pk_bf16(x[bj][1][2], x[bj][1][3]);
;                 *(u32x4*)(rowp + 32 * bj) = w; }
.LBB0_256:
	v_lshl_add_u64 v[192:193], v[22:23], 0, s[12:13]
	v_add_co_u32_e32 v22, vcc, 0x28000, v22
	v_cvt_pk_bf16_f32 v188, v164, v165
	v_cvt_pk_bf16_f32 v189, v32, v33
	v_cvt_pk_bf16_f32 v190, v186, v187
	v_cvt_pk_bf16_f32 v191, v162, v163
	s_nop 1
	v_addc_co_u32_e32 v23, vcc, 0, v23, vcc
	global_store_dwordx4 v[22:23], v[188:191], off
	v_cvt_pk_bf16_f32 v22, v28, v29
	v_cvt_pk_bf16_f32 v23, v24, v25
	v_cvt_pk_bf16_f32 v24, v30, v31
	v_cvt_pk_bf16_f32 v25, v26, v27
	global_store_dwordx4 v[192:193], v[22:25], off offset:64
	s_and_b64 vcc, exec, s[4:5]
	v_mov_b32_e32 v27, v35
	v_mov_b32_e32 v23, v37
	v_mov_b32_e32 v22, v36
	v_mov_b32_e32 v26, v34
	v_mov_b32_e32 v25, v41
	v_mov_b32_e32 v24, v40
	v_mov_b32_e32 v29, v39
	v_mov_b32_e32 v28, v38
	v_mov_b32_e32 v31, v45
	v_mov_b32_e32 v30, v44
	v_mov_b32_e32 v163, v43
	v_mov_b32_e32 v162, v42
	v_mov_b32_e32 v33, v49
	v_mov_b32_e32 v32, v48
	v_mov_b32_e32 v165, v47
	v_mov_b32_e32 v164, v46
	s_cbranch_vccnz .LBB0_258
	v_pk_mul_f32 v[22:23], v[48:49], v[48:49]
	v_pk_mul_f32 v[24:25], v[46:47], v[46:47]
	s_nop 0
	v_pk_mov_b32 v[26:27], v[24:25], v[22:23] op_sel:[1,0]
	v_mov_b32_e32 v25, v23
	v_pk_add_f32 v[22:23], v[26:27], v[24:25]
	v_pk_mul_f32 v[24:25], v[44:45], v[44:45]
	v_pk_mul_f32 v[26:27], v[42:43], v[42:43]
	v_pk_add_f32 v[22:23], v[22:23], v[22:23] op_sel:[0,1] op_sel_hi:[1,0]
	v_pk_mov_b32 v[28:29], v[26:27], v[24:25] op_sel:[1,0]
	v_mov_b32_e32 v27, v25
	v_pk_add_f32 v[24:25], v[28:29], v[26:27]
	v_mul_f32_e32 v26, v34, v34
	v_mul_f32_e32 v27, v35, v35
	v_pk_add_f32 v[24:25], v[24:25], v[24:25] op_sel:[0,1] op_sel_hi:[1,0]
	v_mov_b32_e32 v23, v26
	v_mov_b32_e32 v25, v27
	v_pk_add_f32 v[22:23], v[22:23], v[24:25]
	v_mul_f32_e32 v24, v39, v39
	v_mul_f32_e32 v26, v41, v41
	v_mul_f32_e32 v28, v36, v36
	v_mul_f32_e32 v29, v37, v37
	v_pk_fma_f32 v[24:25], v[38:39], v[38:39], v[24:25] op_sel_hi:[1,1,0]
	v_pk_fma_f32 v[26:27], v[40:41], v[40:41], v[26:27] op_sel_hi:[1,1,0]
	v_mov_b32_e32 v25, v28
	v_mov_b32_e32 v27, v29
	v_pk_add_f32 v[24:25], v[24:25], v[26:27]
	s_nop 0
	v_pk_add_f32 v[22:23], v[22:23], v[24:25]
	v_and_b32_e32 v24, 64, v212
	v_add_f32_e32 v22, v22, v23
	v_xor_b32_e32 v23, 16, v212
	v_add_u32_e32 v24, 64, v24
	v_cmp_lt_i32_e32 vcc, v23, v24
	s_nop 1
	v_cndmask_b32_e32 v23, v212, v23, vcc
	v_lshlrev_b32_e32 v23, 2, v23
	v_mov_b32_e32 v23, v22
	s_nop 1
	v_permlane16_swap_b32_e32 v22, v23
	s_waitcnt lgkmcnt(0)
	v_add_f32_e32 v22, v22, v23
	v_xor_b32_e32 v23, 32, v212
	v_cmp_lt_i32_e32 vcc, v23, v24
	s_nop 1
	v_cndmask_b32_e32 v23, v212, v23, vcc
	v_lshlrev_b32_e32 v23, 2, v23
	v_mov_b32_e32 v23, v22
	s_nop 1
	v_permlane32_swap_b32_e32 v22, v23
	s_waitcnt lgkmcnt(0)
	v_add_f32_e32 v22, v22, v23
	v_fmamk_f32 v22, v22, 0x3c800000, v210
	v_mul_f32_e32 v23, 0x4f800000, v22
	v_cmp_gt_f32_e32 vcc, s28, v22
	s_nop 1
	v_cndmask_b32_e32 v22, v22, v23, vcc
	v_sqrt_f32_e32 v23, v22
	s_nop 0
	v_add_u32_e32 v24, -1, v23
	v_fma_f32 v25, -v24, v23, v22
	v_cmp_ge_f32_e64 s[4:5], 0, v25
	v_add_u32_e32 v25, 1, v23
	s_nop 0
	v_cndmask_b32_e64 v24, v23, v24, s[4:5]
	v_fma_f32 v23, -v25, v23, v22
	v_cmp_lt_f32_e64 s[4:5], 0, v23
	s_nop 1
	v_cndmask_b32_e64 v23, v24, v25, s[4:5]
	v_mul_f32_e32 v24, 0x37800000, v23
	v_cndmask_b32_e32 v23, v23, v24, vcc
	v_cmp_class_f32_e32 vcc, v22, v211
	s_nop 1
	v_cndmask_b32_e32 v22, v23, v22, vcc
	v_div_scale_f32 v23, s[0:1], v22, v22, 1.0
	v_rcp_f32_e32 v24, v23
	s_nop 0
	v_fma_f32 v25, -v23, v24, 1.0
	v_fmac_f32_e32 v24, v25, v24
	v_div_scale_f32 v25, vcc, 1.0, v22, 1.0
	v_mul_f32_e32 v26, v25, v24
	v_fma_f32 v27, -v23, v26, v25
	v_fmac_f32_e32 v26, v27, v24
	v_fma_f32 v23, -v23, v26, v25
	v_div_fmas_f32 v23, v23, v24, v26
	v_div_fixup_f32 v22, v23, v22, 1.0
	v_pk_mul_f32 v[24:25], v[46:47], v[22:23] op_sel_hi:[1,0]
	v_pk_mul_f32 v[26:27], v[48:49], v[22:23] op_sel_hi:[1,0]
	s_waitcnt vmcnt(0)
	v_pk_mul_f32 v[164:165], v[14:15], v[24:25]
	v_pk_mul_f32 v[32:33], v[16:17], v[26:27]
	v_pk_mul_f32 v[14:15], v[42:43], v[22:23] op_sel_hi:[1,0]
	v_pk_mul_f32 v[16:17], v[44:45], v[22:23] op_sel_hi:[1,0]
	v_pk_mul_f32 v[162:163], v[6:7], v[14:15]
	v_pk_mul_f32 v[30:31], v[8:9], v[16:17]
	v_pk_mul_f32 v[6:7], v[38:39], v[22:23] op_sel_hi:[1,0]
	v_pk_mul_f32 v[8:9], v[40:41], v[22:23] op_sel_hi:[1,0]
	v_pk_mul_f32 v[28:29], v[10:11], v[6:7]
	v_pk_mul_f32 v[24:25], v[12:13], v[8:9]
	v_pk_mul_f32 v[6:7], v[34:35], v[22:23] op_sel_hi:[1,0]
	v_pk_mul_f32 v[8:9], v[36:37], v[22:23] op_sel_hi:[1,0]
	v_pk_mul_f32 v[26:27], v[2:3], v[6:7]
	v_pk_mul_f32 v[22:23], v[4:5], v[8:9]

; template <bool F8OUT = false> __device__ __forceinline__ void head_tile_store(const f32x4 (&acc)[2][2][4][2], bf16_t* obase  , int opitch, const float* gain, float scale, const f32x2e* rope, int row0, int fq) {
;     ...
;             if (gain) {
;                 float ss = 0.f;
; #pragma unroll
;                 for (int bj = 0; bj < 2; ++bj)
; #pragma unroll
;                     for (int n = 0; n < 2; ++n) ss += (x[bj][n][0] * x[bj][n][0] + x[bj][n][1] * x[bj][n][1]) + (x[bj][n][2] * x[bj][n][2] + x[bj][n][3] * x[bj][n][3]);
;                 ss += __shfl_xor(ss, 16); ss += __shfl_xor(ss, 32);
;                 const float r = scale / sqrtf(ss * (1.f / 64.f) + 1e-6f);
; #pragma unroll
;                 for (int bj = 0; bj < 2; ++bj)
; #pragma unroll
;                     for (int n = 0; n < 2; ++n) x[bj][n] = x[bj][n] * r * g[bj][n];
;             }
;             if (rope) {
;                 const int t = row & 8191; const bool second = (fq & 2) != 0;
; #pragma unroll
;                 for (int bj = 0; bj < 2; ++bj) { const int pos = bj ? (t & 63) : (t >> 6); const f32x2e* tb = rope + pos * 16 + 8 * (fq & 1);
; #pragma unroll
;                     for (int n = 0; n < 2; ++n)
; #pragma unroll
;                         for (int e = 0; e < 4; ++e) { const float p = __shfl_xor(x[bj][n][e], 32); const f32x2e cs = tb[4 * n + e]; const float v = x[bj][n][e];
;                             x[bj][n][e] = second ? (p * cs.y + v * cs.x) : (v * cs.x - p * cs.y); } }
;             }
;             if constexpr (F8OUT) { unsigned char* rowp8 = (unsigned char*)obase + (size_t)row * opitch + 8 * fq; typedef unsigned u32x2_ __attribute__((ext_vector_type(2)));
; #pragma unroll
;                 for (int bj = 0; bj < 2; ++bj) *(u32x2_*)(rowp8 + 32 * bj) = (u32x2_){pk4_fp8(x[bj][0][0], x[bj][0][1], x[bj][0][2], x[bj][0][3]), pk4_fp8(x[bj][1][0], x[bj][1][1], x[bj][1][2], x[bj][1][3])};
;                 continue; }
;             bf16_t* rowp = obase + (size_t)row * opitch + 8 * fq;
; #pragma unroll
;             for (int bj = 0; bj < 2; ++bj) { u32x4 w; w.x = cvt_pk_bf16(x[bj][0][0], x[bj][0][1]); w.y = cvt_pk_bf16(x[bj][0][2], x[bj][0][3]); w.z = cvt_pk_bf16(x[bj][1][0], x[bj][1][1]); w.w = cvt_pk_bf16(x[bj][1][2], x[bj][1][3]);
;                 *(u32x4*)(rowp + 32 * bj) = w; }
.LBB0_264:
	s_and_b64 vcc, exec, s[4:5]
	s_cbranch_vccnz .LBB0_266
	v_pk_mul_f32 v[20:21], v[160:161], v[160:161]
	v_pk_mul_f32 v[22:23], v[158:159], v[158:159]
	s_nop 0
	v_pk_mov_b32 v[24:25], v[22:23], v[20:21] op_sel:[1,0]
	v_mov_b32_e32 v23, v21
	v_pk_add_f32 v[20:21], v[24:25], v[22:23]
	v_pk_mul_f32 v[22:23], v[156:157], v[156:157]
	v_pk_mul_f32 v[24:25], v[154:155], v[154:155]
	v_pk_add_f32 v[20:21], v[20:21], v[20:21] op_sel:[0,1] op_sel_hi:[1,0]
	v_pk_mov_b32 v[26:27], v[24:25], v[22:23] op_sel:[1,0]
	v_mov_b32_e32 v25, v23
	v_pk_add_f32 v[22:23], v[26:27], v[24:25]
	v_mul_f32_e32 v24, v146, v146
	v_mul_f32_e32 v25, v147, v147
	v_pk_add_f32 v[22:23], v[22:23], v[22:23] op_sel:[0,1] op_sel_hi:[1,0]
	v_mov_b32_e32 v21, v24
	v_mov_b32_e32 v23, v25
	v_pk_add_f32 v[20:21], v[20:21], v[22:23]
	v_mul_f32_e32 v22, v151, v151
	v_mul_f32_e32 v24, v153, v153
	v_mul_f32_e32 v26, v148, v148
	v_mul_f32_e32 v27, v149, v149
	v_pk_fma_f32 v[22:23], v[150:151], v[150:151], v[22:23] op_sel_hi:[1,1,0]
	v_pk_fma_f32 v[24:25], v[152:153], v[152:153], v[24:25] op_sel_hi:[1,1,0]
	v_mov_b32_e32 v23, v26
	v_mov_b32_e32 v25, v27
	v_pk_add_f32 v[22:23], v[22:23], v[24:25]
	s_nop 0
	v_pk_add_f32 v[20:21], v[20:21], v[22:23]
	v_and_b32_e32 v22, 64, v212
	v_add_f32_e32 v20, v20, v21
	v_xor_b32_e32 v21, 16, v212
	v_add_u32_e32 v22, 64, v22
	v_cmp_lt_i32_e32 vcc, v21, v22
	s_nop 1
	v_cndmask_b32_e32 v21, v212, v21, vcc
	v_lshlrev_b32_e32 v21, 2, v21
	v_mov_b32_e32 v21, v20
	s_nop 1
	v_permlane16_swap_b32_e32 v20, v21
	s_waitcnt lgkmcnt(0)
	v_add_f32_e32 v20, v20, v21
	v_xor_b32_e32 v21, 32, v212
	v_cmp_lt_i32_e32 vcc, v21, v22
	s_nop 1
	v_cndmask_b32_e32 v21, v212, v21, vcc
	v_lshlrev_b32_e32 v21, 2, v21
	v_mov_b32_e32 v21, v20
	s_nop 1
	v_permlane32_swap_b32_e32 v20, v21
	s_waitcnt lgkmcnt(0)
	v_add_f32_e32 v20, v20, v21
	v_fmamk_f32 v20, v20, 0x3c800000, v210
	v_mul_f32_e32 v21, 0x4f800000, v20
	v_cmp_gt_f32_e32 vcc, s28, v20
	s_nop 1
	v_cndmask_b32_e32 v20, v20, v21, vcc
	v_sqrt_f32_e32 v21, v20
	s_nop 0
	v_add_u32_e32 v22, -1, v21
	v_fma_f32 v23, -v22, v21, v20
	v_cmp_ge_f32_e64 s[6:7], 0, v23
	v_add_u32_e32 v23, 1, v21
	s_nop 0
	v_cndmask_b32_e64 v22, v21, v22, s[6:7]
	v_fma_f32 v21, -v23, v21, v20
	v_cmp_lt_f32_e64 s[6:7], 0, v21
	s_nop 1
	v_cndmask_b32_e64 v21, v22, v23, s[6:7]
	v_mul_f32_e32 v22, 0x37800000, v21
	v_cndmask_b32_e32 v21, v21, v22, vcc
	v_cmp_class_f32_e32 vcc, v20, v211
	s_nop 1
	v_cndmask_b32_e32 v20, v21, v20, vcc
	v_div_scale_f32 v21, s[0:1], v20, v20, s25
	v_rcp_f32_e32 v22, v21
	s_nop 0
	v_fma_f32 v23, -v21, v22, 1.0
	v_fmac_f32_e32 v22, v23, v22
	v_div_scale_f32 v23, vcc, s25, v20, s25
	v_mul_f32_e32 v24, v23, v22
	v_fma_f32 v25, -v21, v24, v23
	v_fmac_f32_e32 v24, v25, v22
	v_fma_f32 v21, -v21, v24, v23
	v_div_fmas_f32 v21, v21, v22, v24
	v_div_fixup_f32 v20, v21, v20, s25
	v_pk_mul_f32 v[22:23], v[158:159], v[20:21] op_sel_hi:[1,0]
	v_pk_mul_f32 v[24:25], v[160:161], v[20:21] op_sel_hi:[1,0]
	s_waitcnt vmcnt(0)
	v_pk_mul_f32 v[158:159], v[14:15], v[22:23]
	v_pk_mul_f32 v[22:23], v[154:155], v[20:21] op_sel_hi:[1,0]
	v_pk_mul_f32 v[160:161], v[16:17], v[24:25]
	v_pk_mul_f32 v[24:25], v[156:157], v[20:21] op_sel_hi:[1,0]
	v_pk_mul_f32 v[154:155], v[6:7], v[22:23]
	v_pk_mul_f32 v[22:23], v[150:151], v[20:21] op_sel_hi:[1,0]
	v_pk_mul_f32 v[156:157], v[8:9], v[24:25]
	v_pk_mul_f32 v[24:25], v[152:153], v[20:21] op_sel_hi:[1,0]
	v_pk_mul_f32 v[150:151], v[10:11], v[22:23]
	v_pk_mul_f32 v[22:23], v[146:147], v[20:21] op_sel_hi:[1,0]
	v_pk_mul_f32 v[20:21], v[148:149], v[20:21] op_sel_hi:[1,0]
	v_pk_mul_f32 v[152:153], v[12:13], v[24:25]
	v_pk_mul_f32 v[148:149], v[4:5], v[20:21]
	v_pk_mul_f32 v[146:147], v[2:3], v[22:23]
.LBB0_266:
	s_lshl_b32 s0, s18, 7
	s_add_u32 s0, s8, s0
	s_addc_u32 s1, s9, 0
	v_ashrrev_i32_e32 v185, 31, v184
	v_lshl_add_u64 v[18:19], v[18:19], 1, s[0:1]
	v_lshlrev_b64 v[20:21], 10, v[184:185]
	v_lshl_add_u64 v[20:21], v[18:19], 0, v[20:21]
	v_cvt_pk_bf16_f32 v22, v158, v159
	v_cvt_pk_bf16_f32 v23, v160, v161
	v_cvt_pk_bf16_f32 v24, v154, v155
	v_cvt_pk_bf16_f32 v25, v156, v157
	s_and_b64 vcc, exec, s[4:5]
	global_store_dwordx4 v[20:21], v[22:25], off
	s_nop 1
	v_cvt_pk_bf16_f32 v22, v150, v151
	v_cvt_pk_bf16_f32 v23, v152, v153
	v_cvt_pk_bf16_f32 v24, v146, v147
	v_cvt_pk_bf16_f32 v25, v148, v149
	global_store_dwordx4 v[20:21], v[22:25], off offset:64
	s_cbranch_vccnz .LBB0_268
; template <bool F8OUT = false> __device__ __forceinline__ void head_tile_store(const f32x4 (&acc)[2][2][4][2], bf16_t* obase  , int opitch, const float* gain, float scale, const f32x2e* rope, int row0, int fq) {
;     ...
;             if (gain) {
;                 float ss = 0.f;
; #pragma unroll
;                 for (int bj = 0; bj < 2; ++bj)
; #pragma unroll
;                     for (int n = 0; n < 2; ++n) ss += (x[bj][n][0] * x[bj][n][0] + x[bj][n][1] * x[bj][n][1]) + (x[bj][n][2] * x[bj][n][2] + x[bj][n][3] * x[bj][n][3]);
;                 ss += __shfl_xor(ss, 16); ss += __shfl_xor(ss, 32);
;                 const float r = scale / sqrtf(ss * (1.f / 64.f) + 1e-6f);
; #pragma unroll
;                 for (int bj = 0; bj < 2; ++bj)
; #pragma unroll
;                     for (int n = 0; n < 2; ++n) x[bj][n] = x[bj][n] * r * g[bj][n];
;             }
;             if (rope) {
;                 const int t = row & 8191; const bool second = (fq & 2) != 0;
; #pragma unroll
;                 for (int bj = 0; bj < 2; ++bj) { const int pos = bj ? (t & 63) : (t >> 6); const f32x2e* tb = rope + pos * 16 + 8 * (fq & 1);
; #pragma unroll
;                     for (int n = 0; n < 2; ++n)
; #pragma unroll
;                         for (int e = 0; e < 4; ++e) { const float p = __shfl_xor(x[bj][n][e], 32); const f32x2e cs = tb[4 * n + e]; const float v = x[bj][n][e];
;                             x[bj][n][e] = second ? (p * cs.y + v * cs.x) : (v * cs.x - p * cs.y); } }
;             }
;             if constexpr (F8OUT) { unsigned char* rowp8 = (unsigned char*)obase + (size_t)row * opitch + 8 * fq; typedef unsigned u32x2_ __attribute__((ext_vector_type(2)));
; #pragma unroll
;                 for (int bj = 0; bj < 2; ++bj) *(u32x2_*)(rowp8 + 32 * bj) = (u32x2_){pk4_fp8(x[bj][0][0], x[bj][0][1], x[bj][0][2], x[bj][0][3]), pk4_fp8(x[bj][1][0], x[bj][1][1], x[bj][1][2], x[bj][1][3])};
;                 continue; }
;             bf16_t* rowp = obase + (size_t)row * opitch + 8 * fq;
; #pragma unroll
;             for (int bj = 0; bj < 2; ++bj) { u32x4 w; w.x = cvt_pk_bf16(x[bj][0][0], x[bj][0][1]); w.y = cvt_pk_bf16(x[bj][0][2], x[bj][0][3]); w.z = cvt_pk_bf16(x[bj][1][0], x[bj][1][1]); w.w = cvt_pk_bf16(x[bj][1][2], x[bj][1][3]);
;                 *(u32x4*)(rowp + 32 * bj) = w; }
	s_nop 0
	v_pk_mul_f32 v[22:23], v[144:145], v[144:145]
	v_pk_mul_f32 v[24:25], v[142:143], v[142:143]
	s_nop 0
	v_pk_mov_b32 v[26:27], v[24:25], v[22:23] op_sel:[1,0]
	v_mov_b32_e32 v25, v23
	v_pk_add_f32 v[22:23], v[26:27], v[24:25]
	v_pk_mul_f32 v[24:25], v[140:141], v[140:141]
	v_pk_mul_f32 v[26:27], v[138:139], v[138:139]
	v_pk_add_f32 v[22:23], v[22:23], v[22:23] op_sel:[0,1] op_sel_hi:[1,0]
	v_pk_mov_b32 v[28:29], v[26:27], v[24:25] op_sel:[1,0]
	v_mov_b32_e32 v27, v25
	v_pk_add_f32 v[24:25], v[28:29], v[26:27]
	v_mul_f32_e32 v26, v130, v130
	v_mul_f32_e32 v27, v131, v131
	v_pk_add_f32 v[24:25], v[24:25], v[24:25] op_sel:[0,1] op_sel_hi:[1,0]
	v_mov_b32_e32 v23, v26
	v_mov_b32_e32 v25, v27
	v_pk_add_f32 v[22:23], v[22:23], v[24:25]
	v_mul_f32_e32 v24, v135, v135
	v_mul_f32_e32 v26, v137, v137
	v_mul_f32_e32 v28, v132, v132
	v_mul_f32_e32 v29, v133, v133
	v_pk_fma_f32 v[24:25], v[134:135], v[134:135], v[24:25] op_sel_hi:[1,1,0]
	v_pk_fma_f32 v[26:27], v[136:137], v[136:137], v[26:27] op_sel_hi:[1,1,0]
	v_mov_b32_e32 v25, v28
	v_mov_b32_e32 v27, v29
	v_pk_add_f32 v[24:25], v[24:25], v[26:27]
	s_nop 0
	v_pk_add_f32 v[22:23], v[22:23], v[24:25]
	v_and_b32_e32 v24, 64, v212
	v_add_f32_e32 v22, v22, v23
	v_xor_b32_e32 v23, 16, v212
	v_add_u32_e32 v24, 64, v24
	v_cmp_lt_i32_e32 vcc, v23, v24
	s_nop 1
	v_cndmask_b32_e32 v23, v212, v23, vcc
	v_lshlrev_b32_e32 v23, 2, v23
	v_mov_b32_e32 v23, v22
	s_nop 1
	v_permlane16_swap_b32_e32 v22, v23
	s_waitcnt lgkmcnt(0)
	v_add_f32_e32 v22, v22, v23
	v_xor_b32_e32 v23, 32, v212
	v_cmp_lt_i32_e32 vcc, v23, v24
	s_nop 1
	v_cndmask_b32_e32 v23, v212, v23, vcc
	v_lshlrev_b32_e32 v23, 2, v23
	v_mov_b32_e32 v23, v22
	s_nop 1
	v_permlane32_swap_b32_e32 v22, v23
	s_waitcnt lgkmcnt(0)
	v_add_f32_e32 v22, v22, v23
	v_fmamk_f32 v22, v22, 0x3c800000, v210
	v_mul_f32_e32 v23, 0x4f800000, v22
	v_cmp_gt_f32_e32 vcc, s28, v22
	s_nop 1
	v_cndmask_b32_e32 v22, v22, v23, vcc
	v_sqrt_f32_e32 v23, v22
	s_nop 0
	v_add_u32_e32 v24, -1, v23
	v_fma_f32 v25, -v24, v23, v22
	v_cmp_ge_f32_e64 s[6:7], 0, v25
	v_add_u32_e32 v25, 1, v23
	s_nop 0
	v_cndmask_b32_e64 v24, v23, v24, s[6:7]
	v_fma_f32 v23, -v25, v23, v22
	v_cmp_lt_f32_e64 s[6:7], 0, v23
	s_nop 1
	v_cndmask_b32_e64 v23, v24, v25, s[6:7]
	v_mul_f32_e32 v24, 0x37800000, v23
	v_cndmask_b32_e32 v23, v23, v24, vcc
	v_cmp_class_f32_e32 vcc, v22, v211
	s_nop 1
	v_cndmask_b32_e32 v22, v23, v22, vcc
	v_div_scale_f32 v23, s[0:1], v22, v22, s25
	v_rcp_f32_e32 v24, v23
	s_nop 0
	v_fma_f32 v25, -v23, v24, 1.0
	v_fmac_f32_e32 v24, v25, v24
	v_div_scale_f32 v25, vcc, s25, v22, s25
	v_mul_f32_e32 v26, v25, v24
	v_fma_f32 v27, -v23, v26, v25
	v_fmac_f32_e32 v26, v27, v24
	v_fma_f32 v23, -v23, v26, v25
	v_div_fmas_f32 v23, v23, v24, v26
	v_div_fixup_f32 v22, v23, v22, s25
	v_pk_mul_f32 v[24:25], v[142:143], v[22:23] op_sel_hi:[1,0]
	v_pk_mul_f32 v[26:27], v[144:145], v[22:23] op_sel_hi:[1,0]
	s_waitcnt vmcnt(0)
	v_pk_mul_f32 v[142:143], v[14:15], v[24:25]
	v_pk_mul_f32 v[24:25], v[138:139], v[22:23] op_sel_hi:[1,0]
	v_pk_mul_f32 v[144:145], v[16:17], v[26:27]
	v_pk_mul_f32 v[26:27], v[140:141], v[22:23] op_sel_hi:[1,0]
	v_pk_mul_f32 v[138:139], v[6:7], v[24:25]
	v_pk_mul_f32 v[24:25], v[134:135], v[22:23] op_sel_hi:[1,0]
	v_pk_mul_f32 v[140:141], v[8:9], v[26:27]
	v_pk_mul_f32 v[26:27], v[136:137], v[22:23] op_sel_hi:[1,0]
	v_pk_mul_f32 v[134:135], v[10:11], v[24:25]
	v_pk_mul_f32 v[24:25], v[130:131], v[22:23] op_sel_hi:[1,0]
	v_pk_mul_f32 v[22:23], v[132:133], v[22:23] op_sel_hi:[1,0]
	v_pk_mul_f32 v[136:137], v[12:13], v[26:27]
	v_pk_mul_f32 v[132:133], v[4:5], v[22:23]
	v_pk_mul_f32 v[130:131], v[2:3], v[24:25]
.LBB0_268:
	v_add_co_u32_e32 v28, vcc, 0x4000, v20
	v_lshl_add_u64 v[26:27], v[20:21], 0, s[92:93]
	s_nop 0
	v_addc_co_u32_e32 v29, vcc, 0, v21, vcc
	v_cvt_pk_bf16_f32 v22, v142, v143
	v_cvt_pk_bf16_f32 v23, v144, v145
	v_cvt_pk_bf16_f32 v24, v138, v139
	v_cvt_pk_bf16_f32 v25, v140, v141
	s_and_b64 vcc, exec, s[4:5]
	global_store_dwordx4 v[28:29], v[22:25], off
	s_nop 1
	v_cvt_pk_bf16_f32 v22, v134, v135
	v_cvt_pk_bf16_f32 v23, v136, v137
	v_cvt_pk_bf16_f32 v24, v130, v131
	v_cvt_pk_bf16_f32 v25, v132, v133
	global_store_dwordx4 v[26:27], v[22:25], off offset:64
	s_cbranch_vccnz .LBB0_270
	s_nop 0
	v_pk_mul_f32 v[22:23], v[128:129], v[128:129]
	v_pk_mul_f32 v[24:25], v[126:127], v[126:127]
	s_nop 0
	v_pk_mov_b32 v[26:27], v[24:25], v[22:23] op_sel:[1,0]
	v_mov_b32_e32 v25, v23
	v_pk_add_f32 v[22:23], v[26:27], v[24:25]
	v_pk_mul_f32 v[24:25], v[124:125], v[124:125]
	v_pk_mul_f32 v[26:27], v[122:123], v[122:123]
	v_pk_add_f32 v[22:23], v[22:23], v[22:23] op_sel:[0,1] op_sel_hi:[1,0]
	v_pk_mov_b32 v[28:29], v[26:27], v[24:25] op_sel:[1,0]
	v_mov_b32_e32 v27, v25
	v_pk_add_f32 v[24:25], v[28:29], v[26:27]
	v_mul_f32_e32 v26, v114, v114
	v_mul_f32_e32 v27, v115, v115
	v_pk_add_f32 v[24:25], v[24:25], v[24:25] op_sel:[0,1] op_sel_hi:[1,0]
	v_mov_b32_e32 v23, v26
	v_mov_b32_e32 v25, v27
	v_pk_add_f32 v[22:23], v[22:23], v[24:25]
	v_mul_f32_e32 v24, v119, v119
	v_mul_f32_e32 v26, v121, v121
	v_mul_f32_e32 v28, v116, v116
	v_mul_f32_e32 v29, v117, v117
	v_pk_fma_f32 v[24:25], v[118:119], v[118:119], v[24:25] op_sel_hi:[1,1,0]
	v_pk_fma_f32 v[26:27], v[120:121], v[120:121], v[26:27] op_sel_hi:[1,1,0]
	v_mov_b32_e32 v25, v28
	v_mov_b32_e32 v27, v29
	v_pk_add_f32 v[24:25], v[24:25], v[26:27]
	s_nop 0
	v_pk_add_f32 v[22:23], v[22:23], v[24:25]
	v_and_b32_e32 v24, 64, v212
	v_add_f32_e32 v22, v22, v23
	v_xor_b32_e32 v23, 16, v212
	v_add_u32_e32 v24, 64, v24
	v_cmp_lt_i32_e32 vcc, v23, v24
	s_nop 1
	v_cndmask_b32_e32 v23, v212, v23, vcc
	v_lshlrev_b32_e32 v23, 2, v23
	v_mov_b32_e32 v23, v22
	s_nop 1
	v_permlane16_swap_b32_e32 v22, v23
	s_waitcnt lgkmcnt(0)
; template <bool F8OUT = false> __device__ __forceinline__ void head_tile_store(const f32x4 (&acc)[2][2][4][2], bf16_t* obase  , int opitch, const float* gain, float scale, const f32x2e* rope, int row0, int fq) {
;     ...
;             if (gain) {
;                 float ss = 0.f;
; #pragma unroll
;                 for (int bj = 0; bj < 2; ++bj)
; #pragma unroll
;                     for (int n = 0; n < 2; ++n) ss += (x[bj][n][0] * x[bj][n][0] + x[bj][n][1] * x[bj][n][1]) + (x[bj][n][2] * x[bj][n][2] + x[bj][n][3] * x[bj][n][3]);
;                 ss += __shfl_xor(ss, 16); ss += __shfl_xor(ss, 32);
;                 const float r = scale / sqrtf(ss * (1.f / 64.f) + 1e-6f);
; #pragma unroll
;                 for (int bj = 0; bj < 2; ++bj)
; #pragma unroll
;                     for (int n = 0; n < 2; ++n) x[bj][n] = x[bj][n] * r * g[bj][n];
;             }
;             if (rope) {
;                 const int t = row & 8191; const bool second = (fq & 2) != 0;
; #pragma unroll
;                 for (int bj = 0; bj < 2; ++bj) { const int pos = bj ? (t & 63) : (t >> 6); const f32x2e* tb = rope + pos * 16 + 8 * (fq & 1);
; #pragma unroll
;                     for (int n = 0; n < 2; ++n)
; #pragma unroll
;                         for (int e = 0; e < 4; ++e) { const float p = __shfl_xor(x[bj][n][e], 32); const f32x2e cs = tb[4 * n + e]; const float v = x[bj][n][e];
;                             x[bj][n][e] = second ? (p * cs.y + v * cs.x) : (v * cs.x - p * cs.y); } }
;             }
;             if constexpr (F8OUT) { unsigned char* rowp8 = (unsigned char*)obase + (size_t)row * opitch + 8 * fq; typedef unsigned u32x2_ __attribute__((ext_vector_type(2)));
; #pragma unroll
;                 for (int bj = 0; bj < 2; ++bj) *(u32x2_*)(rowp8 + 32 * bj) = (u32x2_){pk4_fp8(x[bj][0][0], x[bj][0][1], x[bj][0][2], x[bj][0][3]), pk4_fp8(x[bj][1][0], x[bj][1][1], x[bj][1][2], x[bj][1][3])};
;                 continue; }
;             bf16_t* rowp = obase + (size_t)row * opitch + 8 * fq;
; #pragma unroll
;             for (int bj = 0; bj < 2; ++bj) { u32x4 w; w.x = cvt_pk_bf16(x[bj][0][0], x[bj][0][1]); w.y = cvt_pk_bf16(x[bj][0][2], x[bj][0][3]); w.z = cvt_pk_bf16(x[bj][1][0], x[bj][1][1]); w.w = cvt_pk_bf16(x[bj][1][2], x[bj][1][3]);
;                 *(u32x4*)(rowp + 32 * bj) = w; }
	v_add_f32_e32 v22, v22, v23
	v_xor_b32_e32 v23, 32, v212
	v_cmp_lt_i32_e32 vcc, v23, v24
	s_nop 1
	v_cndmask_b32_e32 v23, v212, v23, vcc
	v_lshlrev_b32_e32 v23, 2, v23
	v_mov_b32_e32 v23, v22
	s_nop 1
	v_permlane32_swap_b32_e32 v22, v23
	s_waitcnt lgkmcnt(0)
	v_add_f32_e32 v22, v22, v23
	v_fmamk_f32 v22, v22, 0x3c800000, v210
	v_mul_f32_e32 v23, 0x4f800000, v22
	v_cmp_gt_f32_e32 vcc, s28, v22
	s_nop 1
	v_cndmask_b32_e32 v22, v22, v23, vcc
	v_sqrt_f32_e32 v23, v22
	s_nop 0
	v_add_u32_e32 v24, -1, v23
	v_fma_f32 v25, -v24, v23, v22
	v_cmp_ge_f32_e64 s[6:7], 0, v25
	v_add_u32_e32 v25, 1, v23
	s_nop 0
	v_cndmask_b32_e64 v24, v23, v24, s[6:7]
	v_fma_f32 v23, -v25, v23, v22
	v_cmp_lt_f32_e64 s[6:7], 0, v23
	s_nop 1
	v_cndmask_b32_e64 v23, v24, v25, s[6:7]
	v_mul_f32_e32 v24, 0x37800000, v23
	v_cndmask_b32_e32 v23, v23, v24, vcc
	v_cmp_class_f32_e32 vcc, v22, v211
	s_nop 1
	v_cndmask_b32_e32 v22, v23, v22, vcc
	v_div_scale_f32 v23, s[0:1], v22, v22, s25
	v_rcp_f32_e32 v24, v23
	s_nop 0
	v_fma_f32 v25, -v23, v24, 1.0
	v_fmac_f32_e32 v24, v25, v24
	v_div_scale_f32 v25, vcc, s25, v22, s25
	v_mul_f32_e32 v26, v25, v24
	v_fma_f32 v27, -v23, v26, v25
	v_fmac_f32_e32 v26, v27, v24
	v_fma_f32 v23, -v23, v26, v25
	v_div_fmas_f32 v23, v23, v24, v26
	v_div_fixup_f32 v22, v23, v22, s25
	v_pk_mul_f32 v[24:25], v[126:127], v[22:23] op_sel_hi:[1,0]
	v_pk_mul_f32 v[26:27], v[128:129], v[22:23] op_sel_hi:[1,0]
	s_waitcnt vmcnt(0)
	v_pk_mul_f32 v[126:127], v[14:15], v[24:25]
	v_pk_mul_f32 v[24:25], v[122:123], v[22:23] op_sel_hi:[1,0]
	v_pk_mul_f32 v[128:129], v[16:17], v[26:27]
	v_pk_mul_f32 v[26:27], v[124:125], v[22:23] op_sel_hi:[1,0]
	v_pk_mul_f32 v[122:123], v[6:7], v[24:25]
	v_pk_mul_f32 v[24:25], v[118:119], v[22:23] op_sel_hi:[1,0]
	v_pk_mul_f32 v[124:125], v[8:9], v[26:27]
	v_pk_mul_f32 v[26:27], v[120:121], v[22:23] op_sel_hi:[1,0]
	v_pk_mul_f32 v[118:119], v[10:11], v[24:25]
	v_pk_mul_f32 v[24:25], v[114:115], v[22:23] op_sel_hi:[1,0]
	v_pk_mul_f32 v[22:23], v[116:117], v[22:23] op_sel_hi:[1,0]
	v_pk_mul_f32 v[120:121], v[12:13], v[26:27]
	v_pk_mul_f32 v[116:117], v[4:5], v[22:23]
	v_pk_mul_f32 v[114:115], v[2:3], v[24:25]
.LBB0_270:
	s_mov_b64 s[0:1], 0x8000
	v_lshl_add_u64 v[26:27], v[20:21], 0, s[0:1]
	v_add_co_u32_e32 v20, vcc, 0x8000, v20
	v_cvt_pk_bf16_f32 v22, v126, v127
	v_cvt_pk_bf16_f32 v23, v128, v129
	v_cvt_pk_bf16_f32 v24, v122, v123
	v_cvt_pk_bf16_f32 v25, v124, v125
	s_nop 1
	v_addc_co_u32_e32 v21, vcc, 0, v21, vcc
	s_and_b64 vcc, exec, s[4:5]
	global_store_dwordx4 v[20:21], v[22:25], off
	v_cvt_pk_bf16_f32 v20, v118, v119
	v_cvt_pk_bf16_f32 v21, v120, v121
	s_nop 1
	v_cvt_pk_bf16_f32 v22, v114, v115
	v_cvt_pk_bf16_f32 v23, v116, v117
	global_store_dwordx4 v[26:27], v[20:23], off offset:64
	s_cbranch_vccnz .LBB0_272
	s_nop 0
	v_pk_mul_f32 v[20:21], v[112:113], v[112:113]
	v_pk_mul_f32 v[22:23], v[110:111], v[110:111]
	s_nop 0
	v_pk_mov_b32 v[24:25], v[22:23], v[20:21] op_sel:[1,0]
	v_mov_b32_e32 v23, v21
	v_pk_add_f32 v[20:21], v[24:25], v[22:23]
	v_pk_mul_f32 v[22:23], v[108:109], v[108:109]
	v_pk_mul_f32 v[24:25], v[106:107], v[106:107]
	v_pk_add_f32 v[20:21], v[20:21], v[20:21] op_sel:[0,1] op_sel_hi:[1,0]
	v_pk_mov_b32 v[26:27], v[24:25], v[22:23] op_sel:[1,0]
	v_mov_b32_e32 v25, v23
	v_pk_add_f32 v[22:23], v[26:27], v[24:25]
	v_mul_f32_e32 v24, v98, v98
	v_mul_f32_e32 v25, v99, v99
	v_pk_add_f32 v[22:23], v[22:23], v[22:23] op_sel:[0,1] op_sel_hi:[1,0]
	v_mov_b32_e32 v21, v24
	v_mov_b32_e32 v23, v25
	v_pk_add_f32 v[20:21], v[20:21], v[22:23]
	v_mul_f32_e32 v22, v103, v103
	v_mul_f32_e32 v24, v105, v105
	v_mul_f32_e32 v26, v100, v100
	v_mul_f32_e32 v27, v101, v101
	v_pk_fma_f32 v[22:23], v[102:103], v[102:103], v[22:23] op_sel_hi:[1,1,0]
	v_pk_fma_f32 v[24:25], v[104:105], v[104:105], v[24:25] op_sel_hi:[1,1,0]
	v_mov_b32_e32 v23, v26
	v_mov_b32_e32 v25, v27
	v_pk_add_f32 v[22:23], v[22:23], v[24:25]
	s_nop 0
	v_pk_add_f32 v[20:21], v[20:21], v[22:23]
	v_and_b32_e32 v22, 64, v212
	v_add_f32_e32 v20, v20, v21
	v_xor_b32_e32 v21, 16, v212
	v_add_u32_e32 v22, 64, v22
	v_cmp_lt_i32_e32 vcc, v21, v22
	s_nop 1
	v_cndmask_b32_e32 v21, v212, v21, vcc
	v_lshlrev_b32_e32 v21, 2, v21
	v_mov_b32_e32 v21, v20
	s_nop 1
	v_permlane16_swap_b32_e32 v20, v21
	s_waitcnt lgkmcnt(0)
	v_add_f32_e32 v20, v20, v21
	v_xor_b32_e32 v21, 32, v212
	v_cmp_lt_i32_e32 vcc, v21, v22
	s_nop 1
	v_cndmask_b32_e32 v21, v212, v21, vcc
	v_lshlrev_b32_e32 v21, 2, v21
	v_mov_b32_e32 v21, v20
	s_nop 1
	v_permlane32_swap_b32_e32 v20, v21
	s_waitcnt lgkmcnt(0)
	v_add_f32_e32 v20, v20, v21
	v_fmamk_f32 v20, v20, 0x3c800000, v210
	v_mul_f32_e32 v21, 0x4f800000, v20
	v_cmp_gt_f32_e32 vcc, s28, v20
	s_nop 1
	v_cndmask_b32_e32 v20, v20, v21, vcc
	v_sqrt_f32_e32 v21, v20
	s_nop 0
	v_add_u32_e32 v22, -1, v21
	v_fma_f32 v23, -v22, v21, v20
	v_cmp_ge_f32_e64 s[6:7], 0, v23
	v_add_u32_e32 v23, 1, v21
	s_nop 0
	v_cndmask_b32_e64 v22, v21, v22, s[6:7]
	v_fma_f32 v21, -v23, v21, v20
	v_cmp_lt_f32_e64 s[6:7], 0, v21
	s_nop 1
	v_cndmask_b32_e64 v21, v22, v23, s[6:7]
	v_mul_f32_e32 v22, 0x37800000, v21
	v_cndmask_b32_e32 v21, v21, v22, vcc
	v_cmp_class_f32_e32 vcc, v20, v211
	s_nop 1
	v_cndmask_b32_e32 v20, v21, v20, vcc
	v_div_scale_f32 v21, s[0:1], v20, v20, s25
	v_rcp_f32_e32 v22, v21
	s_nop 0
	v_fma_f32 v23, -v21, v22, 1.0
	v_fmac_f32_e32 v22, v23, v22
	v_div_scale_f32 v23, vcc, s25, v20, s25
	v_mul_f32_e32 v24, v23, v22
	v_fma_f32 v25, -v21, v24, v23
	v_fmac_f32_e32 v24, v25, v22
	v_fma_f32 v21, -v21, v24, v23
	v_div_fmas_f32 v21, v21, v22, v24
	v_div_fixup_f32 v20, v21, v20, s25
	v_pk_mul_f32 v[22:23], v[110:111], v[20:21] op_sel_hi:[1,0]
	v_pk_mul_f32 v[24:25], v[112:113], v[20:21] op_sel_hi:[1,0]
	s_waitcnt vmcnt(0)
	v_pk_mul_f32 v[110:111], v[14:15], v[22:23]
	v_pk_mul_f32 v[22:23], v[106:107], v[20:21] op_sel_hi:[1,0]
	v_pk_mul_f32 v[112:113], v[16:17], v[24:25]
	v_pk_mul_f32 v[24:25], v[108:109], v[20:21] op_sel_hi:[1,0]
	v_pk_mul_f32 v[106:107], v[6:7], v[22:23]
	v_pk_mul_f32 v[22:23], v[102:103], v[20:21] op_sel_hi:[1,0]
	v_pk_mul_f32 v[108:109], v[8:9], v[24:25]
	v_pk_mul_f32 v[24:25], v[104:105], v[20:21] op_sel_hi:[1,0]
	v_pk_mul_f32 v[102:103], v[10:11], v[22:23]
	v_pk_mul_f32 v[22:23], v[98:99], v[20:21] op_sel_hi:[1,0]
	v_pk_mul_f32 v[20:21], v[100:101], v[20:21] op_sel_hi:[1,0]
	v_pk_mul_f32 v[104:105], v[12:13], v[24:25]
	v_pk_mul_f32 v[100:101], v[4:5], v[20:21]
	v_pk_mul_f32 v[98:99], v[2:3], v[22:23]
; template <bool F8OUT = false> __device__ __forceinline__ void head_tile_store(const f32x4 (&acc)[2][2][4][2], bf16_t* obase  , int opitch, const float* gain, float scale, const f32x2e* rope, int row0, int fq) {
;     ...
;             if (gain) {
;                 float ss = 0.f;
; #pragma unroll
;                 for (int bj = 0; bj < 2; ++bj)
; #pragma unroll
;                     for (int n = 0; n < 2; ++n) ss += (x[bj][n][0] * x[bj][n][0] + x[bj][n][1] * x[bj][n][1]) + (x[bj][n][2] * x[bj][n][2] + x[bj][n][3] * x[bj][n][3]);
;                 ss += __shfl_xor(ss, 16); ss += __shfl_xor(ss, 32);
;                 const float r = scale / sqrtf(ss * (1.f / 64.f) + 1e-6f);
; #pragma unroll
;                 for (int bj = 0; bj < 2; ++bj)
; #pragma unroll
;                     for (int n = 0; n < 2; ++n) x[bj][n] = x[bj][n] * r * g[bj][n];
;             }
;             if (rope) {
;                 const int t = row & 8191; const bool second = (fq & 2) != 0;
; #pragma unroll
;                 for (int bj = 0; bj < 2; ++bj) { const int pos = bj ? (t & 63) : (t >> 6); const f32x2e* tb = rope + pos * 16 + 8 * (fq & 1);
; #pragma unroll
;                     for (int n = 0; n < 2; ++n)
; #pragma unroll
;                         for (int e = 0; e < 4; ++e) { const float p = __shfl_xor(x[bj][n][e], 32); const f32x2e cs = tb[4 * n + e]; const float v = x[bj][n][e];
;                             x[bj][n][e] = second ? (p * cs.y + v * cs.x) : (v * cs.x - p * cs.y); } }
;             }
;             if constexpr (F8OUT) { unsigned char* rowp8 = (unsigned char*)obase + (size_t)row * opitch + 8 * fq; typedef unsigned u32x2_ __attribute__((ext_vector_type(2)));
; #pragma unroll
;                 for (int bj = 0; bj < 2; ++bj) *(u32x2_*)(rowp8 + 32 * bj) = (u32x2_){pk4_fp8(x[bj][0][0], x[bj][0][1], x[bj][0][2], x[bj][0][3]), pk4_fp8(x[bj][1][0], x[bj][1][1], x[bj][1][2], x[bj][1][3])};
;                 continue; }
;             bf16_t* rowp = obase + (size_t)row * opitch + 8 * fq;
; #pragma unroll
;             for (int bj = 0; bj < 2; ++bj) { u32x4 w; w.x = cvt_pk_bf16(x[bj][0][0], x[bj][0][1]); w.y = cvt_pk_bf16(x[bj][0][2], x[bj][0][3]); w.z = cvt_pk_bf16(x[bj][1][0], x[bj][1][1]); w.w = cvt_pk_bf16(x[bj][1][2], x[bj][1][3]);
;                 *(u32x4*)(rowp + 32 * bj) = w; }
.LBB0_272:
	s_nop 0
	v_lshlrev_b64 v[20:21], 10, v[184:185]
	v_lshl_add_u64 v[20:21], v[18:19], 0, v[20:21]
	v_add_co_u32_e32 v28, vcc, 0xc000, v20
	v_lshl_add_u64 v[26:27], v[20:21], 0, s[34:35]
	s_nop 0
	v_addc_co_u32_e32 v29, vcc, 0, v21, vcc
	v_cvt_pk_bf16_f32 v22, v110, v111
	v_cvt_pk_bf16_f32 v23, v112, v113
	v_cvt_pk_bf16_f32 v24, v106, v107
	v_cvt_pk_bf16_f32 v25, v108, v109
	s_and_b64 vcc, exec, s[4:5]
	global_store_dwordx4 v[28:29], v[22:25], off
	s_nop 1
	v_cvt_pk_bf16_f32 v22, v102, v103
	v_cvt_pk_bf16_f32 v23, v104, v105
	v_cvt_pk_bf16_f32 v24, v98, v99
	v_cvt_pk_bf16_f32 v25, v100, v101
	global_store_dwordx4 v[26:27], v[22:25], off offset:64
	s_cbranch_vccnz .LBB0_274
	s_nop 0
	v_pk_mul_f32 v[22:23], v[96:97], v[96:97]
	v_pk_mul_f32 v[24:25], v[94:95], v[94:95]
	s_nop 0
	v_pk_mov_b32 v[26:27], v[24:25], v[22:23] op_sel:[1,0]
	v_mov_b32_e32 v25, v23
	v_pk_add_f32 v[22:23], v[26:27], v[24:25]
	v_pk_mul_f32 v[24:25], v[92:93], v[92:93]
	v_pk_mul_f32 v[26:27], v[90:91], v[90:91]
	v_pk_add_f32 v[22:23], v[22:23], v[22:23] op_sel:[0,1] op_sel_hi:[1,0]
	v_pk_mov_b32 v[28:29], v[26:27], v[24:25] op_sel:[1,0]
	v_mov_b32_e32 v27, v25
	v_pk_add_f32 v[24:25], v[28:29], v[26:27]
	v_mul_f32_e32 v26, v82, v82
	v_mul_f32_e32 v27, v83, v83
	v_pk_add_f32 v[24:25], v[24:25], v[24:25] op_sel:[0,1] op_sel_hi:[1,0]
	v_mov_b32_e32 v23, v26
	v_mov_b32_e32 v25, v27
	v_pk_add_f32 v[22:23], v[22:23], v[24:25]
	v_mul_f32_e32 v24, v87, v87
	v_mul_f32_e32 v26, v89, v89
	v_mul_f32_e32 v28, v84, v84
	v_mul_f32_e32 v29, v85, v85
	v_pk_fma_f32 v[24:25], v[86:87], v[86:87], v[24:25] op_sel_hi:[1,1,0]
	v_pk_fma_f32 v[26:27], v[88:89], v[88:89], v[26:27] op_sel_hi:[1,1,0]
	v_mov_b32_e32 v25, v28
	v_mov_b32_e32 v27, v29
	v_pk_add_f32 v[24:25], v[24:25], v[26:27]
	s_nop 0
	v_pk_add_f32 v[22:23], v[22:23], v[24:25]
	v_and_b32_e32 v24, 64, v212
	v_add_f32_e32 v22, v22, v23
	v_xor_b32_e32 v23, 16, v212
	v_add_u32_e32 v24, 64, v24
	v_cmp_lt_i32_e32 vcc, v23, v24
	s_nop 1
	v_cndmask_b32_e32 v23, v212, v23, vcc
	v_lshlrev_b32_e32 v23, 2, v23
	v_mov_b32_e32 v23, v22
	s_nop 1
	v_permlane16_swap_b32_e32 v22, v23
	s_waitcnt lgkmcnt(0)
	v_add_f32_e32 v22, v22, v23
	v_xor_b32_e32 v23, 32, v212
	v_cmp_lt_i32_e32 vcc, v23, v24
	s_nop 1
	v_cndmask_b32_e32 v23, v212, v23, vcc
	v_lshlrev_b32_e32 v23, 2, v23
	v_mov_b32_e32 v23, v22
	s_nop 1
	v_permlane32_swap_b32_e32 v22, v23
	s_waitcnt lgkmcnt(0)
	v_add_f32_e32 v22, v22, v23
	v_fmamk_f32 v22, v22, 0x3c800000, v210
	v_mul_f32_e32 v23, 0x4f800000, v22
	v_cmp_gt_f32_e32 vcc, s28, v22
	s_nop 1
	v_cndmask_b32_e32 v22, v22, v23, vcc
	v_sqrt_f32_e32 v23, v22
	s_nop 0
	v_add_u32_e32 v24, -1, v23
	v_fma_f32 v25, -v24, v23, v22
	v_cmp_ge_f32_e64 s[6:7], 0, v25
	v_add_u32_e32 v25, 1, v23
	s_nop 0
	v_cndmask_b32_e64 v24, v23, v24, s[6:7]
	v_fma_f32 v23, -v25, v23, v22
	v_cmp_lt_f32_e64 s[6:7], 0, v23
	s_nop 1
	v_cndmask_b32_e64 v23, v24, v25, s[6:7]
	v_mul_f32_e32 v24, 0x37800000, v23
	v_cndmask_b32_e32 v23, v23, v24, vcc
	v_cmp_class_f32_e32 vcc, v22, v211
	s_nop 1
	v_cndmask_b32_e32 v22, v23, v22, vcc
	v_div_scale_f32 v23, s[0:1], v22, v22, s25
	v_rcp_f32_e32 v24, v23
	s_nop 0
	v_fma_f32 v25, -v23, v24, 1.0
	v_fmac_f32_e32 v24, v25, v24
	v_div_scale_f32 v25, vcc, s25, v22, s25
	v_mul_f32_e32 v26, v25, v24
	v_fma_f32 v27, -v23, v26, v25
	v_fmac_f32_e32 v26, v27, v24
	v_fma_f32 v23, -v23, v26, v25
	v_div_fmas_f32 v23, v23, v24, v26
	v_div_fixup_f32 v22, v23, v22, s25
	v_pk_mul_f32 v[24:25], v[94:95], v[22:23] op_sel_hi:[1,0]
	v_pk_mul_f32 v[26:27], v[96:97], v[22:23] op_sel_hi:[1,0]
	s_waitcnt vmcnt(0)
	v_pk_mul_f32 v[94:95], v[14:15], v[24:25]
	v_pk_mul_f32 v[24:25], v[90:91], v[22:23] op_sel_hi:[1,0]
	v_pk_mul_f32 v[96:97], v[16:17], v[26:27]
	v_pk_mul_f32 v[26:27], v[92:93], v[22:23] op_sel_hi:[1,0]
	v_pk_mul_f32 v[90:91], v[6:7], v[24:25]
	v_pk_mul_f32 v[24:25], v[86:87], v[22:23] op_sel_hi:[1,0]
	v_pk_mul_f32 v[92:93], v[8:9], v[26:27]
	v_pk_mul_f32 v[26:27], v[88:89], v[22:23] op_sel_hi:[1,0]
	v_pk_mul_f32 v[86:87], v[10:11], v[24:25]
	v_pk_mul_f32 v[24:25], v[82:83], v[22:23] op_sel_hi:[1,0]
	v_pk_mul_f32 v[22:23], v[84:85], v[22:23] op_sel_hi:[1,0]
	v_pk_mul_f32 v[88:89], v[12:13], v[26:27]
	v_pk_mul_f32 v[84:85], v[4:5], v[22:23]
	v_pk_mul_f32 v[82:83], v[2:3], v[24:25]
; template <bool F8OUT = false> __device__ __forceinline__ void head_tile_store(const f32x4 (&acc)[2][2][4][2], bf16_t* obase  , int opitch, const float* gain, float scale, const f32x2e* rope, int row0, int fq) {
;     ...
;             if (gain) {
;                 float ss = 0.f;
; #pragma unroll
;                 for (int bj = 0; bj < 2; ++bj)
; #pragma unroll
;                     for (int n = 0; n < 2; ++n) ss += (x[bj][n][0] * x[bj][n][0] + x[bj][n][1] * x[bj][n][1]) + (x[bj][n][2] * x[bj][n][2] + x[bj][n][3] * x[bj][n][3]);
;                 ss += __shfl_xor(ss, 16); ss += __shfl_xor(ss, 32);
;                 const float r = scale / sqrtf(ss * (1.f / 64.f) + 1e-6f);
; #pragma unroll
;                 for (int bj = 0; bj < 2; ++bj)
; #pragma unroll
;                     for (int n = 0; n < 2; ++n) x[bj][n] = x[bj][n] * r * g[bj][n];
;             }
;             if (rope) {
;                 const int t = row & 8191; const bool second = (fq & 2) != 0;
; #pragma unroll
;                 for (int bj = 0; bj < 2; ++bj) { const int pos = bj ? (t & 63) : (t >> 6); const f32x2e* tb = rope + pos * 16 + 8 * (fq & 1);
; #pragma unroll
;                     for (int n = 0; n < 2; ++n)
; #pragma unroll
;                         for (int e = 0; e < 4; ++e) { const float p = __shfl_xor(x[bj][n][e], 32); const f32x2e cs = tb[4 * n + e]; const float v = x[bj][n][e];
;                             x[bj][n][e] = second ? (p * cs.y + v * cs.x) : (v * cs.x - p * cs.y); } }
;             }
;             if constexpr (F8OUT) { unsigned char* rowp8 = (unsigned char*)obase + (size_t)row * opitch + 8 * fq; typedef unsigned u32x2_ __attribute__((ext_vector_type(2)));
; #pragma unroll
;                 for (int bj = 0; bj < 2; ++bj) *(u32x2_*)(rowp8 + 32 * bj) = (u32x2_){pk4_fp8(x[bj][0][0], x[bj][0][1], x[bj][0][2], x[bj][0][3]), pk4_fp8(x[bj][1][0], x[bj][1][1], x[bj][1][2], x[bj][1][3])};
;                 continue; }
;             bf16_t* rowp = obase + (size_t)row * opitch + 8 * fq;
; #pragma unroll
;             for (int bj = 0; bj < 2; ++bj) { u32x4 w; w.x = cvt_pk_bf16(x[bj][0][0], x[bj][0][1]); w.y = cvt_pk_bf16(x[bj][0][2], x[bj][0][3]); w.z = cvt_pk_bf16(x[bj][1][0], x[bj][1][1]); w.w = cvt_pk_bf16(x[bj][1][2], x[bj][1][3]);
;                 *(u32x4*)(rowp + 32 * bj) = w; }
.LBB0_274:
	s_mov_b64 s[0:1], 0x20000
	v_lshl_add_u64 v[26:27], v[20:21], 0, s[0:1]
	v_add_co_u32_e32 v20, vcc, 0x20000, v20
	v_cvt_pk_bf16_f32 v22, v94, v95
	v_cvt_pk_bf16_f32 v23, v96, v97
	v_cvt_pk_bf16_f32 v24, v90, v91
	v_cvt_pk_bf16_f32 v25, v92, v93
	s_nop 1
	v_addc_co_u32_e32 v21, vcc, 0, v21, vcc
	s_and_b64 vcc, exec, s[4:5]
	global_store_dwordx4 v[20:21], v[22:25], off
	v_cvt_pk_bf16_f32 v20, v86, v87
	v_cvt_pk_bf16_f32 v21, v88, v89
	s_nop 1
	v_cvt_pk_bf16_f32 v22, v82, v83
	v_cvt_pk_bf16_f32 v23, v84, v85
	global_store_dwordx4 v[26:27], v[20:23], off offset:64
	s_cbranch_vccnz .LBB0_276
	s_nop 0
	v_pk_mul_f32 v[20:21], v[80:81], v[80:81]
	v_pk_mul_f32 v[22:23], v[78:79], v[78:79]
	s_nop 0
	v_pk_mov_b32 v[24:25], v[22:23], v[20:21] op_sel:[1,0]
	v_mov_b32_e32 v23, v21
	v_pk_add_f32 v[20:21], v[24:25], v[22:23]
	v_pk_mul_f32 v[22:23], v[76:77], v[76:77]
	v_pk_mul_f32 v[24:25], v[74:75], v[74:75]
	v_pk_add_f32 v[20:21], v[20:21], v[20:21] op_sel:[0,1] op_sel_hi:[1,0]
	v_pk_mov_b32 v[26:27], v[24:25], v[22:23] op_sel:[1,0]
	v_mov_b32_e32 v25, v23
	v_pk_add_f32 v[22:23], v[26:27], v[24:25]
	v_mul_f32_e32 v24, v66, v66
	v_mul_f32_e32 v25, v67, v67
	v_pk_add_f32 v[22:23], v[22:23], v[22:23] op_sel:[0,1] op_sel_hi:[1,0]
	v_mov_b32_e32 v21, v24
	v_mov_b32_e32 v23, v25
	v_pk_add_f32 v[20:21], v[20:21], v[22:23]
	v_mul_f32_e32 v22, v71, v71
	v_mul_f32_e32 v24, v73, v73
	v_mul_f32_e32 v26, v68, v68
	v_mul_f32_e32 v27, v69, v69
	v_pk_fma_f32 v[22:23], v[70:71], v[70:71], v[22:23] op_sel_hi:[1,1,0]
	v_pk_fma_f32 v[24:25], v[72:73], v[72:73], v[24:25] op_sel_hi:[1,1,0]
	v_mov_b32_e32 v23, v26
	v_mov_b32_e32 v25, v27
	v_pk_add_f32 v[22:23], v[22:23], v[24:25]
	s_nop 0
	v_pk_add_f32 v[20:21], v[20:21], v[22:23]
	v_and_b32_e32 v22, 64, v212
	v_add_f32_e32 v20, v20, v21
	v_xor_b32_e32 v21, 16, v212
	v_add_u32_e32 v22, 64, v22
	v_cmp_lt_i32_e32 vcc, v21, v22
	s_nop 1
	v_cndmask_b32_e32 v21, v212, v21, vcc
	v_lshlrev_b32_e32 v21, 2, v21
	v_mov_b32_e32 v21, v20
	s_nop 1
	v_permlane16_swap_b32_e32 v20, v21
	s_waitcnt lgkmcnt(0)
	v_add_f32_e32 v20, v20, v21
	v_xor_b32_e32 v21, 32, v212
	v_cmp_lt_i32_e32 vcc, v21, v22
	s_nop 1
	v_cndmask_b32_e32 v21, v212, v21, vcc
	v_lshlrev_b32_e32 v21, 2, v21
	v_mov_b32_e32 v21, v20
	s_nop 1
	v_permlane32_swap_b32_e32 v20, v21
	s_waitcnt lgkmcnt(0)
	v_add_f32_e32 v20, v20, v21
	v_fmamk_f32 v20, v20, 0x3c800000, v210
	v_mul_f32_e32 v21, 0x4f800000, v20
	v_cmp_gt_f32_e32 vcc, s28, v20
	s_nop 1
	v_cndmask_b32_e32 v20, v20, v21, vcc
	v_sqrt_f32_e32 v21, v20
	s_nop 0
	v_add_u32_e32 v22, -1, v21
	v_fma_f32 v23, -v22, v21, v20
	v_cmp_ge_f32_e64 s[6:7], 0, v23
	v_add_u32_e32 v23, 1, v21
	s_nop 0
	v_cndmask_b32_e64 v22, v21, v22, s[6:7]
	v_fma_f32 v21, -v23, v21, v20
	v_cmp_lt_f32_e64 s[6:7], 0, v21
	s_nop 1
	v_cndmask_b32_e64 v21, v22, v23, s[6:7]
	v_mul_f32_e32 v22, 0x37800000, v21
	v_cndmask_b32_e32 v21, v21, v22, vcc
	v_cmp_class_f32_e32 vcc, v20, v211
	s_nop 1
	v_cndmask_b32_e32 v20, v21, v20, vcc
	v_div_scale_f32 v21, s[0:1], v20, v20, s25
	v_rcp_f32_e32 v22, v21
	s_nop 0
	v_fma_f32 v23, -v21, v22, 1.0
	v_fmac_f32_e32 v22, v23, v22
	v_div_scale_f32 v23, vcc, s25, v20, s25
	v_mul_f32_e32 v24, v23, v22
	v_fma_f32 v25, -v21, v24, v23
	v_fmac_f32_e32 v24, v25, v22
	v_fma_f32 v21, -v21, v24, v23
	v_div_fmas_f32 v21, v21, v22, v24
	v_div_fixup_f32 v20, v21, v20, s25
	v_pk_mul_f32 v[22:23], v[78:79], v[20:21] op_sel_hi:[1,0]
	v_pk_mul_f32 v[24:25], v[80:81], v[20:21] op_sel_hi:[1,0]
	s_waitcnt vmcnt(0)
	v_pk_mul_f32 v[78:79], v[14:15], v[22:23]
	v_pk_mul_f32 v[22:23], v[74:75], v[20:21] op_sel_hi:[1,0]
	v_pk_mul_f32 v[80:81], v[16:17], v[24:25]
	v_pk_mul_f32 v[24:25], v[76:77], v[20:21] op_sel_hi:[1,0]
	v_pk_mul_f32 v[74:75], v[6:7], v[22:23]
	v_pk_mul_f32 v[22:23], v[70:71], v[20:21] op_sel_hi:[1,0]
	v_pk_mul_f32 v[76:77], v[8:9], v[24:25]
	v_pk_mul_f32 v[24:25], v[72:73], v[20:21] op_sel_hi:[1,0]
	v_pk_mul_f32 v[70:71], v[10:11], v[22:23]
	v_pk_mul_f32 v[22:23], v[66:67], v[20:21] op_sel_hi:[1,0]
	v_pk_mul_f32 v[20:21], v[68:69], v[20:21] op_sel_hi:[1,0]
	v_pk_mul_f32 v[72:73], v[12:13], v[24:25]
	v_pk_mul_f32 v[68:69], v[4:5], v[20:21]
	v_pk_mul_f32 v[66:67], v[2:3], v[22:23]
.LBB0_276:
	s_nop 0
	v_lshlrev_b64 v[20:21], 10, v[184:185]
	v_lshl_add_u64 v[20:21], v[18:19], 0, v[20:21]
	v_add_co_u32_e32 v28, vcc, 0x24000, v20
	v_lshl_add_u64 v[26:27], v[20:21], 0, s[30:31]
	s_nop 0
	v_addc_co_u32_e32 v29, vcc, 0, v21, vcc
	v_cvt_pk_bf16_f32 v22, v78, v79
	v_cvt_pk_bf16_f32 v23, v80, v81
	v_cvt_pk_bf16_f32 v24, v74, v75
	v_cvt_pk_bf16_f32 v25, v76, v77
	s_and_b64 vcc, exec, s[4:5]
	global_store_dwordx4 v[28:29], v[22:25], off
	s_nop 1
	v_cvt_pk_bf16_f32 v22, v70, v71
	v_cvt_pk_bf16_f32 v23, v72, v73
	v_cvt_pk_bf16_f32 v24, v66, v67
	v_cvt_pk_bf16_f32 v25, v68, v69
	global_store_dwordx4 v[26:27], v[22:25], off offset:64
	s_cbranch_vccnz .LBB0_278
; template <bool F8OUT = false> __device__ __forceinline__ void head_tile_store(const f32x4 (&acc)[2][2][4][2], bf16_t* obase  , int opitch, const float* gain, float scale, const f32x2e* rope, int row0, int fq) {
;     ...
;             if (gain) {
;                 float ss = 0.f;
; #pragma unroll
;                 for (int bj = 0; bj < 2; ++bj)
; #pragma unroll
;                     for (int n = 0; n < 2; ++n) ss += (x[bj][n][0] * x[bj][n][0] + x[bj][n][1] * x[bj][n][1]) + (x[bj][n][2] * x[bj][n][2] + x[bj][n][3] * x[bj][n][3]);
;                 ss += __shfl_xor(ss, 16); ss += __shfl_xor(ss, 32);
;                 const float r = scale / sqrtf(ss * (1.f / 64.f) + 1e-6f);
; #pragma unroll
;                 for (int bj = 0; bj < 2; ++bj)
; #pragma unroll
;                     for (int n = 0; n < 2; ++n) x[bj][n] = x[bj][n] * r * g[bj][n];
;             }
;             if (rope) {
;                 const int t = row & 8191; const bool second = (fq & 2) != 0;
; #pragma unroll
;                 for (int bj = 0; bj < 2; ++bj) { const int pos = bj ? (t & 63) : (t >> 6); const f32x2e* tb = rope + pos * 16 + 8 * (fq & 1);
; #pragma unroll
;                     for (int n = 0; n < 2; ++n)
; #pragma unroll
;                         for (int e = 0; e < 4; ++e) { const float p = __shfl_xor(x[bj][n][e], 32); const f32x2e cs = tb[4 * n + e]; const float v = x[bj][n][e];
;                             x[bj][n][e] = second ? (p * cs.y + v * cs.x) : (v * cs.x - p * cs.y); } }
;             }
;             if constexpr (F8OUT) { unsigned char* rowp8 = (unsigned char*)obase + (size_t)row * opitch + 8 * fq; typedef unsigned u32x2_ __attribute__((ext_vector_type(2)));
; #pragma unroll
;                 for (int bj = 0; bj < 2; ++bj) *(u32x2_*)(rowp8 + 32 * bj) = (u32x2_){pk4_fp8(x[bj][0][0], x[bj][0][1], x[bj][0][2], x[bj][0][3]), pk4_fp8(x[bj][1][0], x[bj][1][1], x[bj][1][2], x[bj][1][3])};
;                 continue; }
;             bf16_t* rowp = obase + (size_t)row * opitch + 8 * fq;
; #pragma unroll
;             for (int bj = 0; bj < 2; ++bj) { u32x4 w; w.x = cvt_pk_bf16(x[bj][0][0], x[bj][0][1]); w.y = cvt_pk_bf16(x[bj][0][2], x[bj][0][3]); w.z = cvt_pk_bf16(x[bj][1][0], x[bj][1][1]); w.w = cvt_pk_bf16(x[bj][1][2], x[bj][1][3]);
;                 *(u32x4*)(rowp + 32 * bj) = w; }
	s_nop 0
	v_pk_mul_f32 v[22:23], v[64:65], v[64:65]
	v_pk_mul_f32 v[24:25], v[62:63], v[62:63]
	s_nop 0
	v_pk_mov_b32 v[26:27], v[24:25], v[22:23] op_sel:[1,0]
	v_mov_b32_e32 v25, v23
	v_pk_add_f32 v[22:23], v[26:27], v[24:25]
	v_pk_mul_f32 v[24:25], v[60:61], v[60:61]
	v_pk_mul_f32 v[26:27], v[58:59], v[58:59]
	v_pk_add_f32 v[22:23], v[22:23], v[22:23] op_sel:[0,1] op_sel_hi:[1,0]
	v_pk_mov_b32 v[28:29], v[26:27], v[24:25] op_sel:[1,0]
	v_mov_b32_e32 v27, v25
	v_pk_add_f32 v[24:25], v[28:29], v[26:27]
	v_mul_f32_e32 v26, v50, v50
	v_mul_f32_e32 v27, v51, v51
	v_pk_add_f32 v[24:25], v[24:25], v[24:25] op_sel:[0,1] op_sel_hi:[1,0]
	v_mov_b32_e32 v23, v26
	v_mov_b32_e32 v25, v27
	v_pk_add_f32 v[22:23], v[22:23], v[24:25]
	v_mul_f32_e32 v24, v55, v55
	v_mul_f32_e32 v26, v57, v57
	v_mul_f32_e32 v28, v52, v52
	v_mul_f32_e32 v29, v53, v53
	v_pk_fma_f32 v[24:25], v[54:55], v[54:55], v[24:25] op_sel_hi:[1,1,0]
	v_pk_fma_f32 v[26:27], v[56:57], v[56:57], v[26:27] op_sel_hi:[1,1,0]
	v_mov_b32_e32 v25, v28
	v_mov_b32_e32 v27, v29
	v_pk_add_f32 v[24:25], v[24:25], v[26:27]
	s_nop 0
	v_pk_add_f32 v[22:23], v[22:23], v[24:25]
	v_and_b32_e32 v24, 64, v212
	v_add_f32_e32 v22, v22, v23
	v_xor_b32_e32 v23, 16, v212
	v_add_u32_e32 v24, 64, v24
	v_cmp_lt_i32_e32 vcc, v23, v24
	s_nop 1
	v_cndmask_b32_e32 v23, v212, v23, vcc
	v_lshlrev_b32_e32 v23, 2, v23
	v_mov_b32_e32 v23, v22
	s_nop 1
	v_permlane16_swap_b32_e32 v22, v23
	s_waitcnt lgkmcnt(0)
	v_add_f32_e32 v22, v22, v23
	v_xor_b32_e32 v23, 32, v212
	v_cmp_lt_i32_e32 vcc, v23, v24
	s_nop 1
	v_cndmask_b32_e32 v23, v212, v23, vcc
	v_lshlrev_b32_e32 v23, 2, v23
	v_mov_b32_e32 v23, v22
	s_nop 1
	v_permlane32_swap_b32_e32 v22, v23
	s_waitcnt lgkmcnt(0)
	v_add_f32_e32 v22, v22, v23
	v_fmamk_f32 v22, v22, 0x3c800000, v210
	v_mul_f32_e32 v23, 0x4f800000, v22
	v_cmp_gt_f32_e32 vcc, s28, v22
	s_nop 1
	v_cndmask_b32_e32 v22, v22, v23, vcc
	v_sqrt_f32_e32 v23, v22
	s_nop 0
	v_add_u32_e32 v24, -1, v23
	v_fma_f32 v25, -v24, v23, v22
	v_cmp_ge_f32_e64 s[6:7], 0, v25
	v_add_u32_e32 v25, 1, v23
	s_nop 0
	v_cndmask_b32_e64 v24, v23, v24, s[6:7]
	v_fma_f32 v23, -v25, v23, v22
	v_cmp_lt_f32_e64 s[6:7], 0, v23
	s_nop 1
	v_cndmask_b32_e64 v23, v24, v25, s[6:7]
	v_mul_f32_e32 v24, 0x37800000, v23
	v_cndmask_b32_e32 v23, v23, v24, vcc
	v_cmp_class_f32_e32 vcc, v22, v211
	s_nop 1
	v_cndmask_b32_e32 v22, v23, v22, vcc
	v_div_scale_f32 v23, s[0:1], v22, v22, s25
	v_rcp_f32_e32 v24, v23
	s_nop 0
	v_fma_f32 v25, -v23, v24, 1.0
	v_fmac_f32_e32 v24, v25, v24
	v_div_scale_f32 v25, vcc, s25, v22, s25
	v_mul_f32_e32 v26, v25, v24
	v_fma_f32 v27, -v23, v26, v25
	v_fmac_f32_e32 v26, v27, v24
	v_fma_f32 v23, -v23, v26, v25
	v_div_fmas_f32 v23, v23, v24, v26
	v_div_fixup_f32 v22, v23, v22, s25
	v_pk_mul_f32 v[24:25], v[62:63], v[22:23] op_sel_hi:[1,0]
	v_pk_mul_f32 v[26:27], v[64:65], v[22:23] op_sel_hi:[1,0]
	s_waitcnt vmcnt(0)
	v_pk_mul_f32 v[62:63], v[14:15], v[24:25]
	v_pk_mul_f32 v[24:25], v[58:59], v[22:23] op_sel_hi:[1,0]
	v_pk_mul_f32 v[64:65], v[16:17], v[26:27]
	v_pk_mul_f32 v[26:27], v[60:61], v[22:23] op_sel_hi:[1,0]
	v_pk_mul_f32 v[58:59], v[6:7], v[24:25]
	v_pk_mul_f32 v[24:25], v[54:55], v[22:23] op_sel_hi:[1,0]
	v_pk_mul_f32 v[60:61], v[8:9], v[26:27]
	v_pk_mul_f32 v[26:27], v[56:57], v[22:23] op_sel_hi:[1,0]
	v_pk_mul_f32 v[54:55], v[10:11], v[24:25]
	v_pk_mul_f32 v[24:25], v[50:51], v[22:23] op_sel_hi:[1,0]
	v_pk_mul_f32 v[22:23], v[52:53], v[22:23] op_sel_hi:[1,0]
	v_pk_mul_f32 v[56:57], v[12:13], v[26:27]
	v_pk_mul_f32 v[52:53], v[4:5], v[22:23]
	v_pk_mul_f32 v[50:51], v[2:3], v[24:25]
; template <bool F8OUT = false> __device__ __forceinline__ void head_tile_store(const f32x4 (&acc)[2][2][4][2], bf16_t* obase  , int opitch, const float* gain, float scale, const f32x2e* rope, int row0, int fq) {
;     ...
;             if (gain) {
;                 float ss = 0.f;
; #pragma unroll
;                 for (int bj = 0; bj < 2; ++bj)
; #pragma unroll
;                     for (int n = 0; n < 2; ++n) ss += (x[bj][n][0] * x[bj][n][0] + x[bj][n][1] * x[bj][n][1]) + (x[bj][n][2] * x[bj][n][2] + x[bj][n][3] * x[bj][n][3]);
;                 ss += __shfl_xor(ss, 16); ss += __shfl_xor(ss, 32);
;                 const float r = scale / sqrtf(ss * (1.f / 64.f) + 1e-6f);
; #pragma unroll
;                 for (int bj = 0; bj < 2; ++bj)
; #pragma unroll
;                     for (int n = 0; n < 2; ++n) x[bj][n] = x[bj][n] * r * g[bj][n];
;             }
;             if (rope) {
;                 const int t = row & 8191; const bool second = (fq & 2) != 0;
; #pragma unroll
;                 for (int bj = 0; bj < 2; ++bj) { const int pos = bj ? (t & 63) : (t >> 6); const f32x2e* tb = rope + pos * 16 + 8 * (fq & 1);
; #pragma unroll
;                     for (int n = 0; n < 2; ++n)
; #pragma unroll
;                         for (int e = 0; e < 4; ++e) { const float p = __shfl_xor(x[bj][n][e], 32); const f32x2e cs = tb[4 * n + e]; const float v = x[bj][n][e];
;                             x[bj][n][e] = second ? (p * cs.y + v * cs.x) : (v * cs.x - p * cs.y); } }
;             }
;             if constexpr (F8OUT) { unsigned char* rowp8 = (unsigned char*)obase + (size_t)row * opitch + 8 * fq; typedef unsigned u32x2_ __attribute__((ext_vector_type(2)));
; #pragma unroll
;                 for (int bj = 0; bj < 2; ++bj) *(u32x2_*)(rowp8 + 32 * bj) = (u32x2_){pk4_fp8(x[bj][0][0], x[bj][0][1], x[bj][0][2], x[bj][0][3]), pk4_fp8(x[bj][1][0], x[bj][1][1], x[bj][1][2], x[bj][1][3])};
;                 continue; }
;             bf16_t* rowp = obase + (size_t)row * opitch + 8 * fq;
; #pragma unroll
;             for (int bj = 0; bj < 2; ++bj) { u32x4 w; w.x = cvt_pk_bf16(x[bj][0][0], x[bj][0][1]); w.y = cvt_pk_bf16(x[bj][0][2], x[bj][0][3]); w.z = cvt_pk_bf16(x[bj][1][0], x[bj][1][1]); w.w = cvt_pk_bf16(x[bj][1][2], x[bj][1][3]);
;                 *(u32x4*)(rowp + 32 * bj) = w; }
.LBB0_278:
	v_lshl_add_u64 v[26:27], v[20:21], 0, s[12:13]
	v_add_co_u32_e32 v20, vcc, 0x28000, v20
	v_cvt_pk_bf16_f32 v22, v62, v63
	v_cvt_pk_bf16_f32 v23, v64, v65
	v_cvt_pk_bf16_f32 v24, v58, v59
	v_cvt_pk_bf16_f32 v25, v60, v61
	s_nop 1
	v_addc_co_u32_e32 v21, vcc, 0, v21, vcc
	s_and_b64 vcc, exec, s[4:5]
	global_store_dwordx4 v[20:21], v[22:25], off
	v_cvt_pk_bf16_f32 v20, v54, v55
	v_cvt_pk_bf16_f32 v21, v56, v57
	s_nop 1
	v_cvt_pk_bf16_f32 v22, v50, v51
	v_cvt_pk_bf16_f32 v23, v52, v53
	global_store_dwordx4 v[26:27], v[20:23], off offset:64
	s_cbranch_vccnz .LBB0_280
	s_nop 0
	v_pk_mul_f32 v[20:21], v[48:49], v[48:49]
	v_pk_mul_f32 v[22:23], v[46:47], v[46:47]
	s_nop 0
	v_pk_mov_b32 v[24:25], v[22:23], v[20:21] op_sel:[1,0]
	v_mov_b32_e32 v23, v21
	v_pk_add_f32 v[20:21], v[24:25], v[22:23]
	v_pk_mul_f32 v[22:23], v[44:45], v[44:45]
	v_pk_mul_f32 v[24:25], v[42:43], v[42:43]
	v_pk_add_f32 v[20:21], v[20:21], v[20:21] op_sel:[0,1] op_sel_hi:[1,0]
	v_pk_mov_b32 v[26:27], v[24:25], v[22:23] op_sel:[1,0]
	v_mov_b32_e32 v25, v23
	v_pk_add_f32 v[22:23], v[26:27], v[24:25]
	v_mul_f32_e32 v24, v34, v34
	v_mul_f32_e32 v25, v35, v35
	v_pk_add_f32 v[22:23], v[22:23], v[22:23] op_sel:[0,1] op_sel_hi:[1,0]
	v_mov_b32_e32 v21, v24
	v_mov_b32_e32 v23, v25
	v_pk_add_f32 v[20:21], v[20:21], v[22:23]
	v_mul_f32_e32 v22, v39, v39
	v_mul_f32_e32 v24, v41, v41
	v_mul_f32_e32 v26, v36, v36
	v_mul_f32_e32 v27, v37, v37
	v_pk_fma_f32 v[22:23], v[38:39], v[38:39], v[22:23] op_sel_hi:[1,1,0]
	v_pk_fma_f32 v[24:25], v[40:41], v[40:41], v[24:25] op_sel_hi:[1,1,0]
	v_mov_b32_e32 v23, v26
	v_mov_b32_e32 v25, v27
	v_pk_add_f32 v[22:23], v[22:23], v[24:25]
	s_nop 0
	v_pk_add_f32 v[20:21], v[20:21], v[22:23]
	v_and_b32_e32 v22, 64, v212
	v_add_f32_e32 v20, v20, v21
	v_xor_b32_e32 v21, 16, v212
	v_add_u32_e32 v22, 64, v22
	v_cmp_lt_i32_e32 vcc, v21, v22
	s_nop 1
	v_cndmask_b32_e32 v21, v212, v21, vcc
	v_lshlrev_b32_e32 v21, 2, v21
	v_mov_b32_e32 v21, v20
	s_nop 1
	v_permlane16_swap_b32_e32 v20, v21
	s_waitcnt lgkmcnt(0)
	v_add_f32_e32 v20, v20, v21
	v_xor_b32_e32 v21, 32, v212
	v_cmp_lt_i32_e32 vcc, v21, v22
	s_nop 1
	v_cndmask_b32_e32 v21, v212, v21, vcc
	v_lshlrev_b32_e32 v21, 2, v21
	v_mov_b32_e32 v21, v20
	s_nop 1
	v_permlane32_swap_b32_e32 v20, v21
	s_waitcnt lgkmcnt(0)
	v_add_f32_e32 v20, v20, v21
	v_fmamk_f32 v20, v20, 0x3c800000, v210
	v_mul_f32_e32 v21, 0x4f800000, v20
	v_cmp_gt_f32_e32 vcc, s28, v20
	s_nop 1
	v_cndmask_b32_e32 v20, v20, v21, vcc
	v_sqrt_f32_e32 v21, v20
	s_nop 0
	v_add_u32_e32 v22, -1, v21
	v_fma_f32 v23, -v22, v21, v20
	v_cmp_ge_f32_e64 s[4:5], 0, v23
	v_add_u32_e32 v23, 1, v21
	s_nop 0
	v_cndmask_b32_e64 v22, v21, v22, s[4:5]
	v_fma_f32 v21, -v23, v21, v20
	v_cmp_lt_f32_e64 s[4:5], 0, v21
	s_nop 1
	v_cndmask_b32_e64 v21, v22, v23, s[4:5]
	v_mul_f32_e32 v22, 0x37800000, v21
	v_cndmask_b32_e32 v21, v21, v22, vcc
	v_cmp_class_f32_e32 vcc, v20, v211
	s_nop 1
	v_cndmask_b32_e32 v20, v21, v20, vcc
	v_div_scale_f32 v21, s[0:1], v20, v20, s25
	v_rcp_f32_e32 v22, v21
	s_nop 0
	v_fma_f32 v23, -v21, v22, 1.0
	v_fmac_f32_e32 v22, v23, v22
	v_div_scale_f32 v23, vcc, s25, v20, s25
	v_mul_f32_e32 v24, v23, v22
	v_fma_f32 v25, -v21, v24, v23
	v_fmac_f32_e32 v24, v25, v22
	v_fma_f32 v21, -v21, v24, v23
	v_div_fmas_f32 v21, v21, v22, v24
	v_div_fixup_f32 v20, v21, v20, s25
	v_pk_mul_f32 v[22:23], v[46:47], v[20:21] op_sel_hi:[1,0]
	v_pk_mul_f32 v[24:25], v[48:49], v[20:21] op_sel_hi:[1,0]
	s_waitcnt vmcnt(0)
	v_pk_mul_f32 v[46:47], v[14:15], v[22:23]
	v_pk_mul_f32 v[48:49], v[16:17], v[24:25]
	v_pk_mul_f32 v[14:15], v[42:43], v[20:21] op_sel_hi:[1,0]
	v_pk_mul_f32 v[16:17], v[44:45], v[20:21] op_sel_hi:[1,0]
	v_pk_mul_f32 v[42:43], v[6:7], v[14:15]
	v_pk_mul_f32 v[44:45], v[8:9], v[16:17]
	v_pk_mul_f32 v[6:7], v[38:39], v[20:21] op_sel_hi:[1,0]
	v_pk_mul_f32 v[8:9], v[40:41], v[20:21] op_sel_hi:[1,0]
	v_pk_mul_f32 v[38:39], v[10:11], v[6:7]
	v_pk_mul_f32 v[40:41], v[12:13], v[8:9]
	v_pk_mul_f32 v[6:7], v[34:35], v[20:21] op_sel_hi:[1,0]
	v_pk_mul_f32 v[8:9], v[36:37], v[20:21] op_sel_hi:[1,0]
	v_pk_mul_f32 v[34:35], v[2:3], v[6:7]
	v_pk_mul_f32 v[36:37], v[4:5], v[8:9]

; template <bool F8OUT = false> __device__ __forceinline__ void head_tile_store(const f32x4 (&acc)[2][2][4][2], bf16_t* obase  , int opitch, const float* gain, float scale, const f32x2e* rope, int row0, int fq) {
;     ...
;             f32x4 x[2][2];
; #pragma unroll
;             for (int bj = 0; bj < 2; ++bj)
; #pragma unroll
;                 for (int n = 0; n < 2; ++n) x[bj][n] = acc[ai][bj][m][n];
;             if (gain) {
;                 float ss = 0.f;
; #pragma unroll
;                 for (int bj = 0; bj < 2; ++bj)
; #pragma unroll
;                     for (int n = 0; n < 2; ++n) ss += (x[bj][n][0] * x[bj][n][0] + x[bj][n][1] * x[bj][n][1]) + (x[bj][n][2] * x[bj][n][2] + x[bj][n][3] * x[bj][n][3]);
;                 ss += __shfl_xor(ss, 16); ss += __shfl_xor(ss, 32);
;                 const float r = scale / sqrtf(ss * (1.f / 64.f) + 1e-6f);
; #pragma unroll
;                 for (int bj = 0; bj < 2; ++bj)
; #pragma unroll
;                     for (int n = 0; n < 2; ++n) x[bj][n] = x[bj][n] * r * g[bj][n];
;             }
;             if (rope) {
;                 const int t = row & 8191; const bool second = (fq & 2) != 0;
; #pragma unroll
;                 for (int bj = 0; bj < 2; ++bj) { const int pos = bj ? (t & 63) : (t >> 6); const f32x2e* tb = rope + pos * 16 + 8 * (fq & 1);
; #pragma unroll
;                     for (int n = 0; n < 2; ++n)
; #pragma unroll
;                         for (int e = 0; e < 4; ++e) { const float p = __shfl_xor(x[bj][n][e], 32); const f32x2e cs = tb[4 * n + e]; const float v = x[bj][n][e];
;                             x[bj][n][e] = second ? (p * cs.y + v * cs.x) : (v * cs.x - p * cs.y); } }
;             }
;             if constexpr (F8OUT) { unsigned char* rowp8 = (unsigned char*)obase + (size_t)row * opitch + 8 * fq; typedef unsigned u32x2_ __attribute__((ext_vector_type(2)));
; #pragma unroll
;                 for (int bj = 0; bj < 2; ++bj) *(u32x2_*)(rowp8 + 32 * bj) = (u32x2_){pk4_fp8(x[bj][0][0], x[bj][0][1], x[bj][0][2], x[bj][0][3]), pk4_fp8(x[bj][1][0], x[bj][1][1], x[bj][1][2], x[bj][1][3])};
;                 continue; }
;             bf16_t* rowp = obase + (size_t)row * opitch + 8 * fq;
; #pragma unroll
.LBB0_1035:
	s_and_b64 vcc, exec, s[4:5]
	v_mov_b32_e32 v29, v149
	v_mov_b32_e32 v28, v148
	v_mov_b32_e32 v181, v147
	v_mov_b32_e32 v180, v146
	v_mov_b32_e32 v27, v153
	v_mov_b32_e32 v26, v152
	v_mov_b32_e32 v31, v151
	v_mov_b32_e32 v30, v150
	v_mov_b32_e32 v179, v157
	v_mov_b32_e32 v178, v156
	v_mov_b32_e32 v185, v155
	v_mov_b32_e32 v184, v154
	v_mov_b32_e32 v33, v161
	v_mov_b32_e32 v32, v160
	v_mov_b32_e32 v183, v159
	v_mov_b32_e32 v182, v158
	s_cbranch_vccnz .LBB0_1037
	v_pk_mul_f32 v[24:25], v[160:161], v[160:161]
	v_pk_mul_f32 v[26:27], v[158:159], v[158:159]
	v_mul_f32_e32 v19, v146, v146
	v_pk_mov_b32 v[28:29], v[26:27], v[24:25] op_sel:[1,0]
	v_mov_b32_e32 v27, v25
	v_pk_add_f32 v[24:25], v[28:29], v[26:27]
	v_pk_mul_f32 v[26:27], v[156:157], v[156:157]
	v_pk_mul_f32 v[28:29], v[154:155], v[154:155]
	v_mul_f32_e32 v21, v147, v147
	v_pk_mov_b32 v[30:31], v[28:29], v[26:27] op_sel:[1,0]
	v_mov_b32_e32 v29, v27
	v_pk_add_f32 v[26:27], v[30:31], v[28:29]
	v_pk_add_f32 v[24:25], v[24:25], v[24:25] op_sel:[0,1] op_sel_hi:[1,0]
	v_pk_add_f32 v[26:27], v[26:27], v[26:27] op_sel:[0,1] op_sel_hi:[1,0]
	v_mov_b32_e32 v25, v19
	v_mov_b32_e32 v27, v21
	v_pk_add_f32 v[24:25], v[24:25], v[26:27]
	v_mul_f32_e32 v26, v151, v151
	v_mul_f32_e32 v28, v148, v148
	v_pk_fma_f32 v[26:27], v[150:151], v[150:151], v[26:27] op_sel_hi:[1,1,0]
	v_mul_f32_e32 v30, v149, v149
	v_mov_b32_e32 v27, v28
	v_mul_f32_e32 v28, v153, v153
	v_pk_fma_f32 v[28:29], v[152:153], v[152:153], v[28:29] op_sel_hi:[1,1,0]
	v_xor_b32_e32 v21, 16, v195
	v_mov_b32_e32 v29, v30
	v_pk_add_f32 v[26:27], v[26:27], v[28:29]
	s_nop 0
	v_pk_add_f32 v[24:25], v[24:25], v[26:27]
	s_nop 0
	v_add_f32_e32 v19, v24, v25
	v_and_b32_e32 v24, 64, v195
	v_add_u32_e32 v24, 64, v24
	v_cmp_lt_i32_e32 vcc, v21, v24
	s_nop 1
	v_cndmask_b32_e32 v21, v195, v21, vcc
	v_lshlrev_b32_e32 v21, 2, v21
	v_mov_b32_e32 v21, v19
	s_nop 1
	v_permlane16_swap_b32_e32 v19, v21
	s_waitcnt lgkmcnt(0)
	v_add_f32_e32 v19, v19, v21
	v_xor_b32_e32 v21, 32, v195
	v_cmp_lt_i32_e32 vcc, v21, v24
	s_nop 1
	v_cndmask_b32_e32 v21, v195, v21, vcc
	v_lshlrev_b32_e32 v21, 2, v21
	v_mov_b32_e32 v21, v19
	s_nop 1
	v_permlane32_swap_b32_e32 v19, v21
	s_waitcnt lgkmcnt(0)
	v_add_f32_e32 v19, v19, v21
	v_fmamk_f32 v19, v19, 0x3c800000, v193
	v_mul_f32_e32 v21, 0x4f800000, v19
	v_cmp_gt_f32_e32 vcc, s69, v19
	s_nop 1
	v_cndmask_b32_e32 v19, v19, v21, vcc
	v_sqrt_f32_e32 v21, v19
	s_nop 0
	v_add_u32_e32 v24, -1, v21
	v_fma_f32 v25, -v24, v21, v19
	v_cmp_ge_f32_e64 s[6:7], 0, v25
	v_add_u32_e32 v25, 1, v21
	s_nop 0
	v_cndmask_b32_e64 v24, v21, v24, s[6:7]
	v_fma_f32 v21, -v25, v21, v19
	v_cmp_lt_f32_e64 s[6:7], 0, v21
	s_nop 1
	v_cndmask_b32_e64 v21, v24, v25, s[6:7]
	v_mul_f32_e32 v24, 0x37800000, v21
	v_cndmask_b32_e32 v21, v21, v24, vcc
	v_cmp_class_f32_e32 vcc, v19, v194
	s_nop 1
	v_cndmask_b32_e32 v19, v21, v19, vcc
	v_div_scale_f32 v21, s[6:7], v19, v19, 1.0
	v_rcp_f32_e32 v24, v21
	s_nop 0
	v_fma_f32 v25, -v21, v24, 1.0
	v_fmac_f32_e32 v24, v25, v24
	v_div_scale_f32 v25, vcc, 1.0, v19, 1.0
	v_mul_f32_e32 v26, v25, v24
	v_fma_f32 v27, -v21, v26, v25
	v_fmac_f32_e32 v26, v27, v24
	v_fma_f32 v21, -v21, v26, v25
	v_div_fmas_f32 v21, v21, v24, v26
	v_div_fixup_f32 v24, v21, v19, 1.0
	v_pk_mul_f32 v[26:27], v[158:159], v[24:25] op_sel_hi:[1,0]
	v_pk_mul_f32 v[28:29], v[160:161], v[24:25] op_sel_hi:[1,0]
	s_waitcnt vmcnt(0)
	v_pk_mul_f32 v[182:183], v[14:15], v[26:27]
	v_pk_mul_f32 v[32:33], v[16:17], v[28:29]
	v_pk_mul_f32 v[26:27], v[154:155], v[24:25] op_sel_hi:[1,0]
	v_pk_mul_f32 v[28:29], v[156:157], v[24:25] op_sel_hi:[1,0]
	v_pk_mul_f32 v[184:185], v[6:7], v[26:27]
	v_pk_mul_f32 v[178:179], v[8:9], v[28:29]
	v_pk_mul_f32 v[28:29], v[150:151], v[24:25] op_sel_hi:[1,0]
	v_pk_mul_f32 v[26:27], v[152:153], v[24:25] op_sel_hi:[1,0]
	v_pk_mul_f32 v[180:181], v[146:147], v[24:25] op_sel_hi:[1,0]
	v_pk_mul_f32 v[24:25], v[148:149], v[24:25] op_sel_hi:[1,0]
	v_pk_mul_f32 v[26:27], v[12:13], v[26:27]
	v_pk_mul_f32 v[30:31], v[10:11], v[28:29]
	v_pk_mul_f32 v[28:29], v[4:5], v[24:25]
	v_pk_mul_f32 v[180:181], v[2:3], v[180:181]
.LBB0_1037:
	v_ashrrev_i32_e32 v21, 31, v20
	v_lshl_add_u64 v[22:23], v[22:23], 1, s[24:25]
	v_lshlrev_b64 v[24:25], 9, v[20:21]
	v_lshl_add_u64 v[24:25], v[22:23], 0, v[24:25]
	v_cvt_pk_bf16_f32 v182, v182, v183
	v_cvt_pk_bf16_f32 v183, v32, v33
	v_cvt_pk_bf16_f32 v184, v184, v185
	v_cvt_pk_bf16_f32 v185, v178, v179
	global_store_dwordx4 v[24:25], v[182:185], off
	v_cvt_pk_bf16_f32 v30, v30, v31
	v_cvt_pk_bf16_f32 v31, v26, v27
	v_cvt_pk_bf16_f32 v32, v180, v181
	v_cvt_pk_bf16_f32 v33, v28, v29
	global_store_dwordx4 v[24:25], v[30:33], off offset:64
	s_and_b64 vcc, exec, s[4:5]
	v_mov_b32_e32 v29, v133
	v_mov_b32_e32 v28, v132
	v_mov_b32_e32 v33, v131
	v_mov_b32_e32 v32, v130
	v_mov_b32_e32 v27, v137
	v_mov_b32_e32 v26, v136
	v_mov_b32_e32 v31, v135
	v_mov_b32_e32 v30, v134
	v_mov_b32_e32 v181, v141
	v_mov_b32_e32 v180, v140
	v_mov_b32_e32 v185, v139
	v_mov_b32_e32 v184, v138
	v_mov_b32_e32 v179, v145
	v_mov_b32_e32 v178, v144
	v_mov_b32_e32 v183, v143
	v_mov_b32_e32 v182, v142
	s_cbranch_vccnz .LBB0_1039
; template <bool F8OUT = false> __device__ __forceinline__ void head_tile_store(const f32x4 (&acc)[2][2][4][2], bf16_t* obase  , int opitch, const float* gain, float scale, const f32x2e* rope, int row0, int fq) {
;     ...
;             f32x4 x[2][2];
; #pragma unroll
;             for (int bj = 0; bj < 2; ++bj)
; #pragma unroll
;                 for (int n = 0; n < 2; ++n) x[bj][n] = acc[ai][bj][m][n];
;             if (gain) {
;                 float ss = 0.f;
; #pragma unroll
;                 for (int bj = 0; bj < 2; ++bj)
; #pragma unroll
;                     for (int n = 0; n < 2; ++n) ss += (x[bj][n][0] * x[bj][n][0] + x[bj][n][1] * x[bj][n][1]) + (x[bj][n][2] * x[bj][n][2] + x[bj][n][3] * x[bj][n][3]);
;                 ss += __shfl_xor(ss, 16); ss += __shfl_xor(ss, 32);
;                 const float r = scale / sqrtf(ss * (1.f / 64.f) + 1e-6f);
; #pragma unroll
;                 for (int bj = 0; bj < 2; ++bj)
; #pragma unroll
;                     for (int n = 0; n < 2; ++n) x[bj][n] = x[bj][n] * r * g[bj][n];
;             }
;             if (rope) {
;                 const int t = row & 8191; const bool second = (fq & 2) != 0;
; #pragma unroll
;                 for (int bj = 0; bj < 2; ++bj) { const int pos = bj ? (t & 63) : (t >> 6); const f32x2e* tb = rope + pos * 16 + 8 * (fq & 1);
; #pragma unroll
;                     for (int n = 0; n < 2; ++n)
; #pragma unroll
;                         for (int e = 0; e < 4; ++e) { const float p = __shfl_xor(x[bj][n][e], 32); const f32x2e cs = tb[4 * n + e]; const float v = x[bj][n][e];
;                             x[bj][n][e] = second ? (p * cs.y + v * cs.x) : (v * cs.x - p * cs.y); } }
;             }
;             if constexpr (F8OUT) { unsigned char* rowp8 = (unsigned char*)obase + (size_t)row * opitch + 8 * fq; typedef unsigned u32x2_ __attribute__((ext_vector_type(2)));
; #pragma unroll
;                 for (int bj = 0; bj < 2; ++bj) *(u32x2_*)(rowp8 + 32 * bj) = (u32x2_){pk4_fp8(x[bj][0][0], x[bj][0][1], x[bj][0][2], x[bj][0][3]), pk4_fp8(x[bj][1][0], x[bj][1][1], x[bj][1][2], x[bj][1][3])};
;                 continue; }
;             bf16_t* rowp = obase + (size_t)row * opitch + 8 * fq;
; #pragma unroll
	v_pk_mul_f32 v[26:27], v[144:145], v[144:145]
	v_pk_mul_f32 v[28:29], v[142:143], v[142:143]
	v_mul_f32_e32 v19, v130, v130
	v_pk_mov_b32 v[30:31], v[28:29], v[26:27] op_sel:[1,0]
	v_mov_b32_e32 v29, v27
	v_pk_add_f32 v[26:27], v[30:31], v[28:29]
	v_pk_mul_f32 v[28:29], v[140:141], v[140:141]
	v_pk_mul_f32 v[30:31], v[138:139], v[138:139]
	v_pk_add_f32 v[26:27], v[26:27], v[26:27] op_sel:[0,1] op_sel_hi:[1,0]
	v_pk_mov_b32 v[32:33], v[30:31], v[28:29] op_sel:[1,0]
	v_mov_b32_e32 v31, v29
	v_pk_add_f32 v[28:29], v[32:33], v[30:31]
	v_mul_f32_e32 v30, v131, v131
	v_pk_add_f32 v[28:29], v[28:29], v[28:29] op_sel:[0,1] op_sel_hi:[1,0]
	v_mov_b32_e32 v27, v19
	v_mov_b32_e32 v29, v30
	v_pk_add_f32 v[26:27], v[26:27], v[28:29]
	v_mul_f32_e32 v28, v135, v135
	v_mul_f32_e32 v31, v132, v132
	v_pk_fma_f32 v[28:29], v[134:135], v[134:135], v[28:29] op_sel_hi:[1,1,0]
	v_mul_f32_e32 v30, v137, v137
	v_mul_f32_e32 v32, v133, v133
	v_mov_b32_e32 v29, v31
	v_pk_fma_f32 v[30:31], v[136:137], v[136:137], v[30:31] op_sel_hi:[1,1,0]
	s_nop 0
	v_mov_b32_e32 v31, v32
	v_pk_add_f32 v[28:29], v[28:29], v[30:31]
	s_nop 0
	v_pk_add_f32 v[26:27], v[26:27], v[28:29]
	s_nop 0
	v_add_f32_e32 v19, v26, v27
	v_and_b32_e32 v27, 64, v195
	v_xor_b32_e32 v26, 16, v195
	v_add_u32_e32 v27, 64, v27
	v_cmp_lt_i32_e32 vcc, v26, v27
	s_nop 1
	v_cndmask_b32_e32 v26, v195, v26, vcc
	v_lshlrev_b32_e32 v26, 2, v26
	v_mov_b32_e32 v26, v19
	s_nop 1
	v_permlane16_swap_b32_e32 v19, v26
	s_waitcnt lgkmcnt(0)
	v_add_f32_e32 v19, v19, v26
	v_xor_b32_e32 v26, 32, v195
	v_cmp_lt_i32_e32 vcc, v26, v27
	s_nop 1
	v_cndmask_b32_e32 v26, v195, v26, vcc
	v_lshlrev_b32_e32 v26, 2, v26
	v_mov_b32_e32 v26, v19
	s_nop 1
	v_permlane32_swap_b32_e32 v19, v26
	s_waitcnt lgkmcnt(0)
	v_add_f32_e32 v19, v19, v26
	v_fmamk_f32 v19, v19, 0x3c800000, v193
	v_mul_f32_e32 v26, 0x4f800000, v19
	v_cmp_gt_f32_e32 vcc, s69, v19
	s_nop 1
	v_cndmask_b32_e32 v19, v19, v26, vcc
	v_sqrt_f32_e32 v26, v19
	s_nop 0
	v_add_u32_e32 v27, -1, v26
	v_fma_f32 v28, -v27, v26, v19
	v_cmp_ge_f32_e64 s[6:7], 0, v28
	v_add_u32_e32 v28, 1, v26
	s_nop 0
	v_cndmask_b32_e64 v27, v26, v27, s[6:7]
	v_fma_f32 v26, -v28, v26, v19
	v_cmp_lt_f32_e64 s[6:7], 0, v26
	s_nop 1
	v_cndmask_b32_e64 v26, v27, v28, s[6:7]
	v_mul_f32_e32 v27, 0x37800000, v26
	v_cndmask_b32_e32 v26, v26, v27, vcc
	v_cmp_class_f32_e32 vcc, v19, v194
	s_nop 1
	v_cndmask_b32_e32 v19, v26, v19, vcc
	v_div_scale_f32 v26, s[6:7], v19, v19, 1.0
	v_rcp_f32_e32 v27, v26
	s_nop 0
	v_fma_f32 v28, -v26, v27, 1.0
	v_fmac_f32_e32 v27, v28, v27
	v_div_scale_f32 v28, vcc, 1.0, v19, 1.0
	v_mul_f32_e32 v29, v28, v27
	v_fma_f32 v30, -v26, v29, v28
	v_fmac_f32_e32 v29, v30, v27
	v_fma_f32 v26, -v26, v29, v28
	v_div_fmas_f32 v26, v26, v27, v29
	v_div_fixup_f32 v28, v26, v19, 1.0
	v_pk_mul_f32 v[26:27], v[142:143], v[28:29] op_sel_hi:[1,0]
	v_pk_mul_f32 v[30:31], v[144:145], v[28:29] op_sel_hi:[1,0]
	s_nop 0
	v_pk_mul_f32 v[182:183], v[14:15], v[26:27]
	v_pk_mul_f32 v[178:179], v[16:17], v[30:31]
	v_pk_mul_f32 v[26:27], v[138:139], v[28:29] op_sel_hi:[1,0]
	v_pk_mul_f32 v[30:31], v[140:141], v[28:29] op_sel_hi:[1,0]
	v_pk_mul_f32 v[184:185], v[6:7], v[26:27]
	v_pk_mul_f32 v[180:181], v[8:9], v[30:31]
	v_pk_mul_f32 v[30:31], v[134:135], v[28:29] op_sel_hi:[1,0]
	v_pk_mul_f32 v[26:27], v[136:137], v[28:29] op_sel_hi:[1,0]
	v_pk_mul_f32 v[32:33], v[130:131], v[28:29] op_sel_hi:[1,0]
	v_pk_mul_f32 v[28:29], v[132:133], v[28:29] op_sel_hi:[1,0]
	v_pk_mul_f32 v[26:27], v[12:13], v[26:27]
	v_pk_mul_f32 v[30:31], v[10:11], v[30:31]
	v_pk_mul_f32 v[28:29], v[4:5], v[28:29]
	v_pk_mul_f32 v[32:33], v[2:3], v[32:33]
.LBB0_1039:
	v_cvt_pk_bf16_f32 v182, v182, v183
	v_cvt_pk_bf16_f32 v183, v178, v179
	v_add_co_u32_e32 v178, vcc, 0x2000, v24
	v_lshl_add_u64 v[196:197], v[24:25], 0, s[26:27]
	s_nop 0
	v_addc_co_u32_e32 v179, vcc, 0, v25, vcc
	v_cvt_pk_bf16_f32 v184, v184, v185
	v_cvt_pk_bf16_f32 v185, v180, v181
	global_store_dwordx4 v[178:179], v[182:185], off
	v_cvt_pk_bf16_f32 v30, v30, v31
	v_cvt_pk_bf16_f32 v31, v26, v27
	v_cvt_pk_bf16_f32 v32, v32, v33
	v_cvt_pk_bf16_f32 v33, v28, v29
	global_store_dwordx4 v[196:197], v[30:33], off offset:64
	s_and_b64 vcc, exec, s[4:5]
	v_mov_b32_e32 v29, v117
	v_mov_b32_e32 v28, v116
	v_mov_b32_e32 v33, v115
	v_mov_b32_e32 v32, v114
	v_mov_b32_e32 v27, v121
	v_mov_b32_e32 v26, v120
	v_mov_b32_e32 v31, v119
	v_mov_b32_e32 v30, v118
	v_mov_b32_e32 v181, v125
	v_mov_b32_e32 v180, v124
	v_mov_b32_e32 v185, v123
	v_mov_b32_e32 v184, v122
	v_mov_b32_e32 v179, v129
	v_mov_b32_e32 v178, v128
	v_mov_b32_e32 v183, v127
	v_mov_b32_e32 v182, v126
	s_cbranch_vccnz .LBB0_1041
; template <bool F8OUT = false> __device__ __forceinline__ void head_tile_store(const f32x4 (&acc)[2][2][4][2], bf16_t* obase  , int opitch, const float* gain, float scale, const f32x2e* rope, int row0, int fq) {
;     ...
;             f32x4 x[2][2];
; #pragma unroll
;             for (int bj = 0; bj < 2; ++bj)
; #pragma unroll
;                 for (int n = 0; n < 2; ++n) x[bj][n] = acc[ai][bj][m][n];
;             if (gain) {
;                 float ss = 0.f;
; #pragma unroll
;                 for (int bj = 0; bj < 2; ++bj)
; #pragma unroll
;                     for (int n = 0; n < 2; ++n) ss += (x[bj][n][0] * x[bj][n][0] + x[bj][n][1] * x[bj][n][1]) + (x[bj][n][2] * x[bj][n][2] + x[bj][n][3] * x[bj][n][3]);
;                 ss += __shfl_xor(ss, 16); ss += __shfl_xor(ss, 32);
;                 const float r = scale / sqrtf(ss * (1.f / 64.f) + 1e-6f);
; #pragma unroll
;                 for (int bj = 0; bj < 2; ++bj)
; #pragma unroll
;                     for (int n = 0; n < 2; ++n) x[bj][n] = x[bj][n] * r * g[bj][n];
;             }
;             if (rope) {
;                 const int t = row & 8191; const bool second = (fq & 2) != 0;
; #pragma unroll
;                 for (int bj = 0; bj < 2; ++bj) { const int pos = bj ? (t & 63) : (t >> 6); const f32x2e* tb = rope + pos * 16 + 8 * (fq & 1);
; #pragma unroll
;                     for (int n = 0; n < 2; ++n)
; #pragma unroll
;                         for (int e = 0; e < 4; ++e) { const float p = __shfl_xor(x[bj][n][e], 32); const f32x2e cs = tb[4 * n + e]; const float v = x[bj][n][e];
;                             x[bj][n][e] = second ? (p * cs.y + v * cs.x) : (v * cs.x - p * cs.y); } }
;             }
;             if constexpr (F8OUT) { unsigned char* rowp8 = (unsigned char*)obase + (size_t)row * opitch + 8 * fq; typedef unsigned u32x2_ __attribute__((ext_vector_type(2)));
; #pragma unroll
;                 for (int bj = 0; bj < 2; ++bj) *(u32x2_*)(rowp8 + 32 * bj) = (u32x2_){pk4_fp8(x[bj][0][0], x[bj][0][1], x[bj][0][2], x[bj][0][3]), pk4_fp8(x[bj][1][0], x[bj][1][1], x[bj][1][2], x[bj][1][3])};
;                 continue; }
;             bf16_t* rowp = obase + (size_t)row * opitch + 8 * fq;
; #pragma unroll
	v_pk_mul_f32 v[26:27], v[128:129], v[128:129]
	v_pk_mul_f32 v[28:29], v[126:127], v[126:127]
	v_mul_f32_e32 v19, v114, v114
	v_pk_mov_b32 v[30:31], v[28:29], v[26:27] op_sel:[1,0]
	v_mov_b32_e32 v29, v27
	v_pk_add_f32 v[26:27], v[30:31], v[28:29]
	v_pk_mul_f32 v[28:29], v[124:125], v[124:125]
	v_pk_mul_f32 v[30:31], v[122:123], v[122:123]
	v_pk_add_f32 v[26:27], v[26:27], v[26:27] op_sel:[0,1] op_sel_hi:[1,0]
	v_pk_mov_b32 v[32:33], v[30:31], v[28:29] op_sel:[1,0]
	v_mov_b32_e32 v31, v29
	v_pk_add_f32 v[28:29], v[32:33], v[30:31]
	v_mul_f32_e32 v30, v115, v115
	v_pk_add_f32 v[28:29], v[28:29], v[28:29] op_sel:[0,1] op_sel_hi:[1,0]
	v_mov_b32_e32 v27, v19
	v_mov_b32_e32 v29, v30
	v_pk_add_f32 v[26:27], v[26:27], v[28:29]
	v_mul_f32_e32 v28, v119, v119
	v_mul_f32_e32 v31, v116, v116
	v_pk_fma_f32 v[28:29], v[118:119], v[118:119], v[28:29] op_sel_hi:[1,1,0]
	v_mul_f32_e32 v30, v121, v121
	v_mul_f32_e32 v32, v117, v117
	v_mov_b32_e32 v29, v31
	v_pk_fma_f32 v[30:31], v[120:121], v[120:121], v[30:31] op_sel_hi:[1,1,0]
	s_nop 0
	v_mov_b32_e32 v31, v32
	v_pk_add_f32 v[28:29], v[28:29], v[30:31]
	s_nop 0
	v_pk_add_f32 v[26:27], v[26:27], v[28:29]
	s_nop 0
	v_add_f32_e32 v19, v26, v27
	v_and_b32_e32 v27, 64, v195
	v_xor_b32_e32 v26, 16, v195
	v_add_u32_e32 v27, 64, v27
	v_cmp_lt_i32_e32 vcc, v26, v27
	s_nop 1
	v_cndmask_b32_e32 v26, v195, v26, vcc
	v_lshlrev_b32_e32 v26, 2, v26
	v_mov_b32_e32 v26, v19
	s_nop 1
	v_permlane16_swap_b32_e32 v19, v26
	s_waitcnt lgkmcnt(0)
	v_add_f32_e32 v19, v19, v26
	v_xor_b32_e32 v26, 32, v195
	v_cmp_lt_i32_e32 vcc, v26, v27
	s_nop 1
	v_cndmask_b32_e32 v26, v195, v26, vcc
	v_lshlrev_b32_e32 v26, 2, v26
	v_mov_b32_e32 v26, v19
	s_nop 1
	v_permlane32_swap_b32_e32 v19, v26
	s_waitcnt lgkmcnt(0)
	v_add_f32_e32 v19, v19, v26
	v_fmamk_f32 v19, v19, 0x3c800000, v193
	v_mul_f32_e32 v26, 0x4f800000, v19
	v_cmp_gt_f32_e32 vcc, s69, v19
	s_nop 1
	v_cndmask_b32_e32 v19, v19, v26, vcc
	v_sqrt_f32_e32 v26, v19
	s_nop 0
	v_add_u32_e32 v27, -1, v26
	v_fma_f32 v28, -v27, v26, v19
	v_cmp_ge_f32_e64 s[6:7], 0, v28
	v_add_u32_e32 v28, 1, v26
	s_nop 0
	v_cndmask_b32_e64 v27, v26, v27, s[6:7]
	v_fma_f32 v26, -v28, v26, v19
	v_cmp_lt_f32_e64 s[6:7], 0, v26
	s_nop 1
	v_cndmask_b32_e64 v26, v27, v28, s[6:7]
	v_mul_f32_e32 v27, 0x37800000, v26
	v_cndmask_b32_e32 v26, v26, v27, vcc
	v_cmp_class_f32_e32 vcc, v19, v194
	s_nop 1
	v_cndmask_b32_e32 v19, v26, v19, vcc
	v_div_scale_f32 v26, s[6:7], v19, v19, 1.0
	v_rcp_f32_e32 v27, v26
	s_nop 0
	v_fma_f32 v28, -v26, v27, 1.0
	v_fmac_f32_e32 v27, v28, v27
	v_div_scale_f32 v28, vcc, 1.0, v19, 1.0
	v_mul_f32_e32 v29, v28, v27
	v_fma_f32 v30, -v26, v29, v28
	v_fmac_f32_e32 v29, v30, v27
	v_fma_f32 v26, -v26, v29, v28
	v_div_fmas_f32 v26, v26, v27, v29
	v_div_fixup_f32 v28, v26, v19, 1.0
	v_pk_mul_f32 v[26:27], v[126:127], v[28:29] op_sel_hi:[1,0]
	v_pk_mul_f32 v[30:31], v[128:129], v[28:29] op_sel_hi:[1,0]
	s_nop 0
	v_pk_mul_f32 v[182:183], v[14:15], v[26:27]
	v_pk_mul_f32 v[178:179], v[16:17], v[30:31]
	v_pk_mul_f32 v[26:27], v[122:123], v[28:29] op_sel_hi:[1,0]
	v_pk_mul_f32 v[30:31], v[124:125], v[28:29] op_sel_hi:[1,0]
	v_pk_mul_f32 v[184:185], v[6:7], v[26:27]
	v_pk_mul_f32 v[180:181], v[8:9], v[30:31]
	v_pk_mul_f32 v[30:31], v[118:119], v[28:29] op_sel_hi:[1,0]
	v_pk_mul_f32 v[26:27], v[120:121], v[28:29] op_sel_hi:[1,0]
	v_pk_mul_f32 v[32:33], v[114:115], v[28:29] op_sel_hi:[1,0]
	v_pk_mul_f32 v[28:29], v[116:117], v[28:29] op_sel_hi:[1,0]
	v_pk_mul_f32 v[26:27], v[12:13], v[26:27]
	v_pk_mul_f32 v[30:31], v[10:11], v[30:31]
	v_pk_mul_f32 v[28:29], v[4:5], v[28:29]
	v_pk_mul_f32 v[32:33], v[2:3], v[32:33]
.LBB0_1041:
	v_lshl_add_u64 v[196:197], v[24:25], 0, s[28:29]
	v_add_co_u32_e32 v24, vcc, 0x4000, v24
	v_cvt_pk_bf16_f32 v182, v182, v183
	v_cvt_pk_bf16_f32 v183, v178, v179
	v_cvt_pk_bf16_f32 v184, v184, v185
	v_cvt_pk_bf16_f32 v185, v180, v181
	s_nop 1
	v_addc_co_u32_e32 v25, vcc, 0, v25, vcc
	global_store_dwordx4 v[24:25], v[182:185], off
	v_cvt_pk_bf16_f32 v24, v30, v31
	v_cvt_pk_bf16_f32 v25, v26, v27
	v_cvt_pk_bf16_f32 v26, v32, v33
	v_cvt_pk_bf16_f32 v27, v28, v29
	global_store_dwordx4 v[196:197], v[24:27], off offset:64
	s_and_b64 vcc, exec, s[4:5]
	v_mov_b32_e32 v29, v101
	v_mov_b32_e32 v28, v100
	v_mov_b32_e32 v33, v99
	v_mov_b32_e32 v32, v98
	v_mov_b32_e32 v27, v105
	v_mov_b32_e32 v26, v104
	v_mov_b32_e32 v31, v103
	v_mov_b32_e32 v30, v102
	v_mov_b32_e32 v181, v109
	v_mov_b32_e32 v180, v108
	v_mov_b32_e32 v185, v107
	v_mov_b32_e32 v184, v106
	v_mov_b32_e32 v179, v113
	v_mov_b32_e32 v178, v112
	v_mov_b32_e32 v183, v111
	v_mov_b32_e32 v182, v110
	s_cbranch_vccnz .LBB0_1043
; template <bool F8OUT = false> __device__ __forceinline__ void head_tile_store(const f32x4 (&acc)[2][2][4][2], bf16_t* obase  , int opitch, const float* gain, float scale, const f32x2e* rope, int row0, int fq) {
;     ...
;             f32x4 x[2][2];
; #pragma unroll
;             for (int bj = 0; bj < 2; ++bj)
; #pragma unroll
;                 for (int n = 0; n < 2; ++n) x[bj][n] = acc[ai][bj][m][n];
;             if (gain) {
;                 float ss = 0.f;
; #pragma unroll
;                 for (int bj = 0; bj < 2; ++bj)
; #pragma unroll
;                     for (int n = 0; n < 2; ++n) ss += (x[bj][n][0] * x[bj][n][0] + x[bj][n][1] * x[bj][n][1]) + (x[bj][n][2] * x[bj][n][2] + x[bj][n][3] * x[bj][n][3]);
;                 ss += __shfl_xor(ss, 16); ss += __shfl_xor(ss, 32);
;                 const float r = scale / sqrtf(ss * (1.f / 64.f) + 1e-6f);
; #pragma unroll
;                 for (int bj = 0; bj < 2; ++bj)
; #pragma unroll
;                     for (int n = 0; n < 2; ++n) x[bj][n] = x[bj][n] * r * g[bj][n];
;             }
;             if (rope) {
;                 const int t = row & 8191; const bool second = (fq & 2) != 0;
; #pragma unroll
;                 for (int bj = 0; bj < 2; ++bj) { const int pos = bj ? (t & 63) : (t >> 6); const f32x2e* tb = rope + pos * 16 + 8 * (fq & 1);
; #pragma unroll
;                     for (int n = 0; n < 2; ++n)
; #pragma unroll
;                         for (int e = 0; e < 4; ++e) { const float p = __shfl_xor(x[bj][n][e], 32); const f32x2e cs = tb[4 * n + e]; const float v = x[bj][n][e];
;                             x[bj][n][e] = second ? (p * cs.y + v * cs.x) : (v * cs.x - p * cs.y); } }
;             }
;             if constexpr (F8OUT) { unsigned char* rowp8 = (unsigned char*)obase + (size_t)row * opitch + 8 * fq; typedef unsigned u32x2_ __attribute__((ext_vector_type(2)));
; #pragma unroll
;                 for (int bj = 0; bj < 2; ++bj) *(u32x2_*)(rowp8 + 32 * bj) = (u32x2_){pk4_fp8(x[bj][0][0], x[bj][0][1], x[bj][0][2], x[bj][0][3]), pk4_fp8(x[bj][1][0], x[bj][1][1], x[bj][1][2], x[bj][1][3])};
;                 continue; }
;             bf16_t* rowp = obase + (size_t)row * opitch + 8 * fq;
; #pragma unroll
	v_pk_mul_f32 v[24:25], v[112:113], v[112:113]
	v_pk_mul_f32 v[26:27], v[110:111], v[110:111]
	v_mul_f32_e32 v19, v98, v98
	v_pk_mov_b32 v[28:29], v[26:27], v[24:25] op_sel:[1,0]
	v_mov_b32_e32 v27, v25
	v_pk_add_f32 v[24:25], v[28:29], v[26:27]
	v_pk_mul_f32 v[26:27], v[108:109], v[108:109]
	v_pk_mul_f32 v[28:29], v[106:107], v[106:107]
	v_pk_add_f32 v[24:25], v[24:25], v[24:25] op_sel:[0,1] op_sel_hi:[1,0]
	v_pk_mov_b32 v[30:31], v[28:29], v[26:27] op_sel:[1,0]
	v_mov_b32_e32 v29, v27
	v_pk_add_f32 v[26:27], v[30:31], v[28:29]
	v_mul_f32_e32 v28, v99, v99
	v_pk_add_f32 v[26:27], v[26:27], v[26:27] op_sel:[0,1] op_sel_hi:[1,0]
	v_mov_b32_e32 v25, v19
	v_mov_b32_e32 v27, v28
	v_pk_add_f32 v[24:25], v[24:25], v[26:27]
	v_mul_f32_e32 v26, v103, v103
	v_mul_f32_e32 v29, v100, v100
	v_pk_fma_f32 v[26:27], v[102:103], v[102:103], v[26:27] op_sel_hi:[1,1,0]
	v_mul_f32_e32 v28, v105, v105
	v_mul_f32_e32 v30, v101, v101
	v_mov_b32_e32 v27, v29
	v_pk_fma_f32 v[28:29], v[104:105], v[104:105], v[28:29] op_sel_hi:[1,1,0]
	s_nop 0
	v_mov_b32_e32 v29, v30
	v_pk_add_f32 v[26:27], v[26:27], v[28:29]
	s_nop 0
	v_pk_add_f32 v[24:25], v[24:25], v[26:27]
	s_nop 0
	v_add_f32_e32 v19, v24, v25
	v_and_b32_e32 v25, 64, v195
	v_xor_b32_e32 v24, 16, v195
	v_add_u32_e32 v25, 64, v25
	v_cmp_lt_i32_e32 vcc, v24, v25
	s_nop 1
	v_cndmask_b32_e32 v24, v195, v24, vcc
	v_lshlrev_b32_e32 v24, 2, v24
	v_mov_b32_e32 v24, v19
	s_nop 1
	v_permlane16_swap_b32_e32 v19, v24
	s_waitcnt lgkmcnt(0)
	v_add_f32_e32 v19, v19, v24
	v_xor_b32_e32 v24, 32, v195
	v_cmp_lt_i32_e32 vcc, v24, v25
	s_nop 1
	v_cndmask_b32_e32 v24, v195, v24, vcc
	v_lshlrev_b32_e32 v24, 2, v24
	v_mov_b32_e32 v24, v19
	s_nop 1
	v_permlane32_swap_b32_e32 v19, v24
	s_waitcnt lgkmcnt(0)
	v_add_f32_e32 v19, v19, v24
	v_fmamk_f32 v19, v19, 0x3c800000, v193
	v_mul_f32_e32 v24, 0x4f800000, v19
	v_cmp_gt_f32_e32 vcc, s69, v19
	s_nop 1
	v_cndmask_b32_e32 v19, v19, v24, vcc
	v_sqrt_f32_e32 v24, v19
	s_nop 0
	v_add_u32_e32 v25, -1, v24
	v_fma_f32 v26, -v25, v24, v19
	v_cmp_ge_f32_e64 s[6:7], 0, v26
	v_add_u32_e32 v26, 1, v24
	s_nop 0
	v_cndmask_b32_e64 v25, v24, v25, s[6:7]
	v_fma_f32 v24, -v26, v24, v19
	v_cmp_lt_f32_e64 s[6:7], 0, v24
	s_nop 1
	v_cndmask_b32_e64 v24, v25, v26, s[6:7]
	v_mul_f32_e32 v25, 0x37800000, v24
	v_cndmask_b32_e32 v24, v24, v25, vcc
	v_cmp_class_f32_e32 vcc, v19, v194
	s_nop 1
	v_cndmask_b32_e32 v19, v24, v19, vcc
	v_div_scale_f32 v24, s[6:7], v19, v19, 1.0
	v_rcp_f32_e32 v25, v24
	s_nop 0
	v_fma_f32 v26, -v24, v25, 1.0
	v_fmac_f32_e32 v25, v26, v25
	v_div_scale_f32 v26, vcc, 1.0, v19, 1.0
	v_mul_f32_e32 v27, v26, v25
	v_fma_f32 v28, -v24, v27, v26
	v_fmac_f32_e32 v27, v28, v25
	v_fma_f32 v24, -v24, v27, v26
	v_div_fmas_f32 v24, v24, v25, v27
	v_div_fixup_f32 v24, v24, v19, 1.0
	v_pk_mul_f32 v[26:27], v[110:111], v[24:25] op_sel_hi:[1,0]
	v_pk_mul_f32 v[28:29], v[112:113], v[24:25] op_sel_hi:[1,0]
	s_nop 0
	v_pk_mul_f32 v[182:183], v[14:15], v[26:27]
	v_pk_mul_f32 v[178:179], v[16:17], v[28:29]
	v_pk_mul_f32 v[26:27], v[106:107], v[24:25] op_sel_hi:[1,0]
	v_pk_mul_f32 v[28:29], v[108:109], v[24:25] op_sel_hi:[1,0]
	v_pk_mul_f32 v[184:185], v[6:7], v[26:27]
	v_pk_mul_f32 v[180:181], v[8:9], v[28:29]
	v_pk_mul_f32 v[28:29], v[102:103], v[24:25] op_sel_hi:[1,0]
	v_pk_mul_f32 v[26:27], v[104:105], v[24:25] op_sel_hi:[1,0]
	v_pk_mul_f32 v[32:33], v[98:99], v[24:25] op_sel_hi:[1,0]
	v_pk_mul_f32 v[24:25], v[100:101], v[24:25] op_sel_hi:[1,0]
	v_pk_mul_f32 v[26:27], v[12:13], v[26:27]
	v_pk_mul_f32 v[30:31], v[10:11], v[28:29]
	v_pk_mul_f32 v[28:29], v[4:5], v[24:25]
	v_pk_mul_f32 v[32:33], v[2:3], v[32:33]
.LBB0_1043:
	v_lshlrev_b64 v[24:25], 9, v[20:21]
	v_lshl_add_u64 v[24:25], v[22:23], 0, v[24:25]
	v_cvt_pk_bf16_f32 v182, v182, v183
	v_cvt_pk_bf16_f32 v183, v178, v179
	v_add_co_u32_e32 v178, vcc, 0x6000, v24
	v_lshl_add_u64 v[196:197], v[24:25], 0, s[30:31]
	s_nop 0
	v_addc_co_u32_e32 v179, vcc, 0, v25, vcc
	v_cvt_pk_bf16_f32 v184, v184, v185
	v_cvt_pk_bf16_f32 v185, v180, v181
	global_store_dwordx4 v[178:179], v[182:185], off
	v_cvt_pk_bf16_f32 v30, v30, v31
	v_cvt_pk_bf16_f32 v31, v26, v27
	v_cvt_pk_bf16_f32 v32, v32, v33
	v_cvt_pk_bf16_f32 v33, v28, v29
	global_store_dwordx4 v[196:197], v[30:33], off offset:64
	s_and_b64 vcc, exec, s[4:5]
	v_mov_b32_e32 v29, v85
	v_mov_b32_e32 v28, v84
	v_mov_b32_e32 v33, v83
	v_mov_b32_e32 v32, v82
	v_mov_b32_e32 v27, v89
	v_mov_b32_e32 v26, v88
	v_mov_b32_e32 v31, v87
	v_mov_b32_e32 v30, v86
	v_mov_b32_e32 v181, v93
	v_mov_b32_e32 v180, v92
	v_mov_b32_e32 v185, v91
	v_mov_b32_e32 v184, v90
	v_mov_b32_e32 v179, v97
	v_mov_b32_e32 v178, v96
	v_mov_b32_e32 v183, v95
	v_mov_b32_e32 v182, v94
	s_cbranch_vccnz .LBB0_1045
; template <bool F8OUT = false> __device__ __forceinline__ void head_tile_store(const f32x4 (&acc)[2][2][4][2], bf16_t* obase  , int opitch, const float* gain, float scale, const f32x2e* rope, int row0, int fq) {
;     ...
;             f32x4 x[2][2];
; #pragma unroll
;             for (int bj = 0; bj < 2; ++bj)
; #pragma unroll
;                 for (int n = 0; n < 2; ++n) x[bj][n] = acc[ai][bj][m][n];
;             if (gain) {
;                 float ss = 0.f;
; #pragma unroll
;                 for (int bj = 0; bj < 2; ++bj)
; #pragma unroll
;                     for (int n = 0; n < 2; ++n) ss += (x[bj][n][0] * x[bj][n][0] + x[bj][n][1] * x[bj][n][1]) + (x[bj][n][2] * x[bj][n][2] + x[bj][n][3] * x[bj][n][3]);
;                 ss += __shfl_xor(ss, 16); ss += __shfl_xor(ss, 32);
;                 const float r = scale / sqrtf(ss * (1.f / 64.f) + 1e-6f);
; #pragma unroll
;                 for (int bj = 0; bj < 2; ++bj)
; #pragma unroll
;                     for (int n = 0; n < 2; ++n) x[bj][n] = x[bj][n] * r * g[bj][n];
;             }
;             if (rope) {
;                 const int t = row & 8191; const bool second = (fq & 2) != 0;
; #pragma unroll
;                 for (int bj = 0; bj < 2; ++bj) { const int pos = bj ? (t & 63) : (t >> 6); const f32x2e* tb = rope + pos * 16 + 8 * (fq & 1);
; #pragma unroll
;                     for (int n = 0; n < 2; ++n)
; #pragma unroll
;                         for (int e = 0; e < 4; ++e) { const float p = __shfl_xor(x[bj][n][e], 32); const f32x2e cs = tb[4 * n + e]; const float v = x[bj][n][e];
;                             x[bj][n][e] = second ? (p * cs.y + v * cs.x) : (v * cs.x - p * cs.y); } }
;             }
;             if constexpr (F8OUT) { unsigned char* rowp8 = (unsigned char*)obase + (size_t)row * opitch + 8 * fq; typedef unsigned u32x2_ __attribute__((ext_vector_type(2)));
; #pragma unroll
;                 for (int bj = 0; bj < 2; ++bj) *(u32x2_*)(rowp8 + 32 * bj) = (u32x2_){pk4_fp8(x[bj][0][0], x[bj][0][1], x[bj][0][2], x[bj][0][3]), pk4_fp8(x[bj][1][0], x[bj][1][1], x[bj][1][2], x[bj][1][3])};
;                 continue; }
;             bf16_t* rowp = obase + (size_t)row * opitch + 8 * fq;
; #pragma unroll
	v_pk_mul_f32 v[26:27], v[96:97], v[96:97]
	v_pk_mul_f32 v[28:29], v[94:95], v[94:95]
	v_mul_f32_e32 v19, v82, v82
	v_pk_mov_b32 v[30:31], v[28:29], v[26:27] op_sel:[1,0]
	v_mov_b32_e32 v29, v27
	v_pk_add_f32 v[26:27], v[30:31], v[28:29]
	v_pk_mul_f32 v[28:29], v[92:93], v[92:93]
	v_pk_mul_f32 v[30:31], v[90:91], v[90:91]
	v_pk_add_f32 v[26:27], v[26:27], v[26:27] op_sel:[0,1] op_sel_hi:[1,0]
	v_pk_mov_b32 v[32:33], v[30:31], v[28:29] op_sel:[1,0]
	v_mov_b32_e32 v31, v29
	v_pk_add_f32 v[28:29], v[32:33], v[30:31]
	v_mul_f32_e32 v30, v83, v83
	v_pk_add_f32 v[28:29], v[28:29], v[28:29] op_sel:[0,1] op_sel_hi:[1,0]
	v_mov_b32_e32 v27, v19
	v_mov_b32_e32 v29, v30
	v_pk_add_f32 v[26:27], v[26:27], v[28:29]
	v_mul_f32_e32 v28, v87, v87
	v_mul_f32_e32 v31, v84, v84
	v_pk_fma_f32 v[28:29], v[86:87], v[86:87], v[28:29] op_sel_hi:[1,1,0]
	v_mul_f32_e32 v30, v89, v89
	v_mul_f32_e32 v32, v85, v85
	v_mov_b32_e32 v29, v31
	v_pk_fma_f32 v[30:31], v[88:89], v[88:89], v[30:31] op_sel_hi:[1,1,0]
	s_nop 0
	v_mov_b32_e32 v31, v32
	v_pk_add_f32 v[28:29], v[28:29], v[30:31]
	s_nop 0
	v_pk_add_f32 v[26:27], v[26:27], v[28:29]
	s_nop 0
	v_add_f32_e32 v19, v26, v27
	v_and_b32_e32 v27, 64, v195
	v_xor_b32_e32 v26, 16, v195
	v_add_u32_e32 v27, 64, v27
	v_cmp_lt_i32_e32 vcc, v26, v27
	s_nop 1
	v_cndmask_b32_e32 v26, v195, v26, vcc
	v_lshlrev_b32_e32 v26, 2, v26
	v_mov_b32_e32 v26, v19
	s_nop 1
	v_permlane16_swap_b32_e32 v19, v26
	s_waitcnt lgkmcnt(0)
	v_add_f32_e32 v19, v19, v26
	v_xor_b32_e32 v26, 32, v195
	v_cmp_lt_i32_e32 vcc, v26, v27
	s_nop 1
	v_cndmask_b32_e32 v26, v195, v26, vcc
	v_lshlrev_b32_e32 v26, 2, v26
	v_mov_b32_e32 v26, v19
	s_nop 1
	v_permlane32_swap_b32_e32 v19, v26
	s_waitcnt lgkmcnt(0)
	v_add_f32_e32 v19, v19, v26
	v_fmamk_f32 v19, v19, 0x3c800000, v193
	v_mul_f32_e32 v26, 0x4f800000, v19
	v_cmp_gt_f32_e32 vcc, s69, v19
	s_nop 1
	v_cndmask_b32_e32 v19, v19, v26, vcc
	v_sqrt_f32_e32 v26, v19
	s_nop 0
	v_add_u32_e32 v27, -1, v26
	v_fma_f32 v28, -v27, v26, v19
	v_cmp_ge_f32_e64 s[6:7], 0, v28
	v_add_u32_e32 v28, 1, v26
	s_nop 0
	v_cndmask_b32_e64 v27, v26, v27, s[6:7]
	v_fma_f32 v26, -v28, v26, v19
	v_cmp_lt_f32_e64 s[6:7], 0, v26
	s_nop 1
	v_cndmask_b32_e64 v26, v27, v28, s[6:7]
	v_mul_f32_e32 v27, 0x37800000, v26
	v_cndmask_b32_e32 v26, v26, v27, vcc
	v_cmp_class_f32_e32 vcc, v19, v194
	s_nop 1
	v_cndmask_b32_e32 v19, v26, v19, vcc
	v_div_scale_f32 v26, s[6:7], v19, v19, 1.0
	v_rcp_f32_e32 v27, v26
	s_nop 0
	v_fma_f32 v28, -v26, v27, 1.0
	v_fmac_f32_e32 v27, v28, v27
	v_div_scale_f32 v28, vcc, 1.0, v19, 1.0
	v_mul_f32_e32 v29, v28, v27
	v_fma_f32 v30, -v26, v29, v28
	v_fmac_f32_e32 v29, v30, v27
	v_fma_f32 v26, -v26, v29, v28
	v_div_fmas_f32 v26, v26, v27, v29
	v_div_fixup_f32 v28, v26, v19, 1.0
	v_pk_mul_f32 v[26:27], v[94:95], v[28:29] op_sel_hi:[1,0]
	v_pk_mul_f32 v[30:31], v[96:97], v[28:29] op_sel_hi:[1,0]
	s_nop 0
	v_pk_mul_f32 v[182:183], v[14:15], v[26:27]
	v_pk_mul_f32 v[178:179], v[16:17], v[30:31]
	v_pk_mul_f32 v[26:27], v[90:91], v[28:29] op_sel_hi:[1,0]
	v_pk_mul_f32 v[30:31], v[92:93], v[28:29] op_sel_hi:[1,0]
	v_pk_mul_f32 v[184:185], v[6:7], v[26:27]
	v_pk_mul_f32 v[180:181], v[8:9], v[30:31]
	v_pk_mul_f32 v[30:31], v[86:87], v[28:29] op_sel_hi:[1,0]
	v_pk_mul_f32 v[26:27], v[88:89], v[28:29] op_sel_hi:[1,0]
	v_pk_mul_f32 v[32:33], v[82:83], v[28:29] op_sel_hi:[1,0]
	v_pk_mul_f32 v[28:29], v[84:85], v[28:29] op_sel_hi:[1,0]
	v_pk_mul_f32 v[26:27], v[12:13], v[26:27]
	v_pk_mul_f32 v[30:31], v[10:11], v[30:31]
	v_pk_mul_f32 v[28:29], v[4:5], v[28:29]
	v_pk_mul_f32 v[32:33], v[2:3], v[32:33]
.LBB0_1045:
	v_lshl_add_u64 v[196:197], v[24:25], 0, s[34:35]
	v_add_co_u32_e32 v24, vcc, 0x10000, v24
	v_cvt_pk_bf16_f32 v182, v182, v183
	v_cvt_pk_bf16_f32 v183, v178, v179
	v_cvt_pk_bf16_f32 v184, v184, v185
	v_cvt_pk_bf16_f32 v185, v180, v181
	s_nop 1
	v_addc_co_u32_e32 v25, vcc, 0, v25, vcc
	global_store_dwordx4 v[24:25], v[182:185], off
	v_cvt_pk_bf16_f32 v24, v30, v31
	v_cvt_pk_bf16_f32 v25, v26, v27
	v_cvt_pk_bf16_f32 v26, v32, v33
	v_cvt_pk_bf16_f32 v27, v28, v29
	global_store_dwordx4 v[196:197], v[24:27], off offset:64
	s_and_b64 vcc, exec, s[4:5]
	v_mov_b32_e32 v29, v69
	v_mov_b32_e32 v28, v68
	v_mov_b32_e32 v33, v67
	v_mov_b32_e32 v32, v66
	v_mov_b32_e32 v27, v73
	v_mov_b32_e32 v26, v72
	v_mov_b32_e32 v31, v71
	v_mov_b32_e32 v30, v70
	v_mov_b32_e32 v181, v77
	v_mov_b32_e32 v180, v76
	v_mov_b32_e32 v185, v75
	v_mov_b32_e32 v184, v74
	v_mov_b32_e32 v179, v81
	v_mov_b32_e32 v178, v80
	v_mov_b32_e32 v183, v79
	v_mov_b32_e32 v182, v78
	s_cbranch_vccnz .LBB0_1047
; template <bool F8OUT = false> __device__ __forceinline__ void head_tile_store(const f32x4 (&acc)[2][2][4][2], bf16_t* obase  , int opitch, const float* gain, float scale, const f32x2e* rope, int row0, int fq) {
;     ...
;             f32x4 x[2][2];
; #pragma unroll
;             for (int bj = 0; bj < 2; ++bj)
; #pragma unroll
;                 for (int n = 0; n < 2; ++n) x[bj][n] = acc[ai][bj][m][n];
;             if (gain) {
;                 float ss = 0.f;
; #pragma unroll
;                 for (int bj = 0; bj < 2; ++bj)
; #pragma unroll
;                     for (int n = 0; n < 2; ++n) ss += (x[bj][n][0] * x[bj][n][0] + x[bj][n][1] * x[bj][n][1]) + (x[bj][n][2] * x[bj][n][2] + x[bj][n][3] * x[bj][n][3]);
;                 ss += __shfl_xor(ss, 16); ss += __shfl_xor(ss, 32);
;                 const float r = scale / sqrtf(ss * (1.f / 64.f) + 1e-6f);
; #pragma unroll
;                 for (int bj = 0; bj < 2; ++bj)
; #pragma unroll
;                     for (int n = 0; n < 2; ++n) x[bj][n] = x[bj][n] * r * g[bj][n];
;             }
;             if (rope) {
;                 const int t = row & 8191; const bool second = (fq & 2) != 0;
; #pragma unroll
;                 for (int bj = 0; bj < 2; ++bj) { const int pos = bj ? (t & 63) : (t >> 6); const f32x2e* tb = rope + pos * 16 + 8 * (fq & 1);
; #pragma unroll
;                     for (int n = 0; n < 2; ++n)
; #pragma unroll
;                         for (int e = 0; e < 4; ++e) { const float p = __shfl_xor(x[bj][n][e], 32); const f32x2e cs = tb[4 * n + e]; const float v = x[bj][n][e];
;                             x[bj][n][e] = second ? (p * cs.y + v * cs.x) : (v * cs.x - p * cs.y); } }
;             }
;             if constexpr (F8OUT) { unsigned char* rowp8 = (unsigned char*)obase + (size_t)row * opitch + 8 * fq; typedef unsigned u32x2_ __attribute__((ext_vector_type(2)));
; #pragma unroll
;                 for (int bj = 0; bj < 2; ++bj) *(u32x2_*)(rowp8 + 32 * bj) = (u32x2_){pk4_fp8(x[bj][0][0], x[bj][0][1], x[bj][0][2], x[bj][0][3]), pk4_fp8(x[bj][1][0], x[bj][1][1], x[bj][1][2], x[bj][1][3])};
;                 continue; }
;             bf16_t* rowp = obase + (size_t)row * opitch + 8 * fq;
; #pragma unroll
	v_pk_mul_f32 v[24:25], v[80:81], v[80:81]
	v_pk_mul_f32 v[26:27], v[78:79], v[78:79]
	v_mul_f32_e32 v19, v66, v66
	v_pk_mov_b32 v[28:29], v[26:27], v[24:25] op_sel:[1,0]
	v_mov_b32_e32 v27, v25
	v_pk_add_f32 v[24:25], v[28:29], v[26:27]
	v_pk_mul_f32 v[26:27], v[76:77], v[76:77]
	v_pk_mul_f32 v[28:29], v[74:75], v[74:75]
	v_pk_add_f32 v[24:25], v[24:25], v[24:25] op_sel:[0,1] op_sel_hi:[1,0]
	v_pk_mov_b32 v[30:31], v[28:29], v[26:27] op_sel:[1,0]
	v_mov_b32_e32 v29, v27
	v_pk_add_f32 v[26:27], v[30:31], v[28:29]
	v_mul_f32_e32 v28, v67, v67
	v_pk_add_f32 v[26:27], v[26:27], v[26:27] op_sel:[0,1] op_sel_hi:[1,0]
	v_mov_b32_e32 v25, v19
	v_mov_b32_e32 v27, v28
	v_pk_add_f32 v[24:25], v[24:25], v[26:27]
	v_mul_f32_e32 v26, v71, v71
	v_mul_f32_e32 v29, v68, v68
	v_pk_fma_f32 v[26:27], v[70:71], v[70:71], v[26:27] op_sel_hi:[1,1,0]
	v_mul_f32_e32 v28, v73, v73
	v_mul_f32_e32 v30, v69, v69
	v_mov_b32_e32 v27, v29
	v_pk_fma_f32 v[28:29], v[72:73], v[72:73], v[28:29] op_sel_hi:[1,1,0]
	s_nop 0
	v_mov_b32_e32 v29, v30
	v_pk_add_f32 v[26:27], v[26:27], v[28:29]
	s_nop 0
	v_pk_add_f32 v[24:25], v[24:25], v[26:27]
	s_nop 0
	v_add_f32_e32 v19, v24, v25
	v_and_b32_e32 v25, 64, v195
	v_xor_b32_e32 v24, 16, v195
	v_add_u32_e32 v25, 64, v25
	v_cmp_lt_i32_e32 vcc, v24, v25
	s_nop 1
	v_cndmask_b32_e32 v24, v195, v24, vcc
	v_lshlrev_b32_e32 v24, 2, v24
	v_mov_b32_e32 v24, v19
	s_nop 1
	v_permlane16_swap_b32_e32 v19, v24
	s_waitcnt lgkmcnt(0)
	v_add_f32_e32 v19, v19, v24
	v_xor_b32_e32 v24, 32, v195
	v_cmp_lt_i32_e32 vcc, v24, v25
	s_nop 1
	v_cndmask_b32_e32 v24, v195, v24, vcc
	v_lshlrev_b32_e32 v24, 2, v24
	v_mov_b32_e32 v24, v19
	s_nop 1
	v_permlane32_swap_b32_e32 v19, v24
	s_waitcnt lgkmcnt(0)
	v_add_f32_e32 v19, v19, v24
	v_fmamk_f32 v19, v19, 0x3c800000, v193
	v_mul_f32_e32 v24, 0x4f800000, v19
	v_cmp_gt_f32_e32 vcc, s69, v19
	s_nop 1
	v_cndmask_b32_e32 v19, v19, v24, vcc
	v_sqrt_f32_e32 v24, v19
	s_nop 0
	v_add_u32_e32 v25, -1, v24
	v_fma_f32 v26, -v25, v24, v19
	v_cmp_ge_f32_e64 s[6:7], 0, v26
	v_add_u32_e32 v26, 1, v24
	s_nop 0
	v_cndmask_b32_e64 v25, v24, v25, s[6:7]
	v_fma_f32 v24, -v26, v24, v19
	v_cmp_lt_f32_e64 s[6:7], 0, v24
	s_nop 1
	v_cndmask_b32_e64 v24, v25, v26, s[6:7]
	v_mul_f32_e32 v25, 0x37800000, v24
	v_cndmask_b32_e32 v24, v24, v25, vcc
	v_cmp_class_f32_e32 vcc, v19, v194
	s_nop 1
	v_cndmask_b32_e32 v19, v24, v19, vcc
	v_div_scale_f32 v24, s[6:7], v19, v19, 1.0
	v_rcp_f32_e32 v25, v24
	s_nop 0
	v_fma_f32 v26, -v24, v25, 1.0
	v_fmac_f32_e32 v25, v26, v25
	v_div_scale_f32 v26, vcc, 1.0, v19, 1.0
	v_mul_f32_e32 v27, v26, v25
	v_fma_f32 v28, -v24, v27, v26
	v_fmac_f32_e32 v27, v28, v25
	v_fma_f32 v24, -v24, v27, v26
	v_div_fmas_f32 v24, v24, v25, v27
	v_div_fixup_f32 v24, v24, v19, 1.0
	v_pk_mul_f32 v[26:27], v[78:79], v[24:25] op_sel_hi:[1,0]
	v_pk_mul_f32 v[28:29], v[80:81], v[24:25] op_sel_hi:[1,0]
	s_nop 0
	v_pk_mul_f32 v[182:183], v[14:15], v[26:27]
	v_pk_mul_f32 v[178:179], v[16:17], v[28:29]
	v_pk_mul_f32 v[26:27], v[74:75], v[24:25] op_sel_hi:[1,0]
	v_pk_mul_f32 v[28:29], v[76:77], v[24:25] op_sel_hi:[1,0]
	v_pk_mul_f32 v[184:185], v[6:7], v[26:27]
	v_pk_mul_f32 v[180:181], v[8:9], v[28:29]
	v_pk_mul_f32 v[28:29], v[70:71], v[24:25] op_sel_hi:[1,0]
	v_pk_mul_f32 v[26:27], v[72:73], v[24:25] op_sel_hi:[1,0]
	v_pk_mul_f32 v[32:33], v[66:67], v[24:25] op_sel_hi:[1,0]
	v_pk_mul_f32 v[24:25], v[68:69], v[24:25] op_sel_hi:[1,0]
	v_pk_mul_f32 v[26:27], v[12:13], v[26:27]
	v_pk_mul_f32 v[30:31], v[10:11], v[28:29]
	v_pk_mul_f32 v[28:29], v[4:5], v[24:25]
	v_pk_mul_f32 v[32:33], v[2:3], v[32:33]
.LBB0_1047:
	v_lshlrev_b64 v[24:25], 9, v[20:21]
	v_lshl_add_u64 v[24:25], v[22:23], 0, v[24:25]
	v_cvt_pk_bf16_f32 v182, v182, v183
	v_cvt_pk_bf16_f32 v183, v178, v179
	v_add_co_u32_e32 v178, vcc, 0x12000, v24
	v_lshl_add_u64 v[196:197], v[24:25], 0, s[36:37]
	s_nop 0
	v_addc_co_u32_e32 v179, vcc, 0, v25, vcc
	v_cvt_pk_bf16_f32 v184, v184, v185
	v_cvt_pk_bf16_f32 v185, v180, v181
	global_store_dwordx4 v[178:179], v[182:185], off
	v_cvt_pk_bf16_f32 v30, v30, v31
	v_cvt_pk_bf16_f32 v31, v26, v27
	v_cvt_pk_bf16_f32 v32, v32, v33
	v_cvt_pk_bf16_f32 v33, v28, v29
	global_store_dwordx4 v[196:197], v[30:33], off offset:64
	s_and_b64 vcc, exec, s[4:5]
	v_mov_b32_e32 v29, v53
	v_mov_b32_e32 v28, v52
	v_mov_b32_e32 v33, v51
	v_mov_b32_e32 v32, v50
	v_mov_b32_e32 v27, v57
	v_mov_b32_e32 v26, v56
	v_mov_b32_e32 v31, v55
	v_mov_b32_e32 v30, v54
	v_mov_b32_e32 v181, v61
	v_mov_b32_e32 v180, v60
	v_mov_b32_e32 v185, v59
	v_mov_b32_e32 v184, v58
	v_mov_b32_e32 v179, v65
	v_mov_b32_e32 v178, v64
	v_mov_b32_e32 v183, v63
	v_mov_b32_e32 v182, v62
	s_cbranch_vccnz .LBB0_1049
; template <bool F8OUT = false> __device__ __forceinline__ void head_tile_store(const f32x4 (&acc)[2][2][4][2], bf16_t* obase  , int opitch, const float* gain, float scale, const f32x2e* rope, int row0, int fq) {
;     ...
;             f32x4 x[2][2];
; #pragma unroll
;             for (int bj = 0; bj < 2; ++bj)
; #pragma unroll
;                 for (int n = 0; n < 2; ++n) x[bj][n] = acc[ai][bj][m][n];
;             if (gain) {
;                 float ss = 0.f;
; #pragma unroll
;                 for (int bj = 0; bj < 2; ++bj)
; #pragma unroll
;                     for (int n = 0; n < 2; ++n) ss += (x[bj][n][0] * x[bj][n][0] + x[bj][n][1] * x[bj][n][1]) + (x[bj][n][2] * x[bj][n][2] + x[bj][n][3] * x[bj][n][3]);
;                 ss += __shfl_xor(ss, 16); ss += __shfl_xor(ss, 32);
;                 const float r = scale / sqrtf(ss * (1.f / 64.f) + 1e-6f);
; #pragma unroll
;                 for (int bj = 0; bj < 2; ++bj)
; #pragma unroll
;                     for (int n = 0; n < 2; ++n) x[bj][n] = x[bj][n] * r * g[bj][n];
;             }
;             if (rope) {
;                 const int t = row & 8191; const bool second = (fq & 2) != 0;
; #pragma unroll
;                 for (int bj = 0; bj < 2; ++bj) { const int pos = bj ? (t & 63) : (t >> 6); const f32x2e* tb = rope + pos * 16 + 8 * (fq & 1);
; #pragma unroll
;                     for (int n = 0; n < 2; ++n)
; #pragma unroll
;                         for (int e = 0; e < 4; ++e) { const float p = __shfl_xor(x[bj][n][e], 32); const f32x2e cs = tb[4 * n + e]; const float v = x[bj][n][e];
;                             x[bj][n][e] = second ? (p * cs.y + v * cs.x) : (v * cs.x - p * cs.y); } }
;             }
;             if constexpr (F8OUT) { unsigned char* rowp8 = (unsigned char*)obase + (size_t)row * opitch + 8 * fq; typedef unsigned u32x2_ __attribute__((ext_vector_type(2)));
; #pragma unroll
;                 for (int bj = 0; bj < 2; ++bj) *(u32x2_*)(rowp8 + 32 * bj) = (u32x2_){pk4_fp8(x[bj][0][0], x[bj][0][1], x[bj][0][2], x[bj][0][3]), pk4_fp8(x[bj][1][0], x[bj][1][1], x[bj][1][2], x[bj][1][3])};
;                 continue; }
;             bf16_t* rowp = obase + (size_t)row * opitch + 8 * fq;
; #pragma unroll
	v_pk_mul_f32 v[26:27], v[64:65], v[64:65]
	v_pk_mul_f32 v[28:29], v[62:63], v[62:63]
	v_mul_f32_e32 v19, v50, v50
	v_pk_mov_b32 v[30:31], v[28:29], v[26:27] op_sel:[1,0]
	v_mov_b32_e32 v29, v27
	v_pk_add_f32 v[26:27], v[30:31], v[28:29]
	v_pk_mul_f32 v[28:29], v[60:61], v[60:61]
	v_pk_mul_f32 v[30:31], v[58:59], v[58:59]
	v_pk_add_f32 v[26:27], v[26:27], v[26:27] op_sel:[0,1] op_sel_hi:[1,0]
	v_pk_mov_b32 v[32:33], v[30:31], v[28:29] op_sel:[1,0]
	v_mov_b32_e32 v31, v29
	v_pk_add_f32 v[28:29], v[32:33], v[30:31]
	v_mul_f32_e32 v30, v51, v51
	v_pk_add_f32 v[28:29], v[28:29], v[28:29] op_sel:[0,1] op_sel_hi:[1,0]
	v_mov_b32_e32 v27, v19
	v_mov_b32_e32 v29, v30
	v_pk_add_f32 v[26:27], v[26:27], v[28:29]
	v_mul_f32_e32 v28, v55, v55
	v_mul_f32_e32 v31, v52, v52
	v_pk_fma_f32 v[28:29], v[54:55], v[54:55], v[28:29] op_sel_hi:[1,1,0]
	v_mul_f32_e32 v30, v57, v57
	v_mul_f32_e32 v32, v53, v53
	v_mov_b32_e32 v29, v31
	v_pk_fma_f32 v[30:31], v[56:57], v[56:57], v[30:31] op_sel_hi:[1,1,0]
	s_nop 0
	v_mov_b32_e32 v31, v32
	v_pk_add_f32 v[28:29], v[28:29], v[30:31]
	s_nop 0
	v_pk_add_f32 v[26:27], v[26:27], v[28:29]
	s_nop 0
	v_add_f32_e32 v19, v26, v27
	v_and_b32_e32 v27, 64, v195
	v_xor_b32_e32 v26, 16, v195
	v_add_u32_e32 v27, 64, v27
	v_cmp_lt_i32_e32 vcc, v26, v27
	s_nop 1
	v_cndmask_b32_e32 v26, v195, v26, vcc
	v_lshlrev_b32_e32 v26, 2, v26
	v_mov_b32_e32 v26, v19
	s_nop 1
	v_permlane16_swap_b32_e32 v19, v26
	s_waitcnt lgkmcnt(0)
	v_add_f32_e32 v19, v19, v26
	v_xor_b32_e32 v26, 32, v195
	v_cmp_lt_i32_e32 vcc, v26, v27
	s_nop 1
	v_cndmask_b32_e32 v26, v195, v26, vcc
	v_lshlrev_b32_e32 v26, 2, v26
	v_mov_b32_e32 v26, v19
	s_nop 1
	v_permlane32_swap_b32_e32 v19, v26
	s_waitcnt lgkmcnt(0)
	v_add_f32_e32 v19, v19, v26
	v_fmamk_f32 v19, v19, 0x3c800000, v193
	v_mul_f32_e32 v26, 0x4f800000, v19
	v_cmp_gt_f32_e32 vcc, s69, v19
	s_nop 1
	v_cndmask_b32_e32 v19, v19, v26, vcc
	v_sqrt_f32_e32 v26, v19
	s_nop 0
	v_add_u32_e32 v27, -1, v26
	v_fma_f32 v28, -v27, v26, v19
	v_cmp_ge_f32_e64 s[6:7], 0, v28
	v_add_u32_e32 v28, 1, v26
	s_nop 0
	v_cndmask_b32_e64 v27, v26, v27, s[6:7]
	v_fma_f32 v26, -v28, v26, v19
	v_cmp_lt_f32_e64 s[6:7], 0, v26
	s_nop 1
	v_cndmask_b32_e64 v26, v27, v28, s[6:7]
	v_mul_f32_e32 v27, 0x37800000, v26
	v_cndmask_b32_e32 v26, v26, v27, vcc
	v_cmp_class_f32_e32 vcc, v19, v194
	s_nop 1
	v_cndmask_b32_e32 v19, v26, v19, vcc
	v_div_scale_f32 v26, s[6:7], v19, v19, 1.0
	v_rcp_f32_e32 v27, v26
	s_nop 0
	v_fma_f32 v28, -v26, v27, 1.0
	v_fmac_f32_e32 v27, v28, v27
	v_div_scale_f32 v28, vcc, 1.0, v19, 1.0
	v_mul_f32_e32 v29, v28, v27
	v_fma_f32 v30, -v26, v29, v28
	v_fmac_f32_e32 v29, v30, v27
	v_fma_f32 v26, -v26, v29, v28
	v_div_fmas_f32 v26, v26, v27, v29
	v_div_fixup_f32 v28, v26, v19, 1.0
	v_pk_mul_f32 v[26:27], v[62:63], v[28:29] op_sel_hi:[1,0]
	v_pk_mul_f32 v[30:31], v[64:65], v[28:29] op_sel_hi:[1,0]
	s_nop 0
	v_pk_mul_f32 v[182:183], v[14:15], v[26:27]
	v_pk_mul_f32 v[178:179], v[16:17], v[30:31]
	v_pk_mul_f32 v[26:27], v[58:59], v[28:29] op_sel_hi:[1,0]
	v_pk_mul_f32 v[30:31], v[60:61], v[28:29] op_sel_hi:[1,0]
	v_pk_mul_f32 v[184:185], v[6:7], v[26:27]
	v_pk_mul_f32 v[180:181], v[8:9], v[30:31]
	v_pk_mul_f32 v[30:31], v[54:55], v[28:29] op_sel_hi:[1,0]
	v_pk_mul_f32 v[26:27], v[56:57], v[28:29] op_sel_hi:[1,0]
	v_pk_mul_f32 v[32:33], v[50:51], v[28:29] op_sel_hi:[1,0]
	v_pk_mul_f32 v[28:29], v[52:53], v[28:29] op_sel_hi:[1,0]
	v_pk_mul_f32 v[26:27], v[12:13], v[26:27]
	v_pk_mul_f32 v[30:31], v[10:11], v[30:31]
	v_pk_mul_f32 v[28:29], v[4:5], v[28:29]
	v_pk_mul_f32 v[32:33], v[2:3], v[32:33]
; template <bool F8OUT = false> __device__ __forceinline__ void head_tile_store(const f32x4 (&acc)[2][2][4][2], bf16_t* obase  , int opitch, const float* gain, float scale, const f32x2e* rope, int row0, int fq) {
;     ...
;             f32x4 x[2][2];
; #pragma unroll
;             for (int bj = 0; bj < 2; ++bj)
; #pragma unroll
;                 for (int n = 0; n < 2; ++n) x[bj][n] = acc[ai][bj][m][n];
;             if (gain) {
;                 float ss = 0.f;
; #pragma unroll
;                 for (int bj = 0; bj < 2; ++bj)
; #pragma unroll
;                     for (int n = 0; n < 2; ++n) ss += (x[bj][n][0] * x[bj][n][0] + x[bj][n][1] * x[bj][n][1]) + (x[bj][n][2] * x[bj][n][2] + x[bj][n][3] * x[bj][n][3]);
;                 ss += __shfl_xor(ss, 16); ss += __shfl_xor(ss, 32);
;                 const float r = scale / sqrtf(ss * (1.f / 64.f) + 1e-6f);
; #pragma unroll
;                 for (int bj = 0; bj < 2; ++bj)
; #pragma unroll
;                     for (int n = 0; n < 2; ++n) x[bj][n] = x[bj][n] * r * g[bj][n];
;             }
;             if (rope) {
;                 const int t = row & 8191; const bool second = (fq & 2) != 0;
; #pragma unroll
;                 for (int bj = 0; bj < 2; ++bj) { const int pos = bj ? (t & 63) : (t >> 6); const f32x2e* tb = rope + pos * 16 + 8 * (fq & 1);
; #pragma unroll
;                     for (int n = 0; n < 2; ++n)
; #pragma unroll
;                         for (int e = 0; e < 4; ++e) { const float p = __shfl_xor(x[bj][n][e], 32); const f32x2e cs = tb[4 * n + e]; const float v = x[bj][n][e];
;                             x[bj][n][e] = second ? (p * cs.y + v * cs.x) : (v * cs.x - p * cs.y); } }
;             }
;             if constexpr (F8OUT) { unsigned char* rowp8 = (unsigned char*)obase + (size_t)row * opitch + 8 * fq; typedef unsigned u32x2_ __attribute__((ext_vector_type(2)));
; #pragma unroll
;                 for (int bj = 0; bj < 2; ++bj) *(u32x2_*)(rowp8 + 32 * bj) = (u32x2_){pk4_fp8(x[bj][0][0], x[bj][0][1], x[bj][0][2], x[bj][0][3]), pk4_fp8(x[bj][1][0], x[bj][1][1], x[bj][1][2], x[bj][1][3])};
;                 continue; }
;             bf16_t* rowp = obase + (size_t)row * opitch + 8 * fq;
; #pragma unroll
.LBB0_1049:
	v_lshl_add_u64 v[196:197], v[24:25], 0, s[38:39]
	v_add_co_u32_e32 v24, vcc, 0x14000, v24
	v_cvt_pk_bf16_f32 v182, v182, v183
	v_cvt_pk_bf16_f32 v183, v178, v179
	v_cvt_pk_bf16_f32 v184, v184, v185
	v_cvt_pk_bf16_f32 v185, v180, v181
	s_nop 1
	v_addc_co_u32_e32 v25, vcc, 0, v25, vcc
	global_store_dwordx4 v[24:25], v[182:185], off
	v_cvt_pk_bf16_f32 v24, v30, v31
	v_cvt_pk_bf16_f32 v25, v26, v27
	v_cvt_pk_bf16_f32 v26, v32, v33
	v_cvt_pk_bf16_f32 v27, v28, v29
	global_store_dwordx4 v[196:197], v[24:27], off offset:64
	s_and_b64 vcc, exec, s[4:5]
	v_mov_b32_e32 v29, v35
	v_mov_b32_e32 v25, v37
	v_mov_b32_e32 v24, v36
	v_mov_b32_e32 v28, v34
	v_mov_b32_e32 v27, v41
	v_mov_b32_e32 v26, v40
	v_mov_b32_e32 v31, v39
	v_mov_b32_e32 v30, v38
	v_mov_b32_e32 v33, v45
	v_mov_b32_e32 v32, v44
	v_mov_b32_e32 v181, v43
	v_mov_b32_e32 v180, v42
	v_mov_b32_e32 v179, v49
	v_mov_b32_e32 v178, v48
	v_mov_b32_e32 v183, v47
	v_mov_b32_e32 v182, v46
	s_cbranch_vccnz .LBB0_1051
	v_pk_mul_f32 v[24:25], v[48:49], v[48:49]
	v_pk_mul_f32 v[26:27], v[46:47], v[46:47]
	v_mul_f32_e32 v19, v34, v34
	v_pk_mov_b32 v[28:29], v[26:27], v[24:25] op_sel:[1,0]
	v_mov_b32_e32 v27, v25
	v_pk_add_f32 v[24:25], v[28:29], v[26:27]
	v_pk_mul_f32 v[26:27], v[44:45], v[44:45]
	v_pk_mul_f32 v[28:29], v[42:43], v[42:43]
	v_pk_add_f32 v[24:25], v[24:25], v[24:25] op_sel:[0,1] op_sel_hi:[1,0]
	v_pk_mov_b32 v[30:31], v[28:29], v[26:27] op_sel:[1,0]
	v_mov_b32_e32 v29, v27
	v_pk_add_f32 v[26:27], v[30:31], v[28:29]
	v_mul_f32_e32 v28, v35, v35
	v_pk_add_f32 v[26:27], v[26:27], v[26:27] op_sel:[0,1] op_sel_hi:[1,0]
	v_mov_b32_e32 v25, v19
	v_mov_b32_e32 v27, v28
	v_pk_add_f32 v[24:25], v[24:25], v[26:27]
	v_mul_f32_e32 v26, v39, v39
	v_mul_f32_e32 v29, v36, v36
	v_pk_fma_f32 v[26:27], v[38:39], v[38:39], v[26:27] op_sel_hi:[1,1,0]
	v_mul_f32_e32 v28, v41, v41
	v_mul_f32_e32 v30, v37, v37
	v_mov_b32_e32 v27, v29
	v_pk_fma_f32 v[28:29], v[40:41], v[40:41], v[28:29] op_sel_hi:[1,1,0]
	s_nop 0
	v_mov_b32_e32 v29, v30
	v_pk_add_f32 v[26:27], v[26:27], v[28:29]
	s_nop 0
	v_pk_add_f32 v[24:25], v[24:25], v[26:27]
	s_nop 0
	v_add_f32_e32 v19, v24, v25
	v_and_b32_e32 v25, 64, v195
	v_xor_b32_e32 v24, 16, v195
	v_add_u32_e32 v25, 64, v25
	v_cmp_lt_i32_e32 vcc, v24, v25
	s_nop 1
	v_cndmask_b32_e32 v24, v195, v24, vcc
	v_lshlrev_b32_e32 v24, 2, v24
	v_mov_b32_e32 v24, v19
	s_nop 1
	v_permlane16_swap_b32_e32 v19, v24
	s_waitcnt lgkmcnt(0)
	v_add_f32_e32 v19, v19, v24
	v_xor_b32_e32 v24, 32, v195
	v_cmp_lt_i32_e32 vcc, v24, v25
	s_nop 1
	v_cndmask_b32_e32 v24, v195, v24, vcc
	v_lshlrev_b32_e32 v24, 2, v24
	v_mov_b32_e32 v24, v19
	s_nop 1
	v_permlane32_swap_b32_e32 v19, v24
	s_waitcnt lgkmcnt(0)
	v_add_f32_e32 v19, v19, v24
	v_fmamk_f32 v19, v19, 0x3c800000, v193
	v_mul_f32_e32 v24, 0x4f800000, v19
	v_cmp_gt_f32_e32 vcc, s69, v19
	s_nop 1
	v_cndmask_b32_e32 v19, v19, v24, vcc
	v_sqrt_f32_e32 v24, v19
	s_nop 0
	v_add_u32_e32 v25, -1, v24
	v_fma_f32 v26, -v25, v24, v19
	v_cmp_ge_f32_e64 s[4:5], 0, v26
	v_add_u32_e32 v26, 1, v24
	s_nop 0
	v_cndmask_b32_e64 v25, v24, v25, s[4:5]
	v_fma_f32 v24, -v26, v24, v19
	v_cmp_lt_f32_e64 s[4:5], 0, v24
	s_nop 1
	v_cndmask_b32_e64 v24, v25, v26, s[4:5]
	v_mul_f32_e32 v25, 0x37800000, v24
	v_cndmask_b32_e32 v24, v24, v25, vcc
	v_cmp_class_f32_e32 vcc, v19, v194
	s_nop 1
	v_cndmask_b32_e32 v19, v24, v19, vcc
	v_div_scale_f32 v24, s[4:5], v19, v19, 1.0
	v_rcp_f32_e32 v25, v24
	s_nop 0
	v_fma_f32 v26, -v24, v25, 1.0
	v_fmac_f32_e32 v25, v26, v25
	v_div_scale_f32 v26, vcc, 1.0, v19, 1.0
	v_mul_f32_e32 v27, v26, v25
	v_fma_f32 v28, -v24, v27, v26
	v_fmac_f32_e32 v27, v28, v25
	v_fma_f32 v24, -v24, v27, v26
	v_div_fmas_f32 v24, v24, v25, v27
	v_div_fixup_f32 v24, v24, v19, 1.0
	v_pk_mul_f32 v[26:27], v[46:47], v[24:25] op_sel_hi:[1,0]
	v_pk_mul_f32 v[28:29], v[48:49], v[24:25] op_sel_hi:[1,0]
	s_nop 0
	v_pk_mul_f32 v[182:183], v[14:15], v[26:27]
	v_pk_mul_f32 v[178:179], v[16:17], v[28:29]
	v_pk_mul_f32 v[14:15], v[42:43], v[24:25] op_sel_hi:[1,0]
	v_pk_mul_f32 v[16:17], v[44:45], v[24:25] op_sel_hi:[1,0]
	v_pk_mul_f32 v[180:181], v[6:7], v[14:15]
	v_pk_mul_f32 v[32:33], v[8:9], v[16:17]
	v_pk_mul_f32 v[6:7], v[38:39], v[24:25] op_sel_hi:[1,0]
	v_pk_mul_f32 v[8:9], v[40:41], v[24:25] op_sel_hi:[1,0]
	v_pk_mul_f32 v[30:31], v[10:11], v[6:7]
	v_pk_mul_f32 v[26:27], v[12:13], v[8:9]
	v_pk_mul_f32 v[6:7], v[34:35], v[24:25] op_sel_hi:[1,0]
	v_pk_mul_f32 v[8:9], v[36:37], v[24:25] op_sel_hi:[1,0]
	v_pk_mul_f32 v[28:29], v[2:3], v[6:7]
	v_pk_mul_f32 v[24:25], v[4:5], v[8:9]

; template <bool F8OUT = false> __device__ __forceinline__ void head_tile_store(const f32x4 (&acc)[2][2][4][2], bf16_t* obase  , int opitch, const float* gain, float scale, const f32x2e* rope, int row0, int fq) {
;     ...
;             if (gain) {
;                 float ss = 0.f;
; #pragma unroll
;                 for (int bj = 0; bj < 2; ++bj)
; #pragma unroll
;                     for (int n = 0; n < 2; ++n) ss += (x[bj][n][0] * x[bj][n][0] + x[bj][n][1] * x[bj][n][1]) + (x[bj][n][2] * x[bj][n][2] + x[bj][n][3] * x[bj][n][3]);
;                 ss += __shfl_xor(ss, 16); ss += __shfl_xor(ss, 32);
;                 const float r = scale / sqrtf(ss * (1.f / 64.f) + 1e-6f);
; #pragma unroll
;                 for (int bj = 0; bj < 2; ++bj)
; #pragma unroll
;                     for (int n = 0; n < 2; ++n) x[bj][n] = x[bj][n] * r * g[bj][n];
;             }
;             if (rope) {
;                 const int t = row & 8191; const bool second = (fq & 2) != 0;
; #pragma unroll
;                 for (int bj = 0; bj < 2; ++bj) { const int pos = bj ? (t & 63) : (t >> 6); const f32x2e* tb = rope + pos * 16 + 8 * (fq & 1);
; #pragma unroll
;                     for (int n = 0; n < 2; ++n)
; #pragma unroll
;                         for (int e = 0; e < 4; ++e) { const float p = __shfl_xor(x[bj][n][e], 32); const f32x2e cs = tb[4 * n + e]; const float v = x[bj][n][e];
;                             x[bj][n][e] = second ? (p * cs.y + v * cs.x) : (v * cs.x - p * cs.y); } }
;             }
;             if constexpr (F8OUT) { unsigned char* rowp8 = (unsigned char*)obase + (size_t)row * opitch + 8 * fq; typedef unsigned u32x2_ __attribute__((ext_vector_type(2)));
; #pragma unroll
;                 for (int bj = 0; bj < 2; ++bj) *(u32x2_*)(rowp8 + 32 * bj) = (u32x2_){pk4_fp8(x[bj][0][0], x[bj][0][1], x[bj][0][2], x[bj][0][3]), pk4_fp8(x[bj][1][0], x[bj][1][1], x[bj][1][2], x[bj][1][3])};
;                 continue; }
;             bf16_t* rowp = obase + (size_t)row * opitch + 8 * fq;
; #pragma unroll
;             for (int bj = 0; bj < 2; ++bj) { u32x4 w; w.x = cvt_pk_bf16(x[bj][0][0], x[bj][0][1]); w.y = cvt_pk_bf16(x[bj][0][2], x[bj][0][3]); w.z = cvt_pk_bf16(x[bj][1][0], x[bj][1][1]); w.w = cvt_pk_bf16(x[bj][1][2], x[bj][1][3]);
;                 *(u32x4*)(rowp + 32 * bj) = w; }
.LBB0_1057:
	s_and_b64 vcc, exec, s[4:5]
	s_cbranch_vccnz .LBB0_1059
	v_pk_mul_f32 v[22:23], v[160:161], v[160:161]
	v_pk_mul_f32 v[24:25], v[158:159], v[158:159]
	v_mul_f32_e32 v19, v146, v146
	v_pk_mov_b32 v[26:27], v[24:25], v[22:23] op_sel:[1,0]
	v_mov_b32_e32 v25, v23
	v_pk_add_f32 v[22:23], v[26:27], v[24:25]
	v_pk_mul_f32 v[24:25], v[156:157], v[156:157]
	v_pk_mul_f32 v[26:27], v[154:155], v[154:155]
	v_pk_add_f32 v[22:23], v[22:23], v[22:23] op_sel:[0,1] op_sel_hi:[1,0]
	v_pk_mov_b32 v[28:29], v[26:27], v[24:25] op_sel:[1,0]
	v_mov_b32_e32 v27, v25
	v_pk_add_f32 v[24:25], v[28:29], v[26:27]
	v_mul_f32_e32 v26, v147, v147
	v_pk_add_f32 v[24:25], v[24:25], v[24:25] op_sel:[0,1] op_sel_hi:[1,0]
	v_mov_b32_e32 v23, v19
	v_mov_b32_e32 v25, v26
	v_pk_add_f32 v[22:23], v[22:23], v[24:25]
	v_mul_f32_e32 v24, v151, v151
	v_mul_f32_e32 v27, v148, v148
	v_pk_fma_f32 v[24:25], v[150:151], v[150:151], v[24:25] op_sel_hi:[1,1,0]
	v_mul_f32_e32 v26, v153, v153
	v_mul_f32_e32 v28, v149, v149
	v_mov_b32_e32 v25, v27
	v_pk_fma_f32 v[26:27], v[152:153], v[152:153], v[26:27] op_sel_hi:[1,1,0]
	s_nop 0
	v_mov_b32_e32 v27, v28
	v_pk_add_f32 v[24:25], v[24:25], v[26:27]
	s_nop 0
	v_pk_add_f32 v[22:23], v[22:23], v[24:25]
	s_nop 0
	v_add_f32_e32 v19, v22, v23
	v_and_b32_e32 v23, 64, v195
	v_xor_b32_e32 v22, 16, v195
	v_add_u32_e32 v23, 64, v23
	v_cmp_lt_i32_e32 vcc, v22, v23
	s_nop 1
	v_cndmask_b32_e32 v22, v195, v22, vcc
	v_lshlrev_b32_e32 v22, 2, v22
	v_mov_b32_e32 v22, v19
	s_nop 1
	v_permlane16_swap_b32_e32 v19, v22
	s_waitcnt lgkmcnt(0)
	v_add_f32_e32 v19, v19, v22
	v_xor_b32_e32 v22, 32, v195
	v_cmp_lt_i32_e32 vcc, v22, v23
	s_nop 1
	v_cndmask_b32_e32 v22, v195, v22, vcc
	v_lshlrev_b32_e32 v22, 2, v22
	v_mov_b32_e32 v22, v19
	s_nop 1
	v_permlane32_swap_b32_e32 v19, v22
	s_waitcnt lgkmcnt(0)
	v_add_f32_e32 v19, v19, v22
	v_fmamk_f32 v19, v19, 0x3c800000, v193
	v_mul_f32_e32 v22, 0x4f800000, v19
	v_cmp_gt_f32_e32 vcc, s69, v19
	s_nop 1
	v_cndmask_b32_e32 v19, v19, v22, vcc
	v_sqrt_f32_e32 v22, v19
	s_nop 0
	v_add_u32_e32 v23, -1, v22
	v_fma_f32 v24, -v23, v22, v19
	v_cmp_ge_f32_e64 s[6:7], 0, v24
	v_add_u32_e32 v24, 1, v22
	s_nop 0
	v_cndmask_b32_e64 v23, v22, v23, s[6:7]
	v_fma_f32 v22, -v24, v22, v19
	v_cmp_lt_f32_e64 s[6:7], 0, v22
	s_nop 1
	v_cndmask_b32_e64 v22, v23, v24, s[6:7]
	v_mul_f32_e32 v23, 0x37800000, v22
	v_cndmask_b32_e32 v22, v22, v23, vcc
	v_cmp_class_f32_e32 vcc, v19, v194
	s_nop 1
	v_cndmask_b32_e32 v19, v22, v19, vcc
	v_div_scale_f32 v22, s[6:7], v19, v19, s70
	v_rcp_f32_e32 v23, v22
	s_nop 0
	v_fma_f32 v24, -v22, v23, 1.0
	v_fmac_f32_e32 v23, v24, v23
	v_div_scale_f32 v24, vcc, s70, v19, s70
	v_mul_f32_e32 v25, v24, v23
	v_fma_f32 v26, -v22, v25, v24
	v_fmac_f32_e32 v25, v26, v23
	v_fma_f32 v22, -v22, v25, v24
	v_div_fmas_f32 v22, v22, v23, v25
	v_div_fixup_f32 v22, v22, v19, s70
	v_pk_mul_f32 v[24:25], v[158:159], v[22:23] op_sel_hi:[1,0]
	v_pk_mul_f32 v[26:27], v[160:161], v[22:23] op_sel_hi:[1,0]
	s_waitcnt vmcnt(0)
	v_pk_mul_f32 v[158:159], v[14:15], v[24:25]
	v_pk_mul_f32 v[24:25], v[154:155], v[22:23] op_sel_hi:[1,0]
	v_pk_mul_f32 v[160:161], v[16:17], v[26:27]
	v_pk_mul_f32 v[26:27], v[156:157], v[22:23] op_sel_hi:[1,0]
	v_pk_mul_f32 v[154:155], v[6:7], v[24:25]
	v_pk_mul_f32 v[24:25], v[150:151], v[22:23] op_sel_hi:[1,0]
	v_pk_mul_f32 v[156:157], v[8:9], v[26:27]
	v_pk_mul_f32 v[26:27], v[152:153], v[22:23] op_sel_hi:[1,0]
	v_pk_mul_f32 v[150:151], v[10:11], v[24:25]
	v_pk_mul_f32 v[24:25], v[146:147], v[22:23] op_sel_hi:[1,0]
	v_pk_mul_f32 v[22:23], v[148:149], v[22:23] op_sel_hi:[1,0]
	v_pk_mul_f32 v[152:153], v[12:13], v[26:27]
	v_pk_mul_f32 v[148:149], v[4:5], v[22:23]
	v_pk_mul_f32 v[146:147], v[2:3], v[24:25]
.LBB0_1059:
	s_lshl_b32 s6, s50, 8
	s_or_b32 s6, s6, s66
	s_ashr_i32 s7, s6, 31
	s_lshl_b64 s[6:7], s[6:7], 1
	v_readlane_b32 s52, v255, 7
	v_readlane_b32 s53, v255, 8
	s_add_u32 s6, s52, s6
	s_addc_u32 s7, s53, s7
	v_ashrrev_i32_e32 v19, 31, v18
	v_lshl_add_u64 v[20:21], v[20:21], 1, s[6:7]
	v_lshlrev_b64 v[22:23], 11, v[18:19]
	v_lshl_add_u64 v[22:23], v[20:21], 0, v[22:23]
	v_cvt_pk_bf16_f32 v24, v158, v159
	v_cvt_pk_bf16_f32 v25, v160, v161
	v_cvt_pk_bf16_f32 v26, v154, v155
	v_cvt_pk_bf16_f32 v27, v156, v157
	s_and_b64 vcc, exec, s[4:5]
	global_store_dwordx4 v[22:23], v[24:27], off
	s_nop 1
	v_cvt_pk_bf16_f32 v24, v150, v151
	v_cvt_pk_bf16_f32 v25, v152, v153
	v_cvt_pk_bf16_f32 v26, v146, v147
	v_cvt_pk_bf16_f32 v27, v148, v149
	global_store_dwordx4 v[22:23], v[24:27], off offset:64
	s_cbranch_vccnz .LBB0_1061
; template <bool F8OUT = false> __device__ __forceinline__ void head_tile_store(const f32x4 (&acc)[2][2][4][2], bf16_t* obase  , int opitch, const float* gain, float scale, const f32x2e* rope, int row0, int fq) {
;     ...
;             if (gain) {
;                 float ss = 0.f;
; #pragma unroll
;                 for (int bj = 0; bj < 2; ++bj)
; #pragma unroll
;                     for (int n = 0; n < 2; ++n) ss += (x[bj][n][0] * x[bj][n][0] + x[bj][n][1] * x[bj][n][1]) + (x[bj][n][2] * x[bj][n][2] + x[bj][n][3] * x[bj][n][3]);
;                 ss += __shfl_xor(ss, 16); ss += __shfl_xor(ss, 32);
;                 const float r = scale / sqrtf(ss * (1.f / 64.f) + 1e-6f);
; #pragma unroll
;                 for (int bj = 0; bj < 2; ++bj)
; #pragma unroll
;                     for (int n = 0; n < 2; ++n) x[bj][n] = x[bj][n] * r * g[bj][n];
;             }
;             if (rope) {
;                 const int t = row & 8191; const bool second = (fq & 2) != 0;
; #pragma unroll
;                 for (int bj = 0; bj < 2; ++bj) { const int pos = bj ? (t & 63) : (t >> 6); const f32x2e* tb = rope + pos * 16 + 8 * (fq & 1);
; #pragma unroll
;                     for (int n = 0; n < 2; ++n)
; #pragma unroll
;                         for (int e = 0; e < 4; ++e) { const float p = __shfl_xor(x[bj][n][e], 32); const f32x2e cs = tb[4 * n + e]; const float v = x[bj][n][e];
;                             x[bj][n][e] = second ? (p * cs.y + v * cs.x) : (v * cs.x - p * cs.y); } }
;             }
;             if constexpr (F8OUT) { unsigned char* rowp8 = (unsigned char*)obase + (size_t)row * opitch + 8 * fq; typedef unsigned u32x2_ __attribute__((ext_vector_type(2)));
; #pragma unroll
;                 for (int bj = 0; bj < 2; ++bj) *(u32x2_*)(rowp8 + 32 * bj) = (u32x2_){pk4_fp8(x[bj][0][0], x[bj][0][1], x[bj][0][2], x[bj][0][3]), pk4_fp8(x[bj][1][0], x[bj][1][1], x[bj][1][2], x[bj][1][3])};
;                 continue; }
;             bf16_t* rowp = obase + (size_t)row * opitch + 8 * fq;
; #pragma unroll
;             for (int bj = 0; bj < 2; ++bj) { u32x4 w; w.x = cvt_pk_bf16(x[bj][0][0], x[bj][0][1]); w.y = cvt_pk_bf16(x[bj][0][2], x[bj][0][3]); w.z = cvt_pk_bf16(x[bj][1][0], x[bj][1][1]); w.w = cvt_pk_bf16(x[bj][1][2], x[bj][1][3]);
;                 *(u32x4*)(rowp + 32 * bj) = w; }
	s_nop 0
	v_pk_mul_f32 v[24:25], v[144:145], v[144:145]
	v_pk_mul_f32 v[26:27], v[142:143], v[142:143]
	s_nop 0
	v_pk_mov_b32 v[28:29], v[26:27], v[24:25] op_sel:[1,0]
	v_mov_b32_e32 v27, v25
	v_pk_add_f32 v[24:25], v[28:29], v[26:27]
	v_pk_mul_f32 v[26:27], v[140:141], v[140:141]
	v_pk_mul_f32 v[28:29], v[138:139], v[138:139]
	v_pk_add_f32 v[24:25], v[24:25], v[24:25] op_sel:[0,1] op_sel_hi:[1,0]
	v_pk_mov_b32 v[30:31], v[28:29], v[26:27] op_sel:[1,0]
	v_mov_b32_e32 v29, v27
	v_pk_add_f32 v[26:27], v[30:31], v[28:29]
	v_mul_f32_e32 v28, v130, v130
	v_mul_f32_e32 v29, v131, v131
	v_pk_add_f32 v[26:27], v[26:27], v[26:27] op_sel:[0,1] op_sel_hi:[1,0]
	v_mov_b32_e32 v25, v28
	v_mov_b32_e32 v27, v29
	v_pk_add_f32 v[24:25], v[24:25], v[26:27]
	v_mul_f32_e32 v26, v135, v135
	v_mul_f32_e32 v28, v137, v137
	v_mul_f32_e32 v30, v132, v132
	v_mul_f32_e32 v31, v133, v133
	v_pk_fma_f32 v[26:27], v[134:135], v[134:135], v[26:27] op_sel_hi:[1,1,0]
	v_pk_fma_f32 v[28:29], v[136:137], v[136:137], v[28:29] op_sel_hi:[1,1,0]
	v_mov_b32_e32 v27, v30
	v_mov_b32_e32 v29, v31
	v_pk_add_f32 v[26:27], v[26:27], v[28:29]
	s_nop 0
	v_pk_add_f32 v[24:25], v[24:25], v[26:27]
	v_and_b32_e32 v26, 64, v195
	v_add_f32_e32 v24, v24, v25
	v_xor_b32_e32 v25, 16, v195
	v_add_u32_e32 v26, 64, v26
	v_cmp_lt_i32_e32 vcc, v25, v26
	s_nop 1
	v_cndmask_b32_e32 v25, v195, v25, vcc
	v_lshlrev_b32_e32 v25, 2, v25
	v_mov_b32_e32 v25, v24
	s_nop 1
	v_permlane16_swap_b32_e32 v24, v25
	s_waitcnt lgkmcnt(0)
	v_add_f32_e32 v24, v24, v25
	v_xor_b32_e32 v25, 32, v195
	v_cmp_lt_i32_e32 vcc, v25, v26
	s_nop 1
	v_cndmask_b32_e32 v25, v195, v25, vcc
	v_lshlrev_b32_e32 v25, 2, v25
	v_mov_b32_e32 v25, v24
	s_nop 1
	v_permlane32_swap_b32_e32 v24, v25
	s_waitcnt lgkmcnt(0)
	v_add_f32_e32 v24, v24, v25
	v_fmamk_f32 v24, v24, 0x3c800000, v193
	v_mul_f32_e32 v25, 0x4f800000, v24
	v_cmp_gt_f32_e32 vcc, s69, v24
	s_nop 1
	v_cndmask_b32_e32 v24, v24, v25, vcc
	v_sqrt_f32_e32 v25, v24
	s_nop 0
	v_add_u32_e32 v26, -1, v25
	v_fma_f32 v27, -v26, v25, v24
	v_cmp_ge_f32_e64 s[6:7], 0, v27
	v_add_u32_e32 v27, 1, v25
	s_nop 0
	v_cndmask_b32_e64 v26, v25, v26, s[6:7]
	v_fma_f32 v25, -v27, v25, v24
	v_cmp_lt_f32_e64 s[6:7], 0, v25
	s_nop 1
	v_cndmask_b32_e64 v25, v26, v27, s[6:7]
	v_mul_f32_e32 v26, 0x37800000, v25
	v_cndmask_b32_e32 v25, v25, v26, vcc
	v_cmp_class_f32_e32 vcc, v24, v194
	s_nop 1
	v_cndmask_b32_e32 v24, v25, v24, vcc
	v_div_scale_f32 v25, s[6:7], v24, v24, s70
	v_rcp_f32_e32 v26, v25
	s_nop 0
	v_fma_f32 v27, -v25, v26, 1.0
	v_fmac_f32_e32 v26, v27, v26
	v_div_scale_f32 v27, vcc, s70, v24, s70
	v_mul_f32_e32 v28, v27, v26
	v_fma_f32 v29, -v25, v28, v27
	v_fmac_f32_e32 v28, v29, v26
	v_fma_f32 v25, -v25, v28, v27
	v_div_fmas_f32 v25, v25, v26, v28
	v_div_fixup_f32 v24, v25, v24, s70
	v_pk_mul_f32 v[26:27], v[142:143], v[24:25] op_sel_hi:[1,0]
	v_pk_mul_f32 v[28:29], v[144:145], v[24:25] op_sel_hi:[1,0]
	s_nop 0
	v_pk_mul_f32 v[142:143], v[14:15], v[26:27]
	v_pk_mul_f32 v[26:27], v[138:139], v[24:25] op_sel_hi:[1,0]
	v_pk_mul_f32 v[144:145], v[16:17], v[28:29]
	v_pk_mul_f32 v[28:29], v[140:141], v[24:25] op_sel_hi:[1,0]
	v_pk_mul_f32 v[138:139], v[6:7], v[26:27]
	v_pk_mul_f32 v[26:27], v[134:135], v[24:25] op_sel_hi:[1,0]
	v_pk_mul_f32 v[140:141], v[8:9], v[28:29]
	v_pk_mul_f32 v[28:29], v[136:137], v[24:25] op_sel_hi:[1,0]
	v_pk_mul_f32 v[134:135], v[10:11], v[26:27]
	v_pk_mul_f32 v[26:27], v[130:131], v[24:25] op_sel_hi:[1,0]
	v_pk_mul_f32 v[24:25], v[132:133], v[24:25] op_sel_hi:[1,0]
	v_pk_mul_f32 v[136:137], v[12:13], v[28:29]
	v_pk_mul_f32 v[132:133], v[4:5], v[24:25]
	v_pk_mul_f32 v[130:131], v[2:3], v[26:27]
.LBB0_1061:
	v_add_co_u32_e32 v30, vcc, 0x8000, v22
	s_mov_b64 s[6:7], 0x8000
	s_nop 0
	v_addc_co_u32_e32 v31, vcc, 0, v23, vcc
	v_lshl_add_u64 v[28:29], v[22:23], 0, s[6:7]
	v_cvt_pk_bf16_f32 v24, v142, v143
	v_cvt_pk_bf16_f32 v25, v144, v145
	v_cvt_pk_bf16_f32 v26, v138, v139
	v_cvt_pk_bf16_f32 v27, v140, v141
	s_and_b64 vcc, exec, s[4:5]
	global_store_dwordx4 v[30:31], v[24:27], off
	s_nop 1
	v_cvt_pk_bf16_f32 v24, v134, v135
	v_cvt_pk_bf16_f32 v25, v136, v137
	v_cvt_pk_bf16_f32 v26, v130, v131
	v_cvt_pk_bf16_f32 v27, v132, v133
	global_store_dwordx4 v[28:29], v[24:27], off offset:64
	s_cbranch_vccnz .LBB0_1063
; template <bool F8OUT = false> __device__ __forceinline__ void head_tile_store(const f32x4 (&acc)[2][2][4][2], bf16_t* obase  , int opitch, const float* gain, float scale, const f32x2e* rope, int row0, int fq) {
;     ...
;             if (gain) {
;                 float ss = 0.f;
; #pragma unroll
;                 for (int bj = 0; bj < 2; ++bj)
; #pragma unroll
;                     for (int n = 0; n < 2; ++n) ss += (x[bj][n][0] * x[bj][n][0] + x[bj][n][1] * x[bj][n][1]) + (x[bj][n][2] * x[bj][n][2] + x[bj][n][3] * x[bj][n][3]);
;                 ss += __shfl_xor(ss, 16); ss += __shfl_xor(ss, 32);
;                 const float r = scale / sqrtf(ss * (1.f / 64.f) + 1e-6f);
; #pragma unroll
;                 for (int bj = 0; bj < 2; ++bj)
; #pragma unroll
;                     for (int n = 0; n < 2; ++n) x[bj][n] = x[bj][n] * r * g[bj][n];
;             }
;             if (rope) {
;                 const int t = row & 8191; const bool second = (fq & 2) != 0;
; #pragma unroll
;                 for (int bj = 0; bj < 2; ++bj) { const int pos = bj ? (t & 63) : (t >> 6); const f32x2e* tb = rope + pos * 16 + 8 * (fq & 1);
; #pragma unroll
;                     for (int n = 0; n < 2; ++n)
; #pragma unroll
;                         for (int e = 0; e < 4; ++e) { const float p = __shfl_xor(x[bj][n][e], 32); const f32x2e cs = tb[4 * n + e]; const float v = x[bj][n][e];
;                             x[bj][n][e] = second ? (p * cs.y + v * cs.x) : (v * cs.x - p * cs.y); } }
;             }
;             if constexpr (F8OUT) { unsigned char* rowp8 = (unsigned char*)obase + (size_t)row * opitch + 8 * fq; typedef unsigned u32x2_ __attribute__((ext_vector_type(2)));
; #pragma unroll
;                 for (int bj = 0; bj < 2; ++bj) *(u32x2_*)(rowp8 + 32 * bj) = (u32x2_){pk4_fp8(x[bj][0][0], x[bj][0][1], x[bj][0][2], x[bj][0][3]), pk4_fp8(x[bj][1][0], x[bj][1][1], x[bj][1][2], x[bj][1][3])};
;                 continue; }
;             bf16_t* rowp = obase + (size_t)row * opitch + 8 * fq;
; #pragma unroll
;             for (int bj = 0; bj < 2; ++bj) { u32x4 w; w.x = cvt_pk_bf16(x[bj][0][0], x[bj][0][1]); w.y = cvt_pk_bf16(x[bj][0][2], x[bj][0][3]); w.z = cvt_pk_bf16(x[bj][1][0], x[bj][1][1]); w.w = cvt_pk_bf16(x[bj][1][2], x[bj][1][3]);
;                 *(u32x4*)(rowp + 32 * bj) = w; }
	s_nop 0
	v_pk_mul_f32 v[24:25], v[128:129], v[128:129]
	v_pk_mul_f32 v[26:27], v[126:127], v[126:127]
	s_nop 0
	v_pk_mov_b32 v[28:29], v[26:27], v[24:25] op_sel:[1,0]
	v_mov_b32_e32 v27, v25
	v_pk_add_f32 v[24:25], v[28:29], v[26:27]
	v_pk_mul_f32 v[26:27], v[124:125], v[124:125]
	v_pk_mul_f32 v[28:29], v[122:123], v[122:123]
	v_pk_add_f32 v[24:25], v[24:25], v[24:25] op_sel:[0,1] op_sel_hi:[1,0]
	v_pk_mov_b32 v[30:31], v[28:29], v[26:27] op_sel:[1,0]
	v_mov_b32_e32 v29, v27
	v_pk_add_f32 v[26:27], v[30:31], v[28:29]
	v_mul_f32_e32 v28, v114, v114
	v_mul_f32_e32 v29, v115, v115
	v_pk_add_f32 v[26:27], v[26:27], v[26:27] op_sel:[0,1] op_sel_hi:[1,0]
	v_mov_b32_e32 v25, v28
	v_mov_b32_e32 v27, v29
	v_pk_add_f32 v[24:25], v[24:25], v[26:27]
	v_mul_f32_e32 v26, v119, v119
	v_mul_f32_e32 v28, v121, v121
	v_mul_f32_e32 v30, v116, v116
	v_mul_f32_e32 v31, v117, v117
	v_pk_fma_f32 v[26:27], v[118:119], v[118:119], v[26:27] op_sel_hi:[1,1,0]
	v_pk_fma_f32 v[28:29], v[120:121], v[120:121], v[28:29] op_sel_hi:[1,1,0]
	v_mov_b32_e32 v27, v30
	v_mov_b32_e32 v29, v31
	v_pk_add_f32 v[26:27], v[26:27], v[28:29]
	s_nop 0
	v_pk_add_f32 v[24:25], v[24:25], v[26:27]
	v_and_b32_e32 v26, 64, v195
	v_add_f32_e32 v24, v24, v25
	v_xor_b32_e32 v25, 16, v195
	v_add_u32_e32 v26, 64, v26
	v_cmp_lt_i32_e32 vcc, v25, v26
	s_nop 1
	v_cndmask_b32_e32 v25, v195, v25, vcc
	v_lshlrev_b32_e32 v25, 2, v25
	v_mov_b32_e32 v25, v24
	s_nop 1
	v_permlane16_swap_b32_e32 v24, v25
	s_waitcnt lgkmcnt(0)
	v_add_f32_e32 v24, v24, v25
	v_xor_b32_e32 v25, 32, v195
	v_cmp_lt_i32_e32 vcc, v25, v26
	s_nop 1
	v_cndmask_b32_e32 v25, v195, v25, vcc
	v_lshlrev_b32_e32 v25, 2, v25
	v_mov_b32_e32 v25, v24
	s_nop 1
	v_permlane32_swap_b32_e32 v24, v25
	s_waitcnt lgkmcnt(0)
	v_add_f32_e32 v24, v24, v25
	v_fmamk_f32 v24, v24, 0x3c800000, v193
	v_mul_f32_e32 v25, 0x4f800000, v24
	v_cmp_gt_f32_e32 vcc, s69, v24
	s_nop 1
	v_cndmask_b32_e32 v24, v24, v25, vcc
	v_sqrt_f32_e32 v25, v24
	s_nop 0
	v_add_u32_e32 v26, -1, v25
	v_fma_f32 v27, -v26, v25, v24
	v_cmp_ge_f32_e64 s[6:7], 0, v27
	v_add_u32_e32 v27, 1, v25
	s_nop 0
	v_cndmask_b32_e64 v26, v25, v26, s[6:7]
	v_fma_f32 v25, -v27, v25, v24
	v_cmp_lt_f32_e64 s[6:7], 0, v25
	s_nop 1
	v_cndmask_b32_e64 v25, v26, v27, s[6:7]
	v_mul_f32_e32 v26, 0x37800000, v25
	v_cndmask_b32_e32 v25, v25, v26, vcc
	v_cmp_class_f32_e32 vcc, v24, v194
	s_nop 1
	v_cndmask_b32_e32 v24, v25, v24, vcc
	v_div_scale_f32 v25, s[6:7], v24, v24, s70
	v_rcp_f32_e32 v26, v25
	s_nop 0
	v_fma_f32 v27, -v25, v26, 1.0
	v_fmac_f32_e32 v26, v27, v26
	v_div_scale_f32 v27, vcc, s70, v24, s70
	v_mul_f32_e32 v28, v27, v26
	v_fma_f32 v29, -v25, v28, v27
	v_fmac_f32_e32 v28, v29, v26
	v_fma_f32 v25, -v25, v28, v27
	v_div_fmas_f32 v25, v25, v26, v28
	v_div_fixup_f32 v24, v25, v24, s70
	v_pk_mul_f32 v[26:27], v[126:127], v[24:25] op_sel_hi:[1,0]
	v_pk_mul_f32 v[28:29], v[128:129], v[24:25] op_sel_hi:[1,0]
	s_nop 0
	v_pk_mul_f32 v[126:127], v[14:15], v[26:27]
	v_pk_mul_f32 v[26:27], v[122:123], v[24:25] op_sel_hi:[1,0]
	v_pk_mul_f32 v[128:129], v[16:17], v[28:29]
	v_pk_mul_f32 v[28:29], v[124:125], v[24:25] op_sel_hi:[1,0]
	v_pk_mul_f32 v[122:123], v[6:7], v[26:27]
	v_pk_mul_f32 v[26:27], v[118:119], v[24:25] op_sel_hi:[1,0]
	v_pk_mul_f32 v[124:125], v[8:9], v[28:29]
	v_pk_mul_f32 v[28:29], v[120:121], v[24:25] op_sel_hi:[1,0]
	v_pk_mul_f32 v[118:119], v[10:11], v[26:27]
	v_pk_mul_f32 v[26:27], v[114:115], v[24:25] op_sel_hi:[1,0]
	v_pk_mul_f32 v[24:25], v[116:117], v[24:25] op_sel_hi:[1,0]
	v_pk_mul_f32 v[120:121], v[12:13], v[28:29]
	v_pk_mul_f32 v[116:117], v[4:5], v[24:25]
	v_pk_mul_f32 v[114:115], v[2:3], v[26:27]
.LBB0_1063:
	v_lshl_add_u64 v[28:29], v[22:23], 0, s[34:35]
	v_add_co_u32_e32 v22, vcc, 0x10000, v22
	v_cvt_pk_bf16_f32 v24, v126, v127
	v_cvt_pk_bf16_f32 v25, v128, v129
	v_cvt_pk_bf16_f32 v26, v122, v123
	v_cvt_pk_bf16_f32 v27, v124, v125
	s_nop 1
	v_addc_co_u32_e32 v23, vcc, 0, v23, vcc
	s_and_b64 vcc, exec, s[4:5]
	global_store_dwordx4 v[22:23], v[24:27], off
	v_cvt_pk_bf16_f32 v22, v118, v119
	v_cvt_pk_bf16_f32 v23, v120, v121
	s_nop 1
	v_cvt_pk_bf16_f32 v24, v114, v115
	v_cvt_pk_bf16_f32 v25, v116, v117
	global_store_dwordx4 v[28:29], v[22:25], off offset:64
	s_cbranch_vccnz .LBB0_1065
	s_nop 0
	v_pk_mul_f32 v[22:23], v[112:113], v[112:113]
	v_pk_mul_f32 v[24:25], v[110:111], v[110:111]
	s_nop 0
	v_pk_mov_b32 v[26:27], v[24:25], v[22:23] op_sel:[1,0]
	v_mov_b32_e32 v25, v23
	v_pk_add_f32 v[22:23], v[26:27], v[24:25]
	v_pk_mul_f32 v[24:25], v[108:109], v[108:109]
	v_pk_mul_f32 v[26:27], v[106:107], v[106:107]
	v_pk_add_f32 v[22:23], v[22:23], v[22:23] op_sel:[0,1] op_sel_hi:[1,0]
	v_pk_mov_b32 v[28:29], v[26:27], v[24:25] op_sel:[1,0]
	v_mov_b32_e32 v27, v25
	v_pk_add_f32 v[24:25], v[28:29], v[26:27]
	v_mul_f32_e32 v26, v98, v98
	v_mul_f32_e32 v27, v99, v99
	v_pk_add_f32 v[24:25], v[24:25], v[24:25] op_sel:[0,1] op_sel_hi:[1,0]
	v_mov_b32_e32 v23, v26
	v_mov_b32_e32 v25, v27
	v_pk_add_f32 v[22:23], v[22:23], v[24:25]
	v_mul_f32_e32 v24, v103, v103
	v_mul_f32_e32 v26, v105, v105
	v_mul_f32_e32 v28, v100, v100
	v_mul_f32_e32 v29, v101, v101
	v_pk_fma_f32 v[24:25], v[102:103], v[102:103], v[24:25] op_sel_hi:[1,1,0]
	v_pk_fma_f32 v[26:27], v[104:105], v[104:105], v[26:27] op_sel_hi:[1,1,0]
	v_mov_b32_e32 v25, v28
	v_mov_b32_e32 v27, v29
	v_pk_add_f32 v[24:25], v[24:25], v[26:27]
	s_nop 0
	v_pk_add_f32 v[22:23], v[22:23], v[24:25]
	v_and_b32_e32 v24, 64, v195
	v_add_f32_e32 v22, v22, v23
	v_xor_b32_e32 v23, 16, v195
	v_add_u32_e32 v24, 64, v24
	v_cmp_lt_i32_e32 vcc, v23, v24
	s_nop 1
	v_cndmask_b32_e32 v23, v195, v23, vcc
	v_lshlrev_b32_e32 v23, 2, v23
	v_mov_b32_e32 v23, v22
	s_nop 1
	v_permlane16_swap_b32_e32 v22, v23
	s_waitcnt lgkmcnt(0)
; template <bool F8OUT = false> __device__ __forceinline__ void head_tile_store(const f32x4 (&acc)[2][2][4][2], bf16_t* obase  , int opitch, const float* gain, float scale, const f32x2e* rope, int row0, int fq) {
;     ...
;             if (gain) {
;                 float ss = 0.f;
; #pragma unroll
;                 for (int bj = 0; bj < 2; ++bj)
; #pragma unroll
;                     for (int n = 0; n < 2; ++n) ss += (x[bj][n][0] * x[bj][n][0] + x[bj][n][1] * x[bj][n][1]) + (x[bj][n][2] * x[bj][n][2] + x[bj][n][3] * x[bj][n][3]);
;                 ss += __shfl_xor(ss, 16); ss += __shfl_xor(ss, 32);
;                 const float r = scale / sqrtf(ss * (1.f / 64.f) + 1e-6f);
; #pragma unroll
;                 for (int bj = 0; bj < 2; ++bj)
; #pragma unroll
;                     for (int n = 0; n < 2; ++n) x[bj][n] = x[bj][n] * r * g[bj][n];
;             }
;             if (rope) {
;                 const int t = row & 8191; const bool second = (fq & 2) != 0;
; #pragma unroll
;                 for (int bj = 0; bj < 2; ++bj) { const int pos = bj ? (t & 63) : (t >> 6); const f32x2e* tb = rope + pos * 16 + 8 * (fq & 1);
; #pragma unroll
;                     for (int n = 0; n < 2; ++n)
; #pragma unroll
;                         for (int e = 0; e < 4; ++e) { const float p = __shfl_xor(x[bj][n][e], 32); const f32x2e cs = tb[4 * n + e]; const float v = x[bj][n][e];
;                             x[bj][n][e] = second ? (p * cs.y + v * cs.x) : (v * cs.x - p * cs.y); } }
;             }
;             if constexpr (F8OUT) { unsigned char* rowp8 = (unsigned char*)obase + (size_t)row * opitch + 8 * fq; typedef unsigned u32x2_ __attribute__((ext_vector_type(2)));
; #pragma unroll
;                 for (int bj = 0; bj < 2; ++bj) *(u32x2_*)(rowp8 + 32 * bj) = (u32x2_){pk4_fp8(x[bj][0][0], x[bj][0][1], x[bj][0][2], x[bj][0][3]), pk4_fp8(x[bj][1][0], x[bj][1][1], x[bj][1][2], x[bj][1][3])};
;                 continue; }
;             bf16_t* rowp = obase + (size_t)row * opitch + 8 * fq;
; #pragma unroll
;             for (int bj = 0; bj < 2; ++bj) { u32x4 w; w.x = cvt_pk_bf16(x[bj][0][0], x[bj][0][1]); w.y = cvt_pk_bf16(x[bj][0][2], x[bj][0][3]); w.z = cvt_pk_bf16(x[bj][1][0], x[bj][1][1]); w.w = cvt_pk_bf16(x[bj][1][2], x[bj][1][3]);
;                 *(u32x4*)(rowp + 32 * bj) = w; }
	v_add_f32_e32 v22, v22, v23
	v_xor_b32_e32 v23, 32, v195
	v_cmp_lt_i32_e32 vcc, v23, v24
	s_nop 1
	v_cndmask_b32_e32 v23, v195, v23, vcc
	v_lshlrev_b32_e32 v23, 2, v23
	v_mov_b32_e32 v23, v22
	s_nop 1
	v_permlane32_swap_b32_e32 v22, v23
	s_waitcnt lgkmcnt(0)
	v_add_f32_e32 v22, v22, v23
	v_fmamk_f32 v22, v22, 0x3c800000, v193
	v_mul_f32_e32 v23, 0x4f800000, v22
	v_cmp_gt_f32_e32 vcc, s69, v22
	s_nop 1
	v_cndmask_b32_e32 v22, v22, v23, vcc
	v_sqrt_f32_e32 v23, v22
	s_nop 0
	v_add_u32_e32 v24, -1, v23
	v_fma_f32 v25, -v24, v23, v22
	v_cmp_ge_f32_e64 s[6:7], 0, v25
	v_add_u32_e32 v25, 1, v23
	s_nop 0
	v_cndmask_b32_e64 v24, v23, v24, s[6:7]
	v_fma_f32 v23, -v25, v23, v22
	v_cmp_lt_f32_e64 s[6:7], 0, v23
	s_nop 1
	v_cndmask_b32_e64 v23, v24, v25, s[6:7]
	v_mul_f32_e32 v24, 0x37800000, v23
	v_cndmask_b32_e32 v23, v23, v24, vcc
	v_cmp_class_f32_e32 vcc, v22, v194
	s_nop 1
	v_cndmask_b32_e32 v22, v23, v22, vcc
	v_div_scale_f32 v23, s[6:7], v22, v22, s70
	v_rcp_f32_e32 v24, v23
	s_nop 0
	v_fma_f32 v25, -v23, v24, 1.0
	v_fmac_f32_e32 v24, v25, v24
	v_div_scale_f32 v25, vcc, s70, v22, s70
	v_mul_f32_e32 v26, v25, v24
	v_fma_f32 v27, -v23, v26, v25
	v_fmac_f32_e32 v26, v27, v24
	v_fma_f32 v23, -v23, v26, v25
	v_div_fmas_f32 v23, v23, v24, v26
	v_div_fixup_f32 v22, v23, v22, s70
	v_pk_mul_f32 v[24:25], v[110:111], v[22:23] op_sel_hi:[1,0]
	v_pk_mul_f32 v[26:27], v[112:113], v[22:23] op_sel_hi:[1,0]
	s_nop 0
	v_pk_mul_f32 v[110:111], v[14:15], v[24:25]
	v_pk_mul_f32 v[24:25], v[106:107], v[22:23] op_sel_hi:[1,0]
	v_pk_mul_f32 v[112:113], v[16:17], v[26:27]
	v_pk_mul_f32 v[26:27], v[108:109], v[22:23] op_sel_hi:[1,0]
	v_pk_mul_f32 v[106:107], v[6:7], v[24:25]
	v_pk_mul_f32 v[24:25], v[102:103], v[22:23] op_sel_hi:[1,0]
	v_pk_mul_f32 v[108:109], v[8:9], v[26:27]
	v_pk_mul_f32 v[26:27], v[104:105], v[22:23] op_sel_hi:[1,0]
	v_pk_mul_f32 v[102:103], v[10:11], v[24:25]
	v_pk_mul_f32 v[24:25], v[98:99], v[22:23] op_sel_hi:[1,0]
	v_pk_mul_f32 v[22:23], v[100:101], v[22:23] op_sel_hi:[1,0]
	v_pk_mul_f32 v[104:105], v[12:13], v[26:27]
	v_pk_mul_f32 v[100:101], v[4:5], v[22:23]
	v_pk_mul_f32 v[98:99], v[2:3], v[24:25]
.LBB0_1065:
	s_nop 0
	v_lshlrev_b64 v[22:23], 11, v[18:19]
	v_lshl_add_u64 v[22:23], v[20:21], 0, v[22:23]
	v_add_co_u32_e32 v30, vcc, 0x18000, v22
	s_mov_b64 s[6:7], 0x18000
	s_nop 0
	v_addc_co_u32_e32 v31, vcc, 0, v23, vcc
	v_lshl_add_u64 v[28:29], v[22:23], 0, s[6:7]
	v_cvt_pk_bf16_f32 v24, v110, v111
	v_cvt_pk_bf16_f32 v25, v112, v113
	v_cvt_pk_bf16_f32 v26, v106, v107
	v_cvt_pk_bf16_f32 v27, v108, v109
	s_and_b64 vcc, exec, s[4:5]
	global_store_dwordx4 v[30:31], v[24:27], off
	s_nop 1
	v_cvt_pk_bf16_f32 v24, v102, v103
	v_cvt_pk_bf16_f32 v25, v104, v105
	v_cvt_pk_bf16_f32 v26, v98, v99
	v_cvt_pk_bf16_f32 v27, v100, v101
	global_store_dwordx4 v[28:29], v[24:27], off offset:64
	s_cbranch_vccnz .LBB0_1067
	s_nop 0
	v_pk_mul_f32 v[24:25], v[96:97], v[96:97]
	v_pk_mul_f32 v[26:27], v[94:95], v[94:95]
	s_nop 0
	v_pk_mov_b32 v[28:29], v[26:27], v[24:25] op_sel:[1,0]
	v_mov_b32_e32 v27, v25
	v_pk_add_f32 v[24:25], v[28:29], v[26:27]
	v_pk_mul_f32 v[26:27], v[92:93], v[92:93]
	v_pk_mul_f32 v[28:29], v[90:91], v[90:91]
	v_pk_add_f32 v[24:25], v[24:25], v[24:25] op_sel:[0,1] op_sel_hi:[1,0]
	v_pk_mov_b32 v[30:31], v[28:29], v[26:27] op_sel:[1,0]
	v_mov_b32_e32 v29, v27
	v_pk_add_f32 v[26:27], v[30:31], v[28:29]
	v_mul_f32_e32 v28, v82, v82
	v_mul_f32_e32 v29, v83, v83
	v_pk_add_f32 v[26:27], v[26:27], v[26:27] op_sel:[0,1] op_sel_hi:[1,0]
	v_mov_b32_e32 v25, v28
	v_mov_b32_e32 v27, v29
	v_pk_add_f32 v[24:25], v[24:25], v[26:27]
	v_mul_f32_e32 v26, v87, v87
	v_mul_f32_e32 v28, v89, v89
	v_mul_f32_e32 v30, v84, v84
	v_mul_f32_e32 v31, v85, v85
	v_pk_fma_f32 v[26:27], v[86:87], v[86:87], v[26:27] op_sel_hi:[1,1,0]
	v_pk_fma_f32 v[28:29], v[88:89], v[88:89], v[28:29] op_sel_hi:[1,1,0]
	v_mov_b32_e32 v27, v30
	v_mov_b32_e32 v29, v31
	v_pk_add_f32 v[26:27], v[26:27], v[28:29]
	s_nop 0
	v_pk_add_f32 v[24:25], v[24:25], v[26:27]
	v_and_b32_e32 v26, 64, v195
	v_add_f32_e32 v24, v24, v25
	v_xor_b32_e32 v25, 16, v195
	v_add_u32_e32 v26, 64, v26
	v_cmp_lt_i32_e32 vcc, v25, v26
	s_nop 1
	v_cndmask_b32_e32 v25, v195, v25, vcc
	v_lshlrev_b32_e32 v25, 2, v25
	v_mov_b32_e32 v25, v24
	s_nop 1
	v_permlane16_swap_b32_e32 v24, v25
	s_waitcnt lgkmcnt(0)
	v_add_f32_e32 v24, v24, v25
	v_xor_b32_e32 v25, 32, v195
	v_cmp_lt_i32_e32 vcc, v25, v26
	s_nop 1
	v_cndmask_b32_e32 v25, v195, v25, vcc
	v_lshlrev_b32_e32 v25, 2, v25
	v_mov_b32_e32 v25, v24
	s_nop 1
	v_permlane32_swap_b32_e32 v24, v25
	s_waitcnt lgkmcnt(0)
	v_add_f32_e32 v24, v24, v25
	v_fmamk_f32 v24, v24, 0x3c800000, v193
	v_mul_f32_e32 v25, 0x4f800000, v24
	v_cmp_gt_f32_e32 vcc, s69, v24
	s_nop 1
	v_cndmask_b32_e32 v24, v24, v25, vcc
	v_sqrt_f32_e32 v25, v24
	s_nop 0
	v_add_u32_e32 v26, -1, v25
	v_fma_f32 v27, -v26, v25, v24
	v_cmp_ge_f32_e64 s[6:7], 0, v27
	v_add_u32_e32 v27, 1, v25
	s_nop 0
	v_cndmask_b32_e64 v26, v25, v26, s[6:7]
	v_fma_f32 v25, -v27, v25, v24
	v_cmp_lt_f32_e64 s[6:7], 0, v25
	s_nop 1
	v_cndmask_b32_e64 v25, v26, v27, s[6:7]
	v_mul_f32_e32 v26, 0x37800000, v25
	v_cndmask_b32_e32 v25, v25, v26, vcc
	v_cmp_class_f32_e32 vcc, v24, v194
	s_nop 1
	v_cndmask_b32_e32 v24, v25, v24, vcc
	v_div_scale_f32 v25, s[6:7], v24, v24, s70
	v_rcp_f32_e32 v26, v25
	s_nop 0
	v_fma_f32 v27, -v25, v26, 1.0
	v_fmac_f32_e32 v26, v27, v26
	v_div_scale_f32 v27, vcc, s70, v24, s70
	v_mul_f32_e32 v28, v27, v26
	v_fma_f32 v29, -v25, v28, v27
	v_fmac_f32_e32 v28, v29, v26
	v_fma_f32 v25, -v25, v28, v27
	v_div_fmas_f32 v25, v25, v26, v28
	v_div_fixup_f32 v24, v25, v24, s70
	v_pk_mul_f32 v[26:27], v[94:95], v[24:25] op_sel_hi:[1,0]
	v_pk_mul_f32 v[28:29], v[96:97], v[24:25] op_sel_hi:[1,0]
	s_nop 0
	v_pk_mul_f32 v[94:95], v[14:15], v[26:27]
	v_pk_mul_f32 v[26:27], v[90:91], v[24:25] op_sel_hi:[1,0]
	v_pk_mul_f32 v[96:97], v[16:17], v[28:29]
	v_pk_mul_f32 v[28:29], v[92:93], v[24:25] op_sel_hi:[1,0]
	v_pk_mul_f32 v[90:91], v[6:7], v[26:27]
	v_pk_mul_f32 v[26:27], v[86:87], v[24:25] op_sel_hi:[1,0]
	v_pk_mul_f32 v[92:93], v[8:9], v[28:29]
	v_pk_mul_f32 v[28:29], v[88:89], v[24:25] op_sel_hi:[1,0]
	v_pk_mul_f32 v[86:87], v[10:11], v[26:27]
	v_pk_mul_f32 v[26:27], v[82:83], v[24:25] op_sel_hi:[1,0]
	v_pk_mul_f32 v[24:25], v[84:85], v[24:25] op_sel_hi:[1,0]
	v_pk_mul_f32 v[88:89], v[12:13], v[28:29]
	v_pk_mul_f32 v[84:85], v[4:5], v[24:25]
	v_pk_mul_f32 v[82:83], v[2:3], v[26:27]
; template <bool F8OUT = false> __device__ __forceinline__ void head_tile_store(const f32x4 (&acc)[2][2][4][2], bf16_t* obase  , int opitch, const float* gain, float scale, const f32x2e* rope, int row0, int fq) {
;     ...
;             if (gain) {
;                 float ss = 0.f;
; #pragma unroll
;                 for (int bj = 0; bj < 2; ++bj)
; #pragma unroll
;                     for (int n = 0; n < 2; ++n) ss += (x[bj][n][0] * x[bj][n][0] + x[bj][n][1] * x[bj][n][1]) + (x[bj][n][2] * x[bj][n][2] + x[bj][n][3] * x[bj][n][3]);
;                 ss += __shfl_xor(ss, 16); ss += __shfl_xor(ss, 32);
;                 const float r = scale / sqrtf(ss * (1.f / 64.f) + 1e-6f);
; #pragma unroll
;                 for (int bj = 0; bj < 2; ++bj)
; #pragma unroll
;                     for (int n = 0; n < 2; ++n) x[bj][n] = x[bj][n] * r * g[bj][n];
;             }
;             if (rope) {
;                 const int t = row & 8191; const bool second = (fq & 2) != 0;
; #pragma unroll
;                 for (int bj = 0; bj < 2; ++bj) { const int pos = bj ? (t & 63) : (t >> 6); const f32x2e* tb = rope + pos * 16 + 8 * (fq & 1);
; #pragma unroll
;                     for (int n = 0; n < 2; ++n)
; #pragma unroll
;                         for (int e = 0; e < 4; ++e) { const float p = __shfl_xor(x[bj][n][e], 32); const f32x2e cs = tb[4 * n + e]; const float v = x[bj][n][e];
;                             x[bj][n][e] = second ? (p * cs.y + v * cs.x) : (v * cs.x - p * cs.y); } }
;             }
;             if constexpr (F8OUT) { unsigned char* rowp8 = (unsigned char*)obase + (size_t)row * opitch + 8 * fq; typedef unsigned u32x2_ __attribute__((ext_vector_type(2)));
; #pragma unroll
;                 for (int bj = 0; bj < 2; ++bj) *(u32x2_*)(rowp8 + 32 * bj) = (u32x2_){pk4_fp8(x[bj][0][0], x[bj][0][1], x[bj][0][2], x[bj][0][3]), pk4_fp8(x[bj][1][0], x[bj][1][1], x[bj][1][2], x[bj][1][3])};
;                 continue; }
;             bf16_t* rowp = obase + (size_t)row * opitch + 8 * fq;
; #pragma unroll
;             for (int bj = 0; bj < 2; ++bj) { u32x4 w; w.x = cvt_pk_bf16(x[bj][0][0], x[bj][0][1]); w.y = cvt_pk_bf16(x[bj][0][2], x[bj][0][3]); w.z = cvt_pk_bf16(x[bj][1][0], x[bj][1][1]); w.w = cvt_pk_bf16(x[bj][1][2], x[bj][1][3]);
;                 *(u32x4*)(rowp + 32 * bj) = w; }
.LBB0_1067:
	s_mov_b64 s[6:7], 0x40000
	v_lshl_add_u64 v[28:29], v[22:23], 0, s[6:7]
	v_add_co_u32_e32 v22, vcc, 0x40000, v22
	v_cvt_pk_bf16_f32 v24, v94, v95
	v_cvt_pk_bf16_f32 v25, v96, v97
	v_cvt_pk_bf16_f32 v26, v90, v91
	v_cvt_pk_bf16_f32 v27, v92, v93
	s_nop 1
	v_addc_co_u32_e32 v23, vcc, 0, v23, vcc
	s_and_b64 vcc, exec, s[4:5]
	global_store_dwordx4 v[22:23], v[24:27], off
	v_cvt_pk_bf16_f32 v22, v86, v87
	v_cvt_pk_bf16_f32 v23, v88, v89
	s_nop 1
	v_cvt_pk_bf16_f32 v24, v82, v83
	v_cvt_pk_bf16_f32 v25, v84, v85
	global_store_dwordx4 v[28:29], v[22:25], off offset:64
	s_cbranch_vccnz .LBB0_1069
	s_nop 0
	v_pk_mul_f32 v[22:23], v[80:81], v[80:81]
	v_pk_mul_f32 v[24:25], v[78:79], v[78:79]
	s_nop 0
	v_pk_mov_b32 v[26:27], v[24:25], v[22:23] op_sel:[1,0]
	v_mov_b32_e32 v25, v23
	v_pk_add_f32 v[22:23], v[26:27], v[24:25]
	v_pk_mul_f32 v[24:25], v[76:77], v[76:77]
	v_pk_mul_f32 v[26:27], v[74:75], v[74:75]
	v_pk_add_f32 v[22:23], v[22:23], v[22:23] op_sel:[0,1] op_sel_hi:[1,0]
	v_pk_mov_b32 v[28:29], v[26:27], v[24:25] op_sel:[1,0]
	v_mov_b32_e32 v27, v25
	v_pk_add_f32 v[24:25], v[28:29], v[26:27]
	v_mul_f32_e32 v26, v66, v66
	v_mul_f32_e32 v27, v67, v67
	v_pk_add_f32 v[24:25], v[24:25], v[24:25] op_sel:[0,1] op_sel_hi:[1,0]
	v_mov_b32_e32 v23, v26
	v_mov_b32_e32 v25, v27
	v_pk_add_f32 v[22:23], v[22:23], v[24:25]
	v_mul_f32_e32 v24, v71, v71
	v_mul_f32_e32 v26, v73, v73
	v_mul_f32_e32 v28, v68, v68
	v_mul_f32_e32 v29, v69, v69
	v_pk_fma_f32 v[24:25], v[70:71], v[70:71], v[24:25] op_sel_hi:[1,1,0]
	v_pk_fma_f32 v[26:27], v[72:73], v[72:73], v[26:27] op_sel_hi:[1,1,0]
	v_mov_b32_e32 v25, v28
	v_mov_b32_e32 v27, v29
	v_pk_add_f32 v[24:25], v[24:25], v[26:27]
	s_nop 0
	v_pk_add_f32 v[22:23], v[22:23], v[24:25]
	v_and_b32_e32 v24, 64, v195
	v_add_f32_e32 v22, v22, v23
	v_xor_b32_e32 v23, 16, v195
	v_add_u32_e32 v24, 64, v24
	v_cmp_lt_i32_e32 vcc, v23, v24
	s_nop 1
	v_cndmask_b32_e32 v23, v195, v23, vcc
	v_lshlrev_b32_e32 v23, 2, v23
	v_mov_b32_e32 v23, v22
	s_nop 1
	v_permlane16_swap_b32_e32 v22, v23
	s_waitcnt lgkmcnt(0)
	v_add_f32_e32 v22, v22, v23
	v_xor_b32_e32 v23, 32, v195
	v_cmp_lt_i32_e32 vcc, v23, v24
	s_nop 1
	v_cndmask_b32_e32 v23, v195, v23, vcc
	v_lshlrev_b32_e32 v23, 2, v23
	v_mov_b32_e32 v23, v22
	s_nop 1
	v_permlane32_swap_b32_e32 v22, v23
	s_waitcnt lgkmcnt(0)
	v_add_f32_e32 v22, v22, v23
	v_fmamk_f32 v22, v22, 0x3c800000, v193
	v_mul_f32_e32 v23, 0x4f800000, v22
	v_cmp_gt_f32_e32 vcc, s69, v22
	s_nop 1
	v_cndmask_b32_e32 v22, v22, v23, vcc
	v_sqrt_f32_e32 v23, v22
	s_nop 0
	v_add_u32_e32 v24, -1, v23
	v_fma_f32 v25, -v24, v23, v22
	v_cmp_ge_f32_e64 s[6:7], 0, v25
	v_add_u32_e32 v25, 1, v23
	s_nop 0
	v_cndmask_b32_e64 v24, v23, v24, s[6:7]
	v_fma_f32 v23, -v25, v23, v22
	v_cmp_lt_f32_e64 s[6:7], 0, v23
	s_nop 1
	v_cndmask_b32_e64 v23, v24, v25, s[6:7]
	v_mul_f32_e32 v24, 0x37800000, v23
	v_cndmask_b32_e32 v23, v23, v24, vcc
	v_cmp_class_f32_e32 vcc, v22, v194
	s_nop 1
	v_cndmask_b32_e32 v22, v23, v22, vcc
	v_div_scale_f32 v23, s[6:7], v22, v22, s70
	v_rcp_f32_e32 v24, v23
	s_nop 0
	v_fma_f32 v25, -v23, v24, 1.0
	v_fmac_f32_e32 v24, v25, v24
	v_div_scale_f32 v25, vcc, s70, v22, s70
	v_mul_f32_e32 v26, v25, v24
	v_fma_f32 v27, -v23, v26, v25
	v_fmac_f32_e32 v26, v27, v24
	v_fma_f32 v23, -v23, v26, v25
	v_div_fmas_f32 v23, v23, v24, v26
	v_div_fixup_f32 v22, v23, v22, s70
	v_pk_mul_f32 v[24:25], v[78:79], v[22:23] op_sel_hi:[1,0]
	v_pk_mul_f32 v[26:27], v[80:81], v[22:23] op_sel_hi:[1,0]
	s_nop 0
	v_pk_mul_f32 v[78:79], v[14:15], v[24:25]
	v_pk_mul_f32 v[24:25], v[74:75], v[22:23] op_sel_hi:[1,0]
	v_pk_mul_f32 v[80:81], v[16:17], v[26:27]
	v_pk_mul_f32 v[26:27], v[76:77], v[22:23] op_sel_hi:[1,0]
	v_pk_mul_f32 v[74:75], v[6:7], v[24:25]
	v_pk_mul_f32 v[24:25], v[70:71], v[22:23] op_sel_hi:[1,0]
	v_pk_mul_f32 v[76:77], v[8:9], v[26:27]
	v_pk_mul_f32 v[26:27], v[72:73], v[22:23] op_sel_hi:[1,0]
	v_pk_mul_f32 v[70:71], v[10:11], v[24:25]
	v_pk_mul_f32 v[24:25], v[66:67], v[22:23] op_sel_hi:[1,0]
	v_pk_mul_f32 v[22:23], v[68:69], v[22:23] op_sel_hi:[1,0]
	v_pk_mul_f32 v[72:73], v[12:13], v[26:27]
	v_pk_mul_f32 v[68:69], v[4:5], v[22:23]
	v_pk_mul_f32 v[66:67], v[2:3], v[24:25]
.LBB0_1069:
	s_nop 0
	v_lshlrev_b64 v[22:23], 11, v[18:19]
	v_lshl_add_u64 v[22:23], v[20:21], 0, v[22:23]
	v_add_co_u32_e32 v30, vcc, 0x48000, v22
	s_mov_b64 s[6:7], 0x48000
	s_nop 0
	v_addc_co_u32_e32 v31, vcc, 0, v23, vcc
	v_lshl_add_u64 v[28:29], v[22:23], 0, s[6:7]
	v_cvt_pk_bf16_f32 v24, v78, v79
	v_cvt_pk_bf16_f32 v25, v80, v81
	v_cvt_pk_bf16_f32 v26, v74, v75
	v_cvt_pk_bf16_f32 v27, v76, v77
	s_and_b64 vcc, exec, s[4:5]
	global_store_dwordx4 v[30:31], v[24:27], off
	s_nop 1
	v_cvt_pk_bf16_f32 v24, v70, v71
	v_cvt_pk_bf16_f32 v25, v72, v73
	v_cvt_pk_bf16_f32 v26, v66, v67
	v_cvt_pk_bf16_f32 v27, v68, v69
	global_store_dwordx4 v[28:29], v[24:27], off offset:64
	s_cbranch_vccnz .LBB0_1071
; template <bool F8OUT = false> __device__ __forceinline__ void head_tile_store(const f32x4 (&acc)[2][2][4][2], bf16_t* obase  , int opitch, const float* gain, float scale, const f32x2e* rope, int row0, int fq) {
;     ...
;             if (gain) {
;                 float ss = 0.f;
; #pragma unroll
;                 for (int bj = 0; bj < 2; ++bj)
; #pragma unroll
;                     for (int n = 0; n < 2; ++n) ss += (x[bj][n][0] * x[bj][n][0] + x[bj][n][1] * x[bj][n][1]) + (x[bj][n][2] * x[bj][n][2] + x[bj][n][3] * x[bj][n][3]);
;                 ss += __shfl_xor(ss, 16); ss += __shfl_xor(ss, 32);
;                 const float r = scale / sqrtf(ss * (1.f / 64.f) + 1e-6f);
; #pragma unroll
;                 for (int bj = 0; bj < 2; ++bj)
; #pragma unroll
;                     for (int n = 0; n < 2; ++n) x[bj][n] = x[bj][n] * r * g[bj][n];
;             }
;             if (rope) {
;                 const int t = row & 8191; const bool second = (fq & 2) != 0;
; #pragma unroll
;                 for (int bj = 0; bj < 2; ++bj) { const int pos = bj ? (t & 63) : (t >> 6); const f32x2e* tb = rope + pos * 16 + 8 * (fq & 1);
; #pragma unroll
;                     for (int n = 0; n < 2; ++n)
; #pragma unroll
;                         for (int e = 0; e < 4; ++e) { const float p = __shfl_xor(x[bj][n][e], 32); const f32x2e cs = tb[4 * n + e]; const float v = x[bj][n][e];
;                             x[bj][n][e] = second ? (p * cs.y + v * cs.x) : (v * cs.x - p * cs.y); } }
;             }
;             if constexpr (F8OUT) { unsigned char* rowp8 = (unsigned char*)obase + (size_t)row * opitch + 8 * fq; typedef unsigned u32x2_ __attribute__((ext_vector_type(2)));
; #pragma unroll
;                 for (int bj = 0; bj < 2; ++bj) *(u32x2_*)(rowp8 + 32 * bj) = (u32x2_){pk4_fp8(x[bj][0][0], x[bj][0][1], x[bj][0][2], x[bj][0][3]), pk4_fp8(x[bj][1][0], x[bj][1][1], x[bj][1][2], x[bj][1][3])};
;                 continue; }
;             bf16_t* rowp = obase + (size_t)row * opitch + 8 * fq;
; #pragma unroll
;             for (int bj = 0; bj < 2; ++bj) { u32x4 w; w.x = cvt_pk_bf16(x[bj][0][0], x[bj][0][1]); w.y = cvt_pk_bf16(x[bj][0][2], x[bj][0][3]); w.z = cvt_pk_bf16(x[bj][1][0], x[bj][1][1]); w.w = cvt_pk_bf16(x[bj][1][2], x[bj][1][3]);
;                 *(u32x4*)(rowp + 32 * bj) = w; }
	s_nop 0
	v_pk_mul_f32 v[24:25], v[64:65], v[64:65]
	v_pk_mul_f32 v[26:27], v[62:63], v[62:63]
	s_nop 0
	v_pk_mov_b32 v[28:29], v[26:27], v[24:25] op_sel:[1,0]
	v_mov_b32_e32 v27, v25
	v_pk_add_f32 v[24:25], v[28:29], v[26:27]
	v_pk_mul_f32 v[26:27], v[60:61], v[60:61]
	v_pk_mul_f32 v[28:29], v[58:59], v[58:59]
	v_pk_add_f32 v[24:25], v[24:25], v[24:25] op_sel:[0,1] op_sel_hi:[1,0]
	v_pk_mov_b32 v[30:31], v[28:29], v[26:27] op_sel:[1,0]
	v_mov_b32_e32 v29, v27
	v_pk_add_f32 v[26:27], v[30:31], v[28:29]
	v_mul_f32_e32 v28, v50, v50
	v_mul_f32_e32 v29, v51, v51
	v_pk_add_f32 v[26:27], v[26:27], v[26:27] op_sel:[0,1] op_sel_hi:[1,0]
	v_mov_b32_e32 v25, v28
	v_mov_b32_e32 v27, v29
	v_pk_add_f32 v[24:25], v[24:25], v[26:27]
	v_mul_f32_e32 v26, v55, v55
	v_mul_f32_e32 v28, v57, v57
	v_mul_f32_e32 v30, v52, v52
	v_mul_f32_e32 v31, v53, v53
	v_pk_fma_f32 v[26:27], v[54:55], v[54:55], v[26:27] op_sel_hi:[1,1,0]
	v_pk_fma_f32 v[28:29], v[56:57], v[56:57], v[28:29] op_sel_hi:[1,1,0]
	v_mov_b32_e32 v27, v30
	v_mov_b32_e32 v29, v31
	v_pk_add_f32 v[26:27], v[26:27], v[28:29]
	s_nop 0
	v_pk_add_f32 v[24:25], v[24:25], v[26:27]
	v_and_b32_e32 v26, 64, v195
	v_add_f32_e32 v24, v24, v25
	v_xor_b32_e32 v25, 16, v195
	v_add_u32_e32 v26, 64, v26
	v_cmp_lt_i32_e32 vcc, v25, v26
	s_nop 1
	v_cndmask_b32_e32 v25, v195, v25, vcc
	v_lshlrev_b32_e32 v25, 2, v25
	v_mov_b32_e32 v25, v24
	s_nop 1
	v_permlane16_swap_b32_e32 v24, v25
	s_waitcnt lgkmcnt(0)
	v_add_f32_e32 v24, v24, v25
	v_xor_b32_e32 v25, 32, v195
	v_cmp_lt_i32_e32 vcc, v25, v26
	s_nop 1
	v_cndmask_b32_e32 v25, v195, v25, vcc
	v_lshlrev_b32_e32 v25, 2, v25
	v_mov_b32_e32 v25, v24
	s_nop 1
	v_permlane32_swap_b32_e32 v24, v25
	s_waitcnt lgkmcnt(0)
	v_add_f32_e32 v24, v24, v25
	v_fmamk_f32 v24, v24, 0x3c800000, v193
	v_mul_f32_e32 v25, 0x4f800000, v24
	v_cmp_gt_f32_e32 vcc, s69, v24
	s_nop 1
	v_cndmask_b32_e32 v24, v24, v25, vcc
	v_sqrt_f32_e32 v25, v24
	s_nop 0
	v_add_u32_e32 v26, -1, v25
	v_fma_f32 v27, -v26, v25, v24
	v_cmp_ge_f32_e64 s[6:7], 0, v27
	v_add_u32_e32 v27, 1, v25
	s_nop 0
	v_cndmask_b32_e64 v26, v25, v26, s[6:7]
	v_fma_f32 v25, -v27, v25, v24
	v_cmp_lt_f32_e64 s[6:7], 0, v25
	s_nop 1
	v_cndmask_b32_e64 v25, v26, v27, s[6:7]
	v_mul_f32_e32 v26, 0x37800000, v25
	v_cndmask_b32_e32 v25, v25, v26, vcc
	v_cmp_class_f32_e32 vcc, v24, v194
	s_nop 1
	v_cndmask_b32_e32 v24, v25, v24, vcc
	v_div_scale_f32 v25, s[6:7], v24, v24, s70
	v_rcp_f32_e32 v26, v25
	s_nop 0
	v_fma_f32 v27, -v25, v26, 1.0
	v_fmac_f32_e32 v26, v27, v26
	v_div_scale_f32 v27, vcc, s70, v24, s70
	v_mul_f32_e32 v28, v27, v26
	v_fma_f32 v29, -v25, v28, v27
	v_fmac_f32_e32 v28, v29, v26
	v_fma_f32 v25, -v25, v28, v27
	v_div_fmas_f32 v25, v25, v26, v28
	v_div_fixup_f32 v24, v25, v24, s70
	v_pk_mul_f32 v[26:27], v[62:63], v[24:25] op_sel_hi:[1,0]
	v_pk_mul_f32 v[28:29], v[64:65], v[24:25] op_sel_hi:[1,0]
	s_nop 0
	v_pk_mul_f32 v[62:63], v[14:15], v[26:27]
	v_pk_mul_f32 v[26:27], v[58:59], v[24:25] op_sel_hi:[1,0]
	v_pk_mul_f32 v[64:65], v[16:17], v[28:29]
	v_pk_mul_f32 v[28:29], v[60:61], v[24:25] op_sel_hi:[1,0]
	v_pk_mul_f32 v[58:59], v[6:7], v[26:27]
	v_pk_mul_f32 v[26:27], v[54:55], v[24:25] op_sel_hi:[1,0]
	v_pk_mul_f32 v[60:61], v[8:9], v[28:29]
	v_pk_mul_f32 v[28:29], v[56:57], v[24:25] op_sel_hi:[1,0]
	v_pk_mul_f32 v[54:55], v[10:11], v[26:27]
	v_pk_mul_f32 v[26:27], v[50:51], v[24:25] op_sel_hi:[1,0]
	v_pk_mul_f32 v[24:25], v[52:53], v[24:25] op_sel_hi:[1,0]
	v_pk_mul_f32 v[56:57], v[12:13], v[28:29]
	v_pk_mul_f32 v[52:53], v[4:5], v[24:25]
	v_pk_mul_f32 v[50:51], v[2:3], v[26:27]
; template <bool F8OUT = false> __device__ __forceinline__ void head_tile_store(const f32x4 (&acc)[2][2][4][2], bf16_t* obase  , int opitch, const float* gain, float scale, const f32x2e* rope, int row0, int fq) {
;     ...
;             if (gain) {
;                 float ss = 0.f;
; #pragma unroll
;                 for (int bj = 0; bj < 2; ++bj)
; #pragma unroll
;                     for (int n = 0; n < 2; ++n) ss += (x[bj][n][0] * x[bj][n][0] + x[bj][n][1] * x[bj][n][1]) + (x[bj][n][2] * x[bj][n][2] + x[bj][n][3] * x[bj][n][3]);
;                 ss += __shfl_xor(ss, 16); ss += __shfl_xor(ss, 32);
;                 const float r = scale / sqrtf(ss * (1.f / 64.f) + 1e-6f);
; #pragma unroll
;                 for (int bj = 0; bj < 2; ++bj)
; #pragma unroll
;                     for (int n = 0; n < 2; ++n) x[bj][n] = x[bj][n] * r * g[bj][n];
;             }
;             if (rope) {
;                 const int t = row & 8191; const bool second = (fq & 2) != 0;
; #pragma unroll
;                 for (int bj = 0; bj < 2; ++bj) { const int pos = bj ? (t & 63) : (t >> 6); const f32x2e* tb = rope + pos * 16 + 8 * (fq & 1);
; #pragma unroll
;                     for (int n = 0; n < 2; ++n)
; #pragma unroll
;                         for (int e = 0; e < 4; ++e) { const float p = __shfl_xor(x[bj][n][e], 32); const f32x2e cs = tb[4 * n + e]; const float v = x[bj][n][e];
;                             x[bj][n][e] = second ? (p * cs.y + v * cs.x) : (v * cs.x - p * cs.y); } }
;             }
;             if constexpr (F8OUT) { unsigned char* rowp8 = (unsigned char*)obase + (size_t)row * opitch + 8 * fq; typedef unsigned u32x2_ __attribute__((ext_vector_type(2)));
; #pragma unroll
;                 for (int bj = 0; bj < 2; ++bj) *(u32x2_*)(rowp8 + 32 * bj) = (u32x2_){pk4_fp8(x[bj][0][0], x[bj][0][1], x[bj][0][2], x[bj][0][3]), pk4_fp8(x[bj][1][0], x[bj][1][1], x[bj][1][2], x[bj][1][3])};
;                 continue; }
;             bf16_t* rowp = obase + (size_t)row * opitch + 8 * fq;
; #pragma unroll
;             for (int bj = 0; bj < 2; ++bj) { u32x4 w; w.x = cvt_pk_bf16(x[bj][0][0], x[bj][0][1]); w.y = cvt_pk_bf16(x[bj][0][2], x[bj][0][3]); w.z = cvt_pk_bf16(x[bj][1][0], x[bj][1][1]); w.w = cvt_pk_bf16(x[bj][1][2], x[bj][1][3]);
;                 *(u32x4*)(rowp + 32 * bj) = w; }
.LBB0_1071:
	s_mov_b64 s[6:7], 0x50000
	v_lshl_add_u64 v[28:29], v[22:23], 0, s[6:7]
	v_add_co_u32_e32 v22, vcc, 0x50000, v22
	v_cvt_pk_bf16_f32 v24, v62, v63
	v_cvt_pk_bf16_f32 v25, v64, v65
	v_cvt_pk_bf16_f32 v26, v58, v59
	v_cvt_pk_bf16_f32 v27, v60, v61
	s_nop 1
	v_addc_co_u32_e32 v23, vcc, 0, v23, vcc
	s_and_b64 vcc, exec, s[4:5]
	global_store_dwordx4 v[22:23], v[24:27], off
	v_cvt_pk_bf16_f32 v22, v54, v55
	v_cvt_pk_bf16_f32 v23, v56, v57
	s_nop 1
	v_cvt_pk_bf16_f32 v24, v50, v51
	v_cvt_pk_bf16_f32 v25, v52, v53
	global_store_dwordx4 v[28:29], v[22:25], off offset:64
	s_cbranch_vccnz .LBB0_1073
	s_nop 0
	v_pk_mul_f32 v[22:23], v[48:49], v[48:49]
	v_pk_mul_f32 v[24:25], v[46:47], v[46:47]
	s_nop 0
	v_pk_mov_b32 v[26:27], v[24:25], v[22:23] op_sel:[1,0]
	v_mov_b32_e32 v25, v23
	v_pk_add_f32 v[22:23], v[26:27], v[24:25]
	v_pk_mul_f32 v[24:25], v[44:45], v[44:45]
	v_pk_mul_f32 v[26:27], v[42:43], v[42:43]
	v_pk_add_f32 v[22:23], v[22:23], v[22:23] op_sel:[0,1] op_sel_hi:[1,0]
	v_pk_mov_b32 v[28:29], v[26:27], v[24:25] op_sel:[1,0]
	v_mov_b32_e32 v27, v25
	v_pk_add_f32 v[24:25], v[28:29], v[26:27]
	v_mul_f32_e32 v26, v34, v34
	v_mul_f32_e32 v27, v35, v35
	v_pk_add_f32 v[24:25], v[24:25], v[24:25] op_sel:[0,1] op_sel_hi:[1,0]
	v_mov_b32_e32 v23, v26
	v_mov_b32_e32 v25, v27
	v_pk_add_f32 v[22:23], v[22:23], v[24:25]
	v_mul_f32_e32 v24, v39, v39
	v_mul_f32_e32 v26, v41, v41
	v_mul_f32_e32 v28, v36, v36
	v_mul_f32_e32 v29, v37, v37
	v_pk_fma_f32 v[24:25], v[38:39], v[38:39], v[24:25] op_sel_hi:[1,1,0]
	v_pk_fma_f32 v[26:27], v[40:41], v[40:41], v[26:27] op_sel_hi:[1,1,0]
	v_mov_b32_e32 v25, v28
	v_mov_b32_e32 v27, v29
	v_pk_add_f32 v[24:25], v[24:25], v[26:27]
	s_nop 0
	v_pk_add_f32 v[22:23], v[22:23], v[24:25]
	v_and_b32_e32 v24, 64, v195
	v_add_f32_e32 v22, v22, v23
	v_xor_b32_e32 v23, 16, v195
	v_add_u32_e32 v24, 64, v24
	v_cmp_lt_i32_e32 vcc, v23, v24
	s_nop 1
	v_cndmask_b32_e32 v23, v195, v23, vcc
	v_lshlrev_b32_e32 v23, 2, v23
	v_mov_b32_e32 v23, v22
	s_nop 1
	v_permlane16_swap_b32_e32 v22, v23
	s_waitcnt lgkmcnt(0)
	v_add_f32_e32 v22, v22, v23
	v_xor_b32_e32 v23, 32, v195
	v_cmp_lt_i32_e32 vcc, v23, v24
	s_nop 1
	v_cndmask_b32_e32 v23, v195, v23, vcc
	v_lshlrev_b32_e32 v23, 2, v23
	v_mov_b32_e32 v23, v22
	s_nop 1
	v_permlane32_swap_b32_e32 v22, v23
	s_waitcnt lgkmcnt(0)
	v_add_f32_e32 v22, v22, v23
	v_fmamk_f32 v22, v22, 0x3c800000, v193
	v_mul_f32_e32 v23, 0x4f800000, v22
	v_cmp_gt_f32_e32 vcc, s69, v22
	s_nop 1
	v_cndmask_b32_e32 v22, v22, v23, vcc
	v_sqrt_f32_e32 v23, v22
	s_nop 0
	v_add_u32_e32 v24, -1, v23
	v_fma_f32 v25, -v24, v23, v22
	v_cmp_ge_f32_e64 s[4:5], 0, v25
	v_add_u32_e32 v25, 1, v23
	s_nop 0
	v_cndmask_b32_e64 v24, v23, v24, s[4:5]
	v_fma_f32 v23, -v25, v23, v22
	v_cmp_lt_f32_e64 s[4:5], 0, v23
	s_nop 1
	v_cndmask_b32_e64 v23, v24, v25, s[4:5]
	v_mul_f32_e32 v24, 0x37800000, v23
	v_cndmask_b32_e32 v23, v23, v24, vcc
	v_cmp_class_f32_e32 vcc, v22, v194
	s_nop 1
	v_cndmask_b32_e32 v22, v23, v22, vcc
	v_div_scale_f32 v23, s[4:5], v22, v22, s70
	v_rcp_f32_e32 v24, v23
	s_nop 0
	v_fma_f32 v25, -v23, v24, 1.0
	v_fmac_f32_e32 v24, v25, v24
	v_div_scale_f32 v25, vcc, s70, v22, s70
	v_mul_f32_e32 v26, v25, v24
	v_fma_f32 v27, -v23, v26, v25
	v_fmac_f32_e32 v26, v27, v24
	v_fma_f32 v23, -v23, v26, v25
	v_div_fmas_f32 v23, v23, v24, v26
	v_div_fixup_f32 v22, v23, v22, s70
	v_pk_mul_f32 v[24:25], v[46:47], v[22:23] op_sel_hi:[1,0]
	v_pk_mul_f32 v[26:27], v[48:49], v[22:23] op_sel_hi:[1,0]
	s_nop 0
	v_pk_mul_f32 v[46:47], v[14:15], v[24:25]
	v_pk_mul_f32 v[48:49], v[16:17], v[26:27]
	v_pk_mul_f32 v[14:15], v[42:43], v[22:23] op_sel_hi:[1,0]
	v_pk_mul_f32 v[16:17], v[44:45], v[22:23] op_sel_hi:[1,0]
	v_pk_mul_f32 v[42:43], v[6:7], v[14:15]
	v_pk_mul_f32 v[44:45], v[8:9], v[16:17]
	v_pk_mul_f32 v[6:7], v[38:39], v[22:23] op_sel_hi:[1,0]
	v_pk_mul_f32 v[8:9], v[40:41], v[22:23] op_sel_hi:[1,0]
	v_pk_mul_f32 v[38:39], v[10:11], v[6:7]
	v_pk_mul_f32 v[40:41], v[12:13], v[8:9]
	v_pk_mul_f32 v[6:7], v[34:35], v[22:23] op_sel_hi:[1,0]
	v_pk_mul_f32 v[8:9], v[36:37], v[22:23] op_sel_hi:[1,0]
	v_pk_mul_f32 v[34:35], v[2:3], v[6:7]
	v_pk_mul_f32 v[36:37], v[4:5], v[8:9]
